# v96: K-loop LDS-DMA address VALU removed (saddr-form DMA, +0x80 via offset:128 with compensated M0): 18 -> 6 VALU per iteration
# speedup vs baseline: 1.0032x; 1.0025x over previous
; #define PG8_STAGE_A(b, h, ptr, NX) do { if constexpr (Sched::GATHER) { unsigned gs_[2]; gs_[0] = ((NX) && last_) ? gN[h][0] : gA[h][0]; gs_[1] = ((NX) && last_) ? gN[h][1] : gA[h][1]; PG8_STAGE(PG8_SA(b, h), ptr, gs_); } \
;         else PG8_STAGE(PG8_SA(b, h), (ptr) + ((h) ? hstep : (size_t)0), voffA); } while (0)
; #define PG8_STAGE(bufoff, gbase, voff) do { _Pragma("unroll") for (int _i = 0; _i < 2; ++_i) \
;         __builtin_amdgcn_global_load_lds((const unsigned*)((const char*)(gbase) + (voff)[_i]), (PG8_LAS unsigned*)(lds + (bufoff) + ldsw + _i * 8192), 16, 0, 0); } while (0)
; #define PG8_WAIT_V(n) asm volatile("s_waitcnt vmcnt(" #n ")" ::: "memory")
; #define PG8_BAR __builtin_amdgcn_s_barrier()
; template <class Epi, class Sched, bool ALIGN_EPI = false, bool SP2 = false>
; __device__ __forceinline__ void gemm_phase(PG8_LAS unsigned char* lds, const Gemm g, const Sched& S, const Epi& E, const bool skip_epi = false) {
;     ...
;     const unsigned ldsw = (unsigned)wid * 1024u;
;     const int aoff = lds_byte(wr * 64 + fr, fq * 8), boff = lds_byte(wc * 32 + fr, fq * 8);
;     ...
;         PG8_WAIT_V(2); PG8_BAR;
;         PG8_STAGE(PG8_SB(1, 0), cB + kstep, voffB); PG8_STAGE_A(1, 0, cA + kstep, false); PG8_STAGE(PG8_SB(1, 1), cB + hstep + kstep, voffB);
;         PG8_WAIT_V(6); PG8_BAR;
.LBB0_247:
	s_lshl_b32 s10, s10, 5
	s_and_b32 s16, s10, 0x60
	s_mov_b64 s[10:11], 0x80
	s_add_i32 m0, s23, 0x18000
	v_lshl_add_u64 v[8:9], v[8:9], 0, s[10:11]
	s_lshl_b32 s13, s5, 13
	s_lshl_b32 s17, s16, 7
	s_waitcnt vmcnt(2)
	s_barrier
	global_load_lds_dwordx4 v[8:9], off
	v_lshl_add_u64 v[6:7], v[6:7], 0, s[10:11]
	s_add_i32 m0, s23, 0x1a000
	s_add_i32 s37, s23, 0x8000
	s_add_i32 s38, s23, 0xa000
	global_load_lds_dwordx4 v[6:7], off
	v_lshl_add_u64 v[2:3], v[2:3], 0, s[10:11]
	s_mov_b32 m0, s37
	s_add_u32 s14, s26, 0x40080
	global_load_lds_dwordx4 v[2:3], off
	v_lshl_add_u64 v[2:3], v[4:5], 0, s[10:11]
	s_mov_b32 m0, s38
	s_addc_u32 s15, s27, 0
	global_load_lds_dwordx4 v[2:3], off
	s_add_i32 m0, s23, 0x1c000
	s_nop 0
	global_load_lds_dwordx4 v134, s[14:15]
	s_add_i32 m0, s23, 0x1e000
	v_and_b32_e32 v1, 48, v12
	global_load_lds_dwordx4 v130, s[14:15]
	v_and_b32_e32 v2, 15, v12
	v_lshlrev_b32_e32 v3, 2, v12
	v_lshl_or_b32 v1, v2, 6, v1
	v_and_b32_e32 v3, 32, v3
	v_bitop3_b32 v4, v1, s13, v3 bitop3:0xde
	v_bitop3_b32 v1, s17, v1, v3 bitop3:0xf6
	v_bfe_u32 v3, v12, 2, 4
	v_lshlrev_b32_e32 v168, 4, v2
	v_lshl_or_b32 v167, s5, 6, v3
	v_and_b32_e32 v2, 48, v168
	v_mov_b32_e32 v3, v135
	v_lshl_add_u64 v[138:139], s[80:81], 0, v[2:3]
	v_lshlrev_b32_e32 v2, 14, v15
	v_and_b32_e32 v2, 0xffff8000, v2
	v_lshl_add_u32 v2, v14, 11, v2
	v_and_b32_e32 v3, 1, v15
	v_lshl_or_b32 v2, v3, 6, v2
	v_lshl_add_u32 v140, v16, 1, v2
	v_lshlrev_b32_e32 v2, 14, v10
	v_and_b32_e32 v2, 0xffff8000, v2
	s_waitcnt vmcnt(6)
	s_cmpk_lt_u32 s12, 0x100
	v_lshl_add_u32 v2, v11, 11, v2
	v_and_b32_e32 v3, 1, v10
	s_cselect_b64 s[12:13], -1, 0
	v_and_b32_e32 v5, 3, v12
	v_and_b32_e32 v6, 60, v12
	v_lshl_or_b32 v2, v3, 6, v2
	s_add_i32 s46, 0, 0x10000
	s_add_i32 s47, 0, 0x14000
	s_sext_i32_i8 s49, s4
	v_lshl_or_b32 v166, v5, 6, v6
	s_ashr_i32 s39, s97, 31
	v_lshl_or_b32 v169, v5, 3, s16
	v_mov_b32_e32 v141, v135
	v_lshl_add_u32 v142, v13, 1, v2
	v_mov_b32_e32 v143, v135
	v_mov_b64_e32 v[144:145], 0x300
	v_mov_b64_e32 v[146:147], 0x2ff
	v_add_u32_e32 v170, s46, v1
	v_add_u32_e32 v171, s47, v1
	v_add_u32_e32 v172, 0, v4
	v_mov_b32_e32 v173, 0x358637bd
	s_movk_i32 s48, 0x1800
	v_mov_b32_e32 v174, 0x3e000000
	v_mov_b32_e32 v175, 0x3e38aa3b
	s_barrier
	s_branch .LBB0_250

; #define PG8_GIDX(G_, PM_) do { if constexpr (Sched::GATHER) { _Pragma("unroll") for (int h_ = 0; h_ < 2; ++h_) _Pragma("unroll") for (int i_ = 0; i_ < 2; ++i_) { int R_, C_; stage_rc(tid * 16 + i_ * 8192, R_, C_); \
;         const int src_ = S.rowsrc[(PM_) * BM + h_ * HALF + R_]; G_[h_][i_] = (unsigned)(src_ * K + C_) * 2u; } } } while (0)
; #define PG8_STAGE_A(b, h, ptr, NX) do { if constexpr (Sched::GATHER) { unsigned gs_[2]; gs_[0] = ((NX) && last_) ? gN[h][0] : gA[h][0]; gs_[1] = ((NX) && last_) ? gN[h][1] : gA[h][1]; PG8_STAGE(PG8_SA(b, h), ptr, gs_); } \
;         else PG8_STAGE(PG8_SA(b, h), (ptr) + ((h) ? hstep : (size_t)0), voffA); } while (0)
; #define PG8_LDA(dst, b, h) do { _Pragma("unroll") for (int m = 0; m < 4; ++m) _Pragma("unroll") for (int k = 0; k < 2; ++k) dst[m][k] = *(const PG8_LAS bf16x8*)(lds + PG8_SA(b, h) + aoff + m * 2048 + k * 1024); } while (0)
; template <class Epi, class Sched, bool ALIGN_EPI = false, bool SP2 = false>
; __device__ __forceinline__ void gemm_phase(PG8_LAS unsigned char* lds, const Gemm g, const Sched& S, const Epi& E, const bool skip_epi = false) {
;     ...
;         const bool has_next = S.next(ui + 1, nxt);
;         if (has_next) PG8_GIDX(gN, nxt.pm);
;         const char* nA = has_next ? (const char*)g.A + (size_t)nxt.pm * pmstepA + nxt.ko : cA; const char* nB = has_next ? (const char*)g.Bt + (size_t)nxt.pn * tstep + nxt.ko : cB;
;         for (int t = 0; t < nt; t += 2) {
;             const bool last = (t == nt - 2); last_ = last && has_next;
;             const char* a1 = cA + (size_t)(t + 1) * kstep;
;             const char* a2 = last ? nA : cA + (size_t)(t + 2) * kstep; const char* b2 = last ? nB : cB + (size_t)(t + 2) * kstep;
;             const char* a3 = a2 + kstep; const char* b3 = b2 + kstep;
;             if (last && has_next) S.a_ready(nxt);
;             if constexpr (SP2) {
;             PG8_LDB(B0, 0, 0); PG8_LDB(B1, 0, 1); PG8_SCHED; PG8_LDA(At, 0, 0); PG8_STAGE_A(1, 1, a1, false);
;             PG8_WAIT_V(8); PG8_WAIT_L(0); PG8_BAR; PG8_MMA(0, 0, At, B0); PG8_MMA(0, 1, At, B1); PG8_BAR; PG8_SCHED;
;             PG8_LDA(At, 0, 1); PG8_STAGE(PG8_SB(0, 0), b2, voffB); PG8_STAGE(PG8_SB(0, 1), b2 + hstep, voffB); PG8_STAGE_A(0, 0, a2, true);
;             PG8_WAIT_V(8); PG8_WAIT_L(0); PG8_BAR; PG8_MMA(1, 0, At, B0); PG8_MMA(1, 1, At, B1); PG8_BAR; PG8_SCHED;
.LBB0_252:
	s_ashr_i32 s17, s16, 31
	s_lshl_b64 s[18:19], s[16:17], 19
	s_add_u32 s18, s86, s18
	s_addc_u32 s19, s87, s19
	s_and_b64 s[20:21], s[4:5], exec
	s_cselect_b32 s17, s19, s25
	s_cselect_b32 s56, s18, s24
	s_ashr_i32 s15, s14, 31
	s_lshl_b64 s[20:21], s[14:15], 19
	v_readlane_b32 s28, v254, 36
	v_readlane_b32 s29, v254, 37
	s_add_u32 s20, s28, s20
	s_addc_u32 s21, s29, s21
	s_and_b64 s[28:29], s[4:5], exec
	s_cselect_b32 s15, s21, s27
	s_cselect_b32 s57, s20, s26
	s_add_u32 s24, s24, 0x40080
	s_addc_u32 s25, s25, 0
	s_add_u32 s58, s26, 0x100
	s_addc_u32 s59, s27, 0
	s_mov_b32 s60, -2
	s_waitcnt vmcnt(0)
	ds_read_b128 v[148:151], v170
	ds_read_b128 v[152:155], v170 offset:1024
	ds_read_b128 v[156:159], v170 offset:2048
	ds_read_b128 v[160:163], v170 offset:3072
	ds_read_b128 v[176:179], v171
	ds_read_b128 v[180:183], v171 offset:1024
	ds_read_b128 v[184:187], v171 offset:2048
	ds_read_b128 v[188:191], v171 offset:3072
	s_add_u32 s26, s24, 0xfffc0080
	s_addc_u32 s27, s25, -1
	s_cmp_eq_u32 s60, 12
	s_cselect_b32 s29, s17, s27
	s_cselect_b32 s28, s56, s26
	s_cselect_b32 s27, s15, s59
	s_cselect_b32 s26, s57, s58
	s_add_i32 m0, s23, 0xc000
	ds_read_b128 v[192:195], v172
	ds_read_b128 v[196:199], v172 offset:1024
	ds_read_b128 v[200:203], v172 offset:2048
	ds_read_b128 v[204:207], v172 offset:3072
	ds_read_b128 v[208:211], v172 offset:4096
	ds_read_b128 v[212:215], v172 offset:5120
	ds_read_b128 v[216:219], v172 offset:6144
	ds_read_b128 v[220:223], v172 offset:7168
	global_load_lds_dwordx4 v140, s[24:25]
	s_add_i32 m0, s23, 0xe000
	s_nop 0
	global_load_lds_dwordx4 v142, s[24:25]
	s_waitcnt vmcnt(8)
	s_waitcnt lgkmcnt(0)
	s_barrier
	s_setprio 3
	s_waitcnt lgkmcnt(0)
	v_mfma_f32_16x16x32_bf16 v[126:129], v[148:151], v[192:195], 0
	v_mfma_f32_16x16x32_bf16 v[122:125], v[156:159], v[192:195], 0
	v_mfma_f32_16x16x32_bf16 v[114:117], v[148:151], v[200:203], 0
	v_mfma_f32_16x16x32_bf16 v[106:109], v[156:159], v[200:203], 0
	v_mfma_f32_16x16x32_bf16 v[98:101], v[148:151], v[208:211], 0
	v_mfma_f32_16x16x32_bf16 v[90:93], v[156:159], v[208:211], 0
	v_mfma_f32_16x16x32_bf16 v[82:85], v[148:151], v[216:219], 0
	v_mfma_f32_16x16x32_bf16 v[74:77], v[156:159], v[216:219], 0
	v_mfma_f32_16x16x32_bf16 v[126:129], v[152:155], v[196:199], v[126:129]
	v_mfma_f32_16x16x32_bf16 v[122:125], v[160:163], v[196:199], v[122:125]
	v_mfma_f32_16x16x32_bf16 v[114:117], v[152:155], v[204:207], v[114:117]
	v_mfma_f32_16x16x32_bf16 v[106:109], v[160:163], v[204:207], v[106:109]
	v_mfma_f32_16x16x32_bf16 v[98:101], v[152:155], v[212:215], v[98:101]
	v_mfma_f32_16x16x32_bf16 v[90:93], v[160:163], v[212:215], v[90:93]
	v_mfma_f32_16x16x32_bf16 v[82:85], v[152:155], v[220:223], v[82:85]
	v_mfma_f32_16x16x32_bf16 v[74:77], v[160:163], v[220:223], v[74:77]
	s_setprio 0
	s_setprio 3
	v_mfma_f32_16x16x32_bf16 v[118:121], v[176:179], v[192:195], 0
	v_mfma_f32_16x16x32_bf16 v[110:113], v[184:187], v[192:195], 0
	v_mfma_f32_16x16x32_bf16 v[102:105], v[176:179], v[200:203], 0
	v_mfma_f32_16x16x32_bf16 v[94:97], v[184:187], v[200:203], 0
	v_mfma_f32_16x16x32_bf16 v[86:89], v[176:179], v[208:211], 0
	v_mfma_f32_16x16x32_bf16 v[78:81], v[184:187], v[208:211], 0
	v_mfma_f32_16x16x32_bf16 v[70:73], v[176:179], v[216:219], 0
	v_mfma_f32_16x16x32_bf16 v[66:69], v[184:187], v[216:219], 0
	v_mfma_f32_16x16x32_bf16 v[118:121], v[180:183], v[196:199], v[118:121]
	v_mfma_f32_16x16x32_bf16 v[110:113], v[188:191], v[196:199], v[110:113]
	v_mfma_f32_16x16x32_bf16 v[102:105], v[180:183], v[204:207], v[102:105]
	v_mfma_f32_16x16x32_bf16 v[94:97], v[188:191], v[204:207], v[94:97]
	v_mfma_f32_16x16x32_bf16 v[86:89], v[180:183], v[212:215], v[86:89]
	v_mfma_f32_16x16x32_bf16 v[78:81], v[188:191], v[212:215], v[78:81]
	v_mfma_f32_16x16x32_bf16 v[70:73], v[180:183], v[220:223], v[70:73]
	v_mfma_f32_16x16x32_bf16 v[66:69], v[188:191], v[220:223], v[66:69]
	s_setprio 0
	s_barrier
	s_add_i32 s61, s46, s2
	v_lshl_add_u64 v[164:165], s[26:27], 0, v[134:135]
	s_mov_b32 m0, s61
	ds_read_b128 v[192:195], v172 offset:16384
	ds_read_b128 v[196:199], v172 offset:17408
	ds_read_b128 v[200:203], v172 offset:18432
	ds_read_b128 v[204:207], v172 offset:19456
	ds_read_b128 v[208:211], v172 offset:20480
	ds_read_b128 v[212:215], v172 offset:21504
	ds_read_b128 v[216:219], v172 offset:22528
	ds_read_b128 v[220:223], v172 offset:23552
	global_load_lds_dwordx4 v[164:165], off
	s_add_i32 m0, s61, 0x2000
	s_add_u32 s62, s26, 0x40000
	v_lshl_add_u64 v[224:225], s[26:27], 0, v[130:131]
	s_addc_u32 s63, s27, 0
	s_add_i32 s61, s47, s2
	global_load_lds_dwordx4 v[224:225], off
	s_mov_b32 m0, s61
	v_lshl_add_u64 v[230:231], s[28:29], 0, v[132:133]
	global_load_lds_dwordx4 v134, s[62:63]
	s_add_i32 m0, s61, 0x2000
	s_nop 0
	global_load_lds_dwordx4 v130, s[62:63]
	v_lshl_add_u64 v[226:227], s[28:29], 0, v[136:137]
	s_mov_b32 m0, s23
	s_nop 0
	global_load_lds_dwordx4 v[226:227], off
	s_mov_b32 m0, s31
	s_nop 0
	global_load_lds_dwordx4 v[230:231], off
	s_waitcnt vmcnt(8)
	s_waitcnt lgkmcnt(0)
	s_barrier
; #define PG8_STAGE_A(b, h, ptr, NX) do { if constexpr (Sched::GATHER) { unsigned gs_[2]; gs_[0] = ((NX) && last_) ? gN[h][0] : gA[h][0]; gs_[1] = ((NX) && last_) ? gN[h][1] : gA[h][1]; PG8_STAGE(PG8_SA(b, h), ptr, gs_); } \
;         else PG8_STAGE(PG8_SA(b, h), (ptr) + ((h) ? hstep : (size_t)0), voffA); } while (0)
; #define PG8_LDA(dst, b, h) do { _Pragma("unroll") for (int m = 0; m < 4; ++m) _Pragma("unroll") for (int k = 0; k < 2; ++k) dst[m][k] = *(const PG8_LAS bf16x8*)(lds + PG8_SA(b, h) + aoff + m * 2048 + k * 1024); } while (0)
; #define PG8_LDB(dst, b, h) do { _Pragma("unroll") for (int n = 0; n < 2; ++n) _Pragma("unroll") for (int k = 0; k < 2; ++k) dst[n][k] = *(const PG8_LAS bf16x8*)(lds + PG8_SB(b, h) + boff + n * 2048 + k * 1024); } while (0)
; #define PG8_MMA(ai, bj, At, Bt) do { __builtin_amdgcn_s_setprio(1); _Pragma("unroll") for (int m = 0; m < 4; ++m) _Pragma("unroll") for (int n = 0; n < 2; ++n) _Pragma("unroll") for (int k = 0; k < 2; ++k) \
;         acc[ai][bj][m][n] = __builtin_amdgcn_mfma_f32_16x16x32_bf16(Bt[n][k], At[m][k], acc[ai][bj][m][n], 0, 0, 0); __builtin_amdgcn_s_setprio(0); } while (0)
; #define PG8_WAIT_V(n) asm volatile("s_waitcnt vmcnt(" #n ")" ::: "memory")
; #define PG8_WAIT_L(n) asm volatile("s_waitcnt lgkmcnt(" #n ")" ::: "memory")
; #define PG8_BAR __builtin_amdgcn_s_barrier()
; #define PG8_SCHED __builtin_amdgcn_sched_barrier(0)
; template <class Epi, class Sched, bool ALIGN_EPI = false, bool SP2 = false>
; __device__ __forceinline__ void gemm_phase(PG8_LAS unsigned char* lds, const Gemm g, const Sched& S, const Epi& E, const bool skip_epi = false) {
;     ...
;             PG8_WAIT_V(8); PG8_WAIT_L(0); PG8_BAR; PG8_MMA(1, 0, At, B0); PG8_MMA(1, 1, At, B1); PG8_BAR; PG8_SCHED;
;             PG8_LDB(B0, 1, 0); PG8_LDB(B1, 1, 1); PG8_SCHED; PG8_LDA(At, 1, 0); PG8_STAGE_A(0, 1, a2, true);
;             PG8_WAIT_V(8); PG8_WAIT_L(0); PG8_BAR; PG8_MMA(0, 0, At, B0); PG8_MMA(0, 1, At, B1); PG8_BAR; PG8_SCHED;
	s_setprio 3
	s_waitcnt lgkmcnt(0)
	v_mfma_f32_16x16x32_bf16 v[62:65], v[148:151], v[192:195], 0
	v_mfma_f32_16x16x32_bf16 v[58:61], v[156:159], v[192:195], 0
	v_mfma_f32_16x16x32_bf16 v[50:53], v[148:151], v[200:203], 0
	v_mfma_f32_16x16x32_bf16 v[42:45], v[156:159], v[200:203], 0
	v_mfma_f32_16x16x32_bf16 v[34:37], v[148:151], v[208:211], 0
	v_mfma_f32_16x16x32_bf16 v[26:29], v[156:159], v[208:211], 0
	v_mfma_f32_16x16x32_bf16 v[18:21], v[148:151], v[216:219], 0
	v_mfma_f32_16x16x32_bf16 v[10:13], v[156:159], v[216:219], 0
	v_mfma_f32_16x16x32_bf16 v[62:65], v[152:155], v[196:199], v[62:65]
	v_mfma_f32_16x16x32_bf16 v[58:61], v[160:163], v[196:199], v[58:61]
	v_mfma_f32_16x16x32_bf16 v[50:53], v[152:155], v[204:207], v[50:53]
	v_mfma_f32_16x16x32_bf16 v[42:45], v[160:163], v[204:207], v[42:45]
	v_mfma_f32_16x16x32_bf16 v[34:37], v[152:155], v[212:215], v[34:37]
	v_mfma_f32_16x16x32_bf16 v[26:29], v[160:163], v[212:215], v[26:29]
	v_mfma_f32_16x16x32_bf16 v[18:21], v[152:155], v[220:223], v[18:21]
	v_mfma_f32_16x16x32_bf16 v[10:13], v[160:163], v[220:223], v[10:13]
	s_setprio 0
	s_setprio 3
	v_mfma_f32_16x16x32_bf16 v[54:57], v[176:179], v[192:195], 0
	v_mfma_f32_16x16x32_bf16 v[46:49], v[184:187], v[192:195], 0
	v_mfma_f32_16x16x32_bf16 v[38:41], v[176:179], v[200:203], 0
	v_mfma_f32_16x16x32_bf16 v[30:33], v[184:187], v[200:203], 0
	v_mfma_f32_16x16x32_bf16 v[22:25], v[176:179], v[208:211], 0
	v_mfma_f32_16x16x32_bf16 v[14:17], v[184:187], v[208:211], 0
	v_mfma_f32_16x16x32_bf16 v[6:9], v[176:179], v[216:219], 0
	v_mfma_f32_16x16x32_bf16 v[2:5], v[184:187], v[216:219], 0
	v_mfma_f32_16x16x32_bf16 v[54:57], v[180:183], v[196:199], v[54:57]
	v_mfma_f32_16x16x32_bf16 v[46:49], v[188:191], v[196:199], v[46:49]
	v_mfma_f32_16x16x32_bf16 v[38:41], v[180:183], v[204:207], v[38:41]
	v_mfma_f32_16x16x32_bf16 v[30:33], v[188:191], v[204:207], v[30:33]
	v_mfma_f32_16x16x32_bf16 v[22:25], v[180:183], v[212:215], v[22:25]
	v_mfma_f32_16x16x32_bf16 v[14:17], v[188:191], v[212:215], v[14:17]
	v_mfma_f32_16x16x32_bf16 v[6:9], v[180:183], v[220:223], v[6:9]
	v_mfma_f32_16x16x32_bf16 v[2:5], v[188:191], v[220:223], v[2:5]
	s_setprio 0
	s_barrier
	s_add_i32 s61, 0, 0x18000
	s_add_i32 s62, 0, 0x1c000
	v_add_u32_e32 v160, s61, v1
	v_add_u32_e32 v188, s62, v1
	ds_read_b128 v[148:151], v160
	ds_read_b128 v[152:155], v160 offset:1024
	ds_read_b128 v[156:159], v160 offset:2048
	ds_read_b128 v[160:163], v160 offset:3072
	ds_read_b128 v[176:179], v188
	ds_read_b128 v[180:183], v188 offset:1024
	ds_read_b128 v[184:187], v188 offset:2048
	ds_read_b128 v[188:191], v188 offset:3072
	s_add_u32 s28, s28, 0x40000
	s_addc_u32 s29, s29, 0
	s_mov_b32 m0, s34
	ds_read_b128 v[192:195], v172 offset:32768
	ds_read_b128 v[196:199], v172 offset:33792
	ds_read_b128 v[200:203], v172 offset:34816
	ds_read_b128 v[204:207], v172 offset:35840
	ds_read_b128 v[208:211], v172 offset:36864
	ds_read_b128 v[212:215], v172 offset:37888
	ds_read_b128 v[216:219], v172 offset:38912
	ds_read_b128 v[220:223], v172 offset:39936
	global_load_lds_dwordx4 v136, s[28:29]
	s_mov_b32 m0, s35
	s_nop 0
	global_load_lds_dwordx4 v132, s[28:29]
	s_waitcnt vmcnt(8)
	s_waitcnt lgkmcnt(0)
	s_barrier
	s_setprio 3
	s_waitcnt lgkmcnt(0)
	v_mfma_f32_16x16x32_bf16 v[126:129], v[148:151], v[192:195], v[126:129]
	v_mfma_f32_16x16x32_bf16 v[122:125], v[156:159], v[192:195], v[122:125]
	v_mfma_f32_16x16x32_bf16 v[114:117], v[148:151], v[200:203], v[114:117]
	v_mfma_f32_16x16x32_bf16 v[106:109], v[156:159], v[200:203], v[106:109]
	v_mfma_f32_16x16x32_bf16 v[98:101], v[148:151], v[208:211], v[98:101]
	v_mfma_f32_16x16x32_bf16 v[90:93], v[156:159], v[208:211], v[90:93]
	v_mfma_f32_16x16x32_bf16 v[82:85], v[148:151], v[216:219], v[82:85]
	v_mfma_f32_16x16x32_bf16 v[74:77], v[156:159], v[216:219], v[74:77]
	v_mfma_f32_16x16x32_bf16 v[126:129], v[152:155], v[196:199], v[126:129]
	v_mfma_f32_16x16x32_bf16 v[122:125], v[160:163], v[196:199], v[122:125]
	v_mfma_f32_16x16x32_bf16 v[114:117], v[152:155], v[204:207], v[114:117]
	v_mfma_f32_16x16x32_bf16 v[106:109], v[160:163], v[204:207], v[106:109]
	v_mfma_f32_16x16x32_bf16 v[98:101], v[152:155], v[212:215], v[98:101]
	v_mfma_f32_16x16x32_bf16 v[90:93], v[160:163], v[212:215], v[90:93]
	v_mfma_f32_16x16x32_bf16 v[82:85], v[152:155], v[220:223], v[82:85]
	v_mfma_f32_16x16x32_bf16 v[74:77], v[160:163], v[220:223], v[74:77]
	s_setprio 0
	s_setprio 3
	v_mfma_f32_16x16x32_bf16 v[118:121], v[176:179], v[192:195], v[118:121]
	v_mfma_f32_16x16x32_bf16 v[110:113], v[184:187], v[192:195], v[110:113]
	v_mfma_f32_16x16x32_bf16 v[102:105], v[176:179], v[200:203], v[102:105]
	v_mfma_f32_16x16x32_bf16 v[94:97], v[184:187], v[200:203], v[94:97]
	v_mfma_f32_16x16x32_bf16 v[86:89], v[176:179], v[208:211], v[86:89]
	v_mfma_f32_16x16x32_bf16 v[78:81], v[184:187], v[208:211], v[78:81]
	v_mfma_f32_16x16x32_bf16 v[70:73], v[176:179], v[216:219], v[70:73]
	v_mfma_f32_16x16x32_bf16 v[66:69], v[184:187], v[216:219], v[66:69]
	v_mfma_f32_16x16x32_bf16 v[118:121], v[180:183], v[196:199], v[118:121]
	v_mfma_f32_16x16x32_bf16 v[110:113], v[188:191], v[196:199], v[110:113]
	v_mfma_f32_16x16x32_bf16 v[102:105], v[180:183], v[204:207], v[102:105]
	v_mfma_f32_16x16x32_bf16 v[94:97], v[188:191], v[204:207], v[94:97]
	v_mfma_f32_16x16x32_bf16 v[86:89], v[180:183], v[212:215], v[86:89]
	v_mfma_f32_16x16x32_bf16 v[78:81], v[188:191], v[212:215], v[78:81]
	v_mfma_f32_16x16x32_bf16 v[70:73], v[180:183], v[220:223], v[70:73]
	v_mfma_f32_16x16x32_bf16 v[66:69], v[188:191], v[220:223], v[66:69]
	s_setprio 0
	s_barrier
; #define PG8_STAGE_A(b, h, ptr, NX) do { if constexpr (Sched::GATHER) { unsigned gs_[2]; gs_[0] = ((NX) && last_) ? gN[h][0] : gA[h][0]; gs_[1] = ((NX) && last_) ? gN[h][1] : gA[h][1]; PG8_STAGE(PG8_SA(b, h), ptr, gs_); } \
;         else PG8_STAGE(PG8_SA(b, h), (ptr) + ((h) ? hstep : (size_t)0), voffA); } while (0)
; #define PG8_STAGE(bufoff, gbase, voff) do { _Pragma("unroll") for (int _i = 0; _i < 2; ++_i) \
;         __builtin_amdgcn_global_load_lds((const unsigned*)((const char*)(gbase) + (voff)[_i]), (PG8_LAS unsigned*)(lds + (bufoff) + ldsw + _i * 8192), 16, 0, 0); } while (0)
; template <class Epi, class Sched, bool ALIGN_EPI = false, bool SP2 = false>
; __device__ __forceinline__ void gemm_phase(PG8_LAS unsigned char* lds, const Gemm g, const Sched& S, const Epi& E, const bool skip_epi = false) {
;     ...
;         for (int t = 0; t < nt; t += 2) {
;             const bool last = (t == nt - 2); last_ = last && has_next;
;             const char* a1 = cA + (size_t)(t + 1) * kstep;
;             const char* a2 = last ? nA : cA + (size_t)(t + 2) * kstep; const char* b2 = last ? nB : cB + (size_t)(t + 2) * kstep;
;             const char* a3 = a2 + kstep; const char* b3 = b2 + kstep;
;             if (last && has_next) S.a_ready(nxt);
;             if constexpr (SP2) {
;             PG8_LDB(B0, 0, 0); PG8_LDB(B1, 0, 1); PG8_SCHED; PG8_LDA(At, 0, 0); PG8_STAGE_A(1, 1, a1, false);
;             PG8_WAIT_V(8); PG8_WAIT_L(0); PG8_BAR; PG8_MMA(0, 0, At, B0); PG8_MMA(0, 1, At, B1); PG8_BAR; PG8_SCHED;
;             PG8_LDA(At, 0, 1); PG8_STAGE(PG8_SB(0, 0), b2, voffB); PG8_STAGE(PG8_SB(0, 1), b2 + hstep, voffB); PG8_STAGE_A(0, 0, a2, true);
;             PG8_WAIT_V(8); PG8_WAIT_L(0); PG8_BAR; PG8_MMA(1, 0, At, B0); PG8_MMA(1, 1, At, B1); PG8_BAR; PG8_SCHED;
;             PG8_LDB(B0, 1, 0); PG8_LDB(B1, 1, 1); PG8_SCHED; PG8_LDA(At, 1, 0); PG8_STAGE_A(0, 1, a2, true);
;             PG8_WAIT_V(8); PG8_WAIT_L(0); PG8_BAR; PG8_MMA(0, 0, At, B0); PG8_MMA(0, 1, At, B1); PG8_BAR; PG8_SCHED;
;             PG8_LDA(At, 1, 1); PG8_STAGE(PG8_SB(1, 0), b3, voffB); PG8_STAGE(PG8_SB(1, 1), b3 + hstep, voffB); PG8_STAGE_A(1, 0, a3, true);
;             PG8_WAIT_V(8); PG8_WAIT_L(0); PG8_BAR; PG8_MMA(1, 0, At, B0); PG8_MMA(1, 1, At, B1); PG8_BAR; PG8_SCHED;
;             } else {
;             PG8_LDB(B0, 0, 0); PG8_SCHED; PG8_LDA(At, 0, 0); PG8_STAGE_A(1, 1, a1, false);
	s_add_i32 s28, s61, s2
	s_add_i32 m0, s28, 0xffffff80
	ds_read_b128 v[192:195], v172 offset:49152
	ds_read_b128 v[196:199], v172 offset:50176
	ds_read_b128 v[200:203], v172 offset:51200
	ds_read_b128 v[204:207], v172 offset:52224
	ds_read_b128 v[208:211], v172 offset:53248
	ds_read_b128 v[212:215], v172 offset:54272
	ds_read_b128 v[216:219], v172 offset:55296
	ds_read_b128 v[220:223], v172 offset:56320
	global_load_lds_dwordx4 v[164:165], off offset:128
	s_add_i32 m0, s28, 0x1f80
	s_add_u32 s26, s26, 0x40080
	s_addc_u32 s27, s27, 0
	s_add_i32 s28, s62, s2
	global_load_lds_dwordx4 v[224:225], off offset:128
	s_mov_b32 m0, s28
	s_nop 0
	global_load_lds_dwordx4 v134, s[26:27]
	s_add_i32 m0, s28, 0x2000
	s_nop 0
	global_load_lds_dwordx4 v130, s[26:27]
	s_add_i32 m0, s37, 0xffffff80
	s_nop 0
	global_load_lds_dwordx4 v[226:227], off offset:128
	s_add_i32 m0, s38, 0xffffff80
	s_nop 0
	global_load_lds_dwordx4 v[230:231], off offset:128
	s_waitcnt vmcnt(8)
	s_waitcnt lgkmcnt(0)
	s_barrier
	s_setprio 3
	s_waitcnt lgkmcnt(0)
	v_mfma_f32_16x16x32_bf16 v[62:65], v[148:151], v[192:195], v[62:65]
	v_mfma_f32_16x16x32_bf16 v[58:61], v[156:159], v[192:195], v[58:61]
	v_mfma_f32_16x16x32_bf16 v[50:53], v[148:151], v[200:203], v[50:53]
	v_mfma_f32_16x16x32_bf16 v[42:45], v[156:159], v[200:203], v[42:45]
	v_mfma_f32_16x16x32_bf16 v[34:37], v[148:151], v[208:211], v[34:37]
	v_mfma_f32_16x16x32_bf16 v[26:29], v[156:159], v[208:211], v[26:29]
	v_mfma_f32_16x16x32_bf16 v[18:21], v[148:151], v[216:219], v[18:21]
	v_mfma_f32_16x16x32_bf16 v[10:13], v[156:159], v[216:219], v[10:13]
	v_mfma_f32_16x16x32_bf16 v[62:65], v[152:155], v[196:199], v[62:65]
	v_mfma_f32_16x16x32_bf16 v[58:61], v[160:163], v[196:199], v[58:61]
	v_mfma_f32_16x16x32_bf16 v[50:53], v[152:155], v[204:207], v[50:53]
	v_mfma_f32_16x16x32_bf16 v[42:45], v[160:163], v[204:207], v[42:45]
	v_mfma_f32_16x16x32_bf16 v[34:37], v[152:155], v[212:215], v[34:37]
	v_mfma_f32_16x16x32_bf16 v[26:29], v[160:163], v[212:215], v[26:29]
	v_mfma_f32_16x16x32_bf16 v[18:21], v[152:155], v[220:223], v[18:21]
	v_mfma_f32_16x16x32_bf16 v[10:13], v[160:163], v[220:223], v[10:13]
	s_setprio 0
	s_setprio 3
	v_mfma_f32_16x16x32_bf16 v[54:57], v[176:179], v[192:195], v[54:57]
	v_mfma_f32_16x16x32_bf16 v[46:49], v[184:187], v[192:195], v[46:49]
	v_mfma_f32_16x16x32_bf16 v[38:41], v[176:179], v[200:203], v[38:41]
	v_mfma_f32_16x16x32_bf16 v[30:33], v[184:187], v[200:203], v[30:33]
	v_mfma_f32_16x16x32_bf16 v[22:25], v[176:179], v[208:211], v[22:25]
	v_mfma_f32_16x16x32_bf16 v[14:17], v[184:187], v[208:211], v[14:17]
	v_mfma_f32_16x16x32_bf16 v[6:9], v[176:179], v[216:219], v[6:9]
	v_mfma_f32_16x16x32_bf16 v[2:5], v[184:187], v[216:219], v[2:5]
	v_mfma_f32_16x16x32_bf16 v[54:57], v[180:183], v[196:199], v[54:57]
	v_mfma_f32_16x16x32_bf16 v[46:49], v[188:191], v[196:199], v[46:49]
	v_mfma_f32_16x16x32_bf16 v[38:41], v[180:183], v[204:207], v[38:41]
	v_mfma_f32_16x16x32_bf16 v[30:33], v[188:191], v[204:207], v[30:33]
	v_mfma_f32_16x16x32_bf16 v[22:25], v[180:183], v[212:215], v[22:25]
	v_mfma_f32_16x16x32_bf16 v[14:17], v[188:191], v[212:215], v[14:17]
	v_mfma_f32_16x16x32_bf16 v[6:9], v[180:183], v[220:223], v[6:9]
	v_mfma_f32_16x16x32_bf16 v[2:5], v[188:191], v[220:223], v[2:5]
	s_setprio 0
	s_barrier
	s_add_i32 s60, s60, 2
	s_add_u32 s24, s24, 0x100
	s_addc_u32 s25, s25, 0
	s_add_u32 s58, s58, 0x100
	s_addc_u32 s59, s59, 0
	s_cmp_gt_u32 s60, 13
.LBB0_253:
	ds_read_b128 v[148:151], v170
	ds_read_b128 v[152:155], v170 offset:1024
	ds_read_b128 v[156:159], v170 offset:2048
	ds_read_b128 v[160:163], v170 offset:3072
	ds_read_b128 v[176:179], v171
	ds_read_b128 v[180:183], v171 offset:1024
	ds_read_b128 v[184:187], v171 offset:2048
	ds_read_b128 v[188:191], v171 offset:3072
	s_add_u32 s26, s24, 0xfffc0080
	s_addc_u32 s27, s25, -1
	s_cmp_eq_u32 s60, 12
	s_cselect_b32 s29, s17, s27
	s_cselect_b32 s28, s56, s26
	s_cselect_b32 s27, s15, s59
	s_cselect_b32 s26, s57, s58
	s_add_i32 m0, s23, 0xc000
	ds_read_b128 v[192:195], v172
	ds_read_b128 v[196:199], v172 offset:1024
	ds_read_b128 v[200:203], v172 offset:2048
	ds_read_b128 v[204:207], v172 offset:3072
	ds_read_b128 v[208:211], v172 offset:4096
	ds_read_b128 v[212:215], v172 offset:5120
	ds_read_b128 v[216:219], v172 offset:6144
	ds_read_b128 v[220:223], v172 offset:7168
	global_load_lds_dwordx4 v140, s[24:25]
	s_add_i32 m0, s23, 0xe000
	s_nop 0
	global_load_lds_dwordx4 v142, s[24:25]
	s_waitcnt vmcnt(8)
	s_waitcnt lgkmcnt(0)
	s_barrier
; #define PG8_STAGE_A(b, h, ptr, NX) do { if constexpr (Sched::GATHER) { unsigned gs_[2]; gs_[0] = ((NX) && last_) ? gN[h][0] : gA[h][0]; gs_[1] = ((NX) && last_) ? gN[h][1] : gA[h][1]; PG8_STAGE(PG8_SA(b, h), ptr, gs_); } \
;         else PG8_STAGE(PG8_SA(b, h), (ptr) + ((h) ? hstep : (size_t)0), voffA); } while (0)
; #define PG8_STAGE(bufoff, gbase, voff) do { _Pragma("unroll") for (int _i = 0; _i < 2; ++_i) \
;         __builtin_amdgcn_global_load_lds((const unsigned*)((const char*)(gbase) + (voff)[_i]), (PG8_LAS unsigned*)(lds + (bufoff) + ldsw + _i * 8192), 16, 0, 0); } while (0)
; #define PG8_LDA(dst, b, h) do { _Pragma("unroll") for (int m = 0; m < 4; ++m) _Pragma("unroll") for (int k = 0; k < 2; ++k) dst[m][k] = *(const PG8_LAS bf16x8*)(lds + PG8_SA(b, h) + aoff + m * 2048 + k * 1024); } while (0)
; #define PG8_MMA(ai, bj, At, Bt) do { __builtin_amdgcn_s_setprio(1); _Pragma("unroll") for (int m = 0; m < 4; ++m) _Pragma("unroll") for (int n = 0; n < 2; ++n) _Pragma("unroll") for (int k = 0; k < 2; ++k) \
;         acc[ai][bj][m][n] = __builtin_amdgcn_mfma_f32_16x16x32_bf16(Bt[n][k], At[m][k], acc[ai][bj][m][n], 0, 0, 0); __builtin_amdgcn_s_setprio(0); } while (0)
; #define PG8_WAIT_V(n) asm volatile("s_waitcnt vmcnt(" #n ")" ::: "memory")
; #define PG8_WAIT_L(n) asm volatile("s_waitcnt lgkmcnt(" #n ")" ::: "memory")
; #define PG8_BAR __builtin_amdgcn_s_barrier()
; #define PG8_SCHED __builtin_amdgcn_sched_barrier(0)
; template <class Epi, class Sched, bool ALIGN_EPI = false, bool SP2 = false>
; __device__ __forceinline__ void gemm_phase(PG8_LAS unsigned char* lds, const Gemm g, const Sched& S, const Epi& E, const bool skip_epi = false) {
;     ...
;             PG8_WAIT_V(8); PG8_WAIT_L(0); PG8_BAR; PG8_MMA(0, 0, At, B0); PG8_MMA(0, 1, At, B1); PG8_BAR; PG8_SCHED;
;             PG8_LDA(At, 0, 1); PG8_STAGE(PG8_SB(0, 0), b2, voffB); PG8_STAGE(PG8_SB(0, 1), b2 + hstep, voffB); PG8_STAGE_A(0, 0, a2, true);
;             PG8_WAIT_V(8); PG8_WAIT_L(0); PG8_BAR; PG8_MMA(1, 0, At, B0); PG8_MMA(1, 1, At, B1); PG8_BAR; PG8_SCHED;
	s_setprio 3
	s_waitcnt lgkmcnt(0)
	v_mfma_f32_16x16x32_bf16 v[126:129], v[148:151], v[192:195], v[126:129]
	v_mfma_f32_16x16x32_bf16 v[122:125], v[156:159], v[192:195], v[122:125]
	v_mfma_f32_16x16x32_bf16 v[114:117], v[148:151], v[200:203], v[114:117]
	v_mfma_f32_16x16x32_bf16 v[106:109], v[156:159], v[200:203], v[106:109]
	v_mfma_f32_16x16x32_bf16 v[98:101], v[148:151], v[208:211], v[98:101]
	v_mfma_f32_16x16x32_bf16 v[90:93], v[156:159], v[208:211], v[90:93]
	v_mfma_f32_16x16x32_bf16 v[82:85], v[148:151], v[216:219], v[82:85]
	v_mfma_f32_16x16x32_bf16 v[74:77], v[156:159], v[216:219], v[74:77]
	v_mfma_f32_16x16x32_bf16 v[126:129], v[152:155], v[196:199], v[126:129]
	v_mfma_f32_16x16x32_bf16 v[122:125], v[160:163], v[196:199], v[122:125]
	v_mfma_f32_16x16x32_bf16 v[114:117], v[152:155], v[204:207], v[114:117]
	v_mfma_f32_16x16x32_bf16 v[106:109], v[160:163], v[204:207], v[106:109]
	v_mfma_f32_16x16x32_bf16 v[98:101], v[152:155], v[212:215], v[98:101]
	v_mfma_f32_16x16x32_bf16 v[90:93], v[160:163], v[212:215], v[90:93]
	v_mfma_f32_16x16x32_bf16 v[82:85], v[152:155], v[220:223], v[82:85]
	v_mfma_f32_16x16x32_bf16 v[74:77], v[160:163], v[220:223], v[74:77]
	s_setprio 0
	s_setprio 3
	v_mfma_f32_16x16x32_bf16 v[118:121], v[176:179], v[192:195], v[118:121]
	v_mfma_f32_16x16x32_bf16 v[110:113], v[184:187], v[192:195], v[110:113]
	v_mfma_f32_16x16x32_bf16 v[102:105], v[176:179], v[200:203], v[102:105]
	v_mfma_f32_16x16x32_bf16 v[94:97], v[184:187], v[200:203], v[94:97]
	v_mfma_f32_16x16x32_bf16 v[86:89], v[176:179], v[208:211], v[86:89]
	v_mfma_f32_16x16x32_bf16 v[78:81], v[184:187], v[208:211], v[78:81]
	v_mfma_f32_16x16x32_bf16 v[70:73], v[176:179], v[216:219], v[70:73]
	v_mfma_f32_16x16x32_bf16 v[66:69], v[184:187], v[216:219], v[66:69]
	v_mfma_f32_16x16x32_bf16 v[118:121], v[180:183], v[196:199], v[118:121]
	v_mfma_f32_16x16x32_bf16 v[110:113], v[188:191], v[196:199], v[110:113]
	v_mfma_f32_16x16x32_bf16 v[102:105], v[180:183], v[204:207], v[102:105]
	v_mfma_f32_16x16x32_bf16 v[94:97], v[188:191], v[204:207], v[94:97]
	v_mfma_f32_16x16x32_bf16 v[86:89], v[180:183], v[212:215], v[86:89]
	v_mfma_f32_16x16x32_bf16 v[78:81], v[188:191], v[212:215], v[78:81]
	v_mfma_f32_16x16x32_bf16 v[70:73], v[180:183], v[220:223], v[70:73]
	v_mfma_f32_16x16x32_bf16 v[66:69], v[188:191], v[220:223], v[66:69]
	s_setprio 0
	s_barrier
	s_add_i32 s61, s46, s2
	v_lshl_add_u64 v[164:165], s[26:27], 0, v[134:135]
	s_mov_b32 m0, s61
	ds_read_b128 v[192:195], v172 offset:16384
	ds_read_b128 v[196:199], v172 offset:17408
	ds_read_b128 v[200:203], v172 offset:18432
	ds_read_b128 v[204:207], v172 offset:19456
	ds_read_b128 v[208:211], v172 offset:20480
	ds_read_b128 v[212:215], v172 offset:21504
	ds_read_b128 v[216:219], v172 offset:22528
	ds_read_b128 v[220:223], v172 offset:23552
	global_load_lds_dwordx4 v[164:165], off
	s_add_i32 m0, s61, 0x2000
	s_add_u32 s62, s26, 0x40000
	v_lshl_add_u64 v[224:225], s[26:27], 0, v[130:131]
	s_addc_u32 s63, s27, 0
	s_add_i32 s61, s47, s2
	global_load_lds_dwordx4 v[224:225], off
	s_mov_b32 m0, s61
	v_lshl_add_u64 v[230:231], s[28:29], 0, v[132:133]
	global_load_lds_dwordx4 v134, s[62:63]
	s_add_i32 m0, s61, 0x2000
	s_nop 0
	global_load_lds_dwordx4 v130, s[62:63]
	v_lshl_add_u64 v[226:227], s[28:29], 0, v[136:137]
	s_mov_b32 m0, s23
	s_nop 0
	global_load_lds_dwordx4 v[226:227], off
	s_mov_b32 m0, s31
	s_nop 0
	global_load_lds_dwordx4 v[230:231], off
	s_waitcnt vmcnt(8)
	s_waitcnt lgkmcnt(0)
	s_barrier
	s_setprio 3
	s_waitcnt lgkmcnt(0)
	v_mfma_f32_16x16x32_bf16 v[62:65], v[148:151], v[192:195], v[62:65]
	v_mfma_f32_16x16x32_bf16 v[58:61], v[156:159], v[192:195], v[58:61]
	v_mfma_f32_16x16x32_bf16 v[50:53], v[148:151], v[200:203], v[50:53]
	v_mfma_f32_16x16x32_bf16 v[42:45], v[156:159], v[200:203], v[42:45]
	v_mfma_f32_16x16x32_bf16 v[34:37], v[148:151], v[208:211], v[34:37]
	v_mfma_f32_16x16x32_bf16 v[26:29], v[156:159], v[208:211], v[26:29]
	v_mfma_f32_16x16x32_bf16 v[18:21], v[148:151], v[216:219], v[18:21]
	v_mfma_f32_16x16x32_bf16 v[10:13], v[156:159], v[216:219], v[10:13]
	v_mfma_f32_16x16x32_bf16 v[62:65], v[152:155], v[196:199], v[62:65]
	v_mfma_f32_16x16x32_bf16 v[58:61], v[160:163], v[196:199], v[58:61]
	v_mfma_f32_16x16x32_bf16 v[50:53], v[152:155], v[204:207], v[50:53]
	v_mfma_f32_16x16x32_bf16 v[42:45], v[160:163], v[204:207], v[42:45]
	v_mfma_f32_16x16x32_bf16 v[34:37], v[152:155], v[212:215], v[34:37]
	v_mfma_f32_16x16x32_bf16 v[26:29], v[160:163], v[212:215], v[26:29]
	v_mfma_f32_16x16x32_bf16 v[18:21], v[152:155], v[220:223], v[18:21]
	v_mfma_f32_16x16x32_bf16 v[10:13], v[160:163], v[220:223], v[10:13]
	s_setprio 0
	s_setprio 3
	v_mfma_f32_16x16x32_bf16 v[54:57], v[176:179], v[192:195], v[54:57]
	v_mfma_f32_16x16x32_bf16 v[46:49], v[184:187], v[192:195], v[46:49]
	v_mfma_f32_16x16x32_bf16 v[38:41], v[176:179], v[200:203], v[38:41]
	v_mfma_f32_16x16x32_bf16 v[30:33], v[184:187], v[200:203], v[30:33]
	v_mfma_f32_16x16x32_bf16 v[22:25], v[176:179], v[208:211], v[22:25]
	v_mfma_f32_16x16x32_bf16 v[14:17], v[184:187], v[208:211], v[14:17]
	v_mfma_f32_16x16x32_bf16 v[6:9], v[176:179], v[216:219], v[6:9]
	v_mfma_f32_16x16x32_bf16 v[2:5], v[184:187], v[216:219], v[2:5]
	v_mfma_f32_16x16x32_bf16 v[54:57], v[180:183], v[196:199], v[54:57]
	v_mfma_f32_16x16x32_bf16 v[46:49], v[188:191], v[196:199], v[46:49]
	v_mfma_f32_16x16x32_bf16 v[38:41], v[180:183], v[204:207], v[38:41]
	v_mfma_f32_16x16x32_bf16 v[30:33], v[188:191], v[204:207], v[30:33]
	v_mfma_f32_16x16x32_bf16 v[22:25], v[180:183], v[212:215], v[22:25]
	v_mfma_f32_16x16x32_bf16 v[14:17], v[188:191], v[212:215], v[14:17]
	v_mfma_f32_16x16x32_bf16 v[6:9], v[180:183], v[220:223], v[6:9]
	v_mfma_f32_16x16x32_bf16 v[2:5], v[188:191], v[220:223], v[2:5]
	s_setprio 0
	s_barrier
; #define PG8_STAGE_A(b, h, ptr, NX) do { if constexpr (Sched::GATHER) { unsigned gs_[2]; gs_[0] = ((NX) && last_) ? gN[h][0] : gA[h][0]; gs_[1] = ((NX) && last_) ? gN[h][1] : gA[h][1]; PG8_STAGE(PG8_SA(b, h), ptr, gs_); } \
;         else PG8_STAGE(PG8_SA(b, h), (ptr) + ((h) ? hstep : (size_t)0), voffA); } while (0)
; #define PG8_LDA(dst, b, h) do { _Pragma("unroll") for (int m = 0; m < 4; ++m) _Pragma("unroll") for (int k = 0; k < 2; ++k) dst[m][k] = *(const PG8_LAS bf16x8*)(lds + PG8_SA(b, h) + aoff + m * 2048 + k * 1024); } while (0)
; #define PG8_LDB(dst, b, h) do { _Pragma("unroll") for (int n = 0; n < 2; ++n) _Pragma("unroll") for (int k = 0; k < 2; ++k) dst[n][k] = *(const PG8_LAS bf16x8*)(lds + PG8_SB(b, h) + boff + n * 2048 + k * 1024); } while (0)
; #define PG8_MMA(ai, bj, At, Bt) do { __builtin_amdgcn_s_setprio(1); _Pragma("unroll") for (int m = 0; m < 4; ++m) _Pragma("unroll") for (int n = 0; n < 2; ++n) _Pragma("unroll") for (int k = 0; k < 2; ++k) \
;         acc[ai][bj][m][n] = __builtin_amdgcn_mfma_f32_16x16x32_bf16(Bt[n][k], At[m][k], acc[ai][bj][m][n], 0, 0, 0); __builtin_amdgcn_s_setprio(0); } while (0)
; #define PG8_WAIT_V(n) asm volatile("s_waitcnt vmcnt(" #n ")" ::: "memory")
; #define PG8_WAIT_L(n) asm volatile("s_waitcnt lgkmcnt(" #n ")" ::: "memory")
; #define PG8_BAR __builtin_amdgcn_s_barrier()
; #define PG8_SCHED __builtin_amdgcn_sched_barrier(0)
; template <class Epi, class Sched, bool ALIGN_EPI = false, bool SP2 = false>
; __device__ __forceinline__ void gemm_phase(PG8_LAS unsigned char* lds, const Gemm g, const Sched& S, const Epi& E, const bool skip_epi = false) {
;     ...
;             PG8_LDB(B0, 1, 0); PG8_LDB(B1, 1, 1); PG8_SCHED; PG8_LDA(At, 1, 0); PG8_STAGE_A(0, 1, a2, true);
;             PG8_WAIT_V(8); PG8_WAIT_L(0); PG8_BAR; PG8_MMA(0, 0, At, B0); PG8_MMA(0, 1, At, B1); PG8_BAR; PG8_SCHED;
	s_add_i32 s61, 0, 0x18000
	s_add_i32 s62, 0, 0x1c000
	v_add_u32_e32 v160, s61, v1
	v_add_u32_e32 v188, s62, v1
	ds_read_b128 v[148:151], v160
	ds_read_b128 v[152:155], v160 offset:1024
	ds_read_b128 v[156:159], v160 offset:2048
	ds_read_b128 v[160:163], v160 offset:3072
	ds_read_b128 v[176:179], v188
	ds_read_b128 v[180:183], v188 offset:1024
	ds_read_b128 v[184:187], v188 offset:2048
	ds_read_b128 v[188:191], v188 offset:3072
	s_add_u32 s28, s28, 0x40000
	s_addc_u32 s29, s29, 0
	s_mov_b32 m0, s34
	ds_read_b128 v[192:195], v172 offset:32768
	ds_read_b128 v[196:199], v172 offset:33792
	ds_read_b128 v[200:203], v172 offset:34816
	ds_read_b128 v[204:207], v172 offset:35840
	ds_read_b128 v[208:211], v172 offset:36864
	ds_read_b128 v[212:215], v172 offset:37888
	ds_read_b128 v[216:219], v172 offset:38912
	ds_read_b128 v[220:223], v172 offset:39936
	global_load_lds_dwordx4 v136, s[28:29]
	s_mov_b32 m0, s35
	s_nop 0
	global_load_lds_dwordx4 v132, s[28:29]
	s_waitcnt vmcnt(8)
	s_waitcnt lgkmcnt(0)
	s_barrier
	s_setprio 3
	s_waitcnt lgkmcnt(0)
	v_mfma_f32_16x16x32_bf16 v[126:129], v[148:151], v[192:195], v[126:129]
	v_mfma_f32_16x16x32_bf16 v[122:125], v[156:159], v[192:195], v[122:125]
	v_mfma_f32_16x16x32_bf16 v[114:117], v[148:151], v[200:203], v[114:117]
	v_mfma_f32_16x16x32_bf16 v[106:109], v[156:159], v[200:203], v[106:109]
	v_mfma_f32_16x16x32_bf16 v[98:101], v[148:151], v[208:211], v[98:101]
	v_mfma_f32_16x16x32_bf16 v[90:93], v[156:159], v[208:211], v[90:93]
	v_mfma_f32_16x16x32_bf16 v[82:85], v[148:151], v[216:219], v[82:85]
	v_mfma_f32_16x16x32_bf16 v[74:77], v[156:159], v[216:219], v[74:77]
	v_mfma_f32_16x16x32_bf16 v[126:129], v[152:155], v[196:199], v[126:129]
	v_mfma_f32_16x16x32_bf16 v[122:125], v[160:163], v[196:199], v[122:125]
	v_mfma_f32_16x16x32_bf16 v[114:117], v[152:155], v[204:207], v[114:117]
	v_mfma_f32_16x16x32_bf16 v[106:109], v[160:163], v[204:207], v[106:109]
	v_mfma_f32_16x16x32_bf16 v[98:101], v[152:155], v[212:215], v[98:101]
	v_mfma_f32_16x16x32_bf16 v[90:93], v[160:163], v[212:215], v[90:93]
	v_mfma_f32_16x16x32_bf16 v[82:85], v[152:155], v[220:223], v[82:85]
	v_mfma_f32_16x16x32_bf16 v[74:77], v[160:163], v[220:223], v[74:77]
	s_setprio 0
	s_setprio 3
	v_mfma_f32_16x16x32_bf16 v[118:121], v[176:179], v[192:195], v[118:121]
	v_mfma_f32_16x16x32_bf16 v[110:113], v[184:187], v[192:195], v[110:113]
	v_mfma_f32_16x16x32_bf16 v[102:105], v[176:179], v[200:203], v[102:105]
	v_mfma_f32_16x16x32_bf16 v[94:97], v[184:187], v[200:203], v[94:97]
	v_mfma_f32_16x16x32_bf16 v[86:89], v[176:179], v[208:211], v[86:89]
	v_mfma_f32_16x16x32_bf16 v[78:81], v[184:187], v[208:211], v[78:81]
	v_mfma_f32_16x16x32_bf16 v[70:73], v[176:179], v[216:219], v[70:73]
	v_mfma_f32_16x16x32_bf16 v[66:69], v[184:187], v[216:219], v[66:69]
	v_mfma_f32_16x16x32_bf16 v[118:121], v[180:183], v[196:199], v[118:121]
	v_mfma_f32_16x16x32_bf16 v[110:113], v[188:191], v[196:199], v[110:113]
	v_mfma_f32_16x16x32_bf16 v[102:105], v[180:183], v[204:207], v[102:105]
	v_mfma_f32_16x16x32_bf16 v[94:97], v[188:191], v[204:207], v[94:97]
	v_mfma_f32_16x16x32_bf16 v[86:89], v[180:183], v[212:215], v[86:89]
	v_mfma_f32_16x16x32_bf16 v[78:81], v[188:191], v[212:215], v[78:81]
	v_mfma_f32_16x16x32_bf16 v[70:73], v[180:183], v[220:223], v[70:73]
	v_mfma_f32_16x16x32_bf16 v[66:69], v[188:191], v[220:223], v[66:69]
	s_setprio 0
	s_barrier
; #define PG8_STAGE_A(b, h, ptr, NX) do { if constexpr (Sched::GATHER) { unsigned gs_[2]; gs_[0] = ((NX) && last_) ? gN[h][0] : gA[h][0]; gs_[1] = ((NX) && last_) ? gN[h][1] : gA[h][1]; PG8_STAGE(PG8_SA(b, h), ptr, gs_); } \
;         else PG8_STAGE(PG8_SA(b, h), (ptr) + ((h) ? hstep : (size_t)0), voffA); } while (0)
; #define PG8_STAGE(bufoff, gbase, voff) do { _Pragma("unroll") for (int _i = 0; _i < 2; ++_i) \
;         __builtin_amdgcn_global_load_lds((const unsigned*)((const char*)(gbase) + (voff)[_i]), (PG8_LAS unsigned*)(lds + (bufoff) + ldsw + _i * 8192), 16, 0, 0); } while (0)
; #define PG8_LDA(dst, b, h) do { _Pragma("unroll") for (int m = 0; m < 4; ++m) _Pragma("unroll") for (int k = 0; k < 2; ++k) dst[m][k] = *(const PG8_LAS bf16x8*)(lds + PG8_SA(b, h) + aoff + m * 2048 + k * 1024); } while (0)
; #define PG8_MMA(ai, bj, At, Bt) do { __builtin_amdgcn_s_setprio(1); _Pragma("unroll") for (int m = 0; m < 4; ++m) _Pragma("unroll") for (int n = 0; n < 2; ++n) _Pragma("unroll") for (int k = 0; k < 2; ++k) \
;         acc[ai][bj][m][n] = __builtin_amdgcn_mfma_f32_16x16x32_bf16(Bt[n][k], At[m][k], acc[ai][bj][m][n], 0, 0, 0); __builtin_amdgcn_s_setprio(0); } while (0)
; #define PG8_WAIT_V(n) asm volatile("s_waitcnt vmcnt(" #n ")" ::: "memory")
; #define PG8_WAIT_L(n) asm volatile("s_waitcnt lgkmcnt(" #n ")" ::: "memory")
; #define PG8_BAR __builtin_amdgcn_s_barrier()
; #define PG8_SCHED __builtin_amdgcn_sched_barrier(0)
; __device__ __forceinline__ void rstd8(const float* SS, int rowb, int lane, float (&rs)[2][4]) {
;     f32x4 p[2][4];
; #pragma unroll
;     for (int ai = 0; ai < 2; ++ai)
; #pragma unroll
;         for (int m = 0; m < 4; ++m) p[ai][m] = *(const f32x4*)(SS + (size_t)(rowb + HALF * ai + 16 * m + (lane >> 2)) * 16 + 4 * (lane & 3));
; template <class Epi, class Sched, bool ALIGN_EPI = false, bool SP2 = false>
; __device__ __forceinline__ void gemm_phase(PG8_LAS unsigned char* lds, const Gemm g, const Sched& S, const Epi& E, const bool skip_epi = false) {
;     ...
;             PG8_LDA(At, 1, 1); PG8_STAGE(PG8_SB(1, 0), b3, voffB); PG8_STAGE(PG8_SB(1, 1), b3 + hstep, voffB); PG8_STAGE_A(1, 0, a3, true);
;             PG8_WAIT_V(8); PG8_WAIT_L(0); PG8_BAR; PG8_MMA(1, 0, At, B0); PG8_MMA(1, 1, At, B1); PG8_BAR; PG8_SCHED;
	s_add_i32 s28, s61, s2
	s_add_i32 m0, s28, 0xffffff80
	ds_read_b128 v[192:195], v172 offset:49152
	ds_read_b128 v[196:199], v172 offset:50176
	ds_read_b128 v[200:203], v172 offset:51200
	ds_read_b128 v[204:207], v172 offset:52224
	ds_read_b128 v[208:211], v172 offset:53248
	ds_read_b128 v[212:215], v172 offset:54272
	ds_read_b128 v[216:219], v172 offset:55296
	ds_read_b128 v[220:223], v172 offset:56320
	global_load_lds_dwordx4 v[164:165], off offset:128
	s_add_i32 m0, s28, 0x1f80
	s_add_u32 s26, s26, 0x40080
	s_addc_u32 s27, s27, 0
	s_add_i32 s28, s62, s2
	global_load_lds_dwordx4 v[224:225], off offset:128
	s_mov_b32 m0, s28
	s_nop 0
	global_load_lds_dwordx4 v134, s[26:27]
	s_add_i32 m0, s28, 0x2000
	s_nop 0
	global_load_lds_dwordx4 v130, s[26:27]
	s_add_i32 m0, s37, 0xffffff80
	s_nop 0
	global_load_lds_dwordx4 v[226:227], off offset:128
	s_add_i32 m0, s38, 0xffffff80
	s_nop 0
	global_load_lds_dwordx4 v[230:231], off offset:128
	s_waitcnt vmcnt(8)
	s_waitcnt lgkmcnt(0)
	s_barrier
	s_setprio 3
	s_waitcnt lgkmcnt(0)
	v_mfma_f32_16x16x32_bf16 v[62:65], v[148:151], v[192:195], v[62:65]
	v_mfma_f32_16x16x32_bf16 v[58:61], v[156:159], v[192:195], v[58:61]
	v_mfma_f32_16x16x32_bf16 v[50:53], v[148:151], v[200:203], v[50:53]
	v_mfma_f32_16x16x32_bf16 v[42:45], v[156:159], v[200:203], v[42:45]
	v_mfma_f32_16x16x32_bf16 v[34:37], v[148:151], v[208:211], v[34:37]
	v_mfma_f32_16x16x32_bf16 v[26:29], v[156:159], v[208:211], v[26:29]
	v_mfma_f32_16x16x32_bf16 v[18:21], v[148:151], v[216:219], v[18:21]
	v_mfma_f32_16x16x32_bf16 v[10:13], v[156:159], v[216:219], v[10:13]
	v_mfma_f32_16x16x32_bf16 v[62:65], v[152:155], v[196:199], v[62:65]
	v_mfma_f32_16x16x32_bf16 v[58:61], v[160:163], v[196:199], v[58:61]
	v_mfma_f32_16x16x32_bf16 v[50:53], v[152:155], v[204:207], v[50:53]
	v_mfma_f32_16x16x32_bf16 v[42:45], v[160:163], v[204:207], v[42:45]
	v_mfma_f32_16x16x32_bf16 v[34:37], v[152:155], v[212:215], v[34:37]
	v_mfma_f32_16x16x32_bf16 v[26:29], v[160:163], v[212:215], v[26:29]
	v_mfma_f32_16x16x32_bf16 v[18:21], v[152:155], v[220:223], v[18:21]
	v_mfma_f32_16x16x32_bf16 v[10:13], v[160:163], v[220:223], v[10:13]
	s_setprio 0
	s_setprio 3
	v_mfma_f32_16x16x32_bf16 v[54:57], v[176:179], v[192:195], v[54:57]
	v_mfma_f32_16x16x32_bf16 v[46:49], v[184:187], v[192:195], v[46:49]
	v_mfma_f32_16x16x32_bf16 v[38:41], v[176:179], v[200:203], v[38:41]
	v_mfma_f32_16x16x32_bf16 v[30:33], v[184:187], v[200:203], v[30:33]
	v_mfma_f32_16x16x32_bf16 v[22:25], v[176:179], v[208:211], v[22:25]
	v_mfma_f32_16x16x32_bf16 v[14:17], v[184:187], v[208:211], v[14:17]
	v_mfma_f32_16x16x32_bf16 v[6:9], v[176:179], v[216:219], v[6:9]
	v_mfma_f32_16x16x32_bf16 v[2:5], v[184:187], v[216:219], v[2:5]
	v_mfma_f32_16x16x32_bf16 v[54:57], v[180:183], v[196:199], v[54:57]
	v_mfma_f32_16x16x32_bf16 v[46:49], v[188:191], v[196:199], v[46:49]
	v_mfma_f32_16x16x32_bf16 v[38:41], v[180:183], v[204:207], v[38:41]
	v_mfma_f32_16x16x32_bf16 v[30:33], v[188:191], v[204:207], v[30:33]
	v_mfma_f32_16x16x32_bf16 v[22:25], v[180:183], v[212:215], v[22:25]
	v_mfma_f32_16x16x32_bf16 v[14:17], v[188:191], v[212:215], v[14:17]
	v_mfma_f32_16x16x32_bf16 v[6:9], v[180:183], v[220:223], v[6:9]
	v_mfma_f32_16x16x32_bf16 v[2:5], v[188:191], v[220:223], v[2:5]
	s_setprio 0
	s_barrier
	s_add_i32 s60, s60, 2
	s_add_u32 s24, s24, 0x100
	s_addc_u32 s25, s25, 0
	s_add_u32 s58, s58, 0x100
	s_addc_u32 s59, s59, 0
	s_cmp_gt_u32 s60, 13
	s_cbranch_scc0 .LBB0_253
	v_lshl_add_u32 v164, s22, 8, v167
	v_ashrrev_i32_e32 v165, 31, v164
	v_lshlrev_b64 v[148:149], 6, v[164:165]
	v_lshl_add_u64 v[148:149], v[138:139], 0, v[148:149]
	v_add_co_u32_e32 v150, vcc, 0x2000, v148
	v_addc_co_u32_e32 v151, vcc, 0, v149, vcc
	global_load_dwordx4 v[176:179], v[148:149], off
	global_load_dwordx4 v[180:183], v[148:149], off offset:1024
	global_load_dwordx4 v[184:187], v[148:149], off offset:2048
	global_load_dwordx4 v[188:191], v[148:149], off offset:3072
	global_load_dwordx4 v[192:195], v[150:151], off
	global_load_dwordx4 v[196:199], v[150:151], off offset:1024
	global_load_dwordx4 v[200:203], v[150:151], off offset:2048
	global_load_dwordx4 v[204:207], v[150:151], off offset:3072
	s_and_b64 vcc, exec, s[12:13]
	s_cbranch_vccz .LBB0_256
	s_barrier

; #define PG8_STAGE_A(b, h, ptr, NX) do { if constexpr (Sched::GATHER) { unsigned gs_[2]; gs_[0] = ((NX) && last_) ? gN[h][0] : gA[h][0]; gs_[1] = ((NX) && last_) ? gN[h][1] : gA[h][1]; PG8_STAGE(PG8_SA(b, h), ptr, gs_); } \
;         else PG8_STAGE(PG8_SA(b, h), (ptr) + ((h) ? hstep : (size_t)0), voffA); } while (0)
; #define PG8_STAGE(bufoff, gbase, voff) do { _Pragma("unroll") for (int _i = 0; _i < 2; ++_i) \
;         __builtin_amdgcn_global_load_lds((const unsigned*)((const char*)(gbase) + (voff)[_i]), (PG8_LAS unsigned*)(lds + (bufoff) + ldsw + _i * 8192), 16, 0, 0); } while (0)
; #define PG8_WAIT_V(n) asm volatile("s_waitcnt vmcnt(" #n ")" ::: "memory")
; #define PG8_BAR __builtin_amdgcn_s_barrier()
; template <class Epi, class Sched, bool ALIGN_EPI = false, bool SP2 = false>
; __device__ __forceinline__ void gemm_phase(PG8_LAS unsigned char* lds, const Gemm g, const Sched& S, const Epi& E, const bool skip_epi = false) {
;     ...
;     const unsigned ldsw = (unsigned)wid * 1024u;
;     const int aoff = lds_byte(wr * 64 + fr, fq * 8), boff = lds_byte(wc * 32 + fr, fq * 8);
;     ...
;         PG8_WAIT_V(2); PG8_BAR;
;         PG8_STAGE(PG8_SB(1, 0), cB + kstep, voffB); PG8_STAGE_A(1, 0, cA + kstep, false); PG8_STAGE(PG8_SB(1, 1), cB + hstep + kstep, voffB);
;         PG8_WAIT_V(6); PG8_BAR;
.LBB0_624:
	v_bfe_u32 v17, v10, 4, 2
	v_and_b32_e32 v1, 15, v10
	s_waitcnt vmcnt(0)
	v_lshlrev_b32_e32 v18, 4, v17
	v_lshlrev_b32_e32 v19, 2, v10
	s_mov_b64 s[12:13], 0x80
	s_and_b32 s37, s4, 3
	v_lshl_or_b32 v18, v1, 6, v18
	s_lshl_b32 s4, s5, 13
	v_and_b32_e32 v19, 32, v19
	s_add_i32 m0, s3, 0x18000
	v_lshl_add_u64 v[8:9], v[8:9], 0, s[12:13]
	s_lshl_b32 s38, s5, 6
	v_bitop3_b32 v20, v18, s4, v19 bitop3:0xde
	s_lshl_b32 s4, s37, 12
	s_waitcnt vmcnt(2)
	s_barrier
	global_load_lds_dwordx4 v[8:9], off
	v_lshl_add_u64 v[4:5], v[4:5], 0, s[12:13]
	s_add_i32 m0, s3, 0x1a000
	s_add_i32 s39, s3, 0x8000
	s_add_i32 s48, s3, 0xa000
	v_bitop3_b32 v229, v18, s4, v19 bitop3:0xde
	global_load_lds_dwordx4 v[4:5], off
	v_lshl_add_u64 v[2:3], v[2:3], 0, s[12:13]
	s_mov_b32 m0, s39
	s_add_u32 s4, s28, 0x40080
	global_load_lds_dwordx4 v[2:3], off
	v_lshl_add_u64 v[2:3], v[6:7], 0, s[12:13]
	s_mov_b32 m0, s48
	s_addc_u32 s5, s29, 0
	global_load_lds_dwordx4 v[2:3], off
	s_add_i32 m0, s3, 0x1c000
	s_nop 0
	global_load_lds_dwordx4 v192, s[4:5]
	s_add_i32 m0, s3, 0x1e000
	s_cmpk_lt_u32 s14, 0x100
	global_load_lds_dwordx4 v196, s[4:5]
	v_and_b32_e32 v2, 3, v10
	v_and_b32_e32 v3, 60, v10
	v_lshl_or_b32 v231, v2, 6, v3
	v_lshlrev_b32_e32 v2, 3, v2
	v_lshl_or_b32 v232, s37, 5, v2
	v_lshlrev_b32_e32 v2, 4, v1
	v_lshl_or_b32 v233, v17, 2, v2
	v_lshlrev_b32_e32 v2, 14, v11
	v_and_b32_e32 v2, 0xffff8000, v2
	v_lshl_add_u32 v2, v12, 11, v2
	v_and_b32_e32 v3, 1, v11
	v_lshl_or_b32 v2, v3, 6, v2
	v_lshl_add_u32 v198, v13, 1, v2
	v_lshlrev_b32_e32 v2, 14, v14
	v_and_b32_e32 v2, 0xffff8000, v2
	s_waitcnt vmcnt(6)
	v_lshl_add_u32 v2, v15, 11, v2
	v_and_b32_e32 v3, 1, v14
	s_cselect_b64 s[14:15], -1, 0
	v_lshl_or_b32 v2, v3, 6, v2
	s_add_i32 s57, 0, 0x10000
	s_add_i32 s58, 0, 0x14000
	v_bfe_u32 v230, v10, 2, 4
	v_cmp_eq_u32_e64 s[4:5], 0, v17
	s_ashr_i32 s49, s97, 31
	s_ashr_i32 s56, s94, 31
	v_mov_b32_e32 v199, v193
	v_lshl_add_u32 v200, v16, 1, v2
	v_mov_b32_e32 v201, v193
	v_mov_b64_e32 v[202:203], 0x100
	v_mov_b64_e32 v[204:205], 0xff
	v_add_u32_e32 v234, s57, v229
	v_add_u32_e32 v235, s58, v229
	v_add_u32_e32 v236, 0, v20
	s_mov_b32 s59, 0
	s_barrier
	s_branch .LBB0_627

; #define PG8_GIDX(G_, PM_) do { if constexpr (Sched::GATHER) { _Pragma("unroll") for (int h_ = 0; h_ < 2; ++h_) _Pragma("unroll") for (int i_ = 0; i_ < 2; ++i_) { int R_, C_; stage_rc(tid * 16 + i_ * 8192, R_, C_); \
;         const int src_ = S.rowsrc[(PM_) * BM + h_ * HALF + R_]; G_[h_][i_] = (unsigned)(src_ * K + C_) * 2u; } } } while (0)
; #define PG8_STAGE_A(b, h, ptr, NX) do { if constexpr (Sched::GATHER) { unsigned gs_[2]; gs_[0] = ((NX) && last_) ? gN[h][0] : gA[h][0]; gs_[1] = ((NX) && last_) ? gN[h][1] : gA[h][1]; PG8_STAGE(PG8_SA(b, h), ptr, gs_); } \
;         else PG8_STAGE(PG8_SA(b, h), (ptr) + ((h) ? hstep : (size_t)0), voffA); } while (0)
; #define PG8_LDA(dst, b, h) do { _Pragma("unroll") for (int m = 0; m < 4; ++m) _Pragma("unroll") for (int k = 0; k < 2; ++k) dst[m][k] = *(const PG8_LAS bf16x8*)(lds + PG8_SA(b, h) + aoff + m * 2048 + k * 1024); } while (0)
; template <class Epi, class Sched, bool ALIGN_EPI = false, bool SP2 = false>
; __device__ __forceinline__ void gemm_phase(PG8_LAS unsigned char* lds, const Gemm g, const Sched& S, const Epi& E, const bool skip_epi = false) {
;     ...
;         const bool has_next = S.next(ui + 1, nxt);
;         if (has_next) PG8_GIDX(gN, nxt.pm);
;         const char* nA = has_next ? (const char*)g.A + (size_t)nxt.pm * pmstepA + nxt.ko : cA; const char* nB = has_next ? (const char*)g.Bt + (size_t)nxt.pn * tstep + nxt.ko : cB;
;         for (int t = 0; t < nt; t += 2) {
;             const bool last = (t == nt - 2); last_ = last && has_next;
;             const char* a1 = cA + (size_t)(t + 1) * kstep;
;             const char* a2 = last ? nA : cA + (size_t)(t + 2) * kstep; const char* b2 = last ? nB : cB + (size_t)(t + 2) * kstep;
;             const char* a3 = a2 + kstep; const char* b3 = b2 + kstep;
;             if (last && has_next) S.a_ready(nxt);
;             if constexpr (SP2) {
;             PG8_LDB(B0, 0, 0); PG8_LDB(B1, 0, 1); PG8_SCHED; PG8_LDA(At, 0, 0); PG8_STAGE_A(1, 1, a1, false);
;             PG8_WAIT_V(8); PG8_WAIT_L(0); PG8_BAR; PG8_MMA(0, 0, At, B0); PG8_MMA(0, 1, At, B1); PG8_BAR; PG8_SCHED;
;             PG8_LDA(At, 0, 1); PG8_STAGE(PG8_SB(0, 0), b2, voffB); PG8_STAGE(PG8_SB(0, 1), b2 + hstep, voffB); PG8_STAGE_A(0, 0, a2, true);
;             PG8_WAIT_V(8); PG8_WAIT_L(0); PG8_BAR; PG8_MMA(1, 0, At, B0); PG8_MMA(1, 1, At, B1); PG8_BAR; PG8_SCHED;
.LBB0_633:
	s_ashr_i32 s19, s18, 31
	s_lshl_b64 s[20:21], s[18:19], 19
	s_add_u32 s20, s46, s20
	s_addc_u32 s21, s47, s21
	s_and_b64 s[22:23], s[6:7], exec
	s_cselect_b32 s19, s21, s27
	s_cselect_b32 s25, s20, s26
	s_ashr_i32 s17, s16, 31
	s_lshl_b64 s[22:23], s[16:17], 19
	v_readlane_b32 s17, v254, 40
	s_add_u32 s22, s17, s22
	v_readlane_b32 s17, v254, 41
	s_addc_u32 s23, s17, s23
	s_and_b64 s[30:31], s[6:7], exec
	s_cselect_b32 s17, s23, s29
	s_cselect_b32 s60, s22, s28
	s_add_u32 s26, s26, 0x40080
	s_addc_u32 s27, s27, 0
	s_add_u32 s61, s28, 0x100
	s_addc_u32 s62, s29, 0
	s_mov_b32 s63, -2
	s_waitcnt lgkmcnt(0)
	ds_read_b128 v[98:101], v234
	ds_read_b128 v[110:113], v234 offset:1024
	ds_read_b128 v[122:125], v234 offset:2048
	ds_read_b128 v[126:129], v234 offset:3072
	ds_read_b128 v[138:141], v235
	ds_read_b128 v[142:145], v235 offset:1024
	ds_read_b128 v[146:149], v235 offset:2048
	ds_read_b128 v[150:153], v235 offset:3072
	s_add_u32 s28, s26, 0xfffc0080
	s_addc_u32 s29, s27, -1
	s_cmp_eq_u32 s63, 12
	s_cselect_b32 s31, s19, s29
	s_cselect_b32 s30, s25, s28
	s_cselect_b32 s29, s17, s62
	s_cselect_b32 s28, s60, s61
	s_add_i32 m0, s3, 0xc000
	ds_read_b128 v[154:157], v236
	ds_read_b128 v[166:169], v236 offset:1024
	ds_read_b128 v[170:173], v236 offset:2048
	ds_read_b128 v[174:177], v236 offset:3072
	ds_read_b128 v[178:181], v236 offset:4096
	ds_read_b128 v[182:185], v236 offset:5120
	ds_read_b128 v[186:189], v236 offset:6144
	ds_read_b128 v[206:209], v236 offset:7168
	global_load_lds_dwordx4 v198, s[26:27]
	s_add_i32 m0, s3, 0xe000
	s_nop 0
	global_load_lds_dwordx4 v200, s[26:27]
	s_waitcnt vmcnt(8)
	s_waitcnt lgkmcnt(0)
	s_barrier
	s_setprio 3
	s_waitcnt lgkmcnt(0)
	v_mfma_f32_16x16x32_bf16 v[162:165], v[98:101], v[154:157], 0
	v_mfma_f32_16x16x32_bf16 v[158:161], v[122:125], v[154:157], 0
	v_mfma_f32_16x16x32_bf16 v[118:121], v[98:101], v[170:173], 0
	v_mfma_f32_16x16x32_bf16 v[114:117], v[122:125], v[170:173], 0
	v_mfma_f32_16x16x32_bf16 v[94:97], v[98:101], v[178:181], 0
	v_mfma_f32_16x16x32_bf16 v[90:93], v[122:125], v[178:181], 0
	v_mfma_f32_16x16x32_bf16 v[78:81], v[98:101], v[186:189], 0
	v_mfma_f32_16x16x32_bf16 v[74:77], v[122:125], v[186:189], 0
	v_mfma_f32_16x16x32_bf16 v[162:165], v[110:113], v[166:169], v[162:165]
	v_mfma_f32_16x16x32_bf16 v[158:161], v[126:129], v[166:169], v[158:161]
	v_mfma_f32_16x16x32_bf16 v[118:121], v[110:113], v[174:177], v[118:121]
	v_mfma_f32_16x16x32_bf16 v[114:117], v[126:129], v[174:177], v[114:117]
	v_mfma_f32_16x16x32_bf16 v[94:97], v[110:113], v[182:185], v[94:97]
	v_mfma_f32_16x16x32_bf16 v[90:93], v[126:129], v[182:185], v[90:93]
	v_mfma_f32_16x16x32_bf16 v[78:81], v[110:113], v[206:209], v[78:81]
	v_mfma_f32_16x16x32_bf16 v[74:77], v[126:129], v[206:209], v[74:77]
	s_setprio 0
	s_setprio 3
	v_mfma_f32_16x16x32_bf16 v[134:137], v[138:141], v[154:157], 0
	v_mfma_f32_16x16x32_bf16 v[130:133], v[146:149], v[154:157], 0
	v_mfma_f32_16x16x32_bf16 v[106:109], v[138:141], v[170:173], 0
	v_mfma_f32_16x16x32_bf16 v[102:105], v[146:149], v[170:173], 0
	v_mfma_f32_16x16x32_bf16 v[86:89], v[138:141], v[178:181], 0
	v_mfma_f32_16x16x32_bf16 v[82:85], v[146:149], v[178:181], 0
	v_mfma_f32_16x16x32_bf16 v[70:73], v[138:141], v[186:189], 0
	v_mfma_f32_16x16x32_bf16 v[66:69], v[146:149], v[186:189], 0
	v_mfma_f32_16x16x32_bf16 v[134:137], v[142:145], v[166:169], v[134:137]
	v_mfma_f32_16x16x32_bf16 v[130:133], v[150:153], v[166:169], v[130:133]
	v_mfma_f32_16x16x32_bf16 v[106:109], v[142:145], v[174:177], v[106:109]
	v_mfma_f32_16x16x32_bf16 v[102:105], v[150:153], v[174:177], v[102:105]
	v_mfma_f32_16x16x32_bf16 v[86:89], v[142:145], v[182:185], v[86:89]
	v_mfma_f32_16x16x32_bf16 v[82:85], v[150:153], v[182:185], v[82:85]
	v_mfma_f32_16x16x32_bf16 v[70:73], v[142:145], v[206:209], v[70:73]
	v_mfma_f32_16x16x32_bf16 v[66:69], v[150:153], v[206:209], v[66:69]
	s_setprio 0
	s_barrier
	s_add_i32 s64, s57, s2
	v_lshl_add_u64 v[210:211], s[28:29], 0, v[192:193]
	s_mov_b32 m0, s64
	ds_read_b128 v[154:157], v236 offset:16384
	ds_read_b128 v[166:169], v236 offset:17408
	ds_read_b128 v[170:173], v236 offset:18432
	ds_read_b128 v[174:177], v236 offset:19456
	ds_read_b128 v[178:181], v236 offset:20480
	ds_read_b128 v[182:185], v236 offset:21504
	ds_read_b128 v[186:189], v236 offset:22528
	ds_read_b128 v[206:209], v236 offset:23552
	global_load_lds_dwordx4 v[210:211], off
	s_add_i32 m0, s64, 0x2000
	s_add_u32 s64, s28, 0x40000
	v_lshl_add_u64 v[212:213], s[28:29], 0, v[196:197]
	s_addc_u32 s65, s29, 0
	s_add_i32 s66, s58, s2
	global_load_lds_dwordx4 v[212:213], off
	s_mov_b32 m0, s66
	v_lshl_add_u64 v[216:217], s[30:31], 0, v[194:195]
	global_load_lds_dwordx4 v192, s[64:65]
	s_add_i32 m0, s66, 0x2000
	s_nop 0
	global_load_lds_dwordx4 v196, s[64:65]
	v_lshl_add_u64 v[214:215], s[30:31], 0, v[190:191]
	s_mov_b32 m0, s3
	s_nop 0
	global_load_lds_dwordx4 v[214:215], off
	s_mov_b32 m0, s34
	s_nop 0
	global_load_lds_dwordx4 v[216:217], off
	s_waitcnt vmcnt(8)
	s_waitcnt lgkmcnt(0)
	s_barrier
; #define PG8_STAGE_A(b, h, ptr, NX) do { if constexpr (Sched::GATHER) { unsigned gs_[2]; gs_[0] = ((NX) && last_) ? gN[h][0] : gA[h][0]; gs_[1] = ((NX) && last_) ? gN[h][1] : gA[h][1]; PG8_STAGE(PG8_SA(b, h), ptr, gs_); } \
;         else PG8_STAGE(PG8_SA(b, h), (ptr) + ((h) ? hstep : (size_t)0), voffA); } while (0)
; #define PG8_LDA(dst, b, h) do { _Pragma("unroll") for (int m = 0; m < 4; ++m) _Pragma("unroll") for (int k = 0; k < 2; ++k) dst[m][k] = *(const PG8_LAS bf16x8*)(lds + PG8_SA(b, h) + aoff + m * 2048 + k * 1024); } while (0)
; #define PG8_LDB(dst, b, h) do { _Pragma("unroll") for (int n = 0; n < 2; ++n) _Pragma("unroll") for (int k = 0; k < 2; ++k) dst[n][k] = *(const PG8_LAS bf16x8*)(lds + PG8_SB(b, h) + boff + n * 2048 + k * 1024); } while (0)
; #define PG8_MMA(ai, bj, At, Bt) do { __builtin_amdgcn_s_setprio(1); _Pragma("unroll") for (int m = 0; m < 4; ++m) _Pragma("unroll") for (int n = 0; n < 2; ++n) _Pragma("unroll") for (int k = 0; k < 2; ++k) \
;         acc[ai][bj][m][n] = __builtin_amdgcn_mfma_f32_16x16x32_bf16(Bt[n][k], At[m][k], acc[ai][bj][m][n], 0, 0, 0); __builtin_amdgcn_s_setprio(0); } while (0)
; #define PG8_WAIT_V(n) asm volatile("s_waitcnt vmcnt(" #n ")" ::: "memory")
; #define PG8_WAIT_L(n) asm volatile("s_waitcnt lgkmcnt(" #n ")" ::: "memory")
; #define PG8_BAR __builtin_amdgcn_s_barrier()
; #define PG8_SCHED __builtin_amdgcn_sched_barrier(0)
; template <class Epi, class Sched, bool ALIGN_EPI = false, bool SP2 = false>
; __device__ __forceinline__ void gemm_phase(PG8_LAS unsigned char* lds, const Gemm g, const Sched& S, const Epi& E, const bool skip_epi = false) {
;     ...
;             PG8_WAIT_V(8); PG8_WAIT_L(0); PG8_BAR; PG8_MMA(1, 0, At, B0); PG8_MMA(1, 1, At, B1); PG8_BAR; PG8_SCHED;
;             PG8_LDB(B0, 1, 0); PG8_LDB(B1, 1, 1); PG8_SCHED; PG8_LDA(At, 1, 0); PG8_STAGE_A(0, 1, a2, true);
;             PG8_WAIT_V(8); PG8_WAIT_L(0); PG8_BAR; PG8_MMA(0, 0, At, B0); PG8_MMA(0, 1, At, B1); PG8_BAR; PG8_SCHED;
	s_setprio 3
	s_waitcnt lgkmcnt(0)
	v_mfma_f32_16x16x32_bf16 v[62:65], v[98:101], v[154:157], 0
	v_mfma_f32_16x16x32_bf16 v[58:61], v[122:125], v[154:157], 0
	v_mfma_f32_16x16x32_bf16 v[46:49], v[98:101], v[170:173], 0
	v_mfma_f32_16x16x32_bf16 v[42:45], v[122:125], v[170:173], 0
	v_mfma_f32_16x16x32_bf16 v[30:33], v[98:101], v[178:181], 0
	v_mfma_f32_16x16x32_bf16 v[26:29], v[122:125], v[178:181], 0
	v_mfma_f32_16x16x32_bf16 v[14:17], v[98:101], v[186:189], 0
	v_mfma_f32_16x16x32_bf16 v[10:13], v[122:125], v[186:189], 0
	v_mfma_f32_16x16x32_bf16 v[62:65], v[110:113], v[166:169], v[62:65]
	v_mfma_f32_16x16x32_bf16 v[58:61], v[126:129], v[166:169], v[58:61]
	v_mfma_f32_16x16x32_bf16 v[46:49], v[110:113], v[174:177], v[46:49]
	v_mfma_f32_16x16x32_bf16 v[42:45], v[126:129], v[174:177], v[42:45]
	v_mfma_f32_16x16x32_bf16 v[30:33], v[110:113], v[182:185], v[30:33]
	v_mfma_f32_16x16x32_bf16 v[26:29], v[126:129], v[182:185], v[26:29]
	v_mfma_f32_16x16x32_bf16 v[14:17], v[110:113], v[206:209], v[14:17]
	v_mfma_f32_16x16x32_bf16 v[10:13], v[126:129], v[206:209], v[10:13]
	s_setprio 0
	s_setprio 3
	v_mfma_f32_16x16x32_bf16 v[54:57], v[138:141], v[154:157], 0
	v_mfma_f32_16x16x32_bf16 v[50:53], v[146:149], v[154:157], 0
	v_mfma_f32_16x16x32_bf16 v[38:41], v[138:141], v[170:173], 0
	v_mfma_f32_16x16x32_bf16 v[34:37], v[146:149], v[170:173], 0
	v_mfma_f32_16x16x32_bf16 v[22:25], v[138:141], v[178:181], 0
	v_mfma_f32_16x16x32_bf16 v[18:21], v[146:149], v[178:181], 0
	v_mfma_f32_16x16x32_bf16 v[6:9], v[138:141], v[186:189], 0
	v_mfma_f32_16x16x32_bf16 v[2:5], v[146:149], v[186:189], 0
	v_mfma_f32_16x16x32_bf16 v[54:57], v[142:145], v[166:169], v[54:57]
	v_mfma_f32_16x16x32_bf16 v[50:53], v[150:153], v[166:169], v[50:53]
	v_mfma_f32_16x16x32_bf16 v[38:41], v[142:145], v[174:177], v[38:41]
	v_mfma_f32_16x16x32_bf16 v[34:37], v[150:153], v[174:177], v[34:37]
	v_mfma_f32_16x16x32_bf16 v[22:25], v[142:145], v[182:185], v[22:25]
	v_mfma_f32_16x16x32_bf16 v[18:21], v[150:153], v[182:185], v[18:21]
	v_mfma_f32_16x16x32_bf16 v[6:9], v[142:145], v[206:209], v[6:9]
	v_mfma_f32_16x16x32_bf16 v[2:5], v[150:153], v[206:209], v[2:5]
	s_setprio 0
	s_barrier
	s_add_i32 s64, 0, 0x18000
	s_add_i32 s65, 0, 0x1c000
	v_add_u32_e32 v126, s64, v229
	v_add_u32_e32 v150, s65, v229
	ds_read_b128 v[98:101], v126
	ds_read_b128 v[110:113], v126 offset:1024
	ds_read_b128 v[122:125], v126 offset:2048
	ds_read_b128 v[126:129], v126 offset:3072
	ds_read_b128 v[138:141], v150
	ds_read_b128 v[142:145], v150 offset:1024
	ds_read_b128 v[146:149], v150 offset:2048
	ds_read_b128 v[150:153], v150 offset:3072
	s_add_u32 s30, s30, 0x40000
	s_addc_u32 s31, s31, 0
	s_mov_b32 m0, s35
	ds_read_b128 v[154:157], v236 offset:32768
	ds_read_b128 v[166:169], v236 offset:33792
	ds_read_b128 v[170:173], v236 offset:34816
	ds_read_b128 v[174:177], v236 offset:35840
	ds_read_b128 v[178:181], v236 offset:36864
	ds_read_b128 v[182:185], v236 offset:37888
	ds_read_b128 v[186:189], v236 offset:38912
	ds_read_b128 v[206:209], v236 offset:39936
	global_load_lds_dwordx4 v190, s[30:31]
	s_mov_b32 m0, s36
	s_nop 0
	global_load_lds_dwordx4 v194, s[30:31]
	s_waitcnt vmcnt(8)
	s_waitcnt lgkmcnt(0)
	s_barrier
	s_setprio 3
	s_waitcnt lgkmcnt(0)
	v_mfma_f32_16x16x32_bf16 v[162:165], v[98:101], v[154:157], v[162:165]
	v_mfma_f32_16x16x32_bf16 v[158:161], v[122:125], v[154:157], v[158:161]
	v_mfma_f32_16x16x32_bf16 v[118:121], v[98:101], v[170:173], v[118:121]
	v_mfma_f32_16x16x32_bf16 v[114:117], v[122:125], v[170:173], v[114:117]
	v_mfma_f32_16x16x32_bf16 v[94:97], v[98:101], v[178:181], v[94:97]
	v_mfma_f32_16x16x32_bf16 v[90:93], v[122:125], v[178:181], v[90:93]
	v_mfma_f32_16x16x32_bf16 v[78:81], v[98:101], v[186:189], v[78:81]
	v_mfma_f32_16x16x32_bf16 v[74:77], v[122:125], v[186:189], v[74:77]
	v_mfma_f32_16x16x32_bf16 v[162:165], v[110:113], v[166:169], v[162:165]
	v_mfma_f32_16x16x32_bf16 v[158:161], v[126:129], v[166:169], v[158:161]
	v_mfma_f32_16x16x32_bf16 v[118:121], v[110:113], v[174:177], v[118:121]
	v_mfma_f32_16x16x32_bf16 v[114:117], v[126:129], v[174:177], v[114:117]
	v_mfma_f32_16x16x32_bf16 v[94:97], v[110:113], v[182:185], v[94:97]
	v_mfma_f32_16x16x32_bf16 v[90:93], v[126:129], v[182:185], v[90:93]
	v_mfma_f32_16x16x32_bf16 v[78:81], v[110:113], v[206:209], v[78:81]
	v_mfma_f32_16x16x32_bf16 v[74:77], v[126:129], v[206:209], v[74:77]
	s_setprio 0
	s_setprio 3
	v_mfma_f32_16x16x32_bf16 v[134:137], v[138:141], v[154:157], v[134:137]
	v_mfma_f32_16x16x32_bf16 v[130:133], v[146:149], v[154:157], v[130:133]
	v_mfma_f32_16x16x32_bf16 v[106:109], v[138:141], v[170:173], v[106:109]
	v_mfma_f32_16x16x32_bf16 v[102:105], v[146:149], v[170:173], v[102:105]
	v_mfma_f32_16x16x32_bf16 v[86:89], v[138:141], v[178:181], v[86:89]
	v_mfma_f32_16x16x32_bf16 v[82:85], v[146:149], v[178:181], v[82:85]
	v_mfma_f32_16x16x32_bf16 v[70:73], v[138:141], v[186:189], v[70:73]
	v_mfma_f32_16x16x32_bf16 v[66:69], v[146:149], v[186:189], v[66:69]
	v_mfma_f32_16x16x32_bf16 v[134:137], v[142:145], v[166:169], v[134:137]
	v_mfma_f32_16x16x32_bf16 v[130:133], v[150:153], v[166:169], v[130:133]
	v_mfma_f32_16x16x32_bf16 v[106:109], v[142:145], v[174:177], v[106:109]
	v_mfma_f32_16x16x32_bf16 v[102:105], v[150:153], v[174:177], v[102:105]
	v_mfma_f32_16x16x32_bf16 v[86:89], v[142:145], v[182:185], v[86:89]
	v_mfma_f32_16x16x32_bf16 v[82:85], v[150:153], v[182:185], v[82:85]
	v_mfma_f32_16x16x32_bf16 v[70:73], v[142:145], v[206:209], v[70:73]
	v_mfma_f32_16x16x32_bf16 v[66:69], v[150:153], v[206:209], v[66:69]
	s_setprio 0
	s_barrier
; #define PG8_STAGE_A(b, h, ptr, NX) do { if constexpr (Sched::GATHER) { unsigned gs_[2]; gs_[0] = ((NX) && last_) ? gN[h][0] : gA[h][0]; gs_[1] = ((NX) && last_) ? gN[h][1] : gA[h][1]; PG8_STAGE(PG8_SA(b, h), ptr, gs_); } \
;         else PG8_STAGE(PG8_SA(b, h), (ptr) + ((h) ? hstep : (size_t)0), voffA); } while (0)
; #define PG8_STAGE(bufoff, gbase, voff) do { _Pragma("unroll") for (int _i = 0; _i < 2; ++_i) \
;         __builtin_amdgcn_global_load_lds((const unsigned*)((const char*)(gbase) + (voff)[_i]), (PG8_LAS unsigned*)(lds + (bufoff) + ldsw + _i * 8192), 16, 0, 0); } while (0)
; template <class Epi, class Sched, bool ALIGN_EPI = false, bool SP2 = false>
; __device__ __forceinline__ void gemm_phase(PG8_LAS unsigned char* lds, const Gemm g, const Sched& S, const Epi& E, const bool skip_epi = false) {
;     ...
;         for (int t = 0; t < nt; t += 2) {
;             const bool last = (t == nt - 2); last_ = last && has_next;
;             const char* a1 = cA + (size_t)(t + 1) * kstep;
;             const char* a2 = last ? nA : cA + (size_t)(t + 2) * kstep; const char* b2 = last ? nB : cB + (size_t)(t + 2) * kstep;
;             const char* a3 = a2 + kstep; const char* b3 = b2 + kstep;
;             if (last && has_next) S.a_ready(nxt);
;             if constexpr (SP2) {
;             PG8_LDB(B0, 0, 0); PG8_LDB(B1, 0, 1); PG8_SCHED; PG8_LDA(At, 0, 0); PG8_STAGE_A(1, 1, a1, false);
;             PG8_WAIT_V(8); PG8_WAIT_L(0); PG8_BAR; PG8_MMA(0, 0, At, B0); PG8_MMA(0, 1, At, B1); PG8_BAR; PG8_SCHED;
;             PG8_LDA(At, 0, 1); PG8_STAGE(PG8_SB(0, 0), b2, voffB); PG8_STAGE(PG8_SB(0, 1), b2 + hstep, voffB); PG8_STAGE_A(0, 0, a2, true);
;             PG8_WAIT_V(8); PG8_WAIT_L(0); PG8_BAR; PG8_MMA(1, 0, At, B0); PG8_MMA(1, 1, At, B1); PG8_BAR; PG8_SCHED;
;             PG8_LDB(B0, 1, 0); PG8_LDB(B1, 1, 1); PG8_SCHED; PG8_LDA(At, 1, 0); PG8_STAGE_A(0, 1, a2, true);
;             PG8_WAIT_V(8); PG8_WAIT_L(0); PG8_BAR; PG8_MMA(0, 0, At, B0); PG8_MMA(0, 1, At, B1); PG8_BAR; PG8_SCHED;
;             PG8_LDA(At, 1, 1); PG8_STAGE(PG8_SB(1, 0), b3, voffB); PG8_STAGE(PG8_SB(1, 1), b3 + hstep, voffB); PG8_STAGE_A(1, 0, a3, true);
;             PG8_WAIT_V(8); PG8_WAIT_L(0); PG8_BAR; PG8_MMA(1, 0, At, B0); PG8_MMA(1, 1, At, B1); PG8_BAR; PG8_SCHED;
;             } else {
;             PG8_LDB(B0, 0, 0); PG8_SCHED; PG8_LDA(At, 0, 0); PG8_STAGE_A(1, 1, a1, false);
	s_add_i32 s30, s64, s2
	s_add_i32 m0, s30, 0xffffff80
	ds_read_b128 v[154:157], v236 offset:49152
	ds_read_b128 v[166:169], v236 offset:50176
	ds_read_b128 v[170:173], v236 offset:51200
	ds_read_b128 v[174:177], v236 offset:52224
	ds_read_b128 v[178:181], v236 offset:53248
	ds_read_b128 v[182:185], v236 offset:54272
	ds_read_b128 v[186:189], v236 offset:55296
	ds_read_b128 v[206:209], v236 offset:56320
	global_load_lds_dwordx4 v[210:211], off offset:128
	s_add_i32 m0, s30, 0x1f80
	s_add_u32 s28, s28, 0x40080
	s_addc_u32 s29, s29, 0
	s_add_i32 s30, s65, s2
	global_load_lds_dwordx4 v[212:213], off offset:128
	s_mov_b32 m0, s30
	s_nop 0
	global_load_lds_dwordx4 v192, s[28:29]
	s_add_i32 m0, s30, 0x2000
	s_nop 0
	global_load_lds_dwordx4 v196, s[28:29]
	s_add_i32 m0, s39, 0xffffff80
	s_nop 0
	global_load_lds_dwordx4 v[214:215], off offset:128
	s_add_i32 m0, s48, 0xffffff80
	s_nop 0
	global_load_lds_dwordx4 v[216:217], off offset:128
	s_waitcnt vmcnt(8)
	s_waitcnt lgkmcnt(0)
	s_barrier
	s_setprio 3
	s_waitcnt lgkmcnt(0)
	v_mfma_f32_16x16x32_bf16 v[62:65], v[98:101], v[154:157], v[62:65]
	v_mfma_f32_16x16x32_bf16 v[58:61], v[122:125], v[154:157], v[58:61]
	v_mfma_f32_16x16x32_bf16 v[46:49], v[98:101], v[170:173], v[46:49]
	v_mfma_f32_16x16x32_bf16 v[42:45], v[122:125], v[170:173], v[42:45]
	v_mfma_f32_16x16x32_bf16 v[30:33], v[98:101], v[178:181], v[30:33]
	v_mfma_f32_16x16x32_bf16 v[26:29], v[122:125], v[178:181], v[26:29]
	v_mfma_f32_16x16x32_bf16 v[14:17], v[98:101], v[186:189], v[14:17]
	v_mfma_f32_16x16x32_bf16 v[10:13], v[122:125], v[186:189], v[10:13]
	v_mfma_f32_16x16x32_bf16 v[62:65], v[110:113], v[166:169], v[62:65]
	v_mfma_f32_16x16x32_bf16 v[58:61], v[126:129], v[166:169], v[58:61]
	v_mfma_f32_16x16x32_bf16 v[46:49], v[110:113], v[174:177], v[46:49]
	v_mfma_f32_16x16x32_bf16 v[42:45], v[126:129], v[174:177], v[42:45]
	v_mfma_f32_16x16x32_bf16 v[30:33], v[110:113], v[182:185], v[30:33]
	v_mfma_f32_16x16x32_bf16 v[26:29], v[126:129], v[182:185], v[26:29]
	v_mfma_f32_16x16x32_bf16 v[14:17], v[110:113], v[206:209], v[14:17]
	v_mfma_f32_16x16x32_bf16 v[10:13], v[126:129], v[206:209], v[10:13]
	s_setprio 0
	s_setprio 3
	v_mfma_f32_16x16x32_bf16 v[54:57], v[138:141], v[154:157], v[54:57]
	v_mfma_f32_16x16x32_bf16 v[50:53], v[146:149], v[154:157], v[50:53]
	v_mfma_f32_16x16x32_bf16 v[38:41], v[138:141], v[170:173], v[38:41]
	v_mfma_f32_16x16x32_bf16 v[34:37], v[146:149], v[170:173], v[34:37]
	v_mfma_f32_16x16x32_bf16 v[22:25], v[138:141], v[178:181], v[22:25]
	v_mfma_f32_16x16x32_bf16 v[18:21], v[146:149], v[178:181], v[18:21]
	v_mfma_f32_16x16x32_bf16 v[6:9], v[138:141], v[186:189], v[6:9]
	v_mfma_f32_16x16x32_bf16 v[2:5], v[146:149], v[186:189], v[2:5]
	v_mfma_f32_16x16x32_bf16 v[54:57], v[142:145], v[166:169], v[54:57]
	v_mfma_f32_16x16x32_bf16 v[50:53], v[150:153], v[166:169], v[50:53]
	v_mfma_f32_16x16x32_bf16 v[38:41], v[142:145], v[174:177], v[38:41]
	v_mfma_f32_16x16x32_bf16 v[34:37], v[150:153], v[174:177], v[34:37]
	v_mfma_f32_16x16x32_bf16 v[22:25], v[142:145], v[182:185], v[22:25]
	v_mfma_f32_16x16x32_bf16 v[18:21], v[150:153], v[182:185], v[18:21]
	v_mfma_f32_16x16x32_bf16 v[6:9], v[142:145], v[206:209], v[6:9]
	v_mfma_f32_16x16x32_bf16 v[2:5], v[150:153], v[206:209], v[2:5]
	s_setprio 0
	s_barrier
	s_add_i32 s63, s63, 2
	s_add_u32 s26, s26, 0x100
	s_addc_u32 s27, s27, 0
	s_add_u32 s61, s61, 0x100
	s_addc_u32 s62, s62, 0
	s_cmp_gt_u32 s63, 13
.LBB0_634:
	ds_read_b128 v[98:101], v234
	ds_read_b128 v[110:113], v234 offset:1024
	ds_read_b128 v[122:125], v234 offset:2048
	ds_read_b128 v[126:129], v234 offset:3072
	ds_read_b128 v[138:141], v235
	ds_read_b128 v[142:145], v235 offset:1024
	ds_read_b128 v[146:149], v235 offset:2048
	ds_read_b128 v[150:153], v235 offset:3072
	s_add_u32 s28, s26, 0xfffc0080
	s_addc_u32 s29, s27, -1
	s_cmp_eq_u32 s63, 12
	s_cselect_b32 s31, s19, s29
	s_cselect_b32 s30, s25, s28
	s_cselect_b32 s29, s17, s62
	s_cselect_b32 s28, s60, s61
	s_add_i32 m0, s3, 0xc000
	ds_read_b128 v[154:157], v236
	ds_read_b128 v[166:169], v236 offset:1024
	ds_read_b128 v[170:173], v236 offset:2048
	ds_read_b128 v[174:177], v236 offset:3072
	ds_read_b128 v[178:181], v236 offset:4096
	ds_read_b128 v[182:185], v236 offset:5120
	ds_read_b128 v[186:189], v236 offset:6144
	ds_read_b128 v[206:209], v236 offset:7168
	global_load_lds_dwordx4 v198, s[26:27]
	s_add_i32 m0, s3, 0xe000
	s_nop 0
	global_load_lds_dwordx4 v200, s[26:27]
	s_waitcnt vmcnt(8)
	s_waitcnt lgkmcnt(0)
	s_barrier
; #define PG8_STAGE_A(b, h, ptr, NX) do { if constexpr (Sched::GATHER) { unsigned gs_[2]; gs_[0] = ((NX) && last_) ? gN[h][0] : gA[h][0]; gs_[1] = ((NX) && last_) ? gN[h][1] : gA[h][1]; PG8_STAGE(PG8_SA(b, h), ptr, gs_); } \
;         else PG8_STAGE(PG8_SA(b, h), (ptr) + ((h) ? hstep : (size_t)0), voffA); } while (0)
; #define PG8_STAGE(bufoff, gbase, voff) do { _Pragma("unroll") for (int _i = 0; _i < 2; ++_i) \
;         __builtin_amdgcn_global_load_lds((const unsigned*)((const char*)(gbase) + (voff)[_i]), (PG8_LAS unsigned*)(lds + (bufoff) + ldsw + _i * 8192), 16, 0, 0); } while (0)
; #define PG8_LDA(dst, b, h) do { _Pragma("unroll") for (int m = 0; m < 4; ++m) _Pragma("unroll") for (int k = 0; k < 2; ++k) dst[m][k] = *(const PG8_LAS bf16x8*)(lds + PG8_SA(b, h) + aoff + m * 2048 + k * 1024); } while (0)
; #define PG8_MMA(ai, bj, At, Bt) do { __builtin_amdgcn_s_setprio(1); _Pragma("unroll") for (int m = 0; m < 4; ++m) _Pragma("unroll") for (int n = 0; n < 2; ++n) _Pragma("unroll") for (int k = 0; k < 2; ++k) \
;         acc[ai][bj][m][n] = __builtin_amdgcn_mfma_f32_16x16x32_bf16(Bt[n][k], At[m][k], acc[ai][bj][m][n], 0, 0, 0); __builtin_amdgcn_s_setprio(0); } while (0)
; #define PG8_WAIT_V(n) asm volatile("s_waitcnt vmcnt(" #n ")" ::: "memory")
; #define PG8_WAIT_L(n) asm volatile("s_waitcnt lgkmcnt(" #n ")" ::: "memory")
; #define PG8_BAR __builtin_amdgcn_s_barrier()
; #define PG8_SCHED __builtin_amdgcn_sched_barrier(0)
; template <class Epi, class Sched, bool ALIGN_EPI = false, bool SP2 = false>
; __device__ __forceinline__ void gemm_phase(PG8_LAS unsigned char* lds, const Gemm g, const Sched& S, const Epi& E, const bool skip_epi = false) {
;     ...
;             PG8_WAIT_V(8); PG8_WAIT_L(0); PG8_BAR; PG8_MMA(0, 0, At, B0); PG8_MMA(0, 1, At, B1); PG8_BAR; PG8_SCHED;
;             PG8_LDA(At, 0, 1); PG8_STAGE(PG8_SB(0, 0), b2, voffB); PG8_STAGE(PG8_SB(0, 1), b2 + hstep, voffB); PG8_STAGE_A(0, 0, a2, true);
;             PG8_WAIT_V(8); PG8_WAIT_L(0); PG8_BAR; PG8_MMA(1, 0, At, B0); PG8_MMA(1, 1, At, B1); PG8_BAR; PG8_SCHED;
	s_setprio 3
	s_waitcnt lgkmcnt(0)
	v_mfma_f32_16x16x32_bf16 v[162:165], v[98:101], v[154:157], v[162:165]
	v_mfma_f32_16x16x32_bf16 v[158:161], v[122:125], v[154:157], v[158:161]
	v_mfma_f32_16x16x32_bf16 v[118:121], v[98:101], v[170:173], v[118:121]
	v_mfma_f32_16x16x32_bf16 v[114:117], v[122:125], v[170:173], v[114:117]
	v_mfma_f32_16x16x32_bf16 v[94:97], v[98:101], v[178:181], v[94:97]
	v_mfma_f32_16x16x32_bf16 v[90:93], v[122:125], v[178:181], v[90:93]
	v_mfma_f32_16x16x32_bf16 v[78:81], v[98:101], v[186:189], v[78:81]
	v_mfma_f32_16x16x32_bf16 v[74:77], v[122:125], v[186:189], v[74:77]
	v_mfma_f32_16x16x32_bf16 v[162:165], v[110:113], v[166:169], v[162:165]
	v_mfma_f32_16x16x32_bf16 v[158:161], v[126:129], v[166:169], v[158:161]
	v_mfma_f32_16x16x32_bf16 v[118:121], v[110:113], v[174:177], v[118:121]
	v_mfma_f32_16x16x32_bf16 v[114:117], v[126:129], v[174:177], v[114:117]
	v_mfma_f32_16x16x32_bf16 v[94:97], v[110:113], v[182:185], v[94:97]
	v_mfma_f32_16x16x32_bf16 v[90:93], v[126:129], v[182:185], v[90:93]
	v_mfma_f32_16x16x32_bf16 v[78:81], v[110:113], v[206:209], v[78:81]
	v_mfma_f32_16x16x32_bf16 v[74:77], v[126:129], v[206:209], v[74:77]
	s_setprio 0
	s_setprio 3
	v_mfma_f32_16x16x32_bf16 v[134:137], v[138:141], v[154:157], v[134:137]
	v_mfma_f32_16x16x32_bf16 v[130:133], v[146:149], v[154:157], v[130:133]
	v_mfma_f32_16x16x32_bf16 v[106:109], v[138:141], v[170:173], v[106:109]
	v_mfma_f32_16x16x32_bf16 v[102:105], v[146:149], v[170:173], v[102:105]
	v_mfma_f32_16x16x32_bf16 v[86:89], v[138:141], v[178:181], v[86:89]
	v_mfma_f32_16x16x32_bf16 v[82:85], v[146:149], v[178:181], v[82:85]
	v_mfma_f32_16x16x32_bf16 v[70:73], v[138:141], v[186:189], v[70:73]
	v_mfma_f32_16x16x32_bf16 v[66:69], v[146:149], v[186:189], v[66:69]
	v_mfma_f32_16x16x32_bf16 v[134:137], v[142:145], v[166:169], v[134:137]
	v_mfma_f32_16x16x32_bf16 v[130:133], v[150:153], v[166:169], v[130:133]
	v_mfma_f32_16x16x32_bf16 v[106:109], v[142:145], v[174:177], v[106:109]
	v_mfma_f32_16x16x32_bf16 v[102:105], v[150:153], v[174:177], v[102:105]
	v_mfma_f32_16x16x32_bf16 v[86:89], v[142:145], v[182:185], v[86:89]
	v_mfma_f32_16x16x32_bf16 v[82:85], v[150:153], v[182:185], v[82:85]
	v_mfma_f32_16x16x32_bf16 v[70:73], v[142:145], v[206:209], v[70:73]
	v_mfma_f32_16x16x32_bf16 v[66:69], v[150:153], v[206:209], v[66:69]
	s_setprio 0
	s_barrier
	s_add_i32 s64, s57, s2
	v_lshl_add_u64 v[210:211], s[28:29], 0, v[192:193]
	s_mov_b32 m0, s64
	ds_read_b128 v[154:157], v236 offset:16384
	ds_read_b128 v[166:169], v236 offset:17408
	ds_read_b128 v[170:173], v236 offset:18432
	ds_read_b128 v[174:177], v236 offset:19456
	ds_read_b128 v[178:181], v236 offset:20480
	ds_read_b128 v[182:185], v236 offset:21504
	ds_read_b128 v[186:189], v236 offset:22528
	ds_read_b128 v[206:209], v236 offset:23552
	global_load_lds_dwordx4 v[210:211], off
	s_add_i32 m0, s64, 0x2000
	s_add_u32 s64, s28, 0x40000
	v_lshl_add_u64 v[212:213], s[28:29], 0, v[196:197]
	s_addc_u32 s65, s29, 0
	s_add_i32 s66, s58, s2
	global_load_lds_dwordx4 v[212:213], off
	s_mov_b32 m0, s66
	v_lshl_add_u64 v[216:217], s[30:31], 0, v[194:195]
	global_load_lds_dwordx4 v192, s[64:65]
	s_add_i32 m0, s66, 0x2000
	s_nop 0
	global_load_lds_dwordx4 v196, s[64:65]
	v_lshl_add_u64 v[214:215], s[30:31], 0, v[190:191]
	s_mov_b32 m0, s3
	s_nop 0
	global_load_lds_dwordx4 v[214:215], off
	s_mov_b32 m0, s34
	s_nop 0
	global_load_lds_dwordx4 v[216:217], off
	s_waitcnt vmcnt(8)
	s_waitcnt lgkmcnt(0)
	s_barrier
	s_setprio 3
	s_waitcnt lgkmcnt(0)
	v_mfma_f32_16x16x32_bf16 v[62:65], v[98:101], v[154:157], v[62:65]
	v_mfma_f32_16x16x32_bf16 v[58:61], v[122:125], v[154:157], v[58:61]
	v_mfma_f32_16x16x32_bf16 v[46:49], v[98:101], v[170:173], v[46:49]
	v_mfma_f32_16x16x32_bf16 v[42:45], v[122:125], v[170:173], v[42:45]
	v_mfma_f32_16x16x32_bf16 v[30:33], v[98:101], v[178:181], v[30:33]
	v_mfma_f32_16x16x32_bf16 v[26:29], v[122:125], v[178:181], v[26:29]
	v_mfma_f32_16x16x32_bf16 v[14:17], v[98:101], v[186:189], v[14:17]
	v_mfma_f32_16x16x32_bf16 v[10:13], v[122:125], v[186:189], v[10:13]
	v_mfma_f32_16x16x32_bf16 v[62:65], v[110:113], v[166:169], v[62:65]
	v_mfma_f32_16x16x32_bf16 v[58:61], v[126:129], v[166:169], v[58:61]
	v_mfma_f32_16x16x32_bf16 v[46:49], v[110:113], v[174:177], v[46:49]
	v_mfma_f32_16x16x32_bf16 v[42:45], v[126:129], v[174:177], v[42:45]
	v_mfma_f32_16x16x32_bf16 v[30:33], v[110:113], v[182:185], v[30:33]
	v_mfma_f32_16x16x32_bf16 v[26:29], v[126:129], v[182:185], v[26:29]
	v_mfma_f32_16x16x32_bf16 v[14:17], v[110:113], v[206:209], v[14:17]
	v_mfma_f32_16x16x32_bf16 v[10:13], v[126:129], v[206:209], v[10:13]
	s_setprio 0
	s_setprio 3
	v_mfma_f32_16x16x32_bf16 v[54:57], v[138:141], v[154:157], v[54:57]
	v_mfma_f32_16x16x32_bf16 v[50:53], v[146:149], v[154:157], v[50:53]
	v_mfma_f32_16x16x32_bf16 v[38:41], v[138:141], v[170:173], v[38:41]
	v_mfma_f32_16x16x32_bf16 v[34:37], v[146:149], v[170:173], v[34:37]
	v_mfma_f32_16x16x32_bf16 v[22:25], v[138:141], v[178:181], v[22:25]
	v_mfma_f32_16x16x32_bf16 v[18:21], v[146:149], v[178:181], v[18:21]
	v_mfma_f32_16x16x32_bf16 v[6:9], v[138:141], v[186:189], v[6:9]
	v_mfma_f32_16x16x32_bf16 v[2:5], v[146:149], v[186:189], v[2:5]
	v_mfma_f32_16x16x32_bf16 v[54:57], v[142:145], v[166:169], v[54:57]
	v_mfma_f32_16x16x32_bf16 v[50:53], v[150:153], v[166:169], v[50:53]
	v_mfma_f32_16x16x32_bf16 v[38:41], v[142:145], v[174:177], v[38:41]
	v_mfma_f32_16x16x32_bf16 v[34:37], v[150:153], v[174:177], v[34:37]
	v_mfma_f32_16x16x32_bf16 v[22:25], v[142:145], v[182:185], v[22:25]
	v_mfma_f32_16x16x32_bf16 v[18:21], v[150:153], v[182:185], v[18:21]
	v_mfma_f32_16x16x32_bf16 v[6:9], v[142:145], v[206:209], v[6:9]
	v_mfma_f32_16x16x32_bf16 v[2:5], v[150:153], v[206:209], v[2:5]
	s_setprio 0
	s_barrier
; #define PG8_STAGE_A(b, h, ptr, NX) do { if constexpr (Sched::GATHER) { unsigned gs_[2]; gs_[0] = ((NX) && last_) ? gN[h][0] : gA[h][0]; gs_[1] = ((NX) && last_) ? gN[h][1] : gA[h][1]; PG8_STAGE(PG8_SA(b, h), ptr, gs_); } \
;         else PG8_STAGE(PG8_SA(b, h), (ptr) + ((h) ? hstep : (size_t)0), voffA); } while (0)
; #define PG8_STAGE(bufoff, gbase, voff) do { _Pragma("unroll") for (int _i = 0; _i < 2; ++_i) \
;         __builtin_amdgcn_global_load_lds((const unsigned*)((const char*)(gbase) + (voff)[_i]), (PG8_LAS unsigned*)(lds + (bufoff) + ldsw + _i * 8192), 16, 0, 0); } while (0)
; #define PG8_LDA(dst, b, h) do { _Pragma("unroll") for (int m = 0; m < 4; ++m) _Pragma("unroll") for (int k = 0; k < 2; ++k) dst[m][k] = *(const PG8_LAS bf16x8*)(lds + PG8_SA(b, h) + aoff + m * 2048 + k * 1024); } while (0)
; #define PG8_LDB(dst, b, h) do { _Pragma("unroll") for (int n = 0; n < 2; ++n) _Pragma("unroll") for (int k = 0; k < 2; ++k) dst[n][k] = *(const PG8_LAS bf16x8*)(lds + PG8_SB(b, h) + boff + n * 2048 + k * 1024); } while (0)
; #define PG8_MMA(ai, bj, At, Bt) do { __builtin_amdgcn_s_setprio(1); _Pragma("unroll") for (int m = 0; m < 4; ++m) _Pragma("unroll") for (int n = 0; n < 2; ++n) _Pragma("unroll") for (int k = 0; k < 2; ++k) \
;         acc[ai][bj][m][n] = __builtin_amdgcn_mfma_f32_16x16x32_bf16(Bt[n][k], At[m][k], acc[ai][bj][m][n], 0, 0, 0); __builtin_amdgcn_s_setprio(0); } while (0)
; #define PG8_WAIT_V(n) asm volatile("s_waitcnt vmcnt(" #n ")" ::: "memory")
; #define PG8_WAIT_L(n) asm volatile("s_waitcnt lgkmcnt(" #n ")" ::: "memory")
; #define PG8_BAR __builtin_amdgcn_s_barrier()
; template <class Epi, class Sched, bool ALIGN_EPI = false, bool SP2 = false>
; __device__ __forceinline__ void gemm_phase(PG8_LAS unsigned char* lds, const Gemm g, const Sched& S, const Epi& E, const bool skip_epi = false) {
;     ...
;             PG8_LDB(B0, 1, 0); PG8_LDB(B1, 1, 1); PG8_SCHED; PG8_LDA(At, 1, 0); PG8_STAGE_A(0, 1, a2, true);
;             PG8_WAIT_V(8); PG8_WAIT_L(0); PG8_BAR; PG8_MMA(0, 0, At, B0); PG8_MMA(0, 1, At, B1); PG8_BAR; PG8_SCHED;
;             PG8_LDA(At, 1, 1); PG8_STAGE(PG8_SB(1, 0), b3, voffB); PG8_STAGE(PG8_SB(1, 1), b3 + hstep, voffB); PG8_STAGE_A(1, 0, a3, true);
;             PG8_WAIT_V(8); PG8_WAIT_L(0); PG8_BAR; PG8_MMA(1, 0, At, B0); PG8_MMA(1, 1, At, B1); PG8_BAR; PG8_SCHED;
;     ...
;         if constexpr (ALIGN_EPI) { if (wr == 0) PG8_BAR; }
	s_add_i32 s64, 0, 0x18000
	s_add_i32 s65, 0, 0x1c000
	v_add_u32_e32 v126, s64, v229
	v_add_u32_e32 v150, s65, v229
	ds_read_b128 v[98:101], v126
	ds_read_b128 v[110:113], v126 offset:1024
	ds_read_b128 v[122:125], v126 offset:2048
	ds_read_b128 v[126:129], v126 offset:3072
	ds_read_b128 v[138:141], v150
	ds_read_b128 v[142:145], v150 offset:1024
	ds_read_b128 v[146:149], v150 offset:2048
	ds_read_b128 v[150:153], v150 offset:3072
	s_add_u32 s30, s30, 0x40000
	s_addc_u32 s31, s31, 0
	s_mov_b32 m0, s35
	ds_read_b128 v[154:157], v236 offset:32768
	ds_read_b128 v[166:169], v236 offset:33792
	ds_read_b128 v[170:173], v236 offset:34816
	ds_read_b128 v[174:177], v236 offset:35840
	ds_read_b128 v[178:181], v236 offset:36864
	ds_read_b128 v[182:185], v236 offset:37888
	ds_read_b128 v[186:189], v236 offset:38912
	ds_read_b128 v[206:209], v236 offset:39936
	global_load_lds_dwordx4 v190, s[30:31]
	s_mov_b32 m0, s36
	s_nop 0
	global_load_lds_dwordx4 v194, s[30:31]
	s_waitcnt vmcnt(8)
	s_waitcnt lgkmcnt(0)
	s_barrier
	s_setprio 3
	s_waitcnt lgkmcnt(0)
	v_mfma_f32_16x16x32_bf16 v[162:165], v[98:101], v[154:157], v[162:165]
	v_mfma_f32_16x16x32_bf16 v[158:161], v[122:125], v[154:157], v[158:161]
	v_mfma_f32_16x16x32_bf16 v[118:121], v[98:101], v[170:173], v[118:121]
	v_mfma_f32_16x16x32_bf16 v[114:117], v[122:125], v[170:173], v[114:117]
	v_mfma_f32_16x16x32_bf16 v[94:97], v[98:101], v[178:181], v[94:97]
	v_mfma_f32_16x16x32_bf16 v[90:93], v[122:125], v[178:181], v[90:93]
	v_mfma_f32_16x16x32_bf16 v[78:81], v[98:101], v[186:189], v[78:81]
	v_mfma_f32_16x16x32_bf16 v[74:77], v[122:125], v[186:189], v[74:77]
	v_mfma_f32_16x16x32_bf16 v[162:165], v[110:113], v[166:169], v[162:165]
	v_mfma_f32_16x16x32_bf16 v[158:161], v[126:129], v[166:169], v[158:161]
	v_mfma_f32_16x16x32_bf16 v[118:121], v[110:113], v[174:177], v[118:121]
	v_mfma_f32_16x16x32_bf16 v[114:117], v[126:129], v[174:177], v[114:117]
	v_mfma_f32_16x16x32_bf16 v[94:97], v[110:113], v[182:185], v[94:97]
	v_mfma_f32_16x16x32_bf16 v[90:93], v[126:129], v[182:185], v[90:93]
	v_mfma_f32_16x16x32_bf16 v[78:81], v[110:113], v[206:209], v[78:81]
	v_mfma_f32_16x16x32_bf16 v[74:77], v[126:129], v[206:209], v[74:77]
	s_setprio 0
	s_setprio 3
	v_mfma_f32_16x16x32_bf16 v[134:137], v[138:141], v[154:157], v[134:137]
	v_mfma_f32_16x16x32_bf16 v[130:133], v[146:149], v[154:157], v[130:133]
	v_mfma_f32_16x16x32_bf16 v[106:109], v[138:141], v[170:173], v[106:109]
	v_mfma_f32_16x16x32_bf16 v[102:105], v[146:149], v[170:173], v[102:105]
	v_mfma_f32_16x16x32_bf16 v[86:89], v[138:141], v[178:181], v[86:89]
	v_mfma_f32_16x16x32_bf16 v[82:85], v[146:149], v[178:181], v[82:85]
	v_mfma_f32_16x16x32_bf16 v[70:73], v[138:141], v[186:189], v[70:73]
	v_mfma_f32_16x16x32_bf16 v[66:69], v[146:149], v[186:189], v[66:69]
	v_mfma_f32_16x16x32_bf16 v[134:137], v[142:145], v[166:169], v[134:137]
	v_mfma_f32_16x16x32_bf16 v[130:133], v[150:153], v[166:169], v[130:133]
	v_mfma_f32_16x16x32_bf16 v[106:109], v[142:145], v[174:177], v[106:109]
	v_mfma_f32_16x16x32_bf16 v[102:105], v[150:153], v[174:177], v[102:105]
	v_mfma_f32_16x16x32_bf16 v[86:89], v[142:145], v[182:185], v[86:89]
	v_mfma_f32_16x16x32_bf16 v[82:85], v[150:153], v[182:185], v[82:85]
	v_mfma_f32_16x16x32_bf16 v[70:73], v[142:145], v[206:209], v[70:73]
	v_mfma_f32_16x16x32_bf16 v[66:69], v[150:153], v[206:209], v[66:69]
	s_setprio 0
	s_barrier
	s_add_i32 s30, s64, s2
	s_add_i32 m0, s30, 0xffffff80
	ds_read_b128 v[154:157], v236 offset:49152
	ds_read_b128 v[166:169], v236 offset:50176
	ds_read_b128 v[170:173], v236 offset:51200
	ds_read_b128 v[174:177], v236 offset:52224
	ds_read_b128 v[178:181], v236 offset:53248
	ds_read_b128 v[182:185], v236 offset:54272
	ds_read_b128 v[186:189], v236 offset:55296
	ds_read_b128 v[206:209], v236 offset:56320
	global_load_lds_dwordx4 v[210:211], off offset:128
	s_add_i32 m0, s30, 0x1f80
	s_add_u32 s28, s28, 0x40080
	s_addc_u32 s29, s29, 0
	s_add_i32 s30, s65, s2
	global_load_lds_dwordx4 v[212:213], off offset:128
	s_mov_b32 m0, s30
	s_nop 0
	global_load_lds_dwordx4 v192, s[28:29]
	s_add_i32 m0, s30, 0x2000
	s_nop 0
	global_load_lds_dwordx4 v196, s[28:29]
	s_add_i32 m0, s39, 0xffffff80
	s_nop 0
	global_load_lds_dwordx4 v[214:215], off offset:128
	s_add_i32 m0, s48, 0xffffff80
	s_nop 0
	global_load_lds_dwordx4 v[216:217], off offset:128
	s_waitcnt vmcnt(8)
	s_waitcnt lgkmcnt(0)
	s_barrier
	s_setprio 3
	s_waitcnt lgkmcnt(0)
	v_mfma_f32_16x16x32_bf16 v[62:65], v[98:101], v[154:157], v[62:65]
	v_mfma_f32_16x16x32_bf16 v[58:61], v[122:125], v[154:157], v[58:61]
	v_mfma_f32_16x16x32_bf16 v[46:49], v[98:101], v[170:173], v[46:49]
	v_mfma_f32_16x16x32_bf16 v[42:45], v[122:125], v[170:173], v[42:45]
	v_mfma_f32_16x16x32_bf16 v[30:33], v[98:101], v[178:181], v[30:33]
	v_mfma_f32_16x16x32_bf16 v[26:29], v[122:125], v[178:181], v[26:29]
	v_mfma_f32_16x16x32_bf16 v[14:17], v[98:101], v[186:189], v[14:17]
	v_mfma_f32_16x16x32_bf16 v[10:13], v[122:125], v[186:189], v[10:13]
	v_mfma_f32_16x16x32_bf16 v[62:65], v[110:113], v[166:169], v[62:65]
	v_mfma_f32_16x16x32_bf16 v[58:61], v[126:129], v[166:169], v[58:61]
	v_mfma_f32_16x16x32_bf16 v[46:49], v[110:113], v[174:177], v[46:49]
	v_mfma_f32_16x16x32_bf16 v[42:45], v[126:129], v[174:177], v[42:45]
	v_mfma_f32_16x16x32_bf16 v[30:33], v[110:113], v[182:185], v[30:33]
	v_mfma_f32_16x16x32_bf16 v[26:29], v[126:129], v[182:185], v[26:29]
	v_mfma_f32_16x16x32_bf16 v[14:17], v[110:113], v[206:209], v[14:17]
	v_mfma_f32_16x16x32_bf16 v[10:13], v[126:129], v[206:209], v[10:13]
	s_setprio 0
	s_setprio 3
	v_mfma_f32_16x16x32_bf16 v[54:57], v[138:141], v[154:157], v[54:57]
	v_mfma_f32_16x16x32_bf16 v[50:53], v[146:149], v[154:157], v[50:53]
	v_mfma_f32_16x16x32_bf16 v[38:41], v[138:141], v[170:173], v[38:41]
	v_mfma_f32_16x16x32_bf16 v[34:37], v[146:149], v[170:173], v[34:37]
	v_mfma_f32_16x16x32_bf16 v[22:25], v[138:141], v[178:181], v[22:25]
	v_mfma_f32_16x16x32_bf16 v[18:21], v[146:149], v[178:181], v[18:21]
	v_mfma_f32_16x16x32_bf16 v[6:9], v[138:141], v[186:189], v[6:9]
	v_mfma_f32_16x16x32_bf16 v[2:5], v[146:149], v[186:189], v[2:5]
	v_mfma_f32_16x16x32_bf16 v[54:57], v[142:145], v[166:169], v[54:57]
	v_mfma_f32_16x16x32_bf16 v[50:53], v[150:153], v[166:169], v[50:53]
	v_mfma_f32_16x16x32_bf16 v[38:41], v[142:145], v[174:177], v[38:41]
	v_mfma_f32_16x16x32_bf16 v[34:37], v[150:153], v[174:177], v[34:37]
	v_mfma_f32_16x16x32_bf16 v[22:25], v[142:145], v[182:185], v[22:25]
	v_mfma_f32_16x16x32_bf16 v[18:21], v[150:153], v[182:185], v[18:21]
	v_mfma_f32_16x16x32_bf16 v[6:9], v[142:145], v[206:209], v[6:9]
	v_mfma_f32_16x16x32_bf16 v[2:5], v[150:153], v[206:209], v[2:5]
	s_setprio 0
	s_barrier
	s_add_i32 s63, s63, 2
	s_add_u32 s26, s26, 0x100
	s_addc_u32 s27, s27, 0
	s_add_u32 s61, s61, 0x100
	s_addc_u32 s62, s62, 0
	s_cmp_gt_u32 s63, 13
	s_cbranch_scc0 .LBB0_634
	s_and_b64 vcc, exec, s[14:15]
	s_cbranch_vccz .LBB0_637
	s_barrier

; #define PG8_STAGE_A(b, h, ptr, NX) do { if constexpr (Sched::GATHER) { unsigned gs_[2]; gs_[0] = ((NX) && last_) ? gN[h][0] : gA[h][0]; gs_[1] = ((NX) && last_) ? gN[h][1] : gA[h][1]; PG8_STAGE(PG8_SA(b, h), ptr, gs_); } \
;         else PG8_STAGE(PG8_SA(b, h), (ptr) + ((h) ? hstep : (size_t)0), voffA); } while (0)
; #define PG8_STAGE(bufoff, gbase, voff) do { _Pragma("unroll") for (int _i = 0; _i < 2; ++_i) \
;         __builtin_amdgcn_global_load_lds((const unsigned*)((const char*)(gbase) + (voff)[_i]), (PG8_LAS unsigned*)(lds + (bufoff) + ldsw + _i * 8192), 16, 0, 0); } while (0)
; #define PG8_WAIT_V(n) asm volatile("s_waitcnt vmcnt(" #n ")" ::: "memory")
; #define PG8_BAR __builtin_amdgcn_s_barrier()
; template <class Epi, class Sched, bool ALIGN_EPI = false, bool SP2 = false>
; __device__ __forceinline__ void gemm_phase(PG8_LAS unsigned char* lds, const Gemm g, const Sched& S, const Epi& E, const bool skip_epi = false) {
;     ...
;     const unsigned ldsw = (unsigned)wid * 1024u;
;     const int aoff = lds_byte(wr * 64 + fr, fq * 8), boff = lds_byte(wc * 32 + fr, fq * 8);
;     ...
;         PG8_WAIT_V(2); PG8_BAR;
;         PG8_STAGE(PG8_SB(1, 0), cB + kstep, voffB); PG8_STAGE_A(1, 0, cA + kstep, false); PG8_STAGE(PG8_SB(1, 1), cB + hstep + kstep, voffB);
;         PG8_WAIT_V(6); PG8_BAR;
.LBB0_715:
	s_lshl_b32 s8, s8, 5
	s_and_b32 s14, s8, 0x60
	s_mov_b64 s[8:9], 0x80
	s_add_i32 m0, s29, 0x18000
	v_lshl_add_u64 v[8:9], v[8:9], 0, s[8:9]
	s_lshl_b32 s11, s5, 13
	s_lshl_b32 s15, s14, 7
	s_waitcnt vmcnt(2)
	s_barrier
	global_load_lds_dwordx4 v[8:9], off
	v_lshl_add_u64 v[6:7], v[6:7], 0, s[8:9]
	s_add_i32 m0, s29, 0x1a000
	s_add_i32 s36, s29, 0x8000
	s_add_i32 s37, s29, 0xa000
	global_load_lds_dwordx4 v[6:7], off
	v_lshl_add_u64 v[2:3], v[2:3], 0, s[8:9]
	s_mov_b32 m0, s36
	s_add_u32 s12, s24, 0x40080
	global_load_lds_dwordx4 v[2:3], off
	v_lshl_add_u64 v[2:3], v[4:5], 0, s[8:9]
	s_mov_b32 m0, s37
	s_addc_u32 s13, s25, 0
	global_load_lds_dwordx4 v[2:3], off
	s_add_i32 m0, s29, 0x1c000
	s_nop 0
	global_load_lds_dwordx4 v146, s[12:13]
	s_add_i32 m0, s29, 0x1e000
	v_and_b32_e32 v1, 48, v12
	global_load_lds_dwordx4 v142, s[12:13]
	v_and_b32_e32 v2, 15, v12
	v_lshlrev_b32_e32 v3, 2, v12
	v_lshl_or_b32 v1, v2, 6, v1
	v_and_b32_e32 v3, 32, v3
	v_bitop3_b32 v4, v1, s11, v3 bitop3:0xde
	v_bitop3_b32 v1, s15, v1, v3 bitop3:0xf6
	v_bfe_u32 v3, v12, 2, 4
	s_waitcnt lgkmcnt(0)
	v_lshlrev_b32_e32 v179, 4, v2
	v_lshl_or_b32 v175, s5, 6, v3
	v_and_b32_e32 v2, 48, v179
	v_mov_b32_e32 v3, v147
	v_lshl_add_u64 v[150:151], s[80:81], 0, v[2:3]
	v_lshlrev_b32_e32 v2, 14, v15
	v_and_b32_e32 v2, 0xffff8000, v2
	v_lshl_add_u32 v2, v14, 11, v2
	v_and_b32_e32 v3, 1, v15
	v_lshl_or_b32 v2, v3, 6, v2
	v_lshl_add_u32 v152, v16, 1, v2
	v_lshlrev_b32_e32 v2, 14, v10
	v_and_b32_e32 v2, 0xffff8000, v2
	s_waitcnt vmcnt(6)
	s_cmpk_lt_u32 s10, 0x100
	v_lshl_add_u32 v2, v11, 11, v2
	v_and_b32_e32 v3, 1, v10
	s_cselect_b64 s[10:11], -1, 0
	v_and_b32_e32 v5, 3, v12
	v_and_b32_e32 v6, 60, v12
	v_lshl_or_b32 v2, v3, 6, v2
	s_add_i32 s39, 0, 0x10000
	s_add_i32 s48, 0, 0x14000
	s_sext_i32_i16 s21, s4
	v_lshl_or_b32 v171, v5, 6, v6
	s_ashr_i32 s38, s97, 31
	v_lshl_or_b32 v181, v5, 3, s14
	v_mov_b32_e32 v153, v147
	v_lshl_add_u32 v154, v13, 1, v2
	v_mov_b32_e32 v155, v147
	v_mov_b64_e32 v[156:157], 0x580
	v_mov_b64_e32 v[158:159], 0x57f
	v_add_u32_e32 v187, s39, v1
	v_add_u32_e32 v188, s48, v1
	v_add_u32_e32 v189, 0, v4
	v_mov_b32_e32 v190, 0x358637bd
	s_movk_i32 s49, 0x1600
	s_barrier
	s_branch .LBB0_718

; #define PG8_GIDX(G_, PM_) do { if constexpr (Sched::GATHER) { _Pragma("unroll") for (int h_ = 0; h_ < 2; ++h_) _Pragma("unroll") for (int i_ = 0; i_ < 2; ++i_) { int R_, C_; stage_rc(tid * 16 + i_ * 8192, R_, C_); \
;         const int src_ = S.rowsrc[(PM_) * BM + h_ * HALF + R_]; G_[h_][i_] = (unsigned)(src_ * K + C_) * 2u; } } } while (0)
; #define PG8_STAGE_A(b, h, ptr, NX) do { if constexpr (Sched::GATHER) { unsigned gs_[2]; gs_[0] = ((NX) && last_) ? gN[h][0] : gA[h][0]; gs_[1] = ((NX) && last_) ? gN[h][1] : gA[h][1]; PG8_STAGE(PG8_SA(b, h), ptr, gs_); } \
;         else PG8_STAGE(PG8_SA(b, h), (ptr) + ((h) ? hstep : (size_t)0), voffA); } while (0)
; #define PG8_LDA(dst, b, h) do { _Pragma("unroll") for (int m = 0; m < 4; ++m) _Pragma("unroll") for (int k = 0; k < 2; ++k) dst[m][k] = *(const PG8_LAS bf16x8*)(lds + PG8_SA(b, h) + aoff + m * 2048 + k * 1024); } while (0)
; template <class Epi, class Sched, bool ALIGN_EPI = false, bool SP2 = false>
; __device__ __forceinline__ void gemm_phase(PG8_LAS unsigned char* lds, const Gemm g, const Sched& S, const Epi& E, const bool skip_epi = false) {
;     ...
;         const bool has_next = S.next(ui + 1, nxt);
;         if (has_next) PG8_GIDX(gN, nxt.pm);
;         const char* nA = has_next ? (const char*)g.A + (size_t)nxt.pm * pmstepA + nxt.ko : cA; const char* nB = has_next ? (const char*)g.Bt + (size_t)nxt.pn * tstep + nxt.ko : cB;
;         for (int t = 0; t < nt; t += 2) {
;             const bool last = (t == nt - 2); last_ = last && has_next;
;             const char* a1 = cA + (size_t)(t + 1) * kstep;
;             const char* a2 = last ? nA : cA + (size_t)(t + 2) * kstep; const char* b2 = last ? nB : cB + (size_t)(t + 2) * kstep;
;             const char* a3 = a2 + kstep; const char* b3 = b2 + kstep;
;             if (last && has_next) S.a_ready(nxt);
;             if constexpr (SP2) {
;             PG8_LDB(B0, 0, 0); PG8_LDB(B1, 0, 1); PG8_SCHED; PG8_LDA(At, 0, 0); PG8_STAGE_A(1, 1, a1, false);
;             PG8_WAIT_V(8); PG8_WAIT_L(0); PG8_BAR; PG8_MMA(0, 0, At, B0); PG8_MMA(0, 1, At, B1); PG8_BAR; PG8_SCHED;
;             PG8_LDA(At, 0, 1); PG8_STAGE(PG8_SB(0, 0), b2, voffB); PG8_STAGE(PG8_SB(0, 1), b2 + hstep, voffB); PG8_STAGE_A(0, 0, a2, true);
;             PG8_WAIT_V(8); PG8_WAIT_L(0); PG8_BAR; PG8_MMA(1, 0, At, B0); PG8_MMA(1, 1, At, B1); PG8_BAR; PG8_SCHED;
.LBB0_720:
	s_ashr_i32 s15, s14, 31
	s_lshl_b64 s[16:17], s[14:15], 19
	s_add_u32 s16, s86, s16
	s_addc_u32 s17, s87, s17
	s_and_b64 s[18:19], s[4:5], exec
	s_cselect_b32 s15, s17, s23
	s_cselect_b32 s56, s16, s22
	s_ashr_i32 s13, s12, 31
	s_lshl_b64 s[18:19], s[12:13], 19
	v_readlane_b32 s26, v254, 15
	v_readlane_b32 s27, v254, 16
	s_add_u32 s18, s26, s18
	s_addc_u32 s19, s27, s19
	s_and_b64 s[26:27], s[4:5], exec
	s_cselect_b32 s13, s19, s25
	s_cselect_b32 s57, s18, s24
	s_add_u32 s22, s22, 0x40080
	s_addc_u32 s23, s23, 0
	s_add_u32 s58, s24, 0x100
	s_addc_u32 s59, s25, 0
	s_mov_b32 s60, -2
	s_waitcnt vmcnt(0)
	v_lshl_add_u32 v130, s20, 8, v175
	v_ashrrev_i32_e32 v131, 31, v130
	v_lshlrev_b64 v[130:131], 6, v[130:131]
	v_lshl_add_u64 v[130:131], v[150:151], 0, v[130:131]
	global_load_dwordx4 v[238:241], v[130:131], off
	global_load_dwordx4 v[242:245], v[130:131], off offset:1024
	global_load_dwordx4 v[246:249], v[130:131], off offset:2048
	global_load_dwordx4 v[250:253], v[130:131], off offset:3072
	ds_read_b128 v[130:133], v187
	ds_read_b128 v[134:137], v187 offset:1024
	ds_read_b128 v[138:141], v187 offset:2048
	ds_read_b128 v[160:163], v187 offset:3072
	ds_read_b128 v[164:167], v188
	ds_read_b128 v[182:185], v188 offset:1024
	ds_read_b128 v[192:195], v188 offset:2048
	ds_read_b128 v[196:199], v188 offset:3072
	s_add_u32 s24, s22, 0xfffc0080
	s_addc_u32 s25, s23, -1
	s_cmp_eq_u32 s60, 12
	s_cselect_b32 s27, s15, s25
	s_cselect_b32 s26, s56, s24
	s_cselect_b32 s25, s13, s59
	s_cselect_b32 s24, s57, s58
	s_add_i32 m0, s29, 0xc000
	ds_read_b128 v[200:203], v189
	ds_read_b128 v[204:207], v189 offset:1024
	ds_read_b128 v[208:211], v189 offset:2048
	ds_read_b128 v[212:215], v189 offset:3072
	ds_read_b128 v[216:219], v189 offset:4096
	ds_read_b128 v[220:223], v189 offset:5120
	ds_read_b128 v[224:227], v189 offset:6144
	ds_read_b128 v[230:233], v189 offset:7168
	global_load_lds_dwordx4 v152, s[22:23]
	s_add_i32 m0, s29, 0xe000
	s_nop 0
	global_load_lds_dwordx4 v154, s[22:23]
	s_waitcnt vmcnt(8)
	s_waitcnt lgkmcnt(0)
	s_barrier
	s_setprio 3
	s_waitcnt lgkmcnt(0)
	v_mfma_f32_16x16x32_bf16 v[126:129], v[130:133], v[200:203], 0
	v_mfma_f32_16x16x32_bf16 v[122:125], v[138:141], v[200:203], 0
	v_mfma_f32_16x16x32_bf16 v[110:113], v[130:133], v[208:211], 0
	v_mfma_f32_16x16x32_bf16 v[106:109], v[138:141], v[208:211], 0
	v_mfma_f32_16x16x32_bf16 v[94:97], v[130:133], v[216:219], 0
	v_mfma_f32_16x16x32_bf16 v[90:93], v[138:141], v[216:219], 0
	v_mfma_f32_16x16x32_bf16 v[78:81], v[130:133], v[224:227], 0
	v_mfma_f32_16x16x32_bf16 v[74:77], v[138:141], v[224:227], 0
	v_mfma_f32_16x16x32_bf16 v[126:129], v[134:137], v[204:207], v[126:129]
	v_mfma_f32_16x16x32_bf16 v[122:125], v[160:163], v[204:207], v[122:125]
	v_mfma_f32_16x16x32_bf16 v[110:113], v[134:137], v[212:215], v[110:113]
	v_mfma_f32_16x16x32_bf16 v[106:109], v[160:163], v[212:215], v[106:109]
	v_mfma_f32_16x16x32_bf16 v[94:97], v[134:137], v[220:223], v[94:97]
	v_mfma_f32_16x16x32_bf16 v[90:93], v[160:163], v[220:223], v[90:93]
	v_mfma_f32_16x16x32_bf16 v[78:81], v[134:137], v[230:233], v[78:81]
	v_mfma_f32_16x16x32_bf16 v[74:77], v[160:163], v[230:233], v[74:77]
	s_setprio 0
	s_setprio 3
	v_mfma_f32_16x16x32_bf16 v[118:121], v[164:167], v[200:203], 0
	v_mfma_f32_16x16x32_bf16 v[114:117], v[192:195], v[200:203], 0
	v_mfma_f32_16x16x32_bf16 v[102:105], v[164:167], v[208:211], 0
	v_mfma_f32_16x16x32_bf16 v[98:101], v[192:195], v[208:211], 0
	v_mfma_f32_16x16x32_bf16 v[86:89], v[164:167], v[216:219], 0
	v_mfma_f32_16x16x32_bf16 v[82:85], v[192:195], v[216:219], 0
	v_mfma_f32_16x16x32_bf16 v[70:73], v[164:167], v[224:227], 0
	v_mfma_f32_16x16x32_bf16 v[66:69], v[192:195], v[224:227], 0
	v_mfma_f32_16x16x32_bf16 v[118:121], v[182:185], v[204:207], v[118:121]
	v_mfma_f32_16x16x32_bf16 v[114:117], v[196:199], v[204:207], v[114:117]
	v_mfma_f32_16x16x32_bf16 v[102:105], v[182:185], v[212:215], v[102:105]
	v_mfma_f32_16x16x32_bf16 v[98:101], v[196:199], v[212:215], v[98:101]
	v_mfma_f32_16x16x32_bf16 v[86:89], v[182:185], v[220:223], v[86:89]
	v_mfma_f32_16x16x32_bf16 v[82:85], v[196:199], v[220:223], v[82:85]
	v_mfma_f32_16x16x32_bf16 v[70:73], v[182:185], v[230:233], v[70:73]
	v_mfma_f32_16x16x32_bf16 v[66:69], v[196:199], v[230:233], v[66:69]
	s_setprio 0
	s_barrier
	s_add_i32 s61, s39, s2
	v_lshl_add_u64 v[168:169], s[24:25], 0, v[146:147]
	s_mov_b32 m0, s61
	ds_read_b128 v[200:203], v189 offset:16384
	ds_read_b128 v[204:207], v189 offset:17408
	ds_read_b128 v[208:211], v189 offset:18432
	ds_read_b128 v[212:215], v189 offset:19456
	ds_read_b128 v[216:219], v189 offset:20480
	ds_read_b128 v[220:223], v189 offset:21504
	ds_read_b128 v[224:227], v189 offset:22528
	ds_read_b128 v[230:233], v189 offset:23552
	global_load_lds_dwordx4 v[168:169], off
	s_add_i32 m0, s61, 0x2000
	s_add_u32 s62, s24, 0x40000
	v_lshl_add_u64 v[172:173], s[24:25], 0, v[142:143]
	s_addc_u32 s63, s25, 0
	s_add_i32 s61, s48, s2
	global_load_lds_dwordx4 v[172:173], off
	s_mov_b32 m0, s61
	v_lshl_add_u64 v[234:235], s[26:27], 0, v[144:145]
	global_load_lds_dwordx4 v146, s[62:63]
	s_add_i32 m0, s61, 0x2000
	s_nop 0
	global_load_lds_dwordx4 v142, s[62:63]
	v_lshl_add_u64 v[176:177], s[26:27], 0, v[148:149]
	s_mov_b32 m0, s29
	s_nop 0
	global_load_lds_dwordx4 v[176:177], off
	s_mov_b32 m0, s30
	s_nop 0
	global_load_lds_dwordx4 v[234:235], off
	s_waitcnt vmcnt(8)
	s_waitcnt lgkmcnt(0)
	s_barrier
; #define PG8_STAGE_A(b, h, ptr, NX) do { if constexpr (Sched::GATHER) { unsigned gs_[2]; gs_[0] = ((NX) && last_) ? gN[h][0] : gA[h][0]; gs_[1] = ((NX) && last_) ? gN[h][1] : gA[h][1]; PG8_STAGE(PG8_SA(b, h), ptr, gs_); } \
;         else PG8_STAGE(PG8_SA(b, h), (ptr) + ((h) ? hstep : (size_t)0), voffA); } while (0)
; #define PG8_LDA(dst, b, h) do { _Pragma("unroll") for (int m = 0; m < 4; ++m) _Pragma("unroll") for (int k = 0; k < 2; ++k) dst[m][k] = *(const PG8_LAS bf16x8*)(lds + PG8_SA(b, h) + aoff + m * 2048 + k * 1024); } while (0)
; #define PG8_LDB(dst, b, h) do { _Pragma("unroll") for (int n = 0; n < 2; ++n) _Pragma("unroll") for (int k = 0; k < 2; ++k) dst[n][k] = *(const PG8_LAS bf16x8*)(lds + PG8_SB(b, h) + boff + n * 2048 + k * 1024); } while (0)
; #define PG8_MMA(ai, bj, At, Bt) do { __builtin_amdgcn_s_setprio(1); _Pragma("unroll") for (int m = 0; m < 4; ++m) _Pragma("unroll") for (int n = 0; n < 2; ++n) _Pragma("unroll") for (int k = 0; k < 2; ++k) \
;         acc[ai][bj][m][n] = __builtin_amdgcn_mfma_f32_16x16x32_bf16(Bt[n][k], At[m][k], acc[ai][bj][m][n], 0, 0, 0); __builtin_amdgcn_s_setprio(0); } while (0)
; #define PG8_WAIT_V(n) asm volatile("s_waitcnt vmcnt(" #n ")" ::: "memory")
; #define PG8_WAIT_L(n) asm volatile("s_waitcnt lgkmcnt(" #n ")" ::: "memory")
; #define PG8_BAR __builtin_amdgcn_s_barrier()
; #define PG8_SCHED __builtin_amdgcn_sched_barrier(0)
; template <class Epi, class Sched, bool ALIGN_EPI = false, bool SP2 = false>
; __device__ __forceinline__ void gemm_phase(PG8_LAS unsigned char* lds, const Gemm g, const Sched& S, const Epi& E, const bool skip_epi = false) {
;     ...
;             PG8_WAIT_V(8); PG8_WAIT_L(0); PG8_BAR; PG8_MMA(1, 0, At, B0); PG8_MMA(1, 1, At, B1); PG8_BAR; PG8_SCHED;
;             PG8_LDB(B0, 1, 0); PG8_LDB(B1, 1, 1); PG8_SCHED; PG8_LDA(At, 1, 0); PG8_STAGE_A(0, 1, a2, true);
;             PG8_WAIT_V(8); PG8_WAIT_L(0); PG8_BAR; PG8_MMA(0, 0, At, B0); PG8_MMA(0, 1, At, B1); PG8_BAR; PG8_SCHED;
	s_setprio 3
	s_waitcnt lgkmcnt(0)
	v_mfma_f32_16x16x32_bf16 v[62:65], v[130:133], v[200:203], 0
	v_mfma_f32_16x16x32_bf16 v[58:61], v[138:141], v[200:203], 0
	v_mfma_f32_16x16x32_bf16 v[46:49], v[130:133], v[208:211], 0
	v_mfma_f32_16x16x32_bf16 v[42:45], v[138:141], v[208:211], 0
	v_mfma_f32_16x16x32_bf16 v[30:33], v[130:133], v[216:219], 0
	v_mfma_f32_16x16x32_bf16 v[26:29], v[138:141], v[216:219], 0
	v_mfma_f32_16x16x32_bf16 v[14:17], v[130:133], v[224:227], 0
	v_mfma_f32_16x16x32_bf16 v[10:13], v[138:141], v[224:227], 0
	v_mfma_f32_16x16x32_bf16 v[62:65], v[134:137], v[204:207], v[62:65]
	v_mfma_f32_16x16x32_bf16 v[58:61], v[160:163], v[204:207], v[58:61]
	v_mfma_f32_16x16x32_bf16 v[46:49], v[134:137], v[212:215], v[46:49]
	v_mfma_f32_16x16x32_bf16 v[42:45], v[160:163], v[212:215], v[42:45]
	v_mfma_f32_16x16x32_bf16 v[30:33], v[134:137], v[220:223], v[30:33]
	v_mfma_f32_16x16x32_bf16 v[26:29], v[160:163], v[220:223], v[26:29]
	v_mfma_f32_16x16x32_bf16 v[14:17], v[134:137], v[230:233], v[14:17]
	v_mfma_f32_16x16x32_bf16 v[10:13], v[160:163], v[230:233], v[10:13]
	s_setprio 0
	s_setprio 3
	v_mfma_f32_16x16x32_bf16 v[54:57], v[164:167], v[200:203], 0
	v_mfma_f32_16x16x32_bf16 v[50:53], v[192:195], v[200:203], 0
	v_mfma_f32_16x16x32_bf16 v[38:41], v[164:167], v[208:211], 0
	v_mfma_f32_16x16x32_bf16 v[34:37], v[192:195], v[208:211], 0
	v_mfma_f32_16x16x32_bf16 v[22:25], v[164:167], v[216:219], 0
	v_mfma_f32_16x16x32_bf16 v[18:21], v[192:195], v[216:219], 0
	v_mfma_f32_16x16x32_bf16 v[6:9], v[164:167], v[224:227], 0
	v_mfma_f32_16x16x32_bf16 v[2:5], v[192:195], v[224:227], 0
	v_mfma_f32_16x16x32_bf16 v[54:57], v[182:185], v[204:207], v[54:57]
	v_mfma_f32_16x16x32_bf16 v[50:53], v[196:199], v[204:207], v[50:53]
	v_mfma_f32_16x16x32_bf16 v[38:41], v[182:185], v[212:215], v[38:41]
	v_mfma_f32_16x16x32_bf16 v[34:37], v[196:199], v[212:215], v[34:37]
	v_mfma_f32_16x16x32_bf16 v[22:25], v[182:185], v[220:223], v[22:25]
	v_mfma_f32_16x16x32_bf16 v[18:21], v[196:199], v[220:223], v[18:21]
	v_mfma_f32_16x16x32_bf16 v[6:9], v[182:185], v[230:233], v[6:9]
	v_mfma_f32_16x16x32_bf16 v[2:5], v[196:199], v[230:233], v[2:5]
	s_setprio 0
	s_barrier
	s_add_i32 s61, 0, 0x18000
	s_add_i32 s62, 0, 0x1c000
	v_add_u32_e32 v160, s61, v1
	v_add_u32_e32 v170, s62, v1
	ds_read_b128 v[130:133], v160
	ds_read_b128 v[134:137], v160 offset:1024
	ds_read_b128 v[138:141], v160 offset:2048
	ds_read_b128 v[160:163], v160 offset:3072
	ds_read_b128 v[164:167], v170
	ds_read_b128 v[182:185], v170 offset:1024
	ds_read_b128 v[192:195], v170 offset:2048
	ds_read_b128 v[196:199], v170 offset:3072
	s_add_u32 s26, s26, 0x40000
	s_addc_u32 s27, s27, 0
	s_mov_b32 m0, s31
	ds_read_b128 v[200:203], v189 offset:32768
	ds_read_b128 v[204:207], v189 offset:33792
	ds_read_b128 v[208:211], v189 offset:34816
	ds_read_b128 v[212:215], v189 offset:35840
	ds_read_b128 v[216:219], v189 offset:36864
	ds_read_b128 v[220:223], v189 offset:37888
	ds_read_b128 v[224:227], v189 offset:38912
	ds_read_b128 v[230:233], v189 offset:39936
	global_load_lds_dwordx4 v148, s[26:27]
	s_mov_b32 m0, s34
	s_nop 0
	global_load_lds_dwordx4 v144, s[26:27]
	s_waitcnt vmcnt(8)
	s_waitcnt lgkmcnt(0)
	s_barrier
	s_setprio 3
	s_waitcnt lgkmcnt(0)
	v_mfma_f32_16x16x32_bf16 v[126:129], v[130:133], v[200:203], v[126:129]
	v_mfma_f32_16x16x32_bf16 v[122:125], v[138:141], v[200:203], v[122:125]
	v_mfma_f32_16x16x32_bf16 v[110:113], v[130:133], v[208:211], v[110:113]
	v_mfma_f32_16x16x32_bf16 v[106:109], v[138:141], v[208:211], v[106:109]
	v_mfma_f32_16x16x32_bf16 v[94:97], v[130:133], v[216:219], v[94:97]
	v_mfma_f32_16x16x32_bf16 v[90:93], v[138:141], v[216:219], v[90:93]
	v_mfma_f32_16x16x32_bf16 v[78:81], v[130:133], v[224:227], v[78:81]
	v_mfma_f32_16x16x32_bf16 v[74:77], v[138:141], v[224:227], v[74:77]
	v_mfma_f32_16x16x32_bf16 v[126:129], v[134:137], v[204:207], v[126:129]
	v_mfma_f32_16x16x32_bf16 v[122:125], v[160:163], v[204:207], v[122:125]
	v_mfma_f32_16x16x32_bf16 v[110:113], v[134:137], v[212:215], v[110:113]
	v_mfma_f32_16x16x32_bf16 v[106:109], v[160:163], v[212:215], v[106:109]
	v_mfma_f32_16x16x32_bf16 v[94:97], v[134:137], v[220:223], v[94:97]
	v_mfma_f32_16x16x32_bf16 v[90:93], v[160:163], v[220:223], v[90:93]
	v_mfma_f32_16x16x32_bf16 v[78:81], v[134:137], v[230:233], v[78:81]
	v_mfma_f32_16x16x32_bf16 v[74:77], v[160:163], v[230:233], v[74:77]
	s_setprio 0
	s_setprio 3
	v_mfma_f32_16x16x32_bf16 v[118:121], v[164:167], v[200:203], v[118:121]
	v_mfma_f32_16x16x32_bf16 v[114:117], v[192:195], v[200:203], v[114:117]
	v_mfma_f32_16x16x32_bf16 v[102:105], v[164:167], v[208:211], v[102:105]
	v_mfma_f32_16x16x32_bf16 v[98:101], v[192:195], v[208:211], v[98:101]
	v_mfma_f32_16x16x32_bf16 v[86:89], v[164:167], v[216:219], v[86:89]
	v_mfma_f32_16x16x32_bf16 v[82:85], v[192:195], v[216:219], v[82:85]
	v_mfma_f32_16x16x32_bf16 v[70:73], v[164:167], v[224:227], v[70:73]
	v_mfma_f32_16x16x32_bf16 v[66:69], v[192:195], v[224:227], v[66:69]
	v_mfma_f32_16x16x32_bf16 v[118:121], v[182:185], v[204:207], v[118:121]
	v_mfma_f32_16x16x32_bf16 v[114:117], v[196:199], v[204:207], v[114:117]
	v_mfma_f32_16x16x32_bf16 v[102:105], v[182:185], v[212:215], v[102:105]
	v_mfma_f32_16x16x32_bf16 v[98:101], v[196:199], v[212:215], v[98:101]
	v_mfma_f32_16x16x32_bf16 v[86:89], v[182:185], v[220:223], v[86:89]
	v_mfma_f32_16x16x32_bf16 v[82:85], v[196:199], v[220:223], v[82:85]
	v_mfma_f32_16x16x32_bf16 v[70:73], v[182:185], v[230:233], v[70:73]
	v_mfma_f32_16x16x32_bf16 v[66:69], v[196:199], v[230:233], v[66:69]
	s_setprio 0
	s_barrier
; #define PG8_STAGE_A(b, h, ptr, NX) do { if constexpr (Sched::GATHER) { unsigned gs_[2]; gs_[0] = ((NX) && last_) ? gN[h][0] : gA[h][0]; gs_[1] = ((NX) && last_) ? gN[h][1] : gA[h][1]; PG8_STAGE(PG8_SA(b, h), ptr, gs_); } \
;         else PG8_STAGE(PG8_SA(b, h), (ptr) + ((h) ? hstep : (size_t)0), voffA); } while (0)
; #define PG8_STAGE(bufoff, gbase, voff) do { _Pragma("unroll") for (int _i = 0; _i < 2; ++_i) \
;         __builtin_amdgcn_global_load_lds((const unsigned*)((const char*)(gbase) + (voff)[_i]), (PG8_LAS unsigned*)(lds + (bufoff) + ldsw + _i * 8192), 16, 0, 0); } while (0)
; template <class Epi, class Sched, bool ALIGN_EPI = false, bool SP2 = false>
; __device__ __forceinline__ void gemm_phase(PG8_LAS unsigned char* lds, const Gemm g, const Sched& S, const Epi& E, const bool skip_epi = false) {
;     ...
;         for (int t = 0; t < nt; t += 2) {
;             const bool last = (t == nt - 2); last_ = last && has_next;
;             const char* a1 = cA + (size_t)(t + 1) * kstep;
;             const char* a2 = last ? nA : cA + (size_t)(t + 2) * kstep; const char* b2 = last ? nB : cB + (size_t)(t + 2) * kstep;
;             const char* a3 = a2 + kstep; const char* b3 = b2 + kstep;
;             if (last && has_next) S.a_ready(nxt);
;             if constexpr (SP2) {
;             PG8_LDB(B0, 0, 0); PG8_LDB(B1, 0, 1); PG8_SCHED; PG8_LDA(At, 0, 0); PG8_STAGE_A(1, 1, a1, false);
;             PG8_WAIT_V(8); PG8_WAIT_L(0); PG8_BAR; PG8_MMA(0, 0, At, B0); PG8_MMA(0, 1, At, B1); PG8_BAR; PG8_SCHED;
;             PG8_LDA(At, 0, 1); PG8_STAGE(PG8_SB(0, 0), b2, voffB); PG8_STAGE(PG8_SB(0, 1), b2 + hstep, voffB); PG8_STAGE_A(0, 0, a2, true);
;             PG8_WAIT_V(8); PG8_WAIT_L(0); PG8_BAR; PG8_MMA(1, 0, At, B0); PG8_MMA(1, 1, At, B1); PG8_BAR; PG8_SCHED;
;             PG8_LDB(B0, 1, 0); PG8_LDB(B1, 1, 1); PG8_SCHED; PG8_LDA(At, 1, 0); PG8_STAGE_A(0, 1, a2, true);
;             PG8_WAIT_V(8); PG8_WAIT_L(0); PG8_BAR; PG8_MMA(0, 0, At, B0); PG8_MMA(0, 1, At, B1); PG8_BAR; PG8_SCHED;
;             PG8_LDA(At, 1, 1); PG8_STAGE(PG8_SB(1, 0), b3, voffB); PG8_STAGE(PG8_SB(1, 1), b3 + hstep, voffB); PG8_STAGE_A(1, 0, a3, true);
;             PG8_WAIT_V(8); PG8_WAIT_L(0); PG8_BAR; PG8_MMA(1, 0, At, B0); PG8_MMA(1, 1, At, B1); PG8_BAR; PG8_SCHED;
;             } else {
;             PG8_LDB(B0, 0, 0); PG8_SCHED; PG8_LDA(At, 0, 0); PG8_STAGE_A(1, 1, a1, false);
	s_add_i32 s26, s61, s2
	s_add_i32 m0, s26, 0xffffff80
	ds_read_b128 v[200:203], v189 offset:49152
	ds_read_b128 v[204:207], v189 offset:50176
	ds_read_b128 v[208:211], v189 offset:51200
	ds_read_b128 v[212:215], v189 offset:52224
	ds_read_b128 v[216:219], v189 offset:53248
	ds_read_b128 v[220:223], v189 offset:54272
	ds_read_b128 v[224:227], v189 offset:55296
	ds_read_b128 v[230:233], v189 offset:56320
	global_load_lds_dwordx4 v[168:169], off offset:128
	s_add_i32 m0, s26, 0x1f80
	s_add_u32 s24, s24, 0x40080
	s_addc_u32 s25, s25, 0
	s_add_i32 s26, s62, s2
	global_load_lds_dwordx4 v[172:173], off offset:128
	s_mov_b32 m0, s26
	s_nop 0
	global_load_lds_dwordx4 v146, s[24:25]
	s_add_i32 m0, s26, 0x2000
	s_nop 0
	global_load_lds_dwordx4 v142, s[24:25]
	s_add_i32 m0, s36, 0xffffff80
	s_nop 0
	global_load_lds_dwordx4 v[176:177], off offset:128
	s_add_i32 m0, s37, 0xffffff80
	s_nop 0
	global_load_lds_dwordx4 v[234:235], off offset:128
	s_waitcnt vmcnt(8)
	s_waitcnt lgkmcnt(0)
	s_barrier
	s_setprio 3
	s_waitcnt lgkmcnt(0)
	v_mfma_f32_16x16x32_bf16 v[62:65], v[130:133], v[200:203], v[62:65]
	v_mfma_f32_16x16x32_bf16 v[58:61], v[138:141], v[200:203], v[58:61]
	v_mfma_f32_16x16x32_bf16 v[46:49], v[130:133], v[208:211], v[46:49]
	v_mfma_f32_16x16x32_bf16 v[42:45], v[138:141], v[208:211], v[42:45]
	v_mfma_f32_16x16x32_bf16 v[30:33], v[130:133], v[216:219], v[30:33]
	v_mfma_f32_16x16x32_bf16 v[26:29], v[138:141], v[216:219], v[26:29]
	v_mfma_f32_16x16x32_bf16 v[14:17], v[130:133], v[224:227], v[14:17]
	v_mfma_f32_16x16x32_bf16 v[10:13], v[138:141], v[224:227], v[10:13]
	v_mfma_f32_16x16x32_bf16 v[62:65], v[134:137], v[204:207], v[62:65]
	v_mfma_f32_16x16x32_bf16 v[58:61], v[160:163], v[204:207], v[58:61]
	v_mfma_f32_16x16x32_bf16 v[46:49], v[134:137], v[212:215], v[46:49]
	v_mfma_f32_16x16x32_bf16 v[42:45], v[160:163], v[212:215], v[42:45]
	v_mfma_f32_16x16x32_bf16 v[30:33], v[134:137], v[220:223], v[30:33]
	v_mfma_f32_16x16x32_bf16 v[26:29], v[160:163], v[220:223], v[26:29]
	v_mfma_f32_16x16x32_bf16 v[14:17], v[134:137], v[230:233], v[14:17]
	v_mfma_f32_16x16x32_bf16 v[10:13], v[160:163], v[230:233], v[10:13]
	s_setprio 0
	s_setprio 3
	v_mfma_f32_16x16x32_bf16 v[54:57], v[164:167], v[200:203], v[54:57]
	v_mfma_f32_16x16x32_bf16 v[50:53], v[192:195], v[200:203], v[50:53]
	v_mfma_f32_16x16x32_bf16 v[38:41], v[164:167], v[208:211], v[38:41]
	v_mfma_f32_16x16x32_bf16 v[34:37], v[192:195], v[208:211], v[34:37]
	v_mfma_f32_16x16x32_bf16 v[22:25], v[164:167], v[216:219], v[22:25]
	v_mfma_f32_16x16x32_bf16 v[18:21], v[192:195], v[216:219], v[18:21]
	v_mfma_f32_16x16x32_bf16 v[6:9], v[164:167], v[224:227], v[6:9]
	v_mfma_f32_16x16x32_bf16 v[2:5], v[192:195], v[224:227], v[2:5]
	v_mfma_f32_16x16x32_bf16 v[54:57], v[182:185], v[204:207], v[54:57]
	v_mfma_f32_16x16x32_bf16 v[50:53], v[196:199], v[204:207], v[50:53]
	v_mfma_f32_16x16x32_bf16 v[38:41], v[182:185], v[212:215], v[38:41]
	v_mfma_f32_16x16x32_bf16 v[34:37], v[196:199], v[212:215], v[34:37]
	v_mfma_f32_16x16x32_bf16 v[22:25], v[182:185], v[220:223], v[22:25]
	v_mfma_f32_16x16x32_bf16 v[18:21], v[196:199], v[220:223], v[18:21]
	v_mfma_f32_16x16x32_bf16 v[6:9], v[182:185], v[230:233], v[6:9]
	v_mfma_f32_16x16x32_bf16 v[2:5], v[196:199], v[230:233], v[2:5]
	s_setprio 0
	s_barrier
	s_add_i32 s60, s60, 2
	s_add_u32 s22, s22, 0x100
	s_addc_u32 s23, s23, 0
	s_add_u32 s58, s58, 0x100
	s_addc_u32 s59, s59, 0
	s_cmp_gt_u32 s60, 13
.LBB0_721:
	ds_read_b128 v[130:133], v187
	ds_read_b128 v[134:137], v187 offset:1024
	ds_read_b128 v[138:141], v187 offset:2048
	ds_read_b128 v[160:163], v187 offset:3072
	ds_read_b128 v[164:167], v188
	ds_read_b128 v[182:185], v188 offset:1024
	ds_read_b128 v[192:195], v188 offset:2048
	ds_read_b128 v[196:199], v188 offset:3072
	s_add_u32 s24, s22, 0xfffc0080
	s_addc_u32 s25, s23, -1
	s_cmp_eq_u32 s60, 12
	s_cselect_b32 s27, s15, s25
	s_cselect_b32 s26, s56, s24
	s_cselect_b32 s25, s13, s59
	s_cselect_b32 s24, s57, s58
	s_add_i32 m0, s29, 0xc000
	ds_read_b128 v[200:203], v189
	ds_read_b128 v[204:207], v189 offset:1024
	ds_read_b128 v[208:211], v189 offset:2048
	ds_read_b128 v[212:215], v189 offset:3072
	ds_read_b128 v[216:219], v189 offset:4096
	ds_read_b128 v[220:223], v189 offset:5120
	ds_read_b128 v[224:227], v189 offset:6144
	ds_read_b128 v[230:233], v189 offset:7168
	global_load_lds_dwordx4 v152, s[22:23]
	s_add_i32 m0, s29, 0xe000
	s_nop 0
	global_load_lds_dwordx4 v154, s[22:23]
	s_waitcnt vmcnt(8)
	s_waitcnt lgkmcnt(0)
	s_barrier
; #define PG8_STAGE_A(b, h, ptr, NX) do { if constexpr (Sched::GATHER) { unsigned gs_[2]; gs_[0] = ((NX) && last_) ? gN[h][0] : gA[h][0]; gs_[1] = ((NX) && last_) ? gN[h][1] : gA[h][1]; PG8_STAGE(PG8_SA(b, h), ptr, gs_); } \
;         else PG8_STAGE(PG8_SA(b, h), (ptr) + ((h) ? hstep : (size_t)0), voffA); } while (0)
; #define PG8_STAGE(bufoff, gbase, voff) do { _Pragma("unroll") for (int _i = 0; _i < 2; ++_i) \
;         __builtin_amdgcn_global_load_lds((const unsigned*)((const char*)(gbase) + (voff)[_i]), (PG8_LAS unsigned*)(lds + (bufoff) + ldsw + _i * 8192), 16, 0, 0); } while (0)
; #define PG8_LDA(dst, b, h) do { _Pragma("unroll") for (int m = 0; m < 4; ++m) _Pragma("unroll") for (int k = 0; k < 2; ++k) dst[m][k] = *(const PG8_LAS bf16x8*)(lds + PG8_SA(b, h) + aoff + m * 2048 + k * 1024); } while (0)
; #define PG8_MMA(ai, bj, At, Bt) do { __builtin_amdgcn_s_setprio(1); _Pragma("unroll") for (int m = 0; m < 4; ++m) _Pragma("unroll") for (int n = 0; n < 2; ++n) _Pragma("unroll") for (int k = 0; k < 2; ++k) \
;         acc[ai][bj][m][n] = __builtin_amdgcn_mfma_f32_16x16x32_bf16(Bt[n][k], At[m][k], acc[ai][bj][m][n], 0, 0, 0); __builtin_amdgcn_s_setprio(0); } while (0)
; #define PG8_WAIT_V(n) asm volatile("s_waitcnt vmcnt(" #n ")" ::: "memory")
; #define PG8_WAIT_L(n) asm volatile("s_waitcnt lgkmcnt(" #n ")" ::: "memory")
; #define PG8_BAR __builtin_amdgcn_s_barrier()
; #define PG8_SCHED __builtin_amdgcn_sched_barrier(0)
; template <class Epi, class Sched, bool ALIGN_EPI = false, bool SP2 = false>
; __device__ __forceinline__ void gemm_phase(PG8_LAS unsigned char* lds, const Gemm g, const Sched& S, const Epi& E, const bool skip_epi = false) {
;     ...
;             PG8_WAIT_V(8); PG8_WAIT_L(0); PG8_BAR; PG8_MMA(0, 0, At, B0); PG8_MMA(0, 1, At, B1); PG8_BAR; PG8_SCHED;
;             PG8_LDA(At, 0, 1); PG8_STAGE(PG8_SB(0, 0), b2, voffB); PG8_STAGE(PG8_SB(0, 1), b2 + hstep, voffB); PG8_STAGE_A(0, 0, a2, true);
;             PG8_WAIT_V(8); PG8_WAIT_L(0); PG8_BAR; PG8_MMA(1, 0, At, B0); PG8_MMA(1, 1, At, B1); PG8_BAR; PG8_SCHED;
	s_setprio 3
	s_waitcnt lgkmcnt(0)
	v_mfma_f32_16x16x32_bf16 v[126:129], v[130:133], v[200:203], v[126:129]
	v_mfma_f32_16x16x32_bf16 v[122:125], v[138:141], v[200:203], v[122:125]
	v_mfma_f32_16x16x32_bf16 v[110:113], v[130:133], v[208:211], v[110:113]
	v_mfma_f32_16x16x32_bf16 v[106:109], v[138:141], v[208:211], v[106:109]
	v_mfma_f32_16x16x32_bf16 v[94:97], v[130:133], v[216:219], v[94:97]
	v_mfma_f32_16x16x32_bf16 v[90:93], v[138:141], v[216:219], v[90:93]
	v_mfma_f32_16x16x32_bf16 v[78:81], v[130:133], v[224:227], v[78:81]
	v_mfma_f32_16x16x32_bf16 v[74:77], v[138:141], v[224:227], v[74:77]
	v_mfma_f32_16x16x32_bf16 v[126:129], v[134:137], v[204:207], v[126:129]
	v_mfma_f32_16x16x32_bf16 v[122:125], v[160:163], v[204:207], v[122:125]
	v_mfma_f32_16x16x32_bf16 v[110:113], v[134:137], v[212:215], v[110:113]
	v_mfma_f32_16x16x32_bf16 v[106:109], v[160:163], v[212:215], v[106:109]
	v_mfma_f32_16x16x32_bf16 v[94:97], v[134:137], v[220:223], v[94:97]
	v_mfma_f32_16x16x32_bf16 v[90:93], v[160:163], v[220:223], v[90:93]
	v_mfma_f32_16x16x32_bf16 v[78:81], v[134:137], v[230:233], v[78:81]
	v_mfma_f32_16x16x32_bf16 v[74:77], v[160:163], v[230:233], v[74:77]
	s_setprio 0
	s_setprio 3
	v_mfma_f32_16x16x32_bf16 v[118:121], v[164:167], v[200:203], v[118:121]
	v_mfma_f32_16x16x32_bf16 v[114:117], v[192:195], v[200:203], v[114:117]
	v_mfma_f32_16x16x32_bf16 v[102:105], v[164:167], v[208:211], v[102:105]
	v_mfma_f32_16x16x32_bf16 v[98:101], v[192:195], v[208:211], v[98:101]
	v_mfma_f32_16x16x32_bf16 v[86:89], v[164:167], v[216:219], v[86:89]
	v_mfma_f32_16x16x32_bf16 v[82:85], v[192:195], v[216:219], v[82:85]
	v_mfma_f32_16x16x32_bf16 v[70:73], v[164:167], v[224:227], v[70:73]
	v_mfma_f32_16x16x32_bf16 v[66:69], v[192:195], v[224:227], v[66:69]
	v_mfma_f32_16x16x32_bf16 v[118:121], v[182:185], v[204:207], v[118:121]
	v_mfma_f32_16x16x32_bf16 v[114:117], v[196:199], v[204:207], v[114:117]
	v_mfma_f32_16x16x32_bf16 v[102:105], v[182:185], v[212:215], v[102:105]
	v_mfma_f32_16x16x32_bf16 v[98:101], v[196:199], v[212:215], v[98:101]
	v_mfma_f32_16x16x32_bf16 v[86:89], v[182:185], v[220:223], v[86:89]
	v_mfma_f32_16x16x32_bf16 v[82:85], v[196:199], v[220:223], v[82:85]
	v_mfma_f32_16x16x32_bf16 v[70:73], v[182:185], v[230:233], v[70:73]
	v_mfma_f32_16x16x32_bf16 v[66:69], v[196:199], v[230:233], v[66:69]
	s_setprio 0
	s_barrier
	s_add_i32 s61, s39, s2
	v_lshl_add_u64 v[168:169], s[24:25], 0, v[146:147]
	s_mov_b32 m0, s61
	ds_read_b128 v[200:203], v189 offset:16384
	ds_read_b128 v[204:207], v189 offset:17408
	ds_read_b128 v[208:211], v189 offset:18432
	ds_read_b128 v[212:215], v189 offset:19456
	ds_read_b128 v[216:219], v189 offset:20480
	ds_read_b128 v[220:223], v189 offset:21504
	ds_read_b128 v[224:227], v189 offset:22528
	ds_read_b128 v[230:233], v189 offset:23552
	global_load_lds_dwordx4 v[168:169], off
	s_add_i32 m0, s61, 0x2000
	s_add_u32 s62, s24, 0x40000
	v_lshl_add_u64 v[172:173], s[24:25], 0, v[142:143]
	s_addc_u32 s63, s25, 0
	s_add_i32 s61, s48, s2
	global_load_lds_dwordx4 v[172:173], off
	s_mov_b32 m0, s61
	v_lshl_add_u64 v[234:235], s[26:27], 0, v[144:145]
	global_load_lds_dwordx4 v146, s[62:63]
	s_add_i32 m0, s61, 0x2000
	s_nop 0
	global_load_lds_dwordx4 v142, s[62:63]
	v_lshl_add_u64 v[176:177], s[26:27], 0, v[148:149]
	s_mov_b32 m0, s29
	s_nop 0
	global_load_lds_dwordx4 v[176:177], off
	s_mov_b32 m0, s30
	s_nop 0
	global_load_lds_dwordx4 v[234:235], off
	s_waitcnt vmcnt(8)
	s_waitcnt lgkmcnt(0)
	s_barrier
	s_setprio 3
	s_waitcnt lgkmcnt(0)
	v_mfma_f32_16x16x32_bf16 v[62:65], v[130:133], v[200:203], v[62:65]
	v_mfma_f32_16x16x32_bf16 v[58:61], v[138:141], v[200:203], v[58:61]
	v_mfma_f32_16x16x32_bf16 v[46:49], v[130:133], v[208:211], v[46:49]
	v_mfma_f32_16x16x32_bf16 v[42:45], v[138:141], v[208:211], v[42:45]
	v_mfma_f32_16x16x32_bf16 v[30:33], v[130:133], v[216:219], v[30:33]
	v_mfma_f32_16x16x32_bf16 v[26:29], v[138:141], v[216:219], v[26:29]
	v_mfma_f32_16x16x32_bf16 v[14:17], v[130:133], v[224:227], v[14:17]
	v_mfma_f32_16x16x32_bf16 v[10:13], v[138:141], v[224:227], v[10:13]
	v_mfma_f32_16x16x32_bf16 v[62:65], v[134:137], v[204:207], v[62:65]
	v_mfma_f32_16x16x32_bf16 v[58:61], v[160:163], v[204:207], v[58:61]
	v_mfma_f32_16x16x32_bf16 v[46:49], v[134:137], v[212:215], v[46:49]
	v_mfma_f32_16x16x32_bf16 v[42:45], v[160:163], v[212:215], v[42:45]
	v_mfma_f32_16x16x32_bf16 v[30:33], v[134:137], v[220:223], v[30:33]
	v_mfma_f32_16x16x32_bf16 v[26:29], v[160:163], v[220:223], v[26:29]
	v_mfma_f32_16x16x32_bf16 v[14:17], v[134:137], v[230:233], v[14:17]
	v_mfma_f32_16x16x32_bf16 v[10:13], v[160:163], v[230:233], v[10:13]
	s_setprio 0
	s_setprio 3
	v_mfma_f32_16x16x32_bf16 v[54:57], v[164:167], v[200:203], v[54:57]
	v_mfma_f32_16x16x32_bf16 v[50:53], v[192:195], v[200:203], v[50:53]
	v_mfma_f32_16x16x32_bf16 v[38:41], v[164:167], v[208:211], v[38:41]
	v_mfma_f32_16x16x32_bf16 v[34:37], v[192:195], v[208:211], v[34:37]
	v_mfma_f32_16x16x32_bf16 v[22:25], v[164:167], v[216:219], v[22:25]
	v_mfma_f32_16x16x32_bf16 v[18:21], v[192:195], v[216:219], v[18:21]
	v_mfma_f32_16x16x32_bf16 v[6:9], v[164:167], v[224:227], v[6:9]
	v_mfma_f32_16x16x32_bf16 v[2:5], v[192:195], v[224:227], v[2:5]
	v_mfma_f32_16x16x32_bf16 v[54:57], v[182:185], v[204:207], v[54:57]
	v_mfma_f32_16x16x32_bf16 v[50:53], v[196:199], v[204:207], v[50:53]
	v_mfma_f32_16x16x32_bf16 v[38:41], v[182:185], v[212:215], v[38:41]
	v_mfma_f32_16x16x32_bf16 v[34:37], v[196:199], v[212:215], v[34:37]
	v_mfma_f32_16x16x32_bf16 v[22:25], v[182:185], v[220:223], v[22:25]
	v_mfma_f32_16x16x32_bf16 v[18:21], v[196:199], v[220:223], v[18:21]
	v_mfma_f32_16x16x32_bf16 v[6:9], v[182:185], v[230:233], v[6:9]
	v_mfma_f32_16x16x32_bf16 v[2:5], v[196:199], v[230:233], v[2:5]
	s_setprio 0
	s_barrier
; #define PG8_STAGE_A(b, h, ptr, NX) do { if constexpr (Sched::GATHER) { unsigned gs_[2]; gs_[0] = ((NX) && last_) ? gN[h][0] : gA[h][0]; gs_[1] = ((NX) && last_) ? gN[h][1] : gA[h][1]; PG8_STAGE(PG8_SA(b, h), ptr, gs_); } \
;         else PG8_STAGE(PG8_SA(b, h), (ptr) + ((h) ? hstep : (size_t)0), voffA); } while (0)
; #define PG8_STAGE(bufoff, gbase, voff) do { _Pragma("unroll") for (int _i = 0; _i < 2; ++_i) \
;         __builtin_amdgcn_global_load_lds((const unsigned*)((const char*)(gbase) + (voff)[_i]), (PG8_LAS unsigned*)(lds + (bufoff) + ldsw + _i * 8192), 16, 0, 0); } while (0)
; #define PG8_LDA(dst, b, h) do { _Pragma("unroll") for (int m = 0; m < 4; ++m) _Pragma("unroll") for (int k = 0; k < 2; ++k) dst[m][k] = *(const PG8_LAS bf16x8*)(lds + PG8_SA(b, h) + aoff + m * 2048 + k * 1024); } while (0)
; #define PG8_LDB(dst, b, h) do { _Pragma("unroll") for (int n = 0; n < 2; ++n) _Pragma("unroll") for (int k = 0; k < 2; ++k) dst[n][k] = *(const PG8_LAS bf16x8*)(lds + PG8_SB(b, h) + boff + n * 2048 + k * 1024); } while (0)
; #define PG8_MMA(ai, bj, At, Bt) do { __builtin_amdgcn_s_setprio(1); _Pragma("unroll") for (int m = 0; m < 4; ++m) _Pragma("unroll") for (int n = 0; n < 2; ++n) _Pragma("unroll") for (int k = 0; k < 2; ++k) \
;         acc[ai][bj][m][n] = __builtin_amdgcn_mfma_f32_16x16x32_bf16(Bt[n][k], At[m][k], acc[ai][bj][m][n], 0, 0, 0); __builtin_amdgcn_s_setprio(0); } while (0)
; #define PG8_WAIT_V(n) asm volatile("s_waitcnt vmcnt(" #n ")" ::: "memory")
; #define PG8_WAIT_L(n) asm volatile("s_waitcnt lgkmcnt(" #n ")" ::: "memory")
; #define PG8_BAR __builtin_amdgcn_s_barrier()
; template <class Epi, class Sched, bool ALIGN_EPI = false, bool SP2 = false>
; __device__ __forceinline__ void gemm_phase(PG8_LAS unsigned char* lds, const Gemm g, const Sched& S, const Epi& E, const bool skip_epi = false) {
;     ...
;             PG8_LDB(B0, 1, 0); PG8_LDB(B1, 1, 1); PG8_SCHED; PG8_LDA(At, 1, 0); PG8_STAGE_A(0, 1, a2, true);
;             PG8_WAIT_V(8); PG8_WAIT_L(0); PG8_BAR; PG8_MMA(0, 0, At, B0); PG8_MMA(0, 1, At, B1); PG8_BAR; PG8_SCHED;
;             PG8_LDA(At, 1, 1); PG8_STAGE(PG8_SB(1, 0), b3, voffB); PG8_STAGE(PG8_SB(1, 1), b3 + hstep, voffB); PG8_STAGE_A(1, 0, a3, true);
;             PG8_WAIT_V(8); PG8_WAIT_L(0); PG8_BAR; PG8_MMA(1, 0, At, B0); PG8_MMA(1, 1, At, B1); PG8_BAR; PG8_SCHED;
;     ...
;         if constexpr (ALIGN_EPI) { if (wr == 0) PG8_BAR; }
	s_add_i32 s61, 0, 0x18000
	s_add_i32 s62, 0, 0x1c000
	v_add_u32_e32 v160, s61, v1
	v_add_u32_e32 v170, s62, v1
	ds_read_b128 v[130:133], v160
	ds_read_b128 v[134:137], v160 offset:1024
	ds_read_b128 v[138:141], v160 offset:2048
	ds_read_b128 v[160:163], v160 offset:3072
	ds_read_b128 v[164:167], v170
	ds_read_b128 v[182:185], v170 offset:1024
	ds_read_b128 v[192:195], v170 offset:2048
	ds_read_b128 v[196:199], v170 offset:3072
	s_add_u32 s26, s26, 0x40000
	s_addc_u32 s27, s27, 0
	s_mov_b32 m0, s31
	ds_read_b128 v[200:203], v189 offset:32768
	ds_read_b128 v[204:207], v189 offset:33792
	ds_read_b128 v[208:211], v189 offset:34816
	ds_read_b128 v[212:215], v189 offset:35840
	ds_read_b128 v[216:219], v189 offset:36864
	ds_read_b128 v[220:223], v189 offset:37888
	ds_read_b128 v[224:227], v189 offset:38912
	ds_read_b128 v[230:233], v189 offset:39936
	global_load_lds_dwordx4 v148, s[26:27]
	s_mov_b32 m0, s34
	s_nop 0
	global_load_lds_dwordx4 v144, s[26:27]
	s_waitcnt vmcnt(8)
	s_waitcnt lgkmcnt(0)
	s_barrier
	s_setprio 3
	s_waitcnt lgkmcnt(0)
	v_mfma_f32_16x16x32_bf16 v[126:129], v[130:133], v[200:203], v[126:129]
	v_mfma_f32_16x16x32_bf16 v[122:125], v[138:141], v[200:203], v[122:125]
	v_mfma_f32_16x16x32_bf16 v[110:113], v[130:133], v[208:211], v[110:113]
	v_mfma_f32_16x16x32_bf16 v[106:109], v[138:141], v[208:211], v[106:109]
	v_mfma_f32_16x16x32_bf16 v[94:97], v[130:133], v[216:219], v[94:97]
	v_mfma_f32_16x16x32_bf16 v[90:93], v[138:141], v[216:219], v[90:93]
	v_mfma_f32_16x16x32_bf16 v[78:81], v[130:133], v[224:227], v[78:81]
	v_mfma_f32_16x16x32_bf16 v[74:77], v[138:141], v[224:227], v[74:77]
	v_mfma_f32_16x16x32_bf16 v[126:129], v[134:137], v[204:207], v[126:129]
	v_mfma_f32_16x16x32_bf16 v[122:125], v[160:163], v[204:207], v[122:125]
	v_mfma_f32_16x16x32_bf16 v[110:113], v[134:137], v[212:215], v[110:113]
	v_mfma_f32_16x16x32_bf16 v[106:109], v[160:163], v[212:215], v[106:109]
	v_mfma_f32_16x16x32_bf16 v[94:97], v[134:137], v[220:223], v[94:97]
	v_mfma_f32_16x16x32_bf16 v[90:93], v[160:163], v[220:223], v[90:93]
	v_mfma_f32_16x16x32_bf16 v[78:81], v[134:137], v[230:233], v[78:81]
	v_mfma_f32_16x16x32_bf16 v[74:77], v[160:163], v[230:233], v[74:77]
	s_setprio 0
	s_setprio 3
	v_mfma_f32_16x16x32_bf16 v[118:121], v[164:167], v[200:203], v[118:121]
	v_mfma_f32_16x16x32_bf16 v[114:117], v[192:195], v[200:203], v[114:117]
	v_mfma_f32_16x16x32_bf16 v[102:105], v[164:167], v[208:211], v[102:105]
	v_mfma_f32_16x16x32_bf16 v[98:101], v[192:195], v[208:211], v[98:101]
	v_mfma_f32_16x16x32_bf16 v[86:89], v[164:167], v[216:219], v[86:89]
	v_mfma_f32_16x16x32_bf16 v[82:85], v[192:195], v[216:219], v[82:85]
	v_mfma_f32_16x16x32_bf16 v[70:73], v[164:167], v[224:227], v[70:73]
	v_mfma_f32_16x16x32_bf16 v[66:69], v[192:195], v[224:227], v[66:69]
	v_mfma_f32_16x16x32_bf16 v[118:121], v[182:185], v[204:207], v[118:121]
	v_mfma_f32_16x16x32_bf16 v[114:117], v[196:199], v[204:207], v[114:117]
	v_mfma_f32_16x16x32_bf16 v[102:105], v[182:185], v[212:215], v[102:105]
	v_mfma_f32_16x16x32_bf16 v[98:101], v[196:199], v[212:215], v[98:101]
	v_mfma_f32_16x16x32_bf16 v[86:89], v[182:185], v[220:223], v[86:89]
	v_mfma_f32_16x16x32_bf16 v[82:85], v[196:199], v[220:223], v[82:85]
	v_mfma_f32_16x16x32_bf16 v[70:73], v[182:185], v[230:233], v[70:73]
	v_mfma_f32_16x16x32_bf16 v[66:69], v[196:199], v[230:233], v[66:69]
	s_setprio 0
	s_barrier
	s_add_i32 s26, s61, s2
	s_add_i32 m0, s26, 0xffffff80
	ds_read_b128 v[200:203], v189 offset:49152
	ds_read_b128 v[204:207], v189 offset:50176
	ds_read_b128 v[208:211], v189 offset:51200
	ds_read_b128 v[212:215], v189 offset:52224
	ds_read_b128 v[216:219], v189 offset:53248
	ds_read_b128 v[220:223], v189 offset:54272
	ds_read_b128 v[224:227], v189 offset:55296
	ds_read_b128 v[230:233], v189 offset:56320
	global_load_lds_dwordx4 v[168:169], off offset:128
	s_add_i32 m0, s26, 0x1f80
	s_add_u32 s24, s24, 0x40080
	s_addc_u32 s25, s25, 0
	s_add_i32 s26, s62, s2
	global_load_lds_dwordx4 v[172:173], off offset:128
	s_mov_b32 m0, s26
	s_nop 0
	global_load_lds_dwordx4 v146, s[24:25]
	s_add_i32 m0, s26, 0x2000
	s_nop 0
	global_load_lds_dwordx4 v142, s[24:25]
	s_add_i32 m0, s36, 0xffffff80
	s_nop 0
	global_load_lds_dwordx4 v[176:177], off offset:128
	s_add_i32 m0, s37, 0xffffff80
	s_nop 0
	global_load_lds_dwordx4 v[234:235], off offset:128
	s_waitcnt vmcnt(8)
	s_waitcnt lgkmcnt(0)
	s_barrier
	s_setprio 3
	s_waitcnt lgkmcnt(0)
	v_mfma_f32_16x16x32_bf16 v[62:65], v[130:133], v[200:203], v[62:65]
	v_mfma_f32_16x16x32_bf16 v[58:61], v[138:141], v[200:203], v[58:61]
	v_mfma_f32_16x16x32_bf16 v[46:49], v[130:133], v[208:211], v[46:49]
	v_mfma_f32_16x16x32_bf16 v[42:45], v[138:141], v[208:211], v[42:45]
	v_mfma_f32_16x16x32_bf16 v[30:33], v[130:133], v[216:219], v[30:33]
	v_mfma_f32_16x16x32_bf16 v[26:29], v[138:141], v[216:219], v[26:29]
	v_mfma_f32_16x16x32_bf16 v[14:17], v[130:133], v[224:227], v[14:17]
	v_mfma_f32_16x16x32_bf16 v[10:13], v[138:141], v[224:227], v[10:13]
	v_mfma_f32_16x16x32_bf16 v[62:65], v[134:137], v[204:207], v[62:65]
	v_mfma_f32_16x16x32_bf16 v[58:61], v[160:163], v[204:207], v[58:61]
	v_mfma_f32_16x16x32_bf16 v[46:49], v[134:137], v[212:215], v[46:49]
	v_mfma_f32_16x16x32_bf16 v[42:45], v[160:163], v[212:215], v[42:45]
	v_mfma_f32_16x16x32_bf16 v[30:33], v[134:137], v[220:223], v[30:33]
	v_mfma_f32_16x16x32_bf16 v[26:29], v[160:163], v[220:223], v[26:29]
	v_mfma_f32_16x16x32_bf16 v[14:17], v[134:137], v[230:233], v[14:17]
	v_mfma_f32_16x16x32_bf16 v[10:13], v[160:163], v[230:233], v[10:13]
	s_setprio 0
	s_setprio 3
	v_mfma_f32_16x16x32_bf16 v[54:57], v[164:167], v[200:203], v[54:57]
	v_mfma_f32_16x16x32_bf16 v[50:53], v[192:195], v[200:203], v[50:53]
	v_mfma_f32_16x16x32_bf16 v[38:41], v[164:167], v[208:211], v[38:41]
	v_mfma_f32_16x16x32_bf16 v[34:37], v[192:195], v[208:211], v[34:37]
	v_mfma_f32_16x16x32_bf16 v[22:25], v[164:167], v[216:219], v[22:25]
	v_mfma_f32_16x16x32_bf16 v[18:21], v[192:195], v[216:219], v[18:21]
	v_mfma_f32_16x16x32_bf16 v[6:9], v[164:167], v[224:227], v[6:9]
	v_mfma_f32_16x16x32_bf16 v[2:5], v[192:195], v[224:227], v[2:5]
	v_mfma_f32_16x16x32_bf16 v[54:57], v[182:185], v[204:207], v[54:57]
	v_mfma_f32_16x16x32_bf16 v[50:53], v[196:199], v[204:207], v[50:53]
	v_mfma_f32_16x16x32_bf16 v[38:41], v[182:185], v[212:215], v[38:41]
	v_mfma_f32_16x16x32_bf16 v[34:37], v[196:199], v[212:215], v[34:37]
	v_mfma_f32_16x16x32_bf16 v[22:25], v[182:185], v[220:223], v[22:25]
	v_mfma_f32_16x16x32_bf16 v[18:21], v[196:199], v[220:223], v[18:21]
	v_mfma_f32_16x16x32_bf16 v[6:9], v[182:185], v[230:233], v[6:9]
	v_mfma_f32_16x16x32_bf16 v[2:5], v[196:199], v[230:233], v[2:5]
	s_setprio 0
	s_barrier
	s_add_i32 s60, s60, 2
	s_add_u32 s22, s22, 0x100
	s_addc_u32 s23, s23, 0
	s_add_u32 s58, s58, 0x100
	s_addc_u32 s59, s59, 0
	s_cmp_gt_u32 s60, 13
	s_cbranch_scc0 .LBB0_721
	s_and_b64 vcc, exec, s[10:11]
	s_cbranch_vccz .LBB0_724
	s_barrier

; #define PG8_GIDX(G_, PM_) do { if constexpr (Sched::GATHER) { _Pragma("unroll") for (int h_ = 0; h_ < 2; ++h_) _Pragma("unroll") for (int i_ = 0; i_ < 2; ++i_) { int R_, C_; stage_rc(tid * 16 + i_ * 8192, R_, C_); \
;         const int src_ = S.rowsrc[(PM_) * BM + h_ * HALF + R_]; G_[h_][i_] = (unsigned)(src_ * K + C_) * 2u; } } } while (0)
; #define PG8_STAGE_A(b, h, ptr, NX) do { if constexpr (Sched::GATHER) { unsigned gs_[2]; gs_[0] = ((NX) && last_) ? gN[h][0] : gA[h][0]; gs_[1] = ((NX) && last_) ? gN[h][1] : gA[h][1]; PG8_STAGE(PG8_SA(b, h), ptr, gs_); } \
;         else PG8_STAGE(PG8_SA(b, h), (ptr) + ((h) ? hstep : (size_t)0), voffA); } while (0)
; #define PG8_STAGE(bufoff, gbase, voff) do { _Pragma("unroll") for (int _i = 0; _i < 2; ++_i) \
;         __builtin_amdgcn_global_load_lds((const unsigned*)((const char*)(gbase) + (voff)[_i]), (PG8_LAS unsigned*)(lds + (bufoff) + ldsw + _i * 8192), 16, 0, 0); } while (0)
; #define PG8_WAIT_V(n) asm volatile("s_waitcnt vmcnt(" #n ")" ::: "memory")
; #define PG8_BAR __builtin_amdgcn_s_barrier()
; template <class Epi, class Sched, bool ALIGN_EPI = false, bool SP2 = false>
; __device__ __forceinline__ void gemm_phase(PG8_LAS unsigned char* lds, const Gemm g, const Sched& S, const Epi& E, const bool skip_epi = false) {
;     ...
;         PG8_STAGE(PG8_SB(1, 0), cB + kstep, voffB); PG8_STAGE_A(1, 0, cA + kstep, false); PG8_STAGE(PG8_SB(1, 1), cB + hstep + kstep, voffB);
;         PG8_WAIT_V(6); PG8_BAR;
;     } else {
;         PG8_STAGE(PG8_SB(0, 0), cB, voffB); PG8_STAGE_A(0, 0, cA, false); PG8_STAGE(PG8_SB(0, 1), cB + hstep, voffB); PG8_STAGE_A(0, 1, cA, false);
;         if (wr == 1) PG8_BAR;
;         PG8_WAIT_V(4); PG8_BAR;
;         PG8_STAGE(PG8_SB(1, 0), cB + kstep, voffB); PG8_STAGE_A(1, 0, cA + kstep, false); PG8_STAGE(PG8_SB(1, 1), cB + hstep + kstep, voffB);
;         PG8_WAIT_V(6); PG8_BAR;
;     }
;     for (;;) {
;         const bool has_next = S.next(ui + 1, nxt);
;         if (has_next) PG8_GIDX(gN, nxt.pm);
;         const char* nA = has_next ? (const char*)g.A + (size_t)nxt.pm * pmstepA + nxt.ko : cA; const char* nB = has_next ? (const char*)g.Bt + (size_t)nxt.pn * tstep + nxt.ko : cB;
.LBB0_843:
	s_mov_b64 s[14:15], 0x80
	s_and_b32 s31, s4, 3
	s_add_i32 m0, s3, 0x18000
	v_lshl_add_u64 v[8:9], v[8:9], 0, s[14:15]
	s_lshl_b32 s34, s5, 6
	s_lshl_b32 s7, s5, 13
	s_lshl_b32 s9, s31, 12
	s_waitcnt vmcnt(2)
	s_barrier
	global_load_lds_dwordx4 v[8:9], off
	v_lshl_add_u64 v[6:7], v[6:7], 0, s[14:15]
	s_add_i32 m0, s3, 0x1a000
	s_add_i32 s35, s3, 0x8000
	s_add_i32 s36, s3, 0xa000
	global_load_lds_dwordx4 v[6:7], off
	v_lshl_add_u64 v[2:3], v[2:3], 0, s[14:15]
	s_mov_b32 m0, s35
	s_add_u32 s4, s22, 0xb0080
	global_load_lds_dwordx4 v[2:3], off
	v_lshl_add_u64 v[2:3], v[4:5], 0, s[14:15]
	s_mov_b32 m0, s36
	s_addc_u32 s5, s23, 0
	global_load_lds_dwordx4 v[2:3], off
	s_add_i32 m0, s3, 0x1c000
	s_nop 0
	global_load_lds_dwordx4 v192, s[4:5]
	s_add_i32 m0, s3, 0x1e000
	v_and_b32_e32 v1, 15, v10
	global_load_lds_dwordx4 v196, s[4:5]
	v_bfe_u32 v2, v10, 4, 2
	v_lshlrev_b32_e32 v3, 4, v2
	v_lshlrev_b32_e32 v4, 2, v10
	v_lshl_or_b32 v3, v1, 6, v3
	v_and_b32_e32 v4, 32, v4
	v_bitop3_b32 v5, v3, s7, v4 bitop3:0xde
	v_bitop3_b32 v229, v3, s9, v4 bitop3:0xde
	v_and_b32_e32 v3, 3, v10
	v_and_b32_e32 v4, 60, v10
	v_lshl_or_b32 v231, v3, 6, v4
	v_lshlrev_b32_e32 v3, 3, v3
	v_lshl_or_b32 v232, s31, 5, v3
	v_lshlrev_b32_e32 v3, 4, v1
	v_lshl_or_b32 v233, v2, 2, v3
	v_cmp_eq_u32_e64 s[4:5], 0, v2
	v_lshrrev_b32_e32 v3, 1, v11
	v_mul_lo_u32 v2, v13, s6
	s_mov_b32 s7, 0xb000
	s_cmpk_lt_u32 s8, 0x100
	v_mad_u64_u32 v[2:3], s[8:9], v3, s7, v[2:3]
	v_or_b32_e32 v2, v2, v12
	s_mov_b64 s[18:19], 0xb0080
	v_add_lshl_u32 v2, v2, v14, 1
	v_mov_b32_e32 v3, v193
	v_lshl_add_u64 v[198:199], v[2:3], 0, s[18:19]
	v_lshrrev_b32_e32 v3, 1, v15
	v_mul_lo_u32 v2, v16, s6
	v_mad_u64_u32 v[2:3], s[6:7], v3, s7, v[2:3]
	s_waitcnt vmcnt(6)
	v_or_b32_e32 v2, v2, v17
	s_cselect_b64 s[16:17], -1, 0
	v_add_lshl_u32 v2, v2, v18, 1
	v_mov_b32_e32 v3, v193
	s_add_i32 s39, 0, 0x10000
	s_add_i32 s48, 0, 0x14000
	v_bfe_u32 v230, v10, 2, 4
	s_ashr_i32 s37, s97, 31
	s_ashr_i32 s38, s94, 31
	v_lshl_add_u64 v[200:201], v[2:3], 0, s[18:19]
	v_mov_b64_e32 v[202:203], 0x100
	v_mov_b64_e32 v[204:205], 0xff
	v_add_u32_e32 v234, s39, v229
	v_add_u32_e32 v235, s48, v229
	v_add_u32_e32 v236, 0, v5
	s_mov_b32 s49, 0
	s_barrier
	s_branch .LBB0_846

; #define PG8_GIDX(G_, PM_) do { if constexpr (Sched::GATHER) { _Pragma("unroll") for (int h_ = 0; h_ < 2; ++h_) _Pragma("unroll") for (int i_ = 0; i_ < 2; ++i_) { int R_, C_; stage_rc(tid * 16 + i_ * 8192, R_, C_); \
;         const int src_ = S.rowsrc[(PM_) * BM + h_ * HALF + R_]; G_[h_][i_] = (unsigned)(src_ * K + C_) * 2u; } } } while (0)
; #define PG8_STAGE_A(b, h, ptr, NX) do { if constexpr (Sched::GATHER) { unsigned gs_[2]; gs_[0] = ((NX) && last_) ? gN[h][0] : gA[h][0]; gs_[1] = ((NX) && last_) ? gN[h][1] : gA[h][1]; PG8_STAGE(PG8_SA(b, h), ptr, gs_); } \
;         else PG8_STAGE(PG8_SA(b, h), (ptr) + ((h) ? hstep : (size_t)0), voffA); } while (0)
; #define PG8_LDA(dst, b, h) do { _Pragma("unroll") for (int m = 0; m < 4; ++m) _Pragma("unroll") for (int k = 0; k < 2; ++k) dst[m][k] = *(const PG8_LAS bf16x8*)(lds + PG8_SA(b, h) + aoff + m * 2048 + k * 1024); } while (0)
; template <class Epi, class Sched, bool ALIGN_EPI = false, bool SP2 = false>
; __device__ __forceinline__ void gemm_phase(PG8_LAS unsigned char* lds, const Gemm g, const Sched& S, const Epi& E, const bool skip_epi = false) {
;     ...
;         const bool has_next = S.next(ui + 1, nxt);
;         if (has_next) PG8_GIDX(gN, nxt.pm);
;         const char* nA = has_next ? (const char*)g.A + (size_t)nxt.pm * pmstepA + nxt.ko : cA; const char* nB = has_next ? (const char*)g.Bt + (size_t)nxt.pn * tstep + nxt.ko : cB;
;         for (int t = 0; t < nt; t += 2) {
;             const bool last = (t == nt - 2); last_ = last && has_next;
;             const char* a1 = cA + (size_t)(t + 1) * kstep;
;             const char* a2 = last ? nA : cA + (size_t)(t + 2) * kstep; const char* b2 = last ? nB : cB + (size_t)(t + 2) * kstep;
;             const char* a3 = a2 + kstep; const char* b3 = b2 + kstep;
;             if (last && has_next) S.a_ready(nxt);
;             if constexpr (SP2) {
;             PG8_LDB(B0, 0, 0); PG8_LDB(B1, 0, 1); PG8_SCHED; PG8_LDA(At, 0, 0); PG8_STAGE_A(1, 1, a1, false);
;             PG8_WAIT_V(8); PG8_WAIT_L(0); PG8_BAR; PG8_MMA(0, 0, At, B0); PG8_MMA(0, 1, At, B1); PG8_BAR; PG8_SCHED;
;             PG8_LDA(At, 0, 1); PG8_STAGE(PG8_SB(0, 0), b2, voffB); PG8_STAGE(PG8_SB(0, 1), b2 + hstep, voffB); PG8_STAGE_A(0, 0, a2, true);
;             PG8_WAIT_V(8); PG8_WAIT_L(0); PG8_BAR; PG8_MMA(1, 0, At, B0); PG8_MMA(1, 1, At, B1); PG8_BAR; PG8_SCHED;
.LBB0_856:
	s_add_u32 s55, s22, 0x100
	s_addc_u32 s56, s23, 0
	s_mov_b32 s57, -2
	s_waitcnt vmcnt(0)
	s_waitcnt lgkmcnt(0)
	ds_read_b128 v[98:101], v234
	ds_read_b128 v[110:113], v234 offset:1024
	ds_read_b128 v[122:125], v234 offset:2048
	ds_read_b128 v[126:129], v234 offset:3072
	ds_read_b128 v[138:141], v235
	ds_read_b128 v[142:145], v235 offset:1024
	ds_read_b128 v[146:149], v235 offset:2048
	ds_read_b128 v[150:153], v235 offset:3072
	s_add_u32 s22, s20, 0x100
	s_addc_u32 s23, s21, 0
	s_cmp_eq_u32 s57, 40
	s_cselect_b32 s27, s9, s23
	s_cselect_b32 s26, s8, s22
	s_cselect_b32 s25, s19, s56
	s_cselect_b32 s24, s18, s55
	v_lshl_add_u64 v[210:211], s[20:21], 0, v[198:199]
	s_add_i32 m0, s3, 0xc000
	ds_read_b128 v[154:157], v236
	ds_read_b128 v[166:169], v236 offset:1024
	ds_read_b128 v[170:173], v236 offset:2048
	ds_read_b128 v[174:177], v236 offset:3072
	ds_read_b128 v[178:181], v236 offset:4096
	ds_read_b128 v[182:185], v236 offset:5120
	ds_read_b128 v[186:189], v236 offset:6144
	ds_read_b128 v[206:209], v236 offset:7168
	global_load_lds_dwordx4 v[210:211], off
	v_lshl_add_u64 v[210:211], s[20:21], 0, v[200:201]
	s_add_i32 m0, s3, 0xe000
	s_nop 0
	global_load_lds_dwordx4 v[210:211], off
	s_waitcnt vmcnt(8)
	s_waitcnt lgkmcnt(0)
	s_barrier
	s_setprio 3
	s_waitcnt lgkmcnt(0)
	v_mfma_f32_16x16x32_bf16 v[162:165], v[98:101], v[154:157], 0
	v_mfma_f32_16x16x32_bf16 v[158:161], v[122:125], v[154:157], 0
	v_mfma_f32_16x16x32_bf16 v[118:121], v[98:101], v[170:173], 0
	v_mfma_f32_16x16x32_bf16 v[114:117], v[122:125], v[170:173], 0
	v_mfma_f32_16x16x32_bf16 v[94:97], v[98:101], v[178:181], 0
	v_mfma_f32_16x16x32_bf16 v[90:93], v[122:125], v[178:181], 0
	v_mfma_f32_16x16x32_bf16 v[78:81], v[98:101], v[186:189], 0
	v_mfma_f32_16x16x32_bf16 v[74:77], v[122:125], v[186:189], 0
	v_mfma_f32_16x16x32_bf16 v[162:165], v[110:113], v[166:169], v[162:165]
	v_mfma_f32_16x16x32_bf16 v[158:161], v[126:129], v[166:169], v[158:161]
	v_mfma_f32_16x16x32_bf16 v[118:121], v[110:113], v[174:177], v[118:121]
	v_mfma_f32_16x16x32_bf16 v[114:117], v[126:129], v[174:177], v[114:117]
	v_mfma_f32_16x16x32_bf16 v[94:97], v[110:113], v[182:185], v[94:97]
	v_mfma_f32_16x16x32_bf16 v[90:93], v[126:129], v[182:185], v[90:93]
	v_mfma_f32_16x16x32_bf16 v[78:81], v[110:113], v[206:209], v[78:81]
	v_mfma_f32_16x16x32_bf16 v[74:77], v[126:129], v[206:209], v[74:77]
	s_setprio 0
	s_setprio 3
	v_mfma_f32_16x16x32_bf16 v[134:137], v[138:141], v[154:157], 0
	v_mfma_f32_16x16x32_bf16 v[130:133], v[146:149], v[154:157], 0
	v_mfma_f32_16x16x32_bf16 v[106:109], v[138:141], v[170:173], 0
	v_mfma_f32_16x16x32_bf16 v[102:105], v[146:149], v[170:173], 0
	v_mfma_f32_16x16x32_bf16 v[86:89], v[138:141], v[178:181], 0
	v_mfma_f32_16x16x32_bf16 v[82:85], v[146:149], v[178:181], 0
	v_mfma_f32_16x16x32_bf16 v[70:73], v[138:141], v[186:189], 0
	v_mfma_f32_16x16x32_bf16 v[66:69], v[146:149], v[186:189], 0
	v_mfma_f32_16x16x32_bf16 v[134:137], v[142:145], v[166:169], v[134:137]
	v_mfma_f32_16x16x32_bf16 v[130:133], v[150:153], v[166:169], v[130:133]
	v_mfma_f32_16x16x32_bf16 v[106:109], v[142:145], v[174:177], v[106:109]
	v_mfma_f32_16x16x32_bf16 v[102:105], v[150:153], v[174:177], v[102:105]
	v_mfma_f32_16x16x32_bf16 v[86:89], v[142:145], v[182:185], v[86:89]
	v_mfma_f32_16x16x32_bf16 v[82:85], v[150:153], v[182:185], v[82:85]
	v_mfma_f32_16x16x32_bf16 v[70:73], v[142:145], v[206:209], v[70:73]
	v_mfma_f32_16x16x32_bf16 v[66:69], v[150:153], v[206:209], v[66:69]
	s_setprio 0
	s_barrier
	s_add_i32 s20, s39, s2
	v_lshl_add_u64 v[210:211], s[24:25], 0, v[192:193]
	s_mov_b32 m0, s20
	ds_read_b128 v[154:157], v236 offset:16384
	ds_read_b128 v[166:169], v236 offset:17408
	ds_read_b128 v[170:173], v236 offset:18432
	ds_read_b128 v[174:177], v236 offset:19456
	ds_read_b128 v[178:181], v236 offset:20480
	ds_read_b128 v[182:185], v236 offset:21504
	ds_read_b128 v[186:189], v236 offset:22528
	ds_read_b128 v[206:209], v236 offset:23552
	global_load_lds_dwordx4 v[210:211], off
	s_add_i32 m0, s20, 0x2000
	s_add_u32 s20, s24, 0xb0000
	v_lshl_add_u64 v[212:213], s[24:25], 0, v[196:197]
	s_addc_u32 s21, s25, 0
	s_add_i32 s58, s48, s2
	global_load_lds_dwordx4 v[212:213], off
	s_mov_b32 m0, s58
	v_lshl_add_u64 v[216:217], s[26:27], 0, v[194:195]
	global_load_lds_dwordx4 v192, s[20:21]
	s_add_i32 m0, s58, 0x2000
	s_nop 0
	global_load_lds_dwordx4 v196, s[20:21]
	v_lshl_add_u64 v[214:215], s[26:27], 0, v[190:191]
	s_mov_b32 m0, s3
	s_nop 0
	global_load_lds_dwordx4 v[214:215], off
	s_mov_b32 m0, s28
	s_nop 0
	global_load_lds_dwordx4 v[216:217], off
	s_waitcnt vmcnt(8)
	s_waitcnt lgkmcnt(0)
	s_barrier
; #define PG8_STAGE_A(b, h, ptr, NX) do { if constexpr (Sched::GATHER) { unsigned gs_[2]; gs_[0] = ((NX) && last_) ? gN[h][0] : gA[h][0]; gs_[1] = ((NX) && last_) ? gN[h][1] : gA[h][1]; PG8_STAGE(PG8_SA(b, h), ptr, gs_); } \
;         else PG8_STAGE(PG8_SA(b, h), (ptr) + ((h) ? hstep : (size_t)0), voffA); } while (0)
; #define PG8_LDA(dst, b, h) do { _Pragma("unroll") for (int m = 0; m < 4; ++m) _Pragma("unroll") for (int k = 0; k < 2; ++k) dst[m][k] = *(const PG8_LAS bf16x8*)(lds + PG8_SA(b, h) + aoff + m * 2048 + k * 1024); } while (0)
; #define PG8_LDB(dst, b, h) do { _Pragma("unroll") for (int n = 0; n < 2; ++n) _Pragma("unroll") for (int k = 0; k < 2; ++k) dst[n][k] = *(const PG8_LAS bf16x8*)(lds + PG8_SB(b, h) + boff + n * 2048 + k * 1024); } while (0)
; #define PG8_MMA(ai, bj, At, Bt) do { __builtin_amdgcn_s_setprio(1); _Pragma("unroll") for (int m = 0; m < 4; ++m) _Pragma("unroll") for (int n = 0; n < 2; ++n) _Pragma("unroll") for (int k = 0; k < 2; ++k) \
;         acc[ai][bj][m][n] = __builtin_amdgcn_mfma_f32_16x16x32_bf16(Bt[n][k], At[m][k], acc[ai][bj][m][n], 0, 0, 0); __builtin_amdgcn_s_setprio(0); } while (0)
; #define PG8_WAIT_V(n) asm volatile("s_waitcnt vmcnt(" #n ")" ::: "memory")
; #define PG8_WAIT_L(n) asm volatile("s_waitcnt lgkmcnt(" #n ")" ::: "memory")
; #define PG8_BAR __builtin_amdgcn_s_barrier()
; #define PG8_SCHED __builtin_amdgcn_sched_barrier(0)
; template <class Epi, class Sched, bool ALIGN_EPI = false, bool SP2 = false>
; __device__ __forceinline__ void gemm_phase(PG8_LAS unsigned char* lds, const Gemm g, const Sched& S, const Epi& E, const bool skip_epi = false) {
;     ...
;             PG8_WAIT_V(8); PG8_WAIT_L(0); PG8_BAR; PG8_MMA(1, 0, At, B0); PG8_MMA(1, 1, At, B1); PG8_BAR; PG8_SCHED;
;             PG8_LDB(B0, 1, 0); PG8_LDB(B1, 1, 1); PG8_SCHED; PG8_LDA(At, 1, 0); PG8_STAGE_A(0, 1, a2, true);
;             PG8_WAIT_V(8); PG8_WAIT_L(0); PG8_BAR; PG8_MMA(0, 0, At, B0); PG8_MMA(0, 1, At, B1); PG8_BAR; PG8_SCHED;
	s_setprio 3
	s_waitcnt lgkmcnt(0)
	v_mfma_f32_16x16x32_bf16 v[62:65], v[98:101], v[154:157], 0
	v_mfma_f32_16x16x32_bf16 v[58:61], v[122:125], v[154:157], 0
	v_mfma_f32_16x16x32_bf16 v[46:49], v[98:101], v[170:173], 0
	v_mfma_f32_16x16x32_bf16 v[42:45], v[122:125], v[170:173], 0
	v_mfma_f32_16x16x32_bf16 v[30:33], v[98:101], v[178:181], 0
	v_mfma_f32_16x16x32_bf16 v[26:29], v[122:125], v[178:181], 0
	v_mfma_f32_16x16x32_bf16 v[14:17], v[98:101], v[186:189], 0
	v_mfma_f32_16x16x32_bf16 v[10:13], v[122:125], v[186:189], 0
	v_mfma_f32_16x16x32_bf16 v[62:65], v[110:113], v[166:169], v[62:65]
	v_mfma_f32_16x16x32_bf16 v[58:61], v[126:129], v[166:169], v[58:61]
	v_mfma_f32_16x16x32_bf16 v[46:49], v[110:113], v[174:177], v[46:49]
	v_mfma_f32_16x16x32_bf16 v[42:45], v[126:129], v[174:177], v[42:45]
	v_mfma_f32_16x16x32_bf16 v[30:33], v[110:113], v[182:185], v[30:33]
	v_mfma_f32_16x16x32_bf16 v[26:29], v[126:129], v[182:185], v[26:29]
	v_mfma_f32_16x16x32_bf16 v[14:17], v[110:113], v[206:209], v[14:17]
	v_mfma_f32_16x16x32_bf16 v[10:13], v[126:129], v[206:209], v[10:13]
	s_setprio 0
	s_setprio 3
	v_mfma_f32_16x16x32_bf16 v[54:57], v[138:141], v[154:157], 0
	v_mfma_f32_16x16x32_bf16 v[50:53], v[146:149], v[154:157], 0
	v_mfma_f32_16x16x32_bf16 v[38:41], v[138:141], v[170:173], 0
	v_mfma_f32_16x16x32_bf16 v[34:37], v[146:149], v[170:173], 0
	v_mfma_f32_16x16x32_bf16 v[22:25], v[138:141], v[178:181], 0
	v_mfma_f32_16x16x32_bf16 v[18:21], v[146:149], v[178:181], 0
	v_mfma_f32_16x16x32_bf16 v[6:9], v[138:141], v[186:189], 0
	v_mfma_f32_16x16x32_bf16 v[2:5], v[146:149], v[186:189], 0
	v_mfma_f32_16x16x32_bf16 v[54:57], v[142:145], v[166:169], v[54:57]
	v_mfma_f32_16x16x32_bf16 v[50:53], v[150:153], v[166:169], v[50:53]
	v_mfma_f32_16x16x32_bf16 v[38:41], v[142:145], v[174:177], v[38:41]
	v_mfma_f32_16x16x32_bf16 v[34:37], v[150:153], v[174:177], v[34:37]
	v_mfma_f32_16x16x32_bf16 v[22:25], v[142:145], v[182:185], v[22:25]
	v_mfma_f32_16x16x32_bf16 v[18:21], v[150:153], v[182:185], v[18:21]
	v_mfma_f32_16x16x32_bf16 v[6:9], v[142:145], v[206:209], v[6:9]
	v_mfma_f32_16x16x32_bf16 v[2:5], v[150:153], v[206:209], v[2:5]
	s_setprio 0
	s_barrier
	s_add_i32 s58, 0, 0x18000
	s_add_i32 s59, 0, 0x1c000
	v_add_u32_e32 v126, s58, v229
	v_add_u32_e32 v150, s59, v229
	ds_read_b128 v[98:101], v126
	ds_read_b128 v[110:113], v126 offset:1024
	ds_read_b128 v[122:125], v126 offset:2048
	ds_read_b128 v[126:129], v126 offset:3072
	ds_read_b128 v[138:141], v150
	ds_read_b128 v[142:145], v150 offset:1024
	ds_read_b128 v[146:149], v150 offset:2048
	ds_read_b128 v[150:153], v150 offset:3072
	s_add_u32 s20, s26, 0xb0000
	s_addc_u32 s21, s27, 0
	s_mov_b32 m0, s29
	ds_read_b128 v[154:157], v236 offset:32768
	ds_read_b128 v[166:169], v236 offset:33792
	ds_read_b128 v[170:173], v236 offset:34816
	ds_read_b128 v[174:177], v236 offset:35840
	ds_read_b128 v[178:181], v236 offset:36864
	ds_read_b128 v[182:185], v236 offset:37888
	ds_read_b128 v[186:189], v236 offset:38912
	ds_read_b128 v[206:209], v236 offset:39936
	global_load_lds_dwordx4 v190, s[20:21]
	s_mov_b32 m0, s30
	s_nop 0
	global_load_lds_dwordx4 v194, s[20:21]
	s_waitcnt vmcnt(8)
	s_waitcnt lgkmcnt(0)
	s_barrier
	s_setprio 3
	s_waitcnt lgkmcnt(0)
	v_mfma_f32_16x16x32_bf16 v[162:165], v[98:101], v[154:157], v[162:165]
	v_mfma_f32_16x16x32_bf16 v[158:161], v[122:125], v[154:157], v[158:161]
	v_mfma_f32_16x16x32_bf16 v[118:121], v[98:101], v[170:173], v[118:121]
	v_mfma_f32_16x16x32_bf16 v[114:117], v[122:125], v[170:173], v[114:117]
	v_mfma_f32_16x16x32_bf16 v[94:97], v[98:101], v[178:181], v[94:97]
	v_mfma_f32_16x16x32_bf16 v[90:93], v[122:125], v[178:181], v[90:93]
	v_mfma_f32_16x16x32_bf16 v[78:81], v[98:101], v[186:189], v[78:81]
	v_mfma_f32_16x16x32_bf16 v[74:77], v[122:125], v[186:189], v[74:77]
	v_mfma_f32_16x16x32_bf16 v[162:165], v[110:113], v[166:169], v[162:165]
	v_mfma_f32_16x16x32_bf16 v[158:161], v[126:129], v[166:169], v[158:161]
	v_mfma_f32_16x16x32_bf16 v[118:121], v[110:113], v[174:177], v[118:121]
	v_mfma_f32_16x16x32_bf16 v[114:117], v[126:129], v[174:177], v[114:117]
	v_mfma_f32_16x16x32_bf16 v[94:97], v[110:113], v[182:185], v[94:97]
	v_mfma_f32_16x16x32_bf16 v[90:93], v[126:129], v[182:185], v[90:93]
	v_mfma_f32_16x16x32_bf16 v[78:81], v[110:113], v[206:209], v[78:81]
	v_mfma_f32_16x16x32_bf16 v[74:77], v[126:129], v[206:209], v[74:77]
	s_setprio 0
	s_setprio 3
	v_mfma_f32_16x16x32_bf16 v[134:137], v[138:141], v[154:157], v[134:137]
	v_mfma_f32_16x16x32_bf16 v[130:133], v[146:149], v[154:157], v[130:133]
	v_mfma_f32_16x16x32_bf16 v[106:109], v[138:141], v[170:173], v[106:109]
	v_mfma_f32_16x16x32_bf16 v[102:105], v[146:149], v[170:173], v[102:105]
	v_mfma_f32_16x16x32_bf16 v[86:89], v[138:141], v[178:181], v[86:89]
	v_mfma_f32_16x16x32_bf16 v[82:85], v[146:149], v[178:181], v[82:85]
	v_mfma_f32_16x16x32_bf16 v[70:73], v[138:141], v[186:189], v[70:73]
	v_mfma_f32_16x16x32_bf16 v[66:69], v[146:149], v[186:189], v[66:69]
	v_mfma_f32_16x16x32_bf16 v[134:137], v[142:145], v[166:169], v[134:137]
	v_mfma_f32_16x16x32_bf16 v[130:133], v[150:153], v[166:169], v[130:133]
	v_mfma_f32_16x16x32_bf16 v[106:109], v[142:145], v[174:177], v[106:109]
	v_mfma_f32_16x16x32_bf16 v[102:105], v[150:153], v[174:177], v[102:105]
	v_mfma_f32_16x16x32_bf16 v[86:89], v[142:145], v[182:185], v[86:89]
	v_mfma_f32_16x16x32_bf16 v[82:85], v[150:153], v[182:185], v[82:85]
	v_mfma_f32_16x16x32_bf16 v[70:73], v[142:145], v[206:209], v[70:73]
	v_mfma_f32_16x16x32_bf16 v[66:69], v[150:153], v[206:209], v[66:69]
	s_setprio 0
	s_barrier
; #define PG8_STAGE_A(b, h, ptr, NX) do { if constexpr (Sched::GATHER) { unsigned gs_[2]; gs_[0] = ((NX) && last_) ? gN[h][0] : gA[h][0]; gs_[1] = ((NX) && last_) ? gN[h][1] : gA[h][1]; PG8_STAGE(PG8_SA(b, h), ptr, gs_); } \
;         else PG8_STAGE(PG8_SA(b, h), (ptr) + ((h) ? hstep : (size_t)0), voffA); } while (0)
; #define PG8_STAGE(bufoff, gbase, voff) do { _Pragma("unroll") for (int _i = 0; _i < 2; ++_i) \
;         __builtin_amdgcn_global_load_lds((const unsigned*)((const char*)(gbase) + (voff)[_i]), (PG8_LAS unsigned*)(lds + (bufoff) + ldsw + _i * 8192), 16, 0, 0); } while (0)
; #define PG8_LDA(dst, b, h) do { _Pragma("unroll") for (int m = 0; m < 4; ++m) _Pragma("unroll") for (int k = 0; k < 2; ++k) dst[m][k] = *(const PG8_LAS bf16x8*)(lds + PG8_SA(b, h) + aoff + m * 2048 + k * 1024); } while (0)
; #define PG8_LDB(dst, b, h) do { _Pragma("unroll") for (int n = 0; n < 2; ++n) _Pragma("unroll") for (int k = 0; k < 2; ++k) dst[n][k] = *(const PG8_LAS bf16x8*)(lds + PG8_SB(b, h) + boff + n * 2048 + k * 1024); } while (0)
; #define PG8_WAIT_V(n) asm volatile("s_waitcnt vmcnt(" #n ")" ::: "memory")
; #define PG8_WAIT_L(n) asm volatile("s_waitcnt lgkmcnt(" #n ")" ::: "memory")
; #define PG8_BAR __builtin_amdgcn_s_barrier()
; template <class Epi, class Sched, bool ALIGN_EPI = false, bool SP2 = false>
; __device__ __forceinline__ void gemm_phase(PG8_LAS unsigned char* lds, const Gemm g, const Sched& S, const Epi& E, const bool skip_epi = false) {
;     ...
;             const bool last = (t == nt - 2); last_ = last && has_next;
;             const char* a1 = cA + (size_t)(t + 1) * kstep;
;             const char* a2 = last ? nA : cA + (size_t)(t + 2) * kstep; const char* b2 = last ? nB : cB + (size_t)(t + 2) * kstep;
;             const char* a3 = a2 + kstep; const char* b3 = b2 + kstep;
;             if (last && has_next) S.a_ready(nxt);
;             if constexpr (SP2) {
;             PG8_LDB(B0, 0, 0); PG8_LDB(B1, 0, 1); PG8_SCHED; PG8_LDA(At, 0, 0); PG8_STAGE_A(1, 1, a1, false);
;             PG8_WAIT_V(8); PG8_WAIT_L(0); PG8_BAR; PG8_MMA(0, 0, At, B0); PG8_MMA(0, 1, At, B1); PG8_BAR; PG8_SCHED;
;     ...
;             PG8_LDA(At, 1, 1); PG8_STAGE(PG8_SB(1, 0), b3, voffB); PG8_STAGE(PG8_SB(1, 1), b3 + hstep, voffB); PG8_STAGE_A(1, 0, a3, true);
;             PG8_WAIT_V(8); PG8_WAIT_L(0); PG8_BAR; PG8_MMA(1, 0, At, B0); PG8_MMA(1, 1, At, B1); PG8_BAR; PG8_SCHED;
	s_add_i32 s20, s58, s2
	s_add_i32 m0, s20, 0xffffff80
	ds_read_b128 v[154:157], v236 offset:49152
	ds_read_b128 v[166:169], v236 offset:50176
	ds_read_b128 v[170:173], v236 offset:51200
	ds_read_b128 v[174:177], v236 offset:52224
	ds_read_b128 v[178:181], v236 offset:53248
	ds_read_b128 v[182:185], v236 offset:54272
	ds_read_b128 v[186:189], v236 offset:55296
	ds_read_b128 v[206:209], v236 offset:56320
	global_load_lds_dwordx4 v[210:211], off offset:128
	s_add_i32 m0, s20, 0x1f80
	s_add_u32 s20, s24, 0xb0080
	s_addc_u32 s21, s25, 0
	s_add_i32 s24, s59, s2
	global_load_lds_dwordx4 v[212:213], off offset:128
	s_mov_b32 m0, s24
	s_nop 0
	global_load_lds_dwordx4 v192, s[20:21]
	s_add_i32 m0, s24, 0x2000
	s_nop 0
	global_load_lds_dwordx4 v196, s[20:21]
	s_add_i32 m0, s35, 0xffffff80
	s_nop 0
	global_load_lds_dwordx4 v[214:215], off offset:128
	s_add_i32 m0, s36, 0xffffff80
	s_nop 0
	global_load_lds_dwordx4 v[216:217], off offset:128
	s_waitcnt vmcnt(8)
	s_waitcnt lgkmcnt(0)
	s_barrier
	s_setprio 3
	s_waitcnt lgkmcnt(0)
	v_mfma_f32_16x16x32_bf16 v[62:65], v[98:101], v[154:157], v[62:65]
	v_mfma_f32_16x16x32_bf16 v[58:61], v[122:125], v[154:157], v[58:61]
	v_mfma_f32_16x16x32_bf16 v[46:49], v[98:101], v[170:173], v[46:49]
	v_mfma_f32_16x16x32_bf16 v[42:45], v[122:125], v[170:173], v[42:45]
	v_mfma_f32_16x16x32_bf16 v[30:33], v[98:101], v[178:181], v[30:33]
	v_mfma_f32_16x16x32_bf16 v[26:29], v[122:125], v[178:181], v[26:29]
	v_mfma_f32_16x16x32_bf16 v[14:17], v[98:101], v[186:189], v[14:17]
	v_mfma_f32_16x16x32_bf16 v[10:13], v[122:125], v[186:189], v[10:13]
	v_mfma_f32_16x16x32_bf16 v[62:65], v[110:113], v[166:169], v[62:65]
	v_mfma_f32_16x16x32_bf16 v[58:61], v[126:129], v[166:169], v[58:61]
	v_mfma_f32_16x16x32_bf16 v[46:49], v[110:113], v[174:177], v[46:49]
	v_mfma_f32_16x16x32_bf16 v[42:45], v[126:129], v[174:177], v[42:45]
	v_mfma_f32_16x16x32_bf16 v[30:33], v[110:113], v[182:185], v[30:33]
	v_mfma_f32_16x16x32_bf16 v[26:29], v[126:129], v[182:185], v[26:29]
	v_mfma_f32_16x16x32_bf16 v[14:17], v[110:113], v[206:209], v[14:17]
	v_mfma_f32_16x16x32_bf16 v[10:13], v[126:129], v[206:209], v[10:13]
	s_setprio 0
	s_setprio 3
	v_mfma_f32_16x16x32_bf16 v[54:57], v[138:141], v[154:157], v[54:57]
	v_mfma_f32_16x16x32_bf16 v[50:53], v[146:149], v[154:157], v[50:53]
	v_mfma_f32_16x16x32_bf16 v[38:41], v[138:141], v[170:173], v[38:41]
	v_mfma_f32_16x16x32_bf16 v[34:37], v[146:149], v[170:173], v[34:37]
	v_mfma_f32_16x16x32_bf16 v[22:25], v[138:141], v[178:181], v[22:25]
	v_mfma_f32_16x16x32_bf16 v[18:21], v[146:149], v[178:181], v[18:21]
	v_mfma_f32_16x16x32_bf16 v[6:9], v[138:141], v[186:189], v[6:9]
	v_mfma_f32_16x16x32_bf16 v[2:5], v[146:149], v[186:189], v[2:5]
	v_mfma_f32_16x16x32_bf16 v[54:57], v[142:145], v[166:169], v[54:57]
	v_mfma_f32_16x16x32_bf16 v[50:53], v[150:153], v[166:169], v[50:53]
	v_mfma_f32_16x16x32_bf16 v[38:41], v[142:145], v[174:177], v[38:41]
	v_mfma_f32_16x16x32_bf16 v[34:37], v[150:153], v[174:177], v[34:37]
	v_mfma_f32_16x16x32_bf16 v[22:25], v[142:145], v[182:185], v[22:25]
	v_mfma_f32_16x16x32_bf16 v[18:21], v[150:153], v[182:185], v[18:21]
	v_mfma_f32_16x16x32_bf16 v[6:9], v[142:145], v[206:209], v[6:9]
	v_mfma_f32_16x16x32_bf16 v[2:5], v[150:153], v[206:209], v[2:5]
	s_setprio 0
	s_barrier
	s_add_i32 s57, s57, 2
	s_add_u32 s55, s55, 0x100
	s_addc_u32 s56, s56, 0
	s_cmp_gt_u32 s57, 41
	s_mov_b64 s[20:21], s[22:23]
.LBB0_857:
	ds_read_b128 v[98:101], v234
	ds_read_b128 v[110:113], v234 offset:1024
	ds_read_b128 v[122:125], v234 offset:2048
	ds_read_b128 v[126:129], v234 offset:3072
	ds_read_b128 v[138:141], v235
	ds_read_b128 v[142:145], v235 offset:1024
	ds_read_b128 v[146:149], v235 offset:2048
	ds_read_b128 v[150:153], v235 offset:3072
	s_add_u32 s22, s20, 0x100
	s_addc_u32 s23, s21, 0
	s_cmp_eq_u32 s57, 40
	s_cselect_b32 s27, s9, s23
	s_cselect_b32 s26, s8, s22
	s_cselect_b32 s25, s19, s56
	s_cselect_b32 s24, s18, s55
	v_lshl_add_u64 v[210:211], s[20:21], 0, v[198:199]
	s_add_i32 m0, s3, 0xc000
	ds_read_b128 v[154:157], v236
	ds_read_b128 v[166:169], v236 offset:1024
	ds_read_b128 v[170:173], v236 offset:2048
	ds_read_b128 v[174:177], v236 offset:3072
	ds_read_b128 v[178:181], v236 offset:4096
	ds_read_b128 v[182:185], v236 offset:5120
	ds_read_b128 v[186:189], v236 offset:6144
	ds_read_b128 v[206:209], v236 offset:7168
	global_load_lds_dwordx4 v[210:211], off
	v_lshl_add_u64 v[210:211], s[20:21], 0, v[200:201]
	s_add_i32 m0, s3, 0xe000
	s_nop 0
	global_load_lds_dwordx4 v[210:211], off
	s_waitcnt vmcnt(8)
	s_waitcnt lgkmcnt(0)
	s_barrier
; #define PG8_STAGE_A(b, h, ptr, NX) do { if constexpr (Sched::GATHER) { unsigned gs_[2]; gs_[0] = ((NX) && last_) ? gN[h][0] : gA[h][0]; gs_[1] = ((NX) && last_) ? gN[h][1] : gA[h][1]; PG8_STAGE(PG8_SA(b, h), ptr, gs_); } \
;         else PG8_STAGE(PG8_SA(b, h), (ptr) + ((h) ? hstep : (size_t)0), voffA); } while (0)
; #define PG8_STAGE(bufoff, gbase, voff) do { _Pragma("unroll") for (int _i = 0; _i < 2; ++_i) \
;         __builtin_amdgcn_global_load_lds((const unsigned*)((const char*)(gbase) + (voff)[_i]), (PG8_LAS unsigned*)(lds + (bufoff) + ldsw + _i * 8192), 16, 0, 0); } while (0)
; #define PG8_LDA(dst, b, h) do { _Pragma("unroll") for (int m = 0; m < 4; ++m) _Pragma("unroll") for (int k = 0; k < 2; ++k) dst[m][k] = *(const PG8_LAS bf16x8*)(lds + PG8_SA(b, h) + aoff + m * 2048 + k * 1024); } while (0)
; #define PG8_LDB(dst, b, h) do { _Pragma("unroll") for (int n = 0; n < 2; ++n) _Pragma("unroll") for (int k = 0; k < 2; ++k) dst[n][k] = *(const PG8_LAS bf16x8*)(lds + PG8_SB(b, h) + boff + n * 2048 + k * 1024); } while (0)
; #define PG8_MMA(ai, bj, At, Bt) do { __builtin_amdgcn_s_setprio(1); _Pragma("unroll") for (int m = 0; m < 4; ++m) _Pragma("unroll") for (int n = 0; n < 2; ++n) _Pragma("unroll") for (int k = 0; k < 2; ++k) \
;         acc[ai][bj][m][n] = __builtin_amdgcn_mfma_f32_16x16x32_bf16(Bt[n][k], At[m][k], acc[ai][bj][m][n], 0, 0, 0); __builtin_amdgcn_s_setprio(0); } while (0)
; #define PG8_WAIT_V(n) asm volatile("s_waitcnt vmcnt(" #n ")" ::: "memory")
; #define PG8_WAIT_L(n) asm volatile("s_waitcnt lgkmcnt(" #n ")" ::: "memory")
; #define PG8_BAR __builtin_amdgcn_s_barrier()
; #define PG8_SCHED __builtin_amdgcn_sched_barrier(0)
; template <class Epi, class Sched, bool ALIGN_EPI = false, bool SP2 = false>
; __device__ __forceinline__ void gemm_phase(PG8_LAS unsigned char* lds, const Gemm g, const Sched& S, const Epi& E, const bool skip_epi = false) {
;     ...
;             PG8_LDB(B0, 0, 0); PG8_LDB(B1, 0, 1); PG8_SCHED; PG8_LDA(At, 0, 0); PG8_STAGE_A(1, 1, a1, false);
;             PG8_WAIT_V(8); PG8_WAIT_L(0); PG8_BAR; PG8_MMA(0, 0, At, B0); PG8_MMA(0, 1, At, B1); PG8_BAR; PG8_SCHED;
;             PG8_LDA(At, 0, 1); PG8_STAGE(PG8_SB(0, 0), b2, voffB); PG8_STAGE(PG8_SB(0, 1), b2 + hstep, voffB); PG8_STAGE_A(0, 0, a2, true);
;             PG8_WAIT_V(8); PG8_WAIT_L(0); PG8_BAR; PG8_MMA(1, 0, At, B0); PG8_MMA(1, 1, At, B1); PG8_BAR; PG8_SCHED;
	s_setprio 3
	s_waitcnt lgkmcnt(0)
	v_mfma_f32_16x16x32_bf16 v[162:165], v[98:101], v[154:157], v[162:165]
	v_mfma_f32_16x16x32_bf16 v[158:161], v[122:125], v[154:157], v[158:161]
	v_mfma_f32_16x16x32_bf16 v[118:121], v[98:101], v[170:173], v[118:121]
	v_mfma_f32_16x16x32_bf16 v[114:117], v[122:125], v[170:173], v[114:117]
	v_mfma_f32_16x16x32_bf16 v[94:97], v[98:101], v[178:181], v[94:97]
	v_mfma_f32_16x16x32_bf16 v[90:93], v[122:125], v[178:181], v[90:93]
	v_mfma_f32_16x16x32_bf16 v[78:81], v[98:101], v[186:189], v[78:81]
	v_mfma_f32_16x16x32_bf16 v[74:77], v[122:125], v[186:189], v[74:77]
	v_mfma_f32_16x16x32_bf16 v[162:165], v[110:113], v[166:169], v[162:165]
	v_mfma_f32_16x16x32_bf16 v[158:161], v[126:129], v[166:169], v[158:161]
	v_mfma_f32_16x16x32_bf16 v[118:121], v[110:113], v[174:177], v[118:121]
	v_mfma_f32_16x16x32_bf16 v[114:117], v[126:129], v[174:177], v[114:117]
	v_mfma_f32_16x16x32_bf16 v[94:97], v[110:113], v[182:185], v[94:97]
	v_mfma_f32_16x16x32_bf16 v[90:93], v[126:129], v[182:185], v[90:93]
	v_mfma_f32_16x16x32_bf16 v[78:81], v[110:113], v[206:209], v[78:81]
	v_mfma_f32_16x16x32_bf16 v[74:77], v[126:129], v[206:209], v[74:77]
	s_setprio 0
	s_setprio 3
	v_mfma_f32_16x16x32_bf16 v[134:137], v[138:141], v[154:157], v[134:137]
	v_mfma_f32_16x16x32_bf16 v[130:133], v[146:149], v[154:157], v[130:133]
	v_mfma_f32_16x16x32_bf16 v[106:109], v[138:141], v[170:173], v[106:109]
	v_mfma_f32_16x16x32_bf16 v[102:105], v[146:149], v[170:173], v[102:105]
	v_mfma_f32_16x16x32_bf16 v[86:89], v[138:141], v[178:181], v[86:89]
	v_mfma_f32_16x16x32_bf16 v[82:85], v[146:149], v[178:181], v[82:85]
	v_mfma_f32_16x16x32_bf16 v[70:73], v[138:141], v[186:189], v[70:73]
	v_mfma_f32_16x16x32_bf16 v[66:69], v[146:149], v[186:189], v[66:69]
	v_mfma_f32_16x16x32_bf16 v[134:137], v[142:145], v[166:169], v[134:137]
	v_mfma_f32_16x16x32_bf16 v[130:133], v[150:153], v[166:169], v[130:133]
	v_mfma_f32_16x16x32_bf16 v[106:109], v[142:145], v[174:177], v[106:109]
	v_mfma_f32_16x16x32_bf16 v[102:105], v[150:153], v[174:177], v[102:105]
	v_mfma_f32_16x16x32_bf16 v[86:89], v[142:145], v[182:185], v[86:89]
	v_mfma_f32_16x16x32_bf16 v[82:85], v[150:153], v[182:185], v[82:85]
	v_mfma_f32_16x16x32_bf16 v[70:73], v[142:145], v[206:209], v[70:73]
	v_mfma_f32_16x16x32_bf16 v[66:69], v[150:153], v[206:209], v[66:69]
	s_setprio 0
	s_barrier
	s_add_i32 s20, s39, s2
	v_lshl_add_u64 v[210:211], s[24:25], 0, v[192:193]
	s_mov_b32 m0, s20
	ds_read_b128 v[154:157], v236 offset:16384
	ds_read_b128 v[166:169], v236 offset:17408
	ds_read_b128 v[170:173], v236 offset:18432
	ds_read_b128 v[174:177], v236 offset:19456
	ds_read_b128 v[178:181], v236 offset:20480
	ds_read_b128 v[182:185], v236 offset:21504
	ds_read_b128 v[186:189], v236 offset:22528
	ds_read_b128 v[206:209], v236 offset:23552
	global_load_lds_dwordx4 v[210:211], off
	s_add_i32 m0, s20, 0x2000
	s_add_u32 s20, s24, 0xb0000
	v_lshl_add_u64 v[212:213], s[24:25], 0, v[196:197]
	s_addc_u32 s21, s25, 0
	s_add_i32 s58, s48, s2
	global_load_lds_dwordx4 v[212:213], off
	s_mov_b32 m0, s58
	v_lshl_add_u64 v[216:217], s[26:27], 0, v[194:195]
	global_load_lds_dwordx4 v192, s[20:21]
	s_add_i32 m0, s58, 0x2000
	s_nop 0
	global_load_lds_dwordx4 v196, s[20:21]
	v_lshl_add_u64 v[214:215], s[26:27], 0, v[190:191]
	s_mov_b32 m0, s3
	s_nop 0
	global_load_lds_dwordx4 v[214:215], off
	s_mov_b32 m0, s28
	s_nop 0
	global_load_lds_dwordx4 v[216:217], off
	s_waitcnt vmcnt(8)
	s_waitcnt lgkmcnt(0)
	s_barrier
	s_setprio 3
	s_waitcnt lgkmcnt(0)
	v_mfma_f32_16x16x32_bf16 v[62:65], v[98:101], v[154:157], v[62:65]
	v_mfma_f32_16x16x32_bf16 v[58:61], v[122:125], v[154:157], v[58:61]
	v_mfma_f32_16x16x32_bf16 v[46:49], v[98:101], v[170:173], v[46:49]
	v_mfma_f32_16x16x32_bf16 v[42:45], v[122:125], v[170:173], v[42:45]
	v_mfma_f32_16x16x32_bf16 v[30:33], v[98:101], v[178:181], v[30:33]
	v_mfma_f32_16x16x32_bf16 v[26:29], v[122:125], v[178:181], v[26:29]
	v_mfma_f32_16x16x32_bf16 v[14:17], v[98:101], v[186:189], v[14:17]
	v_mfma_f32_16x16x32_bf16 v[10:13], v[122:125], v[186:189], v[10:13]
	v_mfma_f32_16x16x32_bf16 v[62:65], v[110:113], v[166:169], v[62:65]
	v_mfma_f32_16x16x32_bf16 v[58:61], v[126:129], v[166:169], v[58:61]
	v_mfma_f32_16x16x32_bf16 v[46:49], v[110:113], v[174:177], v[46:49]
	v_mfma_f32_16x16x32_bf16 v[42:45], v[126:129], v[174:177], v[42:45]
	v_mfma_f32_16x16x32_bf16 v[30:33], v[110:113], v[182:185], v[30:33]
	v_mfma_f32_16x16x32_bf16 v[26:29], v[126:129], v[182:185], v[26:29]
	v_mfma_f32_16x16x32_bf16 v[14:17], v[110:113], v[206:209], v[14:17]
	v_mfma_f32_16x16x32_bf16 v[10:13], v[126:129], v[206:209], v[10:13]
	s_setprio 0
	s_setprio 3
	v_mfma_f32_16x16x32_bf16 v[54:57], v[138:141], v[154:157], v[54:57]
	v_mfma_f32_16x16x32_bf16 v[50:53], v[146:149], v[154:157], v[50:53]
	v_mfma_f32_16x16x32_bf16 v[38:41], v[138:141], v[170:173], v[38:41]
	v_mfma_f32_16x16x32_bf16 v[34:37], v[146:149], v[170:173], v[34:37]
	v_mfma_f32_16x16x32_bf16 v[22:25], v[138:141], v[178:181], v[22:25]
	v_mfma_f32_16x16x32_bf16 v[18:21], v[146:149], v[178:181], v[18:21]
	v_mfma_f32_16x16x32_bf16 v[6:9], v[138:141], v[186:189], v[6:9]
	v_mfma_f32_16x16x32_bf16 v[2:5], v[146:149], v[186:189], v[2:5]
	v_mfma_f32_16x16x32_bf16 v[54:57], v[142:145], v[166:169], v[54:57]
	v_mfma_f32_16x16x32_bf16 v[50:53], v[150:153], v[166:169], v[50:53]
	v_mfma_f32_16x16x32_bf16 v[38:41], v[142:145], v[174:177], v[38:41]
	v_mfma_f32_16x16x32_bf16 v[34:37], v[150:153], v[174:177], v[34:37]
	v_mfma_f32_16x16x32_bf16 v[22:25], v[142:145], v[182:185], v[22:25]
	v_mfma_f32_16x16x32_bf16 v[18:21], v[150:153], v[182:185], v[18:21]
	v_mfma_f32_16x16x32_bf16 v[6:9], v[142:145], v[206:209], v[6:9]
	v_mfma_f32_16x16x32_bf16 v[2:5], v[150:153], v[206:209], v[2:5]
	s_setprio 0
	s_barrier
; #define PG8_STAGE_A(b, h, ptr, NX) do { if constexpr (Sched::GATHER) { unsigned gs_[2]; gs_[0] = ((NX) && last_) ? gN[h][0] : gA[h][0]; gs_[1] = ((NX) && last_) ? gN[h][1] : gA[h][1]; PG8_STAGE(PG8_SA(b, h), ptr, gs_); } \
;         else PG8_STAGE(PG8_SA(b, h), (ptr) + ((h) ? hstep : (size_t)0), voffA); } while (0)
; #define PG8_STAGE(bufoff, gbase, voff) do { _Pragma("unroll") for (int _i = 0; _i < 2; ++_i) \
;         __builtin_amdgcn_global_load_lds((const unsigned*)((const char*)(gbase) + (voff)[_i]), (PG8_LAS unsigned*)(lds + (bufoff) + ldsw + _i * 8192), 16, 0, 0); } while (0)
; #define PG8_LDA(dst, b, h) do { _Pragma("unroll") for (int m = 0; m < 4; ++m) _Pragma("unroll") for (int k = 0; k < 2; ++k) dst[m][k] = *(const PG8_LAS bf16x8*)(lds + PG8_SA(b, h) + aoff + m * 2048 + k * 1024); } while (0)
; #define PG8_LDB(dst, b, h) do { _Pragma("unroll") for (int n = 0; n < 2; ++n) _Pragma("unroll") for (int k = 0; k < 2; ++k) dst[n][k] = *(const PG8_LAS bf16x8*)(lds + PG8_SB(b, h) + boff + n * 2048 + k * 1024); } while (0)
; #define PG8_MMA(ai, bj, At, Bt) do { __builtin_amdgcn_s_setprio(1); _Pragma("unroll") for (int m = 0; m < 4; ++m) _Pragma("unroll") for (int n = 0; n < 2; ++n) _Pragma("unroll") for (int k = 0; k < 2; ++k) \
;         acc[ai][bj][m][n] = __builtin_amdgcn_mfma_f32_16x16x32_bf16(Bt[n][k], At[m][k], acc[ai][bj][m][n], 0, 0, 0); __builtin_amdgcn_s_setprio(0); } while (0)
; #define PG8_WAIT_V(n) asm volatile("s_waitcnt vmcnt(" #n ")" ::: "memory")
; #define PG8_WAIT_L(n) asm volatile("s_waitcnt lgkmcnt(" #n ")" ::: "memory")
; #define PG8_BAR __builtin_amdgcn_s_barrier()
; #define PG8_SCHED __builtin_amdgcn_sched_barrier(0)
; template <class Epi, class Sched, bool ALIGN_EPI = false, bool SP2 = false>
; __device__ __forceinline__ void gemm_phase(PG8_LAS unsigned char* lds, const Gemm g, const Sched& S, const Epi& E, const bool skip_epi = false) {
;     ...
;             PG8_LDB(B0, 1, 0); PG8_LDB(B1, 1, 1); PG8_SCHED; PG8_LDA(At, 1, 0); PG8_STAGE_A(0, 1, a2, true);
;             PG8_WAIT_V(8); PG8_WAIT_L(0); PG8_BAR; PG8_MMA(0, 0, At, B0); PG8_MMA(0, 1, At, B1); PG8_BAR; PG8_SCHED;
;             PG8_LDA(At, 1, 1); PG8_STAGE(PG8_SB(1, 0), b3, voffB); PG8_STAGE(PG8_SB(1, 1), b3 + hstep, voffB); PG8_STAGE_A(1, 0, a3, true);
;             PG8_WAIT_V(8); PG8_WAIT_L(0); PG8_BAR; PG8_MMA(1, 0, At, B0); PG8_MMA(1, 1, At, B1); PG8_BAR; PG8_SCHED;
	s_add_i32 s58, 0, 0x18000
	s_add_i32 s59, 0, 0x1c000
	v_add_u32_e32 v126, s58, v229
	v_add_u32_e32 v150, s59, v229
	ds_read_b128 v[98:101], v126
	ds_read_b128 v[110:113], v126 offset:1024
	ds_read_b128 v[122:125], v126 offset:2048
	ds_read_b128 v[126:129], v126 offset:3072
	ds_read_b128 v[138:141], v150
	ds_read_b128 v[142:145], v150 offset:1024
	ds_read_b128 v[146:149], v150 offset:2048
	ds_read_b128 v[150:153], v150 offset:3072
	s_add_u32 s20, s26, 0xb0000
	s_addc_u32 s21, s27, 0
	s_mov_b32 m0, s29
	ds_read_b128 v[154:157], v236 offset:32768
	ds_read_b128 v[166:169], v236 offset:33792
	ds_read_b128 v[170:173], v236 offset:34816
	ds_read_b128 v[174:177], v236 offset:35840
	ds_read_b128 v[178:181], v236 offset:36864
	ds_read_b128 v[182:185], v236 offset:37888
	ds_read_b128 v[186:189], v236 offset:38912
	ds_read_b128 v[206:209], v236 offset:39936
	global_load_lds_dwordx4 v190, s[20:21]
	s_mov_b32 m0, s30
	s_nop 0
	global_load_lds_dwordx4 v194, s[20:21]
	s_waitcnt vmcnt(8)
	s_waitcnt lgkmcnt(0)
	s_barrier
	s_setprio 3
	s_waitcnt lgkmcnt(0)
	v_mfma_f32_16x16x32_bf16 v[162:165], v[98:101], v[154:157], v[162:165]
	v_mfma_f32_16x16x32_bf16 v[158:161], v[122:125], v[154:157], v[158:161]
	v_mfma_f32_16x16x32_bf16 v[118:121], v[98:101], v[170:173], v[118:121]
	v_mfma_f32_16x16x32_bf16 v[114:117], v[122:125], v[170:173], v[114:117]
	v_mfma_f32_16x16x32_bf16 v[94:97], v[98:101], v[178:181], v[94:97]
	v_mfma_f32_16x16x32_bf16 v[90:93], v[122:125], v[178:181], v[90:93]
	v_mfma_f32_16x16x32_bf16 v[78:81], v[98:101], v[186:189], v[78:81]
	v_mfma_f32_16x16x32_bf16 v[74:77], v[122:125], v[186:189], v[74:77]
	v_mfma_f32_16x16x32_bf16 v[162:165], v[110:113], v[166:169], v[162:165]
	v_mfma_f32_16x16x32_bf16 v[158:161], v[126:129], v[166:169], v[158:161]
	v_mfma_f32_16x16x32_bf16 v[118:121], v[110:113], v[174:177], v[118:121]
	v_mfma_f32_16x16x32_bf16 v[114:117], v[126:129], v[174:177], v[114:117]
	v_mfma_f32_16x16x32_bf16 v[94:97], v[110:113], v[182:185], v[94:97]
	v_mfma_f32_16x16x32_bf16 v[90:93], v[126:129], v[182:185], v[90:93]
	v_mfma_f32_16x16x32_bf16 v[78:81], v[110:113], v[206:209], v[78:81]
	v_mfma_f32_16x16x32_bf16 v[74:77], v[126:129], v[206:209], v[74:77]
	s_setprio 0
	s_setprio 3
	v_mfma_f32_16x16x32_bf16 v[134:137], v[138:141], v[154:157], v[134:137]
	v_mfma_f32_16x16x32_bf16 v[130:133], v[146:149], v[154:157], v[130:133]
	v_mfma_f32_16x16x32_bf16 v[106:109], v[138:141], v[170:173], v[106:109]
	v_mfma_f32_16x16x32_bf16 v[102:105], v[146:149], v[170:173], v[102:105]
	v_mfma_f32_16x16x32_bf16 v[86:89], v[138:141], v[178:181], v[86:89]
	v_mfma_f32_16x16x32_bf16 v[82:85], v[146:149], v[178:181], v[82:85]
	v_mfma_f32_16x16x32_bf16 v[70:73], v[138:141], v[186:189], v[70:73]
	v_mfma_f32_16x16x32_bf16 v[66:69], v[146:149], v[186:189], v[66:69]
	v_mfma_f32_16x16x32_bf16 v[134:137], v[142:145], v[166:169], v[134:137]
	v_mfma_f32_16x16x32_bf16 v[130:133], v[150:153], v[166:169], v[130:133]
	v_mfma_f32_16x16x32_bf16 v[106:109], v[142:145], v[174:177], v[106:109]
	v_mfma_f32_16x16x32_bf16 v[102:105], v[150:153], v[174:177], v[102:105]
	v_mfma_f32_16x16x32_bf16 v[86:89], v[142:145], v[182:185], v[86:89]
	v_mfma_f32_16x16x32_bf16 v[82:85], v[150:153], v[182:185], v[82:85]
	v_mfma_f32_16x16x32_bf16 v[70:73], v[142:145], v[206:209], v[70:73]
	v_mfma_f32_16x16x32_bf16 v[66:69], v[150:153], v[206:209], v[66:69]
	s_setprio 0
	s_barrier
	s_add_i32 s20, s58, s2
	s_add_i32 m0, s20, 0xffffff80
	ds_read_b128 v[154:157], v236 offset:49152
	ds_read_b128 v[166:169], v236 offset:50176
	ds_read_b128 v[170:173], v236 offset:51200
	ds_read_b128 v[174:177], v236 offset:52224
	ds_read_b128 v[178:181], v236 offset:53248
	ds_read_b128 v[182:185], v236 offset:54272
	ds_read_b128 v[186:189], v236 offset:55296
	ds_read_b128 v[206:209], v236 offset:56320
	global_load_lds_dwordx4 v[210:211], off offset:128
	s_add_i32 m0, s20, 0x1f80
	s_add_u32 s20, s24, 0xb0080
	s_addc_u32 s21, s25, 0
	s_add_i32 s24, s59, s2
	global_load_lds_dwordx4 v[212:213], off offset:128
	s_mov_b32 m0, s24
	s_nop 0
	global_load_lds_dwordx4 v192, s[20:21]
	s_add_i32 m0, s24, 0x2000
	s_nop 0
	global_load_lds_dwordx4 v196, s[20:21]
	s_add_i32 m0, s35, 0xffffff80
	s_nop 0
	global_load_lds_dwordx4 v[214:215], off offset:128
	s_add_i32 m0, s36, 0xffffff80
	s_nop 0
	global_load_lds_dwordx4 v[216:217], off offset:128
	s_waitcnt vmcnt(8)
	s_waitcnt lgkmcnt(0)
	s_barrier
	s_setprio 3
	s_waitcnt lgkmcnt(0)
	v_mfma_f32_16x16x32_bf16 v[62:65], v[98:101], v[154:157], v[62:65]
	v_mfma_f32_16x16x32_bf16 v[58:61], v[122:125], v[154:157], v[58:61]
	v_mfma_f32_16x16x32_bf16 v[46:49], v[98:101], v[170:173], v[46:49]
	v_mfma_f32_16x16x32_bf16 v[42:45], v[122:125], v[170:173], v[42:45]
	v_mfma_f32_16x16x32_bf16 v[30:33], v[98:101], v[178:181], v[30:33]
	v_mfma_f32_16x16x32_bf16 v[26:29], v[122:125], v[178:181], v[26:29]
	v_mfma_f32_16x16x32_bf16 v[14:17], v[98:101], v[186:189], v[14:17]
	v_mfma_f32_16x16x32_bf16 v[10:13], v[122:125], v[186:189], v[10:13]
	v_mfma_f32_16x16x32_bf16 v[62:65], v[110:113], v[166:169], v[62:65]
	v_mfma_f32_16x16x32_bf16 v[58:61], v[126:129], v[166:169], v[58:61]
	v_mfma_f32_16x16x32_bf16 v[46:49], v[110:113], v[174:177], v[46:49]
	v_mfma_f32_16x16x32_bf16 v[42:45], v[126:129], v[174:177], v[42:45]
	v_mfma_f32_16x16x32_bf16 v[30:33], v[110:113], v[182:185], v[30:33]
	v_mfma_f32_16x16x32_bf16 v[26:29], v[126:129], v[182:185], v[26:29]
	v_mfma_f32_16x16x32_bf16 v[14:17], v[110:113], v[206:209], v[14:17]
	v_mfma_f32_16x16x32_bf16 v[10:13], v[126:129], v[206:209], v[10:13]
	s_setprio 0
	s_setprio 3
	v_mfma_f32_16x16x32_bf16 v[54:57], v[138:141], v[154:157], v[54:57]
	v_mfma_f32_16x16x32_bf16 v[50:53], v[146:149], v[154:157], v[50:53]
	v_mfma_f32_16x16x32_bf16 v[38:41], v[138:141], v[170:173], v[38:41]
	v_mfma_f32_16x16x32_bf16 v[34:37], v[146:149], v[170:173], v[34:37]
	v_mfma_f32_16x16x32_bf16 v[22:25], v[138:141], v[178:181], v[22:25]
	v_mfma_f32_16x16x32_bf16 v[18:21], v[146:149], v[178:181], v[18:21]
	v_mfma_f32_16x16x32_bf16 v[6:9], v[138:141], v[186:189], v[6:9]
	v_mfma_f32_16x16x32_bf16 v[2:5], v[146:149], v[186:189], v[2:5]
	v_mfma_f32_16x16x32_bf16 v[54:57], v[142:145], v[166:169], v[54:57]
	v_mfma_f32_16x16x32_bf16 v[50:53], v[150:153], v[166:169], v[50:53]
	v_mfma_f32_16x16x32_bf16 v[38:41], v[142:145], v[174:177], v[38:41]
	v_mfma_f32_16x16x32_bf16 v[34:37], v[150:153], v[174:177], v[34:37]
	v_mfma_f32_16x16x32_bf16 v[22:25], v[142:145], v[182:185], v[22:25]
	v_mfma_f32_16x16x32_bf16 v[18:21], v[150:153], v[182:185], v[18:21]
	v_mfma_f32_16x16x32_bf16 v[6:9], v[142:145], v[206:209], v[6:9]
	v_mfma_f32_16x16x32_bf16 v[2:5], v[150:153], v[206:209], v[2:5]
	s_setprio 0
	s_barrier
	s_add_i32 s57, s57, 2
	s_add_u32 s55, s55, 0x100
	s_addc_u32 s56, s56, 0
	s_cmp_gt_u32 s57, 41
	s_mov_b64 s[20:21], s[22:23]
	s_cbranch_scc0 .LBB0_857
	s_and_b64 vcc, exec, s[16:17]
	s_cbranch_vccz .LBB0_860
	s_barrier

; #define PG8_GIDX(G_, PM_) do { if constexpr (Sched::GATHER) { _Pragma("unroll") for (int h_ = 0; h_ < 2; ++h_) _Pragma("unroll") for (int i_ = 0; i_ < 2; ++i_) { int R_, C_; stage_rc(tid * 16 + i_ * 8192, R_, C_); \
;         const int src_ = S.rowsrc[(PM_) * BM + h_ * HALF + R_]; G_[h_][i_] = (unsigned)(src_ * K + C_) * 2u; } } } while (0)
; #define PG8_STAGE_A(b, h, ptr, NX) do { if constexpr (Sched::GATHER) { unsigned gs_[2]; gs_[0] = ((NX) && last_) ? gN[h][0] : gA[h][0]; gs_[1] = ((NX) && last_) ? gN[h][1] : gA[h][1]; PG8_STAGE(PG8_SA(b, h), ptr, gs_); } \
;         else PG8_STAGE(PG8_SA(b, h), (ptr) + ((h) ? hstep : (size_t)0), voffA); } while (0)
; #define PG8_STAGE(bufoff, gbase, voff) do { _Pragma("unroll") for (int _i = 0; _i < 2; ++_i) \
;         __builtin_amdgcn_global_load_lds((const unsigned*)((const char*)(gbase) + (voff)[_i]), (PG8_LAS unsigned*)(lds + (bufoff) + ldsw + _i * 8192), 16, 0, 0); } while (0)
; #define PG8_WAIT_V(n) asm volatile("s_waitcnt vmcnt(" #n ")" ::: "memory")
; #define PG8_BAR __builtin_amdgcn_s_barrier()
; template <class Epi, class Sched, bool ALIGN_EPI = false, bool SP2 = false>
; __device__ __forceinline__ void gemm_phase(PG8_LAS unsigned char* lds, const Gemm g, const Sched& S, const Epi& E, const bool skip_epi = false) {
;     ...
;         PG8_STAGE(PG8_SB(1, 0), cB + kstep, voffB); PG8_STAGE_A(1, 0, cA + kstep, false); PG8_STAGE(PG8_SB(1, 1), cB + hstep + kstep, voffB);
;         PG8_WAIT_V(6); PG8_BAR;
;     } else {
;         PG8_STAGE(PG8_SB(0, 0), cB, voffB); PG8_STAGE_A(0, 0, cA, false); PG8_STAGE(PG8_SB(0, 1), cB + hstep, voffB); PG8_STAGE_A(0, 1, cA, false);
;         if (wr == 1) PG8_BAR;
;         PG8_WAIT_V(4); PG8_BAR;
;         PG8_STAGE(PG8_SB(1, 0), cB + kstep, voffB); PG8_STAGE_A(1, 0, cA + kstep, false); PG8_STAGE(PG8_SB(1, 1), cB + hstep + kstep, voffB);
;         PG8_WAIT_V(6); PG8_BAR;
;     }
;     for (;;) {
;         const bool has_next = S.next(ui + 1, nxt);
;         if (has_next) PG8_GIDX(gN, nxt.pm);
;         const char* nA = has_next ? (const char*)g.A + (size_t)nxt.pm * pmstepA + nxt.ko : cA; const char* nB = has_next ? (const char*)g.Bt + (size_t)nxt.pn * tstep + nxt.ko : cB;
.LBB0_938:
	s_lshl_b32 s8, s8, 5
	s_and_b32 s14, s8, 0x60
	s_mov_b64 s[8:9], 0x80
	s_add_i32 m0, s21, 0x18000
	v_lshl_add_u64 v[8:9], v[8:9], 0, s[8:9]
	s_lshl_b32 s11, s5, 13
	s_lshl_b32 s15, s14, 7
	s_waitcnt vmcnt(2)
	s_barrier
	global_load_lds_dwordx4 v[8:9], off
	v_lshl_add_u64 v[6:7], v[6:7], 0, s[8:9]
	s_add_i32 m0, s21, 0x1a000
	s_add_i32 s37, s21, 0x8000
	s_add_i32 s38, s21, 0xa000
	global_load_lds_dwordx4 v[6:7], off
	v_lshl_add_u64 v[2:3], v[2:3], 0, s[8:9]
	s_mov_b32 m0, s37
	s_add_u32 s12, s24, 0x40080
	global_load_lds_dwordx4 v[2:3], off
	v_lshl_add_u64 v[2:3], v[4:5], 0, s[8:9]
	s_mov_b32 m0, s38
	s_addc_u32 s13, s25, 0
	global_load_lds_dwordx4 v[2:3], off
	s_add_i32 m0, s21, 0x1c000
	s_nop 0
	global_load_lds_dwordx4 v134, s[12:13]
	s_add_i32 m0, s21, 0x1e000
	v_and_b32_e32 v1, 48, v11
	global_load_lds_dwordx4 v130, s[12:13]
	v_and_b32_e32 v2, 15, v11
	v_lshlrev_b32_e32 v3, 2, v11
	v_lshl_or_b32 v1, v2, 6, v1
	v_and_b32_e32 v3, 32, v3
	v_bitop3_b32 v4, v1, s11, v3 bitop3:0xde
	v_bitop3_b32 v1, s15, v1, v3 bitop3:0xf6
	v_bfe_u32 v3, v11, 2, 4
	v_lshlrev_b32_e32 v168, 4, v2
	v_lshl_or_b32 v167, s5, 6, v3
	v_and_b32_e32 v2, 48, v168
	v_mov_b32_e32 v3, v135
	v_lshl_add_u64 v[138:139], s[80:81], 0, v[2:3]
	v_lshlrev_b32_e32 v2, 14, v15
	v_and_b32_e32 v2, 0xffff8000, v2
	v_lshl_add_u32 v2, v14, 11, v2
	v_and_b32_e32 v3, 1, v15
	v_lshl_or_b32 v2, v3, 6, v2
	v_lshl_add_u32 v140, v16, 1, v2
	v_lshlrev_b32_e32 v2, 14, v10
	v_and_b32_e32 v2, 0xffff8000, v2
	s_waitcnt vmcnt(6)
	s_cmpk_lt_u32 s10, 0x100
	v_lshl_add_u32 v2, v12, 11, v2
	v_and_b32_e32 v3, 1, v10
	s_cselect_b64 s[10:11], -1, 0
	v_and_b32_e32 v5, 3, v11
	v_and_b32_e32 v6, 60, v11
	v_lshl_or_b32 v2, v3, 6, v2
	s_add_i32 s48, 0, 0x10000
	s_add_i32 s49, 0, 0x14000
	s_sext_i32_i8 s53, s4
	v_lshl_or_b32 v166, v5, 6, v6
	s_ashr_i32 s39, s97, 31
	v_lshl_or_b32 v169, v5, 3, s14
	v_mov_b32_e32 v141, v135
	v_lshl_add_u32 v142, v13, 1, v2
	v_mov_b32_e32 v143, v135
	v_mov_b64_e32 v[144:145], 0x300
	v_mov_b64_e32 v[146:147], 0x2ff
	v_add_u32_e32 v170, s48, v1
	v_add_u32_e32 v171, s49, v1
	v_add_u32_e32 v172, 0, v4
	v_mov_b32_e32 v173, 0x358637bd
	s_movk_i32 s52, 0x1800
	v_mov_b32_e32 v174, 0x3e000000
	v_mov_b32_e32 v175, 0x3e38aa3b
	s_barrier
	s_branch .LBB0_941

; #define PG8_GIDX(G_, PM_) do { if constexpr (Sched::GATHER) { _Pragma("unroll") for (int h_ = 0; h_ < 2; ++h_) _Pragma("unroll") for (int i_ = 0; i_ < 2; ++i_) { int R_, C_; stage_rc(tid * 16 + i_ * 8192, R_, C_); \
;         const int src_ = S.rowsrc[(PM_) * BM + h_ * HALF + R_]; G_[h_][i_] = (unsigned)(src_ * K + C_) * 2u; } } } while (0)
; #define PG8_STAGE_A(b, h, ptr, NX) do { if constexpr (Sched::GATHER) { unsigned gs_[2]; gs_[0] = ((NX) && last_) ? gN[h][0] : gA[h][0]; gs_[1] = ((NX) && last_) ? gN[h][1] : gA[h][1]; PG8_STAGE(PG8_SA(b, h), ptr, gs_); } \
;         else PG8_STAGE(PG8_SA(b, h), (ptr) + ((h) ? hstep : (size_t)0), voffA); } while (0)
; #define PG8_LDA(dst, b, h) do { _Pragma("unroll") for (int m = 0; m < 4; ++m) _Pragma("unroll") for (int k = 0; k < 2; ++k) dst[m][k] = *(const PG8_LAS bf16x8*)(lds + PG8_SA(b, h) + aoff + m * 2048 + k * 1024); } while (0)
; template <class Epi, class Sched, bool ALIGN_EPI = false, bool SP2 = false>
; __device__ __forceinline__ void gemm_phase(PG8_LAS unsigned char* lds, const Gemm g, const Sched& S, const Epi& E, const bool skip_epi = false) {
;     ...
;         const bool has_next = S.next(ui + 1, nxt);
;         if (has_next) PG8_GIDX(gN, nxt.pm);
;         const char* nA = has_next ? (const char*)g.A + (size_t)nxt.pm * pmstepA + nxt.ko : cA; const char* nB = has_next ? (const char*)g.Bt + (size_t)nxt.pn * tstep + nxt.ko : cB;
;         for (int t = 0; t < nt; t += 2) {
;             const bool last = (t == nt - 2); last_ = last && has_next;
;             const char* a1 = cA + (size_t)(t + 1) * kstep;
;             const char* a2 = last ? nA : cA + (size_t)(t + 2) * kstep; const char* b2 = last ? nB : cB + (size_t)(t + 2) * kstep;
;             const char* a3 = a2 + kstep; const char* b3 = b2 + kstep;
;             if (last && has_next) S.a_ready(nxt);
;             if constexpr (SP2) {
;             PG8_LDB(B0, 0, 0); PG8_LDB(B1, 0, 1); PG8_SCHED; PG8_LDA(At, 0, 0); PG8_STAGE_A(1, 1, a1, false);
;             PG8_WAIT_V(8); PG8_WAIT_L(0); PG8_BAR; PG8_MMA(0, 0, At, B0); PG8_MMA(0, 1, At, B1); PG8_BAR; PG8_SCHED;
;             PG8_LDA(At, 0, 1); PG8_STAGE(PG8_SB(0, 0), b2, voffB); PG8_STAGE(PG8_SB(0, 1), b2 + hstep, voffB); PG8_STAGE_A(0, 0, a2, true);
;             PG8_WAIT_V(8); PG8_WAIT_L(0); PG8_BAR; PG8_MMA(1, 0, At, B0); PG8_MMA(1, 1, At, B1); PG8_BAR; PG8_SCHED;
.LBB0_943:
	s_ashr_i32 s15, s14, 31
	s_lshl_b64 s[16:17], s[14:15], 19
	s_add_u32 s16, s86, s16
	s_addc_u32 s17, s87, s17
	s_and_b64 s[18:19], s[4:5], exec
	s_cselect_b32 s15, s17, s23
	s_cselect_b32 s54, s16, s22
	s_ashr_i32 s13, s12, 31
	s_lshl_b64 s[18:19], s[12:13], 19
	s_add_u32 s18, s2, s18
	s_addc_u32 s19, s3, s19
	s_and_b64 s[26:27], s[4:5], exec
	s_cselect_b32 s13, s19, s25
	s_cselect_b32 s55, s18, s24
	s_add_u32 s22, s22, 0x40080
	s_addc_u32 s23, s23, 0
	s_add_u32 s56, s24, 0x100
	s_addc_u32 s57, s25, 0
	s_mov_b32 s58, -2
	s_waitcnt vmcnt(0)
	ds_read_b128 v[148:151], v170
	ds_read_b128 v[152:155], v170 offset:1024
	ds_read_b128 v[156:159], v170 offset:2048
	ds_read_b128 v[160:163], v170 offset:3072
	ds_read_b128 v[176:179], v171
	ds_read_b128 v[180:183], v171 offset:1024
	ds_read_b128 v[184:187], v171 offset:2048
	ds_read_b128 v[188:191], v171 offset:3072
	s_add_u32 s24, s22, 0xfffc0080
	s_addc_u32 s25, s23, -1
	s_cmp_eq_u32 s58, 12
	s_cselect_b32 s27, s15, s25
	s_cselect_b32 s26, s54, s24
	s_cselect_b32 s25, s13, s57
	s_cselect_b32 s24, s55, s56
	s_add_i32 m0, s21, 0xc000
	ds_read_b128 v[192:195], v172
	ds_read_b128 v[196:199], v172 offset:1024
	ds_read_b128 v[200:203], v172 offset:2048
	ds_read_b128 v[204:207], v172 offset:3072
	ds_read_b128 v[208:211], v172 offset:4096
	ds_read_b128 v[212:215], v172 offset:5120
	ds_read_b128 v[216:219], v172 offset:6144
	ds_read_b128 v[220:223], v172 offset:7168
	global_load_lds_dwordx4 v140, s[22:23]
	s_add_i32 m0, s21, 0xe000
	s_nop 0
	global_load_lds_dwordx4 v142, s[22:23]
	s_waitcnt vmcnt(8)
	s_waitcnt lgkmcnt(0)
	s_barrier
	s_setprio 3
	s_waitcnt lgkmcnt(0)
	v_mfma_f32_16x16x32_bf16 v[126:129], v[148:151], v[192:195], 0
	v_mfma_f32_16x16x32_bf16 v[122:125], v[156:159], v[192:195], 0
	v_mfma_f32_16x16x32_bf16 v[114:117], v[148:151], v[200:203], 0
	v_mfma_f32_16x16x32_bf16 v[106:109], v[156:159], v[200:203], 0
	v_mfma_f32_16x16x32_bf16 v[98:101], v[148:151], v[208:211], 0
	v_mfma_f32_16x16x32_bf16 v[90:93], v[156:159], v[208:211], 0
	v_mfma_f32_16x16x32_bf16 v[82:85], v[148:151], v[216:219], 0
	v_mfma_f32_16x16x32_bf16 v[74:77], v[156:159], v[216:219], 0
	v_mfma_f32_16x16x32_bf16 v[126:129], v[152:155], v[196:199], v[126:129]
	v_mfma_f32_16x16x32_bf16 v[122:125], v[160:163], v[196:199], v[122:125]
	v_mfma_f32_16x16x32_bf16 v[114:117], v[152:155], v[204:207], v[114:117]
	v_mfma_f32_16x16x32_bf16 v[106:109], v[160:163], v[204:207], v[106:109]
	v_mfma_f32_16x16x32_bf16 v[98:101], v[152:155], v[212:215], v[98:101]
	v_mfma_f32_16x16x32_bf16 v[90:93], v[160:163], v[212:215], v[90:93]
	v_mfma_f32_16x16x32_bf16 v[82:85], v[152:155], v[220:223], v[82:85]
	v_mfma_f32_16x16x32_bf16 v[74:77], v[160:163], v[220:223], v[74:77]
	s_setprio 0
	s_setprio 3
	v_mfma_f32_16x16x32_bf16 v[118:121], v[176:179], v[192:195], 0
	v_mfma_f32_16x16x32_bf16 v[110:113], v[184:187], v[192:195], 0
	v_mfma_f32_16x16x32_bf16 v[102:105], v[176:179], v[200:203], 0
	v_mfma_f32_16x16x32_bf16 v[94:97], v[184:187], v[200:203], 0
	v_mfma_f32_16x16x32_bf16 v[86:89], v[176:179], v[208:211], 0
	v_mfma_f32_16x16x32_bf16 v[78:81], v[184:187], v[208:211], 0
	v_mfma_f32_16x16x32_bf16 v[70:73], v[176:179], v[216:219], 0
	v_mfma_f32_16x16x32_bf16 v[66:69], v[184:187], v[216:219], 0
	v_mfma_f32_16x16x32_bf16 v[118:121], v[180:183], v[196:199], v[118:121]
	v_mfma_f32_16x16x32_bf16 v[110:113], v[188:191], v[196:199], v[110:113]
	v_mfma_f32_16x16x32_bf16 v[102:105], v[180:183], v[204:207], v[102:105]
	v_mfma_f32_16x16x32_bf16 v[94:97], v[188:191], v[204:207], v[94:97]
	v_mfma_f32_16x16x32_bf16 v[86:89], v[180:183], v[212:215], v[86:89]
	v_mfma_f32_16x16x32_bf16 v[78:81], v[188:191], v[212:215], v[78:81]
	v_mfma_f32_16x16x32_bf16 v[70:73], v[180:183], v[220:223], v[70:73]
	v_mfma_f32_16x16x32_bf16 v[66:69], v[188:191], v[220:223], v[66:69]
	s_setprio 0
	s_barrier
	s_add_i32 s59, s48, s28
	v_lshl_add_u64 v[164:165], s[24:25], 0, v[134:135]
	s_mov_b32 m0, s59
	ds_read_b128 v[192:195], v172 offset:16384
	ds_read_b128 v[196:199], v172 offset:17408
	ds_read_b128 v[200:203], v172 offset:18432
	ds_read_b128 v[204:207], v172 offset:19456
	ds_read_b128 v[208:211], v172 offset:20480
	ds_read_b128 v[212:215], v172 offset:21504
	ds_read_b128 v[216:219], v172 offset:22528
	ds_read_b128 v[220:223], v172 offset:23552
	global_load_lds_dwordx4 v[164:165], off
	s_add_i32 m0, s59, 0x2000
	s_add_u32 s60, s24, 0x40000
	v_lshl_add_u64 v[224:225], s[24:25], 0, v[130:131]
	s_addc_u32 s61, s25, 0
	s_add_i32 s59, s49, s28
	global_load_lds_dwordx4 v[224:225], off
	s_mov_b32 m0, s59
	v_lshl_add_u64 v[230:231], s[26:27], 0, v[132:133]
	global_load_lds_dwordx4 v134, s[60:61]
	s_add_i32 m0, s59, 0x2000
	s_nop 0
	global_load_lds_dwordx4 v130, s[60:61]
	v_lshl_add_u64 v[226:227], s[26:27], 0, v[136:137]
	s_mov_b32 m0, s21
	s_nop 0
	global_load_lds_dwordx4 v[226:227], off
	s_mov_b32 m0, s31
	s_nop 0
	global_load_lds_dwordx4 v[230:231], off
	s_waitcnt vmcnt(8)
	s_waitcnt lgkmcnt(0)
	s_barrier
; #define PG8_STAGE_A(b, h, ptr, NX) do { if constexpr (Sched::GATHER) { unsigned gs_[2]; gs_[0] = ((NX) && last_) ? gN[h][0] : gA[h][0]; gs_[1] = ((NX) && last_) ? gN[h][1] : gA[h][1]; PG8_STAGE(PG8_SA(b, h), ptr, gs_); } \
;         else PG8_STAGE(PG8_SA(b, h), (ptr) + ((h) ? hstep : (size_t)0), voffA); } while (0)
; #define PG8_LDA(dst, b, h) do { _Pragma("unroll") for (int m = 0; m < 4; ++m) _Pragma("unroll") for (int k = 0; k < 2; ++k) dst[m][k] = *(const PG8_LAS bf16x8*)(lds + PG8_SA(b, h) + aoff + m * 2048 + k * 1024); } while (0)
; #define PG8_LDB(dst, b, h) do { _Pragma("unroll") for (int n = 0; n < 2; ++n) _Pragma("unroll") for (int k = 0; k < 2; ++k) dst[n][k] = *(const PG8_LAS bf16x8*)(lds + PG8_SB(b, h) + boff + n * 2048 + k * 1024); } while (0)
; #define PG8_MMA(ai, bj, At, Bt) do { __builtin_amdgcn_s_setprio(1); _Pragma("unroll") for (int m = 0; m < 4; ++m) _Pragma("unroll") for (int n = 0; n < 2; ++n) _Pragma("unroll") for (int k = 0; k < 2; ++k) \
;         acc[ai][bj][m][n] = __builtin_amdgcn_mfma_f32_16x16x32_bf16(Bt[n][k], At[m][k], acc[ai][bj][m][n], 0, 0, 0); __builtin_amdgcn_s_setprio(0); } while (0)
; #define PG8_WAIT_V(n) asm volatile("s_waitcnt vmcnt(" #n ")" ::: "memory")
; #define PG8_WAIT_L(n) asm volatile("s_waitcnt lgkmcnt(" #n ")" ::: "memory")
; #define PG8_BAR __builtin_amdgcn_s_barrier()
; #define PG8_SCHED __builtin_amdgcn_sched_barrier(0)
; template <class Epi, class Sched, bool ALIGN_EPI = false, bool SP2 = false>
; __device__ __forceinline__ void gemm_phase(PG8_LAS unsigned char* lds, const Gemm g, const Sched& S, const Epi& E, const bool skip_epi = false) {
;     ...
;             PG8_WAIT_V(8); PG8_WAIT_L(0); PG8_BAR; PG8_MMA(1, 0, At, B0); PG8_MMA(1, 1, At, B1); PG8_BAR; PG8_SCHED;
;             PG8_LDB(B0, 1, 0); PG8_LDB(B1, 1, 1); PG8_SCHED; PG8_LDA(At, 1, 0); PG8_STAGE_A(0, 1, a2, true);
;             PG8_WAIT_V(8); PG8_WAIT_L(0); PG8_BAR; PG8_MMA(0, 0, At, B0); PG8_MMA(0, 1, At, B1); PG8_BAR; PG8_SCHED;
	s_setprio 3
	s_waitcnt lgkmcnt(0)
	v_mfma_f32_16x16x32_bf16 v[62:65], v[148:151], v[192:195], 0
	v_mfma_f32_16x16x32_bf16 v[58:61], v[156:159], v[192:195], 0
	v_mfma_f32_16x16x32_bf16 v[50:53], v[148:151], v[200:203], 0
	v_mfma_f32_16x16x32_bf16 v[42:45], v[156:159], v[200:203], 0
	v_mfma_f32_16x16x32_bf16 v[34:37], v[148:151], v[208:211], 0
	v_mfma_f32_16x16x32_bf16 v[26:29], v[156:159], v[208:211], 0
	v_mfma_f32_16x16x32_bf16 v[18:21], v[148:151], v[216:219], 0
	v_mfma_f32_16x16x32_bf16 v[10:13], v[156:159], v[216:219], 0
	v_mfma_f32_16x16x32_bf16 v[62:65], v[152:155], v[196:199], v[62:65]
	v_mfma_f32_16x16x32_bf16 v[58:61], v[160:163], v[196:199], v[58:61]
	v_mfma_f32_16x16x32_bf16 v[50:53], v[152:155], v[204:207], v[50:53]
	v_mfma_f32_16x16x32_bf16 v[42:45], v[160:163], v[204:207], v[42:45]
	v_mfma_f32_16x16x32_bf16 v[34:37], v[152:155], v[212:215], v[34:37]
	v_mfma_f32_16x16x32_bf16 v[26:29], v[160:163], v[212:215], v[26:29]
	v_mfma_f32_16x16x32_bf16 v[18:21], v[152:155], v[220:223], v[18:21]
	v_mfma_f32_16x16x32_bf16 v[10:13], v[160:163], v[220:223], v[10:13]
	s_setprio 0
	s_setprio 3
	v_mfma_f32_16x16x32_bf16 v[54:57], v[176:179], v[192:195], 0
	v_mfma_f32_16x16x32_bf16 v[46:49], v[184:187], v[192:195], 0
	v_mfma_f32_16x16x32_bf16 v[38:41], v[176:179], v[200:203], 0
	v_mfma_f32_16x16x32_bf16 v[30:33], v[184:187], v[200:203], 0
	v_mfma_f32_16x16x32_bf16 v[22:25], v[176:179], v[208:211], 0
	v_mfma_f32_16x16x32_bf16 v[14:17], v[184:187], v[208:211], 0
	v_mfma_f32_16x16x32_bf16 v[6:9], v[176:179], v[216:219], 0
	v_mfma_f32_16x16x32_bf16 v[2:5], v[184:187], v[216:219], 0
	v_mfma_f32_16x16x32_bf16 v[54:57], v[180:183], v[196:199], v[54:57]
	v_mfma_f32_16x16x32_bf16 v[46:49], v[188:191], v[196:199], v[46:49]
	v_mfma_f32_16x16x32_bf16 v[38:41], v[180:183], v[204:207], v[38:41]
	v_mfma_f32_16x16x32_bf16 v[30:33], v[188:191], v[204:207], v[30:33]
	v_mfma_f32_16x16x32_bf16 v[22:25], v[180:183], v[212:215], v[22:25]
	v_mfma_f32_16x16x32_bf16 v[14:17], v[188:191], v[212:215], v[14:17]
	v_mfma_f32_16x16x32_bf16 v[6:9], v[180:183], v[220:223], v[6:9]
	v_mfma_f32_16x16x32_bf16 v[2:5], v[188:191], v[220:223], v[2:5]
	s_setprio 0
	s_barrier
	s_add_i32 s59, 0, 0x18000
	s_add_i32 s60, 0, 0x1c000
	v_add_u32_e32 v160, s59, v1
	v_add_u32_e32 v188, s60, v1
	ds_read_b128 v[148:151], v160
	ds_read_b128 v[152:155], v160 offset:1024
	ds_read_b128 v[156:159], v160 offset:2048
	ds_read_b128 v[160:163], v160 offset:3072
	ds_read_b128 v[176:179], v188
	ds_read_b128 v[180:183], v188 offset:1024
	ds_read_b128 v[184:187], v188 offset:2048
	ds_read_b128 v[188:191], v188 offset:3072
	s_add_u32 s26, s26, 0x40000
	s_addc_u32 s27, s27, 0
	s_mov_b32 m0, s34
	ds_read_b128 v[192:195], v172 offset:32768
	ds_read_b128 v[196:199], v172 offset:33792
	ds_read_b128 v[200:203], v172 offset:34816
	ds_read_b128 v[204:207], v172 offset:35840
	ds_read_b128 v[208:211], v172 offset:36864
	ds_read_b128 v[212:215], v172 offset:37888
	ds_read_b128 v[216:219], v172 offset:38912
	ds_read_b128 v[220:223], v172 offset:39936
	global_load_lds_dwordx4 v136, s[26:27]
	s_mov_b32 m0, s35
	s_nop 0
	global_load_lds_dwordx4 v132, s[26:27]
	s_waitcnt vmcnt(8)
	s_waitcnt lgkmcnt(0)
	s_barrier
	s_setprio 3
	s_waitcnt lgkmcnt(0)
	v_mfma_f32_16x16x32_bf16 v[126:129], v[148:151], v[192:195], v[126:129]
	v_mfma_f32_16x16x32_bf16 v[122:125], v[156:159], v[192:195], v[122:125]
	v_mfma_f32_16x16x32_bf16 v[114:117], v[148:151], v[200:203], v[114:117]
	v_mfma_f32_16x16x32_bf16 v[106:109], v[156:159], v[200:203], v[106:109]
	v_mfma_f32_16x16x32_bf16 v[98:101], v[148:151], v[208:211], v[98:101]
	v_mfma_f32_16x16x32_bf16 v[90:93], v[156:159], v[208:211], v[90:93]
	v_mfma_f32_16x16x32_bf16 v[82:85], v[148:151], v[216:219], v[82:85]
	v_mfma_f32_16x16x32_bf16 v[74:77], v[156:159], v[216:219], v[74:77]
	v_mfma_f32_16x16x32_bf16 v[126:129], v[152:155], v[196:199], v[126:129]
	v_mfma_f32_16x16x32_bf16 v[122:125], v[160:163], v[196:199], v[122:125]
	v_mfma_f32_16x16x32_bf16 v[114:117], v[152:155], v[204:207], v[114:117]
	v_mfma_f32_16x16x32_bf16 v[106:109], v[160:163], v[204:207], v[106:109]
	v_mfma_f32_16x16x32_bf16 v[98:101], v[152:155], v[212:215], v[98:101]
	v_mfma_f32_16x16x32_bf16 v[90:93], v[160:163], v[212:215], v[90:93]
	v_mfma_f32_16x16x32_bf16 v[82:85], v[152:155], v[220:223], v[82:85]
	v_mfma_f32_16x16x32_bf16 v[74:77], v[160:163], v[220:223], v[74:77]
	s_setprio 0
	s_setprio 3
	v_mfma_f32_16x16x32_bf16 v[118:121], v[176:179], v[192:195], v[118:121]
	v_mfma_f32_16x16x32_bf16 v[110:113], v[184:187], v[192:195], v[110:113]
	v_mfma_f32_16x16x32_bf16 v[102:105], v[176:179], v[200:203], v[102:105]
	v_mfma_f32_16x16x32_bf16 v[94:97], v[184:187], v[200:203], v[94:97]
	v_mfma_f32_16x16x32_bf16 v[86:89], v[176:179], v[208:211], v[86:89]
	v_mfma_f32_16x16x32_bf16 v[78:81], v[184:187], v[208:211], v[78:81]
	v_mfma_f32_16x16x32_bf16 v[70:73], v[176:179], v[216:219], v[70:73]
	v_mfma_f32_16x16x32_bf16 v[66:69], v[184:187], v[216:219], v[66:69]
	v_mfma_f32_16x16x32_bf16 v[118:121], v[180:183], v[196:199], v[118:121]
	v_mfma_f32_16x16x32_bf16 v[110:113], v[188:191], v[196:199], v[110:113]
	v_mfma_f32_16x16x32_bf16 v[102:105], v[180:183], v[204:207], v[102:105]
	v_mfma_f32_16x16x32_bf16 v[94:97], v[188:191], v[204:207], v[94:97]
	v_mfma_f32_16x16x32_bf16 v[86:89], v[180:183], v[212:215], v[86:89]
	v_mfma_f32_16x16x32_bf16 v[78:81], v[188:191], v[212:215], v[78:81]
	v_mfma_f32_16x16x32_bf16 v[70:73], v[180:183], v[220:223], v[70:73]
	v_mfma_f32_16x16x32_bf16 v[66:69], v[188:191], v[220:223], v[66:69]
	s_setprio 0
	s_barrier
; #define PG8_STAGE_A(b, h, ptr, NX) do { if constexpr (Sched::GATHER) { unsigned gs_[2]; gs_[0] = ((NX) && last_) ? gN[h][0] : gA[h][0]; gs_[1] = ((NX) && last_) ? gN[h][1] : gA[h][1]; PG8_STAGE(PG8_SA(b, h), ptr, gs_); } \
;         else PG8_STAGE(PG8_SA(b, h), (ptr) + ((h) ? hstep : (size_t)0), voffA); } while (0)
; #define PG8_STAGE(bufoff, gbase, voff) do { _Pragma("unroll") for (int _i = 0; _i < 2; ++_i) \
;         __builtin_amdgcn_global_load_lds((const unsigned*)((const char*)(gbase) + (voff)[_i]), (PG8_LAS unsigned*)(lds + (bufoff) + ldsw + _i * 8192), 16, 0, 0); } while (0)
; #define PG8_LDA(dst, b, h) do { _Pragma("unroll") for (int m = 0; m < 4; ++m) _Pragma("unroll") for (int k = 0; k < 2; ++k) dst[m][k] = *(const PG8_LAS bf16x8*)(lds + PG8_SA(b, h) + aoff + m * 2048 + k * 1024); } while (0)
; #define PG8_LDB(dst, b, h) do { _Pragma("unroll") for (int n = 0; n < 2; ++n) _Pragma("unroll") for (int k = 0; k < 2; ++k) dst[n][k] = *(const PG8_LAS bf16x8*)(lds + PG8_SB(b, h) + boff + n * 2048 + k * 1024); } while (0)
; #define PG8_WAIT_V(n) asm volatile("s_waitcnt vmcnt(" #n ")" ::: "memory")
; #define PG8_WAIT_L(n) asm volatile("s_waitcnt lgkmcnt(" #n ")" ::: "memory")
; #define PG8_BAR __builtin_amdgcn_s_barrier()
; template <class Epi, class Sched, bool ALIGN_EPI = false, bool SP2 = false>
; __device__ __forceinline__ void gemm_phase(PG8_LAS unsigned char* lds, const Gemm g, const Sched& S, const Epi& E, const bool skip_epi = false) {
;     ...
;             const bool last = (t == nt - 2); last_ = last && has_next;
;             const char* a1 = cA + (size_t)(t + 1) * kstep;
;             const char* a2 = last ? nA : cA + (size_t)(t + 2) * kstep; const char* b2 = last ? nB : cB + (size_t)(t + 2) * kstep;
;             const char* a3 = a2 + kstep; const char* b3 = b2 + kstep;
;             if (last && has_next) S.a_ready(nxt);
;             if constexpr (SP2) {
;             PG8_LDB(B0, 0, 0); PG8_LDB(B1, 0, 1); PG8_SCHED; PG8_LDA(At, 0, 0); PG8_STAGE_A(1, 1, a1, false);
;             PG8_WAIT_V(8); PG8_WAIT_L(0); PG8_BAR; PG8_MMA(0, 0, At, B0); PG8_MMA(0, 1, At, B1); PG8_BAR; PG8_SCHED;
;     ...
;             PG8_LDA(At, 1, 1); PG8_STAGE(PG8_SB(1, 0), b3, voffB); PG8_STAGE(PG8_SB(1, 1), b3 + hstep, voffB); PG8_STAGE_A(1, 0, a3, true);
;             PG8_WAIT_V(8); PG8_WAIT_L(0); PG8_BAR; PG8_MMA(1, 0, At, B0); PG8_MMA(1, 1, At, B1); PG8_BAR; PG8_SCHED;
	s_add_i32 s26, s59, s28
	s_add_i32 m0, s26, 0xffffff80
	ds_read_b128 v[192:195], v172 offset:49152
	ds_read_b128 v[196:199], v172 offset:50176
	ds_read_b128 v[200:203], v172 offset:51200
	ds_read_b128 v[204:207], v172 offset:52224
	ds_read_b128 v[208:211], v172 offset:53248
	ds_read_b128 v[212:215], v172 offset:54272
	ds_read_b128 v[216:219], v172 offset:55296
	ds_read_b128 v[220:223], v172 offset:56320
	global_load_lds_dwordx4 v[164:165], off offset:128
	s_add_i32 m0, s26, 0x1f80
	s_add_u32 s24, s24, 0x40080
	s_addc_u32 s25, s25, 0
	s_add_i32 s26, s60, s28
	global_load_lds_dwordx4 v[224:225], off offset:128
	s_mov_b32 m0, s26
	s_nop 0
	global_load_lds_dwordx4 v134, s[24:25]
	s_add_i32 m0, s26, 0x2000
	s_nop 0
	global_load_lds_dwordx4 v130, s[24:25]
	s_add_i32 m0, s37, 0xffffff80
	s_nop 0
	global_load_lds_dwordx4 v[226:227], off offset:128
	s_add_i32 m0, s38, 0xffffff80
	s_nop 0
	global_load_lds_dwordx4 v[230:231], off offset:128
	s_waitcnt vmcnt(8)
	s_waitcnt lgkmcnt(0)
	s_barrier
	s_setprio 3
	s_waitcnt lgkmcnt(0)
	v_mfma_f32_16x16x32_bf16 v[62:65], v[148:151], v[192:195], v[62:65]
	v_mfma_f32_16x16x32_bf16 v[58:61], v[156:159], v[192:195], v[58:61]
	v_mfma_f32_16x16x32_bf16 v[50:53], v[148:151], v[200:203], v[50:53]
	v_mfma_f32_16x16x32_bf16 v[42:45], v[156:159], v[200:203], v[42:45]
	v_mfma_f32_16x16x32_bf16 v[34:37], v[148:151], v[208:211], v[34:37]
	v_mfma_f32_16x16x32_bf16 v[26:29], v[156:159], v[208:211], v[26:29]
	v_mfma_f32_16x16x32_bf16 v[18:21], v[148:151], v[216:219], v[18:21]
	v_mfma_f32_16x16x32_bf16 v[10:13], v[156:159], v[216:219], v[10:13]
	v_mfma_f32_16x16x32_bf16 v[62:65], v[152:155], v[196:199], v[62:65]
	v_mfma_f32_16x16x32_bf16 v[58:61], v[160:163], v[196:199], v[58:61]
	v_mfma_f32_16x16x32_bf16 v[50:53], v[152:155], v[204:207], v[50:53]
	v_mfma_f32_16x16x32_bf16 v[42:45], v[160:163], v[204:207], v[42:45]
	v_mfma_f32_16x16x32_bf16 v[34:37], v[152:155], v[212:215], v[34:37]
	v_mfma_f32_16x16x32_bf16 v[26:29], v[160:163], v[212:215], v[26:29]
	v_mfma_f32_16x16x32_bf16 v[18:21], v[152:155], v[220:223], v[18:21]
	v_mfma_f32_16x16x32_bf16 v[10:13], v[160:163], v[220:223], v[10:13]
	s_setprio 0
	s_setprio 3
	v_mfma_f32_16x16x32_bf16 v[54:57], v[176:179], v[192:195], v[54:57]
	v_mfma_f32_16x16x32_bf16 v[46:49], v[184:187], v[192:195], v[46:49]
	v_mfma_f32_16x16x32_bf16 v[38:41], v[176:179], v[200:203], v[38:41]
	v_mfma_f32_16x16x32_bf16 v[30:33], v[184:187], v[200:203], v[30:33]
	v_mfma_f32_16x16x32_bf16 v[22:25], v[176:179], v[208:211], v[22:25]
	v_mfma_f32_16x16x32_bf16 v[14:17], v[184:187], v[208:211], v[14:17]
	v_mfma_f32_16x16x32_bf16 v[6:9], v[176:179], v[216:219], v[6:9]
	v_mfma_f32_16x16x32_bf16 v[2:5], v[184:187], v[216:219], v[2:5]
	v_mfma_f32_16x16x32_bf16 v[54:57], v[180:183], v[196:199], v[54:57]
	v_mfma_f32_16x16x32_bf16 v[46:49], v[188:191], v[196:199], v[46:49]
	v_mfma_f32_16x16x32_bf16 v[38:41], v[180:183], v[204:207], v[38:41]
	v_mfma_f32_16x16x32_bf16 v[30:33], v[188:191], v[204:207], v[30:33]
	v_mfma_f32_16x16x32_bf16 v[22:25], v[180:183], v[212:215], v[22:25]
	v_mfma_f32_16x16x32_bf16 v[14:17], v[188:191], v[212:215], v[14:17]
	v_mfma_f32_16x16x32_bf16 v[6:9], v[180:183], v[220:223], v[6:9]
	v_mfma_f32_16x16x32_bf16 v[2:5], v[188:191], v[220:223], v[2:5]
	s_setprio 0
	s_barrier
	s_add_i32 s58, s58, 2
	s_add_u32 s22, s22, 0x100
	s_addc_u32 s23, s23, 0
	s_add_u32 s56, s56, 0x100
	s_addc_u32 s57, s57, 0
	s_cmp_gt_u32 s58, 13
.LBB0_944:
	ds_read_b128 v[148:151], v170
	ds_read_b128 v[152:155], v170 offset:1024
	ds_read_b128 v[156:159], v170 offset:2048
	ds_read_b128 v[160:163], v170 offset:3072
	ds_read_b128 v[176:179], v171
	ds_read_b128 v[180:183], v171 offset:1024
	ds_read_b128 v[184:187], v171 offset:2048
	ds_read_b128 v[188:191], v171 offset:3072
	s_add_u32 s24, s22, 0xfffc0080
	s_addc_u32 s25, s23, -1
	s_cmp_eq_u32 s58, 12
	s_cselect_b32 s27, s15, s25
	s_cselect_b32 s26, s54, s24
	s_cselect_b32 s25, s13, s57
	s_cselect_b32 s24, s55, s56
	s_add_i32 m0, s21, 0xc000
	ds_read_b128 v[192:195], v172
	ds_read_b128 v[196:199], v172 offset:1024
	ds_read_b128 v[200:203], v172 offset:2048
	ds_read_b128 v[204:207], v172 offset:3072
	ds_read_b128 v[208:211], v172 offset:4096
	ds_read_b128 v[212:215], v172 offset:5120
	ds_read_b128 v[216:219], v172 offset:6144
	ds_read_b128 v[220:223], v172 offset:7168
	global_load_lds_dwordx4 v140, s[22:23]
	s_add_i32 m0, s21, 0xe000
	s_nop 0
	global_load_lds_dwordx4 v142, s[22:23]
	s_waitcnt vmcnt(8)
	s_waitcnt lgkmcnt(0)
	s_barrier
; #define PG8_STAGE_A(b, h, ptr, NX) do { if constexpr (Sched::GATHER) { unsigned gs_[2]; gs_[0] = ((NX) && last_) ? gN[h][0] : gA[h][0]; gs_[1] = ((NX) && last_) ? gN[h][1] : gA[h][1]; PG8_STAGE(PG8_SA(b, h), ptr, gs_); } \
;         else PG8_STAGE(PG8_SA(b, h), (ptr) + ((h) ? hstep : (size_t)0), voffA); } while (0)
; #define PG8_STAGE(bufoff, gbase, voff) do { _Pragma("unroll") for (int _i = 0; _i < 2; ++_i) \
;         __builtin_amdgcn_global_load_lds((const unsigned*)((const char*)(gbase) + (voff)[_i]), (PG8_LAS unsigned*)(lds + (bufoff) + ldsw + _i * 8192), 16, 0, 0); } while (0)
; #define PG8_LDA(dst, b, h) do { _Pragma("unroll") for (int m = 0; m < 4; ++m) _Pragma("unroll") for (int k = 0; k < 2; ++k) dst[m][k] = *(const PG8_LAS bf16x8*)(lds + PG8_SA(b, h) + aoff + m * 2048 + k * 1024); } while (0)
; #define PG8_LDB(dst, b, h) do { _Pragma("unroll") for (int n = 0; n < 2; ++n) _Pragma("unroll") for (int k = 0; k < 2; ++k) dst[n][k] = *(const PG8_LAS bf16x8*)(lds + PG8_SB(b, h) + boff + n * 2048 + k * 1024); } while (0)
; #define PG8_MMA(ai, bj, At, Bt) do { __builtin_amdgcn_s_setprio(1); _Pragma("unroll") for (int m = 0; m < 4; ++m) _Pragma("unroll") for (int n = 0; n < 2; ++n) _Pragma("unroll") for (int k = 0; k < 2; ++k) \
;         acc[ai][bj][m][n] = __builtin_amdgcn_mfma_f32_16x16x32_bf16(Bt[n][k], At[m][k], acc[ai][bj][m][n], 0, 0, 0); __builtin_amdgcn_s_setprio(0); } while (0)
; #define PG8_WAIT_V(n) asm volatile("s_waitcnt vmcnt(" #n ")" ::: "memory")
; #define PG8_WAIT_L(n) asm volatile("s_waitcnt lgkmcnt(" #n ")" ::: "memory")
; #define PG8_BAR __builtin_amdgcn_s_barrier()
; #define PG8_SCHED __builtin_amdgcn_sched_barrier(0)
; template <class Epi, class Sched, bool ALIGN_EPI = false, bool SP2 = false>
; __device__ __forceinline__ void gemm_phase(PG8_LAS unsigned char* lds, const Gemm g, const Sched& S, const Epi& E, const bool skip_epi = false) {
;     ...
;             PG8_LDB(B0, 0, 0); PG8_LDB(B1, 0, 1); PG8_SCHED; PG8_LDA(At, 0, 0); PG8_STAGE_A(1, 1, a1, false);
;             PG8_WAIT_V(8); PG8_WAIT_L(0); PG8_BAR; PG8_MMA(0, 0, At, B0); PG8_MMA(0, 1, At, B1); PG8_BAR; PG8_SCHED;
;             PG8_LDA(At, 0, 1); PG8_STAGE(PG8_SB(0, 0), b2, voffB); PG8_STAGE(PG8_SB(0, 1), b2 + hstep, voffB); PG8_STAGE_A(0, 0, a2, true);
;             PG8_WAIT_V(8); PG8_WAIT_L(0); PG8_BAR; PG8_MMA(1, 0, At, B0); PG8_MMA(1, 1, At, B1); PG8_BAR; PG8_SCHED;
	s_setprio 3
	s_waitcnt lgkmcnt(0)
	v_mfma_f32_16x16x32_bf16 v[126:129], v[148:151], v[192:195], v[126:129]
	v_mfma_f32_16x16x32_bf16 v[122:125], v[156:159], v[192:195], v[122:125]
	v_mfma_f32_16x16x32_bf16 v[114:117], v[148:151], v[200:203], v[114:117]
	v_mfma_f32_16x16x32_bf16 v[106:109], v[156:159], v[200:203], v[106:109]
	v_mfma_f32_16x16x32_bf16 v[98:101], v[148:151], v[208:211], v[98:101]
	v_mfma_f32_16x16x32_bf16 v[90:93], v[156:159], v[208:211], v[90:93]
	v_mfma_f32_16x16x32_bf16 v[82:85], v[148:151], v[216:219], v[82:85]
	v_mfma_f32_16x16x32_bf16 v[74:77], v[156:159], v[216:219], v[74:77]
	v_mfma_f32_16x16x32_bf16 v[126:129], v[152:155], v[196:199], v[126:129]
	v_mfma_f32_16x16x32_bf16 v[122:125], v[160:163], v[196:199], v[122:125]
	v_mfma_f32_16x16x32_bf16 v[114:117], v[152:155], v[204:207], v[114:117]
	v_mfma_f32_16x16x32_bf16 v[106:109], v[160:163], v[204:207], v[106:109]
	v_mfma_f32_16x16x32_bf16 v[98:101], v[152:155], v[212:215], v[98:101]
	v_mfma_f32_16x16x32_bf16 v[90:93], v[160:163], v[212:215], v[90:93]
	v_mfma_f32_16x16x32_bf16 v[82:85], v[152:155], v[220:223], v[82:85]
	v_mfma_f32_16x16x32_bf16 v[74:77], v[160:163], v[220:223], v[74:77]
	s_setprio 0
	s_setprio 3
	v_mfma_f32_16x16x32_bf16 v[118:121], v[176:179], v[192:195], v[118:121]
	v_mfma_f32_16x16x32_bf16 v[110:113], v[184:187], v[192:195], v[110:113]
	v_mfma_f32_16x16x32_bf16 v[102:105], v[176:179], v[200:203], v[102:105]
	v_mfma_f32_16x16x32_bf16 v[94:97], v[184:187], v[200:203], v[94:97]
	v_mfma_f32_16x16x32_bf16 v[86:89], v[176:179], v[208:211], v[86:89]
	v_mfma_f32_16x16x32_bf16 v[78:81], v[184:187], v[208:211], v[78:81]
	v_mfma_f32_16x16x32_bf16 v[70:73], v[176:179], v[216:219], v[70:73]
	v_mfma_f32_16x16x32_bf16 v[66:69], v[184:187], v[216:219], v[66:69]
	v_mfma_f32_16x16x32_bf16 v[118:121], v[180:183], v[196:199], v[118:121]
	v_mfma_f32_16x16x32_bf16 v[110:113], v[188:191], v[196:199], v[110:113]
	v_mfma_f32_16x16x32_bf16 v[102:105], v[180:183], v[204:207], v[102:105]
	v_mfma_f32_16x16x32_bf16 v[94:97], v[188:191], v[204:207], v[94:97]
	v_mfma_f32_16x16x32_bf16 v[86:89], v[180:183], v[212:215], v[86:89]
	v_mfma_f32_16x16x32_bf16 v[78:81], v[188:191], v[212:215], v[78:81]
	v_mfma_f32_16x16x32_bf16 v[70:73], v[180:183], v[220:223], v[70:73]
	v_mfma_f32_16x16x32_bf16 v[66:69], v[188:191], v[220:223], v[66:69]
	s_setprio 0
	s_barrier
	s_add_i32 s59, s48, s28
	v_lshl_add_u64 v[164:165], s[24:25], 0, v[134:135]
	s_mov_b32 m0, s59
	ds_read_b128 v[192:195], v172 offset:16384
	ds_read_b128 v[196:199], v172 offset:17408
	ds_read_b128 v[200:203], v172 offset:18432
	ds_read_b128 v[204:207], v172 offset:19456
	ds_read_b128 v[208:211], v172 offset:20480
	ds_read_b128 v[212:215], v172 offset:21504
	ds_read_b128 v[216:219], v172 offset:22528
	ds_read_b128 v[220:223], v172 offset:23552
	global_load_lds_dwordx4 v[164:165], off
	s_add_i32 m0, s59, 0x2000
	s_add_u32 s60, s24, 0x40000
	v_lshl_add_u64 v[224:225], s[24:25], 0, v[130:131]
	s_addc_u32 s61, s25, 0
	s_add_i32 s59, s49, s28
	global_load_lds_dwordx4 v[224:225], off
	s_mov_b32 m0, s59
	v_lshl_add_u64 v[230:231], s[26:27], 0, v[132:133]
	global_load_lds_dwordx4 v134, s[60:61]
	s_add_i32 m0, s59, 0x2000
	s_nop 0
	global_load_lds_dwordx4 v130, s[60:61]
	v_lshl_add_u64 v[226:227], s[26:27], 0, v[136:137]
	s_mov_b32 m0, s21
	s_nop 0
	global_load_lds_dwordx4 v[226:227], off
	s_mov_b32 m0, s31
	s_nop 0
	global_load_lds_dwordx4 v[230:231], off
	s_waitcnt vmcnt(8)
	s_waitcnt lgkmcnt(0)
	s_barrier
	s_setprio 3
	s_waitcnt lgkmcnt(0)
	v_mfma_f32_16x16x32_bf16 v[62:65], v[148:151], v[192:195], v[62:65]
	v_mfma_f32_16x16x32_bf16 v[58:61], v[156:159], v[192:195], v[58:61]
	v_mfma_f32_16x16x32_bf16 v[50:53], v[148:151], v[200:203], v[50:53]
	v_mfma_f32_16x16x32_bf16 v[42:45], v[156:159], v[200:203], v[42:45]
	v_mfma_f32_16x16x32_bf16 v[34:37], v[148:151], v[208:211], v[34:37]
	v_mfma_f32_16x16x32_bf16 v[26:29], v[156:159], v[208:211], v[26:29]
	v_mfma_f32_16x16x32_bf16 v[18:21], v[148:151], v[216:219], v[18:21]
	v_mfma_f32_16x16x32_bf16 v[10:13], v[156:159], v[216:219], v[10:13]
	v_mfma_f32_16x16x32_bf16 v[62:65], v[152:155], v[196:199], v[62:65]
	v_mfma_f32_16x16x32_bf16 v[58:61], v[160:163], v[196:199], v[58:61]
	v_mfma_f32_16x16x32_bf16 v[50:53], v[152:155], v[204:207], v[50:53]
	v_mfma_f32_16x16x32_bf16 v[42:45], v[160:163], v[204:207], v[42:45]
	v_mfma_f32_16x16x32_bf16 v[34:37], v[152:155], v[212:215], v[34:37]
	v_mfma_f32_16x16x32_bf16 v[26:29], v[160:163], v[212:215], v[26:29]
	v_mfma_f32_16x16x32_bf16 v[18:21], v[152:155], v[220:223], v[18:21]
	v_mfma_f32_16x16x32_bf16 v[10:13], v[160:163], v[220:223], v[10:13]
	s_setprio 0
	s_setprio 3
	v_mfma_f32_16x16x32_bf16 v[54:57], v[176:179], v[192:195], v[54:57]
	v_mfma_f32_16x16x32_bf16 v[46:49], v[184:187], v[192:195], v[46:49]
	v_mfma_f32_16x16x32_bf16 v[38:41], v[176:179], v[200:203], v[38:41]
	v_mfma_f32_16x16x32_bf16 v[30:33], v[184:187], v[200:203], v[30:33]
	v_mfma_f32_16x16x32_bf16 v[22:25], v[176:179], v[208:211], v[22:25]
	v_mfma_f32_16x16x32_bf16 v[14:17], v[184:187], v[208:211], v[14:17]
	v_mfma_f32_16x16x32_bf16 v[6:9], v[176:179], v[216:219], v[6:9]
	v_mfma_f32_16x16x32_bf16 v[2:5], v[184:187], v[216:219], v[2:5]
	v_mfma_f32_16x16x32_bf16 v[54:57], v[180:183], v[196:199], v[54:57]
	v_mfma_f32_16x16x32_bf16 v[46:49], v[188:191], v[196:199], v[46:49]
	v_mfma_f32_16x16x32_bf16 v[38:41], v[180:183], v[204:207], v[38:41]
	v_mfma_f32_16x16x32_bf16 v[30:33], v[188:191], v[204:207], v[30:33]
	v_mfma_f32_16x16x32_bf16 v[22:25], v[180:183], v[212:215], v[22:25]
	v_mfma_f32_16x16x32_bf16 v[14:17], v[188:191], v[212:215], v[14:17]
	v_mfma_f32_16x16x32_bf16 v[6:9], v[180:183], v[220:223], v[6:9]
	v_mfma_f32_16x16x32_bf16 v[2:5], v[188:191], v[220:223], v[2:5]
	s_setprio 0
	s_barrier
; #define PG8_STAGE_A(b, h, ptr, NX) do { if constexpr (Sched::GATHER) { unsigned gs_[2]; gs_[0] = ((NX) && last_) ? gN[h][0] : gA[h][0]; gs_[1] = ((NX) && last_) ? gN[h][1] : gA[h][1]; PG8_STAGE(PG8_SA(b, h), ptr, gs_); } \
;         else PG8_STAGE(PG8_SA(b, h), (ptr) + ((h) ? hstep : (size_t)0), voffA); } while (0)
; #define PG8_LDA(dst, b, h) do { _Pragma("unroll") for (int m = 0; m < 4; ++m) _Pragma("unroll") for (int k = 0; k < 2; ++k) dst[m][k] = *(const PG8_LAS bf16x8*)(lds + PG8_SA(b, h) + aoff + m * 2048 + k * 1024); } while (0)
; #define PG8_LDB(dst, b, h) do { _Pragma("unroll") for (int n = 0; n < 2; ++n) _Pragma("unroll") for (int k = 0; k < 2; ++k) dst[n][k] = *(const PG8_LAS bf16x8*)(lds + PG8_SB(b, h) + boff + n * 2048 + k * 1024); } while (0)
; #define PG8_MMA(ai, bj, At, Bt) do { __builtin_amdgcn_s_setprio(1); _Pragma("unroll") for (int m = 0; m < 4; ++m) _Pragma("unroll") for (int n = 0; n < 2; ++n) _Pragma("unroll") for (int k = 0; k < 2; ++k) \
;         acc[ai][bj][m][n] = __builtin_amdgcn_mfma_f32_16x16x32_bf16(Bt[n][k], At[m][k], acc[ai][bj][m][n], 0, 0, 0); __builtin_amdgcn_s_setprio(0); } while (0)
; #define PG8_WAIT_V(n) asm volatile("s_waitcnt vmcnt(" #n ")" ::: "memory")
; #define PG8_WAIT_L(n) asm volatile("s_waitcnt lgkmcnt(" #n ")" ::: "memory")
; #define PG8_BAR __builtin_amdgcn_s_barrier()
; #define PG8_SCHED __builtin_amdgcn_sched_barrier(0)
; template <class Epi, class Sched, bool ALIGN_EPI = false, bool SP2 = false>
; __device__ __forceinline__ void gemm_phase(PG8_LAS unsigned char* lds, const Gemm g, const Sched& S, const Epi& E, const bool skip_epi = false) {
;     ...
;             PG8_LDB(B0, 1, 0); PG8_LDB(B1, 1, 1); PG8_SCHED; PG8_LDA(At, 1, 0); PG8_STAGE_A(0, 1, a2, true);
;             PG8_WAIT_V(8); PG8_WAIT_L(0); PG8_BAR; PG8_MMA(0, 0, At, B0); PG8_MMA(0, 1, At, B1); PG8_BAR; PG8_SCHED;
	s_add_i32 s59, 0, 0x18000
	s_add_i32 s60, 0, 0x1c000
	v_add_u32_e32 v160, s59, v1
	v_add_u32_e32 v188, s60, v1
	ds_read_b128 v[148:151], v160
	ds_read_b128 v[152:155], v160 offset:1024
	ds_read_b128 v[156:159], v160 offset:2048
	ds_read_b128 v[160:163], v160 offset:3072
	ds_read_b128 v[176:179], v188
	ds_read_b128 v[180:183], v188 offset:1024
	ds_read_b128 v[184:187], v188 offset:2048
	ds_read_b128 v[188:191], v188 offset:3072
	s_add_u32 s26, s26, 0x40000
	s_addc_u32 s27, s27, 0
	s_mov_b32 m0, s34
	ds_read_b128 v[192:195], v172 offset:32768
	ds_read_b128 v[196:199], v172 offset:33792
	ds_read_b128 v[200:203], v172 offset:34816
	ds_read_b128 v[204:207], v172 offset:35840
	ds_read_b128 v[208:211], v172 offset:36864
	ds_read_b128 v[212:215], v172 offset:37888
	ds_read_b128 v[216:219], v172 offset:38912
	ds_read_b128 v[220:223], v172 offset:39936
	global_load_lds_dwordx4 v136, s[26:27]
	s_mov_b32 m0, s35
	s_nop 0
	global_load_lds_dwordx4 v132, s[26:27]
	s_waitcnt vmcnt(8)
	s_waitcnt lgkmcnt(0)
	s_barrier
	s_setprio 3
	s_waitcnt lgkmcnt(0)
	v_mfma_f32_16x16x32_bf16 v[126:129], v[148:151], v[192:195], v[126:129]
	v_mfma_f32_16x16x32_bf16 v[122:125], v[156:159], v[192:195], v[122:125]
	v_mfma_f32_16x16x32_bf16 v[114:117], v[148:151], v[200:203], v[114:117]
	v_mfma_f32_16x16x32_bf16 v[106:109], v[156:159], v[200:203], v[106:109]
	v_mfma_f32_16x16x32_bf16 v[98:101], v[148:151], v[208:211], v[98:101]
	v_mfma_f32_16x16x32_bf16 v[90:93], v[156:159], v[208:211], v[90:93]
	v_mfma_f32_16x16x32_bf16 v[82:85], v[148:151], v[216:219], v[82:85]
	v_mfma_f32_16x16x32_bf16 v[74:77], v[156:159], v[216:219], v[74:77]
	v_mfma_f32_16x16x32_bf16 v[126:129], v[152:155], v[196:199], v[126:129]
	v_mfma_f32_16x16x32_bf16 v[122:125], v[160:163], v[196:199], v[122:125]
	v_mfma_f32_16x16x32_bf16 v[114:117], v[152:155], v[204:207], v[114:117]
	v_mfma_f32_16x16x32_bf16 v[106:109], v[160:163], v[204:207], v[106:109]
	v_mfma_f32_16x16x32_bf16 v[98:101], v[152:155], v[212:215], v[98:101]
	v_mfma_f32_16x16x32_bf16 v[90:93], v[160:163], v[212:215], v[90:93]
	v_mfma_f32_16x16x32_bf16 v[82:85], v[152:155], v[220:223], v[82:85]
	v_mfma_f32_16x16x32_bf16 v[74:77], v[160:163], v[220:223], v[74:77]
	s_setprio 0
	s_setprio 3
	v_mfma_f32_16x16x32_bf16 v[118:121], v[176:179], v[192:195], v[118:121]
	v_mfma_f32_16x16x32_bf16 v[110:113], v[184:187], v[192:195], v[110:113]
	v_mfma_f32_16x16x32_bf16 v[102:105], v[176:179], v[200:203], v[102:105]
	v_mfma_f32_16x16x32_bf16 v[94:97], v[184:187], v[200:203], v[94:97]
	v_mfma_f32_16x16x32_bf16 v[86:89], v[176:179], v[208:211], v[86:89]
	v_mfma_f32_16x16x32_bf16 v[78:81], v[184:187], v[208:211], v[78:81]
	v_mfma_f32_16x16x32_bf16 v[70:73], v[176:179], v[216:219], v[70:73]
	v_mfma_f32_16x16x32_bf16 v[66:69], v[184:187], v[216:219], v[66:69]
	v_mfma_f32_16x16x32_bf16 v[118:121], v[180:183], v[196:199], v[118:121]
	v_mfma_f32_16x16x32_bf16 v[110:113], v[188:191], v[196:199], v[110:113]
	v_mfma_f32_16x16x32_bf16 v[102:105], v[180:183], v[204:207], v[102:105]
	v_mfma_f32_16x16x32_bf16 v[94:97], v[188:191], v[204:207], v[94:97]
	v_mfma_f32_16x16x32_bf16 v[86:89], v[180:183], v[212:215], v[86:89]
	v_mfma_f32_16x16x32_bf16 v[78:81], v[188:191], v[212:215], v[78:81]
	v_mfma_f32_16x16x32_bf16 v[70:73], v[180:183], v[220:223], v[70:73]
	v_mfma_f32_16x16x32_bf16 v[66:69], v[188:191], v[220:223], v[66:69]
	s_setprio 0
	s_barrier
; #define PG8_STAGE_A(b, h, ptr, NX) do { if constexpr (Sched::GATHER) { unsigned gs_[2]; gs_[0] = ((NX) && last_) ? gN[h][0] : gA[h][0]; gs_[1] = ((NX) && last_) ? gN[h][1] : gA[h][1]; PG8_STAGE(PG8_SA(b, h), ptr, gs_); } \
;         else PG8_STAGE(PG8_SA(b, h), (ptr) + ((h) ? hstep : (size_t)0), voffA); } while (0)
; #define PG8_STAGE(bufoff, gbase, voff) do { _Pragma("unroll") for (int _i = 0; _i < 2; ++_i) \
;         __builtin_amdgcn_global_load_lds((const unsigned*)((const char*)(gbase) + (voff)[_i]), (PG8_LAS unsigned*)(lds + (bufoff) + ldsw + _i * 8192), 16, 0, 0); } while (0)
; #define PG8_LDA(dst, b, h) do { _Pragma("unroll") for (int m = 0; m < 4; ++m) _Pragma("unroll") for (int k = 0; k < 2; ++k) dst[m][k] = *(const PG8_LAS bf16x8*)(lds + PG8_SA(b, h) + aoff + m * 2048 + k * 1024); } while (0)
; #define PG8_MMA(ai, bj, At, Bt) do { __builtin_amdgcn_s_setprio(1); _Pragma("unroll") for (int m = 0; m < 4; ++m) _Pragma("unroll") for (int n = 0; n < 2; ++n) _Pragma("unroll") for (int k = 0; k < 2; ++k) \
;         acc[ai][bj][m][n] = __builtin_amdgcn_mfma_f32_16x16x32_bf16(Bt[n][k], At[m][k], acc[ai][bj][m][n], 0, 0, 0); __builtin_amdgcn_s_setprio(0); } while (0)
; #define PG8_WAIT_V(n) asm volatile("s_waitcnt vmcnt(" #n ")" ::: "memory")
; #define PG8_WAIT_L(n) asm volatile("s_waitcnt lgkmcnt(" #n ")" ::: "memory")
; #define PG8_BAR __builtin_amdgcn_s_barrier()
; __device__ __forceinline__ void rstd8(const float* SS, int rowb, int lane, float (&rs)[2][4]) {
;     f32x4 p[2][4];
; #pragma unroll
;     for (int ai = 0; ai < 2; ++ai)
; #pragma unroll
;         for (int m = 0; m < 4; ++m) p[ai][m] = *(const f32x4*)(SS + (size_t)(rowb + HALF * ai + 16 * m + (lane >> 2)) * 16 + 4 * (lane & 3));
;     asm volatile("" : "+v"(p[0][0]), "+v"(p[0][1]), "+v"(p[0][2]), "+v"(p[0][3]), "+v"(p[1][0]), "+v"(p[1][1]), "+v"(p[1][2]), "+v"(p[1][3]));
; template <class Epi, class Sched, bool ALIGN_EPI = false, bool SP2 = false>
; __device__ __forceinline__ void gemm_phase(PG8_LAS unsigned char* lds, const Gemm g, const Sched& S, const Epi& E, const bool skip_epi = false) {
;     ...
;             PG8_LDA(At, 1, 1); PG8_STAGE(PG8_SB(1, 0), b3, voffB); PG8_STAGE(PG8_SB(1, 1), b3 + hstep, voffB); PG8_STAGE_A(1, 0, a3, true);
;             PG8_WAIT_V(8); PG8_WAIT_L(0); PG8_BAR; PG8_MMA(1, 0, At, B0); PG8_MMA(1, 1, At, B1); PG8_BAR; PG8_SCHED;
	s_add_i32 s26, s59, s28
	s_add_i32 m0, s26, 0xffffff80
	ds_read_b128 v[192:195], v172 offset:49152
	ds_read_b128 v[196:199], v172 offset:50176
	ds_read_b128 v[200:203], v172 offset:51200
	ds_read_b128 v[204:207], v172 offset:52224
	ds_read_b128 v[208:211], v172 offset:53248
	ds_read_b128 v[212:215], v172 offset:54272
	ds_read_b128 v[216:219], v172 offset:55296
	ds_read_b128 v[220:223], v172 offset:56320
	global_load_lds_dwordx4 v[164:165], off offset:128
	s_add_i32 m0, s26, 0x1f80
	s_add_u32 s24, s24, 0x40080
	s_addc_u32 s25, s25, 0
	s_add_i32 s26, s60, s28
	global_load_lds_dwordx4 v[224:225], off offset:128
	s_mov_b32 m0, s26
	s_nop 0
	global_load_lds_dwordx4 v134, s[24:25]
	s_add_i32 m0, s26, 0x2000
	s_nop 0
	global_load_lds_dwordx4 v130, s[24:25]
	s_add_i32 m0, s37, 0xffffff80
	s_nop 0
	global_load_lds_dwordx4 v[226:227], off offset:128
	s_add_i32 m0, s38, 0xffffff80
	s_nop 0
	global_load_lds_dwordx4 v[230:231], off offset:128
	s_waitcnt vmcnt(8)
	s_waitcnt lgkmcnt(0)
	s_barrier
	s_setprio 3
	s_waitcnt lgkmcnt(0)
	v_mfma_f32_16x16x32_bf16 v[62:65], v[148:151], v[192:195], v[62:65]
	v_mfma_f32_16x16x32_bf16 v[58:61], v[156:159], v[192:195], v[58:61]
	v_mfma_f32_16x16x32_bf16 v[50:53], v[148:151], v[200:203], v[50:53]
	v_mfma_f32_16x16x32_bf16 v[42:45], v[156:159], v[200:203], v[42:45]
	v_mfma_f32_16x16x32_bf16 v[34:37], v[148:151], v[208:211], v[34:37]
	v_mfma_f32_16x16x32_bf16 v[26:29], v[156:159], v[208:211], v[26:29]
	v_mfma_f32_16x16x32_bf16 v[18:21], v[148:151], v[216:219], v[18:21]
	v_mfma_f32_16x16x32_bf16 v[10:13], v[156:159], v[216:219], v[10:13]
	v_mfma_f32_16x16x32_bf16 v[62:65], v[152:155], v[196:199], v[62:65]
	v_mfma_f32_16x16x32_bf16 v[58:61], v[160:163], v[196:199], v[58:61]
	v_mfma_f32_16x16x32_bf16 v[50:53], v[152:155], v[204:207], v[50:53]
	v_mfma_f32_16x16x32_bf16 v[42:45], v[160:163], v[204:207], v[42:45]
	v_mfma_f32_16x16x32_bf16 v[34:37], v[152:155], v[212:215], v[34:37]
	v_mfma_f32_16x16x32_bf16 v[26:29], v[160:163], v[212:215], v[26:29]
	v_mfma_f32_16x16x32_bf16 v[18:21], v[152:155], v[220:223], v[18:21]
	v_mfma_f32_16x16x32_bf16 v[10:13], v[160:163], v[220:223], v[10:13]
	s_setprio 0
	s_setprio 3
	v_mfma_f32_16x16x32_bf16 v[54:57], v[176:179], v[192:195], v[54:57]
	v_mfma_f32_16x16x32_bf16 v[46:49], v[184:187], v[192:195], v[46:49]
	v_mfma_f32_16x16x32_bf16 v[38:41], v[176:179], v[200:203], v[38:41]
	v_mfma_f32_16x16x32_bf16 v[30:33], v[184:187], v[200:203], v[30:33]
	v_mfma_f32_16x16x32_bf16 v[22:25], v[176:179], v[208:211], v[22:25]
	v_mfma_f32_16x16x32_bf16 v[14:17], v[184:187], v[208:211], v[14:17]
	v_mfma_f32_16x16x32_bf16 v[6:9], v[176:179], v[216:219], v[6:9]
	v_mfma_f32_16x16x32_bf16 v[2:5], v[184:187], v[216:219], v[2:5]
	v_mfma_f32_16x16x32_bf16 v[54:57], v[180:183], v[196:199], v[54:57]
	v_mfma_f32_16x16x32_bf16 v[46:49], v[188:191], v[196:199], v[46:49]
	v_mfma_f32_16x16x32_bf16 v[38:41], v[180:183], v[204:207], v[38:41]
	v_mfma_f32_16x16x32_bf16 v[30:33], v[188:191], v[204:207], v[30:33]
	v_mfma_f32_16x16x32_bf16 v[22:25], v[180:183], v[212:215], v[22:25]
	v_mfma_f32_16x16x32_bf16 v[14:17], v[188:191], v[212:215], v[14:17]
	v_mfma_f32_16x16x32_bf16 v[6:9], v[180:183], v[220:223], v[6:9]
	v_mfma_f32_16x16x32_bf16 v[2:5], v[188:191], v[220:223], v[2:5]
	s_setprio 0
	s_barrier
	s_add_i32 s58, s58, 2
	s_add_u32 s22, s22, 0x100
	s_addc_u32 s23, s23, 0
	s_add_u32 s56, s56, 0x100
	s_addc_u32 s57, s57, 0
	s_cmp_gt_u32 s58, 13
	s_cbranch_scc0 .LBB0_944
	v_lshl_add_u32 v164, s20, 8, v167
	v_ashrrev_i32_e32 v165, 31, v164
	v_lshlrev_b64 v[148:149], 6, v[164:165]
	v_lshl_add_u64 v[148:149], v[138:139], 0, v[148:149]
	v_add_co_u32_e32 v150, vcc, 0x2000, v148
	v_addc_co_u32_e32 v151, vcc, 0, v149, vcc
	global_load_dwordx4 v[176:179], v[148:149], off
	global_load_dwordx4 v[180:183], v[148:149], off offset:1024
	global_load_dwordx4 v[184:187], v[148:149], off offset:2048
	global_load_dwordx4 v[188:191], v[148:149], off offset:3072
	global_load_dwordx4 v[192:195], v[150:151], off
	global_load_dwordx4 v[196:199], v[150:151], off offset:1024
	global_load_dwordx4 v[200:203], v[150:151], off offset:2048
	global_load_dwordx4 v[204:207], v[150:151], off offset:3072
	s_and_b64 vcc, exec, s[10:11]
	s_cbranch_vccz .LBB0_947
	s_barrier

; #define PG8_GIDX(G_, PM_) do { if constexpr (Sched::GATHER) { _Pragma("unroll") for (int h_ = 0; h_ < 2; ++h_) _Pragma("unroll") for (int i_ = 0; i_ < 2; ++i_) { int R_, C_; stage_rc(tid * 16 + i_ * 8192, R_, C_); \
;         const int src_ = S.rowsrc[(PM_) * BM + h_ * HALF + R_]; G_[h_][i_] = (unsigned)(src_ * K + C_) * 2u; } } } while (0)
; #define PG8_STAGE_A(b, h, ptr, NX) do { if constexpr (Sched::GATHER) { unsigned gs_[2]; gs_[0] = ((NX) && last_) ? gN[h][0] : gA[h][0]; gs_[1] = ((NX) && last_) ? gN[h][1] : gA[h][1]; PG8_STAGE(PG8_SA(b, h), ptr, gs_); } \
;         else PG8_STAGE(PG8_SA(b, h), (ptr) + ((h) ? hstep : (size_t)0), voffA); } while (0)
; #define PG8_STAGE(bufoff, gbase, voff) do { _Pragma("unroll") for (int _i = 0; _i < 2; ++_i) \
;         __builtin_amdgcn_global_load_lds((const unsigned*)((const char*)(gbase) + (voff)[_i]), (PG8_LAS unsigned*)(lds + (bufoff) + ldsw + _i * 8192), 16, 0, 0); } while (0)
; #define PG8_WAIT_V(n) asm volatile("s_waitcnt vmcnt(" #n ")" ::: "memory")
; #define PG8_BAR __builtin_amdgcn_s_barrier()
; template <class Epi, class Sched, bool ALIGN_EPI = false, bool SP2 = false>
; __device__ __forceinline__ void gemm_phase(PG8_LAS unsigned char* lds, const Gemm g, const Sched& S, const Epi& E, const bool skip_epi = false) {
;     ...
;         PG8_STAGE(PG8_SB(1, 0), cB + kstep, voffB); PG8_STAGE_A(1, 0, cA + kstep, false); PG8_STAGE(PG8_SB(1, 1), cB + hstep + kstep, voffB);
;         PG8_WAIT_V(6); PG8_BAR;
;     } else {
;         PG8_STAGE(PG8_SB(0, 0), cB, voffB); PG8_STAGE_A(0, 0, cA, false); PG8_STAGE(PG8_SB(0, 1), cB + hstep, voffB); PG8_STAGE_A(0, 1, cA, false);
;         if (wr == 1) PG8_BAR;
;         PG8_WAIT_V(4); PG8_BAR;
;         PG8_STAGE(PG8_SB(1, 0), cB + kstep, voffB); PG8_STAGE_A(1, 0, cA + kstep, false); PG8_STAGE(PG8_SB(1, 1), cB + hstep + kstep, voffB);
;         PG8_WAIT_V(6); PG8_BAR;
;     }
;     for (;;) {
;         const bool has_next = S.next(ui + 1, nxt);
;         if (has_next) PG8_GIDX(gN, nxt.pm);
;         const char* nA = has_next ? (const char*)g.A + (size_t)nxt.pm * pmstepA + nxt.ko : cA; const char* nB = has_next ? (const char*)g.Bt + (size_t)nxt.pn * tstep + nxt.ko : cB;
.LBB0_1314:
	s_mov_b64 s[12:13], 0x80
	s_and_b32 s49, s4, 3
	s_add_i32 m0, s41, 0x18000
	v_lshl_add_u64 v[8:9], v[8:9], 0, s[12:13]
	s_lshl_b32 s52, s5, 6
	s_lshl_b32 s6, s5, 13
	s_lshl_b32 s7, s49, 12
	s_waitcnt vmcnt(2)
	s_barrier
	global_load_lds_dwordx4 v[8:9], off
	v_lshl_add_u64 v[4:5], v[4:5], 0, s[12:13]
	s_add_i32 m0, s41, 0x1a000
	s_add_i32 s53, s41, 0x8000
	s_add_i32 s54, s41, 0xa000
	global_load_lds_dwordx4 v[4:5], off
	v_lshl_add_u64 v[2:3], v[2:3], 0, s[12:13]
	s_mov_b32 m0, s53
	s_add_u32 s4, s36, 0x40080
	global_load_lds_dwordx4 v[2:3], off
	v_lshl_add_u64 v[2:3], v[6:7], 0, s[12:13]
	s_mov_b32 m0, s54
	s_addc_u32 s5, s37, 0
	global_load_lds_dwordx4 v[2:3], off
	s_add_i32 m0, s41, 0x1c000
	s_nop 0
	global_load_lds_dwordx4 v188, s[4:5]
	s_add_i32 m0, s41, 0x1e000
	v_and_b32_e32 v1, 15, v10
	global_load_lds_dwordx4 v192, s[4:5]
	v_bfe_u32 v2, v10, 4, 2
	v_lshlrev_b32_e32 v3, 4, v2
	v_lshlrev_b32_e32 v4, 2, v10
	v_lshl_or_b32 v3, v1, 6, v3
	v_and_b32_e32 v4, 32, v4
	v_bitop3_b32 v5, v3, s6, v4 bitop3:0xde
	v_bitop3_b32 v220, v3, s7, v4 bitop3:0xde
	v_and_b32_e32 v3, 3, v10
	v_and_b32_e32 v4, 60, v10
	v_lshl_or_b32 v222, v3, 6, v4
	v_lshlrev_b32_e32 v3, 3, v3
	v_lshl_or_b32 v223, s49, 5, v3
	v_lshlrev_b32_e32 v3, 4, v1
	v_lshl_or_b32 v224, v2, 2, v3
	v_cmp_eq_u32_e64 s[4:5], 0, v2
	v_lshlrev_b32_e32 v2, 14, v11
	v_and_b32_e32 v2, 0xffff8000, v2
	v_lshl_add_u32 v2, v12, 11, v2
	v_and_b32_e32 v3, 1, v11
	v_lshl_or_b32 v2, v3, 6, v2
	v_lshl_add_u32 v194, v13, 1, v2
	v_lshlrev_b32_e32 v2, 14, v14
	v_and_b32_e32 v2, 0xffff8000, v2
	s_waitcnt vmcnt(6)
	s_cmpk_lt_u32 s14, 0x100
	v_lshl_add_u32 v2, v15, 11, v2
	v_and_b32_e32 v3, 1, v14
	s_cselect_b64 s[14:15], -1, 0
	v_lshl_or_b32 v2, v3, 6, v2
	s_add_i32 s57, 0, 0x10000
	s_add_i32 s58, 0, 0x14000
	v_bfe_u32 v221, v10, 2, 4
	s_ashr_i32 s55, s97, 31
	s_ashr_i32 s56, s94, 31
	v_mov_b32_e32 v195, v189
	v_lshl_add_u32 v196, v16, 1, v2
	v_mov_b32_e32 v197, v189
	v_mov_b64_e32 v[198:199], 0x100
	v_mov_b64_e32 v[200:201], 0xff
	v_add_u32_e32 v225, s57, v220
	v_add_u32_e32 v226, s58, v220
	v_add_u32_e32 v227, 0, v5
	s_mov_b64 s[16:17], 0x48000
	s_mov_b64 s[18:19], 0x50000
	s_mov_b64 s[20:21], 0x58000
	s_mov_b32 s59, 0
	s_barrier
	s_branch .LBB0_1317

; #define PG8_GIDX(G_, PM_) do { if constexpr (Sched::GATHER) { _Pragma("unroll") for (int h_ = 0; h_ < 2; ++h_) _Pragma("unroll") for (int i_ = 0; i_ < 2; ++i_) { int R_, C_; stage_rc(tid * 16 + i_ * 8192, R_, C_); \
;         const int src_ = S.rowsrc[(PM_) * BM + h_ * HALF + R_]; G_[h_][i_] = (unsigned)(src_ * K + C_) * 2u; } } } while (0)
; #define PG8_STAGE_A(b, h, ptr, NX) do { if constexpr (Sched::GATHER) { unsigned gs_[2]; gs_[0] = ((NX) && last_) ? gN[h][0] : gA[h][0]; gs_[1] = ((NX) && last_) ? gN[h][1] : gA[h][1]; PG8_STAGE(PG8_SA(b, h), ptr, gs_); } \
;         else PG8_STAGE(PG8_SA(b, h), (ptr) + ((h) ? hstep : (size_t)0), voffA); } while (0)
; #define PG8_LDA(dst, b, h) do { _Pragma("unroll") for (int m = 0; m < 4; ++m) _Pragma("unroll") for (int k = 0; k < 2; ++k) dst[m][k] = *(const PG8_LAS bf16x8*)(lds + PG8_SA(b, h) + aoff + m * 2048 + k * 1024); } while (0)
; template <class Epi, class Sched, bool ALIGN_EPI = false, bool SP2 = false>
; __device__ __forceinline__ void gemm_phase(PG8_LAS unsigned char* lds, const Gemm g, const Sched& S, const Epi& E, const bool skip_epi = false) {
;     ...
;         const bool has_next = S.next(ui + 1, nxt);
;         if (has_next) PG8_GIDX(gN, nxt.pm);
;         const char* nA = has_next ? (const char*)g.A + (size_t)nxt.pm * pmstepA + nxt.ko : cA; const char* nB = has_next ? (const char*)g.Bt + (size_t)nxt.pn * tstep + nxt.ko : cB;
;         for (int t = 0; t < nt; t += 2) {
;             const bool last = (t == nt - 2); last_ = last && has_next;
;             const char* a1 = cA + (size_t)(t + 1) * kstep;
;             const char* a2 = last ? nA : cA + (size_t)(t + 2) * kstep; const char* b2 = last ? nB : cB + (size_t)(t + 2) * kstep;
;             const char* a3 = a2 + kstep; const char* b3 = b2 + kstep;
;             if (last && has_next) S.a_ready(nxt);
;             if constexpr (SP2) {
;             PG8_LDB(B0, 0, 0); PG8_LDB(B1, 0, 1); PG8_SCHED; PG8_LDA(At, 0, 0); PG8_STAGE_A(1, 1, a1, false);
;             PG8_WAIT_V(8); PG8_WAIT_L(0); PG8_BAR; PG8_MMA(0, 0, At, B0); PG8_MMA(0, 1, At, B1); PG8_BAR; PG8_SCHED;
;             PG8_LDA(At, 0, 1); PG8_STAGE(PG8_SB(0, 0), b2, voffB); PG8_STAGE(PG8_SB(0, 1), b2 + hstep, voffB); PG8_STAGE_A(0, 0, a2, true);
;             PG8_WAIT_V(8); PG8_WAIT_L(0); PG8_BAR; PG8_MMA(1, 0, At, B0); PG8_MMA(1, 1, At, B1); PG8_BAR; PG8_SCHED;
.LBB0_1323:
	s_ashr_i32 s25, s24, 31
	s_lshl_b64 s[26:27], s[24:25], 19
	s_add_u32 s26, s46, s26
	s_addc_u32 s27, s47, s27
	s_and_b64 s[28:29], s[6:7], exec
	s_cselect_b32 s25, s27, s35
	s_cselect_b32 s31, s26, s34
	s_ashr_i32 s23, s22, 31
	s_lshl_b64 s[28:29], s[22:23], 19
	s_add_u32 s28, s2, s28
	s_addc_u32 s29, s3, s29
	s_and_b64 s[38:39], s[6:7], exec
	s_cselect_b32 s23, s29, s37
	s_cselect_b32 s60, s28, s36
	s_add_u32 s34, s34, 0x40080
	s_addc_u32 s35, s35, 0
	s_add_u32 s61, s36, 0x100
	s_addc_u32 s62, s37, 0
	s_mov_b32 s63, -2
	s_waitcnt vmcnt(0)
	s_waitcnt lgkmcnt(0)
	ds_read_b128 v[98:101], v225
	ds_read_b128 v[110:113], v225 offset:1024
	ds_read_b128 v[122:125], v225 offset:2048
	ds_read_b128 v[130:133], v225 offset:3072
	ds_read_b128 v[146:149], v226
	ds_read_b128 v[150:153], v226 offset:1024
	ds_read_b128 v[154:157], v226 offset:2048
	ds_read_b128 v[158:161], v226 offset:3072
	s_add_u32 s36, s34, 0xfffc0080
	s_addc_u32 s37, s35, -1
	s_cmp_eq_u32 s63, 12
	s_cselect_b32 s39, s25, s37
	s_cselect_b32 s38, s31, s36
	s_cselect_b32 s37, s23, s62
	s_cselect_b32 s36, s60, s61
	s_add_i32 m0, s41, 0xc000
	ds_read_b128 v[162:165], v227
	ds_read_b128 v[166:169], v227 offset:1024
	ds_read_b128 v[170:173], v227 offset:2048
	ds_read_b128 v[174:177], v227 offset:3072
	ds_read_b128 v[178:181], v227 offset:4096
	ds_read_b128 v[182:185], v227 offset:5120
	ds_read_b128 v[202:205], v227 offset:6144
	ds_read_b128 v[206:209], v227 offset:7168
	global_load_lds_dwordx4 v194, s[34:35]
	s_add_i32 m0, s41, 0xe000
	s_nop 0
	global_load_lds_dwordx4 v196, s[34:35]
	s_waitcnt vmcnt(8)
	s_waitcnt lgkmcnt(0)
	s_barrier
	s_setprio 3
	s_waitcnt lgkmcnt(0)
	v_mfma_f32_16x16x32_bf16 v[142:145], v[98:101], v[162:165], 0
	v_mfma_f32_16x16x32_bf16 v[138:141], v[122:125], v[162:165], 0
	v_mfma_f32_16x16x32_bf16 v[118:121], v[98:101], v[170:173], 0
	v_mfma_f32_16x16x32_bf16 v[114:117], v[122:125], v[170:173], 0
	v_mfma_f32_16x16x32_bf16 v[94:97], v[98:101], v[178:181], 0
	v_mfma_f32_16x16x32_bf16 v[90:93], v[122:125], v[178:181], 0
	v_mfma_f32_16x16x32_bf16 v[78:81], v[98:101], v[202:205], 0
	v_mfma_f32_16x16x32_bf16 v[74:77], v[122:125], v[202:205], 0
	v_mfma_f32_16x16x32_bf16 v[142:145], v[110:113], v[166:169], v[142:145]
	v_mfma_f32_16x16x32_bf16 v[138:141], v[130:133], v[166:169], v[138:141]
	v_mfma_f32_16x16x32_bf16 v[118:121], v[110:113], v[174:177], v[118:121]
	v_mfma_f32_16x16x32_bf16 v[114:117], v[130:133], v[174:177], v[114:117]
	v_mfma_f32_16x16x32_bf16 v[94:97], v[110:113], v[182:185], v[94:97]
	v_mfma_f32_16x16x32_bf16 v[90:93], v[130:133], v[182:185], v[90:93]
	v_mfma_f32_16x16x32_bf16 v[78:81], v[110:113], v[206:209], v[78:81]
	v_mfma_f32_16x16x32_bf16 v[74:77], v[130:133], v[206:209], v[74:77]
	s_setprio 0
	s_setprio 3
	v_mfma_f32_16x16x32_bf16 v[134:137], v[146:149], v[162:165], 0
	v_mfma_f32_16x16x32_bf16 v[126:129], v[154:157], v[162:165], 0
	v_mfma_f32_16x16x32_bf16 v[106:109], v[146:149], v[170:173], 0
	v_mfma_f32_16x16x32_bf16 v[102:105], v[154:157], v[170:173], 0
	v_mfma_f32_16x16x32_bf16 v[86:89], v[146:149], v[178:181], 0
	v_mfma_f32_16x16x32_bf16 v[82:85], v[154:157], v[178:181], 0
	v_mfma_f32_16x16x32_bf16 v[70:73], v[146:149], v[202:205], 0
	v_mfma_f32_16x16x32_bf16 v[66:69], v[154:157], v[202:205], 0
	v_mfma_f32_16x16x32_bf16 v[134:137], v[150:153], v[166:169], v[134:137]
	v_mfma_f32_16x16x32_bf16 v[126:129], v[158:161], v[166:169], v[126:129]
	v_mfma_f32_16x16x32_bf16 v[106:109], v[150:153], v[174:177], v[106:109]
	v_mfma_f32_16x16x32_bf16 v[102:105], v[158:161], v[174:177], v[102:105]
	v_mfma_f32_16x16x32_bf16 v[86:89], v[150:153], v[182:185], v[86:89]
	v_mfma_f32_16x16x32_bf16 v[82:85], v[158:161], v[182:185], v[82:85]
	v_mfma_f32_16x16x32_bf16 v[70:73], v[150:153], v[206:209], v[70:73]
	v_mfma_f32_16x16x32_bf16 v[66:69], v[158:161], v[206:209], v[66:69]
	s_setprio 0
	s_barrier
	s_add_i32 s64, s57, s40
	v_lshl_add_u64 v[210:211], s[36:37], 0, v[188:189]
	s_mov_b32 m0, s64
	ds_read_b128 v[162:165], v227 offset:16384
	ds_read_b128 v[166:169], v227 offset:17408
	ds_read_b128 v[170:173], v227 offset:18432
	ds_read_b128 v[174:177], v227 offset:19456
	ds_read_b128 v[178:181], v227 offset:20480
	ds_read_b128 v[182:185], v227 offset:21504
	ds_read_b128 v[202:205], v227 offset:22528
	ds_read_b128 v[206:209], v227 offset:23552
	global_load_lds_dwordx4 v[210:211], off
	s_add_i32 m0, s64, 0x2000
	s_add_u32 s64, s36, 0x40000
	v_lshl_add_u64 v[212:213], s[36:37], 0, v[192:193]
	s_addc_u32 s65, s37, 0
	s_add_i32 s66, s58, s40
	global_load_lds_dwordx4 v[212:213], off
	s_mov_b32 m0, s66
	v_lshl_add_u64 v[216:217], s[38:39], 0, v[190:191]
	global_load_lds_dwordx4 v188, s[64:65]
	s_add_i32 m0, s66, 0x2000
	s_nop 0
	global_load_lds_dwordx4 v192, s[64:65]
	v_lshl_add_u64 v[214:215], s[38:39], 0, v[186:187]
	s_mov_b32 m0, s41
	s_nop 0
	global_load_lds_dwordx4 v[214:215], off
	s_mov_b32 m0, s44
	s_nop 0
	global_load_lds_dwordx4 v[216:217], off
	s_waitcnt vmcnt(8)
	s_waitcnt lgkmcnt(0)
	s_barrier
; #define PG8_STAGE_A(b, h, ptr, NX) do { if constexpr (Sched::GATHER) { unsigned gs_[2]; gs_[0] = ((NX) && last_) ? gN[h][0] : gA[h][0]; gs_[1] = ((NX) && last_) ? gN[h][1] : gA[h][1]; PG8_STAGE(PG8_SA(b, h), ptr, gs_); } \
;         else PG8_STAGE(PG8_SA(b, h), (ptr) + ((h) ? hstep : (size_t)0), voffA); } while (0)
; #define PG8_LDA(dst, b, h) do { _Pragma("unroll") for (int m = 0; m < 4; ++m) _Pragma("unroll") for (int k = 0; k < 2; ++k) dst[m][k] = *(const PG8_LAS bf16x8*)(lds + PG8_SA(b, h) + aoff + m * 2048 + k * 1024); } while (0)
; #define PG8_LDB(dst, b, h) do { _Pragma("unroll") for (int n = 0; n < 2; ++n) _Pragma("unroll") for (int k = 0; k < 2; ++k) dst[n][k] = *(const PG8_LAS bf16x8*)(lds + PG8_SB(b, h) + boff + n * 2048 + k * 1024); } while (0)
; #define PG8_MMA(ai, bj, At, Bt) do { __builtin_amdgcn_s_setprio(1); _Pragma("unroll") for (int m = 0; m < 4; ++m) _Pragma("unroll") for (int n = 0; n < 2; ++n) _Pragma("unroll") for (int k = 0; k < 2; ++k) \
;         acc[ai][bj][m][n] = __builtin_amdgcn_mfma_f32_16x16x32_bf16(Bt[n][k], At[m][k], acc[ai][bj][m][n], 0, 0, 0); __builtin_amdgcn_s_setprio(0); } while (0)
; #define PG8_WAIT_V(n) asm volatile("s_waitcnt vmcnt(" #n ")" ::: "memory")
; #define PG8_WAIT_L(n) asm volatile("s_waitcnt lgkmcnt(" #n ")" ::: "memory")
; #define PG8_BAR __builtin_amdgcn_s_barrier()
; #define PG8_SCHED __builtin_amdgcn_sched_barrier(0)
; template <class Epi, class Sched, bool ALIGN_EPI = false, bool SP2 = false>
; __device__ __forceinline__ void gemm_phase(PG8_LAS unsigned char* lds, const Gemm g, const Sched& S, const Epi& E, const bool skip_epi = false) {
;     ...
;             PG8_WAIT_V(8); PG8_WAIT_L(0); PG8_BAR; PG8_MMA(1, 0, At, B0); PG8_MMA(1, 1, At, B1); PG8_BAR; PG8_SCHED;
;             PG8_LDB(B0, 1, 0); PG8_LDB(B1, 1, 1); PG8_SCHED; PG8_LDA(At, 1, 0); PG8_STAGE_A(0, 1, a2, true);
;             PG8_WAIT_V(8); PG8_WAIT_L(0); PG8_BAR; PG8_MMA(0, 0, At, B0); PG8_MMA(0, 1, At, B1); PG8_BAR; PG8_SCHED;
	s_setprio 3
	s_waitcnt lgkmcnt(0)
	v_mfma_f32_16x16x32_bf16 v[62:65], v[98:101], v[162:165], 0
	v_mfma_f32_16x16x32_bf16 v[58:61], v[122:125], v[162:165], 0
	v_mfma_f32_16x16x32_bf16 v[46:49], v[98:101], v[170:173], 0
	v_mfma_f32_16x16x32_bf16 v[42:45], v[122:125], v[170:173], 0
	v_mfma_f32_16x16x32_bf16 v[30:33], v[98:101], v[178:181], 0
	v_mfma_f32_16x16x32_bf16 v[26:29], v[122:125], v[178:181], 0
	v_mfma_f32_16x16x32_bf16 v[14:17], v[98:101], v[202:205], 0
	v_mfma_f32_16x16x32_bf16 v[10:13], v[122:125], v[202:205], 0
	v_mfma_f32_16x16x32_bf16 v[62:65], v[110:113], v[166:169], v[62:65]
	v_mfma_f32_16x16x32_bf16 v[58:61], v[130:133], v[166:169], v[58:61]
	v_mfma_f32_16x16x32_bf16 v[46:49], v[110:113], v[174:177], v[46:49]
	v_mfma_f32_16x16x32_bf16 v[42:45], v[130:133], v[174:177], v[42:45]
	v_mfma_f32_16x16x32_bf16 v[30:33], v[110:113], v[182:185], v[30:33]
	v_mfma_f32_16x16x32_bf16 v[26:29], v[130:133], v[182:185], v[26:29]
	v_mfma_f32_16x16x32_bf16 v[14:17], v[110:113], v[206:209], v[14:17]
	v_mfma_f32_16x16x32_bf16 v[10:13], v[130:133], v[206:209], v[10:13]
	s_setprio 0
	s_setprio 3
	v_mfma_f32_16x16x32_bf16 v[54:57], v[146:149], v[162:165], 0
	v_mfma_f32_16x16x32_bf16 v[50:53], v[154:157], v[162:165], 0
	v_mfma_f32_16x16x32_bf16 v[38:41], v[146:149], v[170:173], 0
	v_mfma_f32_16x16x32_bf16 v[34:37], v[154:157], v[170:173], 0
	v_mfma_f32_16x16x32_bf16 v[22:25], v[146:149], v[178:181], 0
	v_mfma_f32_16x16x32_bf16 v[18:21], v[154:157], v[178:181], 0
	v_mfma_f32_16x16x32_bf16 v[6:9], v[146:149], v[202:205], 0
	v_mfma_f32_16x16x32_bf16 v[2:5], v[154:157], v[202:205], 0
	v_mfma_f32_16x16x32_bf16 v[54:57], v[150:153], v[166:169], v[54:57]
	v_mfma_f32_16x16x32_bf16 v[50:53], v[158:161], v[166:169], v[50:53]
	v_mfma_f32_16x16x32_bf16 v[38:41], v[150:153], v[174:177], v[38:41]
	v_mfma_f32_16x16x32_bf16 v[34:37], v[158:161], v[174:177], v[34:37]
	v_mfma_f32_16x16x32_bf16 v[22:25], v[150:153], v[182:185], v[22:25]
	v_mfma_f32_16x16x32_bf16 v[18:21], v[158:161], v[182:185], v[18:21]
	v_mfma_f32_16x16x32_bf16 v[6:9], v[150:153], v[206:209], v[6:9]
	v_mfma_f32_16x16x32_bf16 v[2:5], v[158:161], v[206:209], v[2:5]
	s_setprio 0
	s_barrier
	s_add_i32 s64, 0, 0x18000
	s_add_i32 s65, 0, 0x1c000
	v_add_u32_e32 v130, s64, v220
	v_add_u32_e32 v158, s65, v220
	ds_read_b128 v[98:101], v130
	ds_read_b128 v[110:113], v130 offset:1024
	ds_read_b128 v[122:125], v130 offset:2048
	ds_read_b128 v[130:133], v130 offset:3072
	ds_read_b128 v[146:149], v158
	ds_read_b128 v[150:153], v158 offset:1024
	ds_read_b128 v[154:157], v158 offset:2048
	ds_read_b128 v[158:161], v158 offset:3072
	s_add_u32 s38, s38, 0x40000
	s_addc_u32 s39, s39, 0
	s_mov_b32 m0, s45
	ds_read_b128 v[162:165], v227 offset:32768
	ds_read_b128 v[166:169], v227 offset:33792
	ds_read_b128 v[170:173], v227 offset:34816
	ds_read_b128 v[174:177], v227 offset:35840
	ds_read_b128 v[178:181], v227 offset:36864
	ds_read_b128 v[182:185], v227 offset:37888
	ds_read_b128 v[202:205], v227 offset:38912
	ds_read_b128 v[206:209], v227 offset:39936
	global_load_lds_dwordx4 v186, s[38:39]
	s_mov_b32 m0, s48
	s_nop 0
	global_load_lds_dwordx4 v190, s[38:39]
	s_waitcnt vmcnt(8)
	s_waitcnt lgkmcnt(0)
	s_barrier
	s_setprio 3
	s_waitcnt lgkmcnt(0)
	v_mfma_f32_16x16x32_bf16 v[142:145], v[98:101], v[162:165], v[142:145]
	v_mfma_f32_16x16x32_bf16 v[138:141], v[122:125], v[162:165], v[138:141]
	v_mfma_f32_16x16x32_bf16 v[118:121], v[98:101], v[170:173], v[118:121]
	v_mfma_f32_16x16x32_bf16 v[114:117], v[122:125], v[170:173], v[114:117]
	v_mfma_f32_16x16x32_bf16 v[94:97], v[98:101], v[178:181], v[94:97]
	v_mfma_f32_16x16x32_bf16 v[90:93], v[122:125], v[178:181], v[90:93]
	v_mfma_f32_16x16x32_bf16 v[78:81], v[98:101], v[202:205], v[78:81]
	v_mfma_f32_16x16x32_bf16 v[74:77], v[122:125], v[202:205], v[74:77]
	v_mfma_f32_16x16x32_bf16 v[142:145], v[110:113], v[166:169], v[142:145]
	v_mfma_f32_16x16x32_bf16 v[138:141], v[130:133], v[166:169], v[138:141]
	v_mfma_f32_16x16x32_bf16 v[118:121], v[110:113], v[174:177], v[118:121]
	v_mfma_f32_16x16x32_bf16 v[114:117], v[130:133], v[174:177], v[114:117]
	v_mfma_f32_16x16x32_bf16 v[94:97], v[110:113], v[182:185], v[94:97]
	v_mfma_f32_16x16x32_bf16 v[90:93], v[130:133], v[182:185], v[90:93]
	v_mfma_f32_16x16x32_bf16 v[78:81], v[110:113], v[206:209], v[78:81]
	v_mfma_f32_16x16x32_bf16 v[74:77], v[130:133], v[206:209], v[74:77]
	s_setprio 0
	s_setprio 3
	v_mfma_f32_16x16x32_bf16 v[134:137], v[146:149], v[162:165], v[134:137]
	v_mfma_f32_16x16x32_bf16 v[126:129], v[154:157], v[162:165], v[126:129]
	v_mfma_f32_16x16x32_bf16 v[106:109], v[146:149], v[170:173], v[106:109]
	v_mfma_f32_16x16x32_bf16 v[102:105], v[154:157], v[170:173], v[102:105]
	v_mfma_f32_16x16x32_bf16 v[86:89], v[146:149], v[178:181], v[86:89]
	v_mfma_f32_16x16x32_bf16 v[82:85], v[154:157], v[178:181], v[82:85]
	v_mfma_f32_16x16x32_bf16 v[70:73], v[146:149], v[202:205], v[70:73]
	v_mfma_f32_16x16x32_bf16 v[66:69], v[154:157], v[202:205], v[66:69]
	v_mfma_f32_16x16x32_bf16 v[134:137], v[150:153], v[166:169], v[134:137]
	v_mfma_f32_16x16x32_bf16 v[126:129], v[158:161], v[166:169], v[126:129]
	v_mfma_f32_16x16x32_bf16 v[106:109], v[150:153], v[174:177], v[106:109]
	v_mfma_f32_16x16x32_bf16 v[102:105], v[158:161], v[174:177], v[102:105]
	v_mfma_f32_16x16x32_bf16 v[86:89], v[150:153], v[182:185], v[86:89]
	v_mfma_f32_16x16x32_bf16 v[82:85], v[158:161], v[182:185], v[82:85]
	v_mfma_f32_16x16x32_bf16 v[70:73], v[150:153], v[206:209], v[70:73]
	v_mfma_f32_16x16x32_bf16 v[66:69], v[158:161], v[206:209], v[66:69]
	s_setprio 0
	s_barrier
; #define PG8_STAGE_A(b, h, ptr, NX) do { if constexpr (Sched::GATHER) { unsigned gs_[2]; gs_[0] = ((NX) && last_) ? gN[h][0] : gA[h][0]; gs_[1] = ((NX) && last_) ? gN[h][1] : gA[h][1]; PG8_STAGE(PG8_SA(b, h), ptr, gs_); } \
;         else PG8_STAGE(PG8_SA(b, h), (ptr) + ((h) ? hstep : (size_t)0), voffA); } while (0)
; #define PG8_STAGE(bufoff, gbase, voff) do { _Pragma("unroll") for (int _i = 0; _i < 2; ++_i) \
;         __builtin_amdgcn_global_load_lds((const unsigned*)((const char*)(gbase) + (voff)[_i]), (PG8_LAS unsigned*)(lds + (bufoff) + ldsw + _i * 8192), 16, 0, 0); } while (0)
; #define PG8_LDA(dst, b, h) do { _Pragma("unroll") for (int m = 0; m < 4; ++m) _Pragma("unroll") for (int k = 0; k < 2; ++k) dst[m][k] = *(const PG8_LAS bf16x8*)(lds + PG8_SA(b, h) + aoff + m * 2048 + k * 1024); } while (0)
; #define PG8_LDB(dst, b, h) do { _Pragma("unroll") for (int n = 0; n < 2; ++n) _Pragma("unroll") for (int k = 0; k < 2; ++k) dst[n][k] = *(const PG8_LAS bf16x8*)(lds + PG8_SB(b, h) + boff + n * 2048 + k * 1024); } while (0)
; #define PG8_WAIT_V(n) asm volatile("s_waitcnt vmcnt(" #n ")" ::: "memory")
; #define PG8_WAIT_L(n) asm volatile("s_waitcnt lgkmcnt(" #n ")" ::: "memory")
; #define PG8_BAR __builtin_amdgcn_s_barrier()
; template <class Epi, class Sched, bool ALIGN_EPI = false, bool SP2 = false>
; __device__ __forceinline__ void gemm_phase(PG8_LAS unsigned char* lds, const Gemm g, const Sched& S, const Epi& E, const bool skip_epi = false) {
;     ...
;             const bool last = (t == nt - 2); last_ = last && has_next;
;             const char* a1 = cA + (size_t)(t + 1) * kstep;
;             const char* a2 = last ? nA : cA + (size_t)(t + 2) * kstep; const char* b2 = last ? nB : cB + (size_t)(t + 2) * kstep;
;             const char* a3 = a2 + kstep; const char* b3 = b2 + kstep;
;             if (last && has_next) S.a_ready(nxt);
;             if constexpr (SP2) {
;             PG8_LDB(B0, 0, 0); PG8_LDB(B1, 0, 1); PG8_SCHED; PG8_LDA(At, 0, 0); PG8_STAGE_A(1, 1, a1, false);
;             PG8_WAIT_V(8); PG8_WAIT_L(0); PG8_BAR; PG8_MMA(0, 0, At, B0); PG8_MMA(0, 1, At, B1); PG8_BAR; PG8_SCHED;
;     ...
;             PG8_LDA(At, 1, 1); PG8_STAGE(PG8_SB(1, 0), b3, voffB); PG8_STAGE(PG8_SB(1, 1), b3 + hstep, voffB); PG8_STAGE_A(1, 0, a3, true);
;             PG8_WAIT_V(8); PG8_WAIT_L(0); PG8_BAR; PG8_MMA(1, 0, At, B0); PG8_MMA(1, 1, At, B1); PG8_BAR; PG8_SCHED;
	s_add_i32 s38, s64, s40
	s_add_i32 m0, s38, 0xffffff80
	ds_read_b128 v[162:165], v227 offset:49152
	ds_read_b128 v[166:169], v227 offset:50176
	ds_read_b128 v[170:173], v227 offset:51200
	ds_read_b128 v[174:177], v227 offset:52224
	ds_read_b128 v[178:181], v227 offset:53248
	ds_read_b128 v[182:185], v227 offset:54272
	ds_read_b128 v[202:205], v227 offset:55296
	ds_read_b128 v[206:209], v227 offset:56320
	global_load_lds_dwordx4 v[210:211], off offset:128
	s_add_i32 m0, s38, 0x1f80
	s_add_u32 s36, s36, 0x40080
	s_addc_u32 s37, s37, 0
	s_add_i32 s38, s65, s40
	global_load_lds_dwordx4 v[212:213], off offset:128
	s_mov_b32 m0, s38
	s_nop 0
	global_load_lds_dwordx4 v188, s[36:37]
	s_add_i32 m0, s38, 0x2000
	s_nop 0
	global_load_lds_dwordx4 v192, s[36:37]
	s_add_i32 m0, s53, 0xffffff80
	s_nop 0
	global_load_lds_dwordx4 v[214:215], off offset:128
	s_add_i32 m0, s54, 0xffffff80
	s_nop 0
	global_load_lds_dwordx4 v[216:217], off offset:128
	s_waitcnt vmcnt(8)
	s_waitcnt lgkmcnt(0)
	s_barrier
	s_setprio 3
	s_waitcnt lgkmcnt(0)
	v_mfma_f32_16x16x32_bf16 v[62:65], v[98:101], v[162:165], v[62:65]
	v_mfma_f32_16x16x32_bf16 v[58:61], v[122:125], v[162:165], v[58:61]
	v_mfma_f32_16x16x32_bf16 v[46:49], v[98:101], v[170:173], v[46:49]
	v_mfma_f32_16x16x32_bf16 v[42:45], v[122:125], v[170:173], v[42:45]
	v_mfma_f32_16x16x32_bf16 v[30:33], v[98:101], v[178:181], v[30:33]
	v_mfma_f32_16x16x32_bf16 v[26:29], v[122:125], v[178:181], v[26:29]
	v_mfma_f32_16x16x32_bf16 v[14:17], v[98:101], v[202:205], v[14:17]
	v_mfma_f32_16x16x32_bf16 v[10:13], v[122:125], v[202:205], v[10:13]
	v_mfma_f32_16x16x32_bf16 v[62:65], v[110:113], v[166:169], v[62:65]
	v_mfma_f32_16x16x32_bf16 v[58:61], v[130:133], v[166:169], v[58:61]
	v_mfma_f32_16x16x32_bf16 v[46:49], v[110:113], v[174:177], v[46:49]
	v_mfma_f32_16x16x32_bf16 v[42:45], v[130:133], v[174:177], v[42:45]
	v_mfma_f32_16x16x32_bf16 v[30:33], v[110:113], v[182:185], v[30:33]
	v_mfma_f32_16x16x32_bf16 v[26:29], v[130:133], v[182:185], v[26:29]
	v_mfma_f32_16x16x32_bf16 v[14:17], v[110:113], v[206:209], v[14:17]
	v_mfma_f32_16x16x32_bf16 v[10:13], v[130:133], v[206:209], v[10:13]
	s_setprio 0
	s_setprio 3
	v_mfma_f32_16x16x32_bf16 v[54:57], v[146:149], v[162:165], v[54:57]
	v_mfma_f32_16x16x32_bf16 v[50:53], v[154:157], v[162:165], v[50:53]
	v_mfma_f32_16x16x32_bf16 v[38:41], v[146:149], v[170:173], v[38:41]
	v_mfma_f32_16x16x32_bf16 v[34:37], v[154:157], v[170:173], v[34:37]
	v_mfma_f32_16x16x32_bf16 v[22:25], v[146:149], v[178:181], v[22:25]
	v_mfma_f32_16x16x32_bf16 v[18:21], v[154:157], v[178:181], v[18:21]
	v_mfma_f32_16x16x32_bf16 v[6:9], v[146:149], v[202:205], v[6:9]
	v_mfma_f32_16x16x32_bf16 v[2:5], v[154:157], v[202:205], v[2:5]
	v_mfma_f32_16x16x32_bf16 v[54:57], v[150:153], v[166:169], v[54:57]
	v_mfma_f32_16x16x32_bf16 v[50:53], v[158:161], v[166:169], v[50:53]
	v_mfma_f32_16x16x32_bf16 v[38:41], v[150:153], v[174:177], v[38:41]
	v_mfma_f32_16x16x32_bf16 v[34:37], v[158:161], v[174:177], v[34:37]
	v_mfma_f32_16x16x32_bf16 v[22:25], v[150:153], v[182:185], v[22:25]
	v_mfma_f32_16x16x32_bf16 v[18:21], v[158:161], v[182:185], v[18:21]
	v_mfma_f32_16x16x32_bf16 v[6:9], v[150:153], v[206:209], v[6:9]
	v_mfma_f32_16x16x32_bf16 v[2:5], v[158:161], v[206:209], v[2:5]
	s_setprio 0
	s_barrier
	s_add_i32 s63, s63, 2
	s_add_u32 s34, s34, 0x100
	s_addc_u32 s35, s35, 0
	s_add_u32 s61, s61, 0x100
	s_addc_u32 s62, s62, 0
	s_cmp_gt_u32 s63, 13
.LBB0_1324:
	ds_read_b128 v[98:101], v225
	ds_read_b128 v[110:113], v225 offset:1024
	ds_read_b128 v[122:125], v225 offset:2048
	ds_read_b128 v[130:133], v225 offset:3072
	ds_read_b128 v[146:149], v226
	ds_read_b128 v[150:153], v226 offset:1024
	ds_read_b128 v[154:157], v226 offset:2048
	ds_read_b128 v[158:161], v226 offset:3072
	s_add_u32 s36, s34, 0xfffc0080
	s_addc_u32 s37, s35, -1
	s_cmp_eq_u32 s63, 12
	s_cselect_b32 s39, s25, s37
	s_cselect_b32 s38, s31, s36
	s_cselect_b32 s37, s23, s62
	s_cselect_b32 s36, s60, s61
	s_add_i32 m0, s41, 0xc000
	ds_read_b128 v[162:165], v227
	ds_read_b128 v[166:169], v227 offset:1024
	ds_read_b128 v[170:173], v227 offset:2048
	ds_read_b128 v[174:177], v227 offset:3072
	ds_read_b128 v[178:181], v227 offset:4096
	ds_read_b128 v[182:185], v227 offset:5120
	ds_read_b128 v[202:205], v227 offset:6144
	ds_read_b128 v[206:209], v227 offset:7168
	global_load_lds_dwordx4 v194, s[34:35]
	s_add_i32 m0, s41, 0xe000
	s_nop 0
	global_load_lds_dwordx4 v196, s[34:35]
	s_waitcnt vmcnt(8)
	s_waitcnt lgkmcnt(0)
	s_barrier
; #define PG8_STAGE_A(b, h, ptr, NX) do { if constexpr (Sched::GATHER) { unsigned gs_[2]; gs_[0] = ((NX) && last_) ? gN[h][0] : gA[h][0]; gs_[1] = ((NX) && last_) ? gN[h][1] : gA[h][1]; PG8_STAGE(PG8_SA(b, h), ptr, gs_); } \
;         else PG8_STAGE(PG8_SA(b, h), (ptr) + ((h) ? hstep : (size_t)0), voffA); } while (0)
; #define PG8_STAGE(bufoff, gbase, voff) do { _Pragma("unroll") for (int _i = 0; _i < 2; ++_i) \
;         __builtin_amdgcn_global_load_lds((const unsigned*)((const char*)(gbase) + (voff)[_i]), (PG8_LAS unsigned*)(lds + (bufoff) + ldsw + _i * 8192), 16, 0, 0); } while (0)
; #define PG8_LDA(dst, b, h) do { _Pragma("unroll") for (int m = 0; m < 4; ++m) _Pragma("unroll") for (int k = 0; k < 2; ++k) dst[m][k] = *(const PG8_LAS bf16x8*)(lds + PG8_SA(b, h) + aoff + m * 2048 + k * 1024); } while (0)
; #define PG8_LDB(dst, b, h) do { _Pragma("unroll") for (int n = 0; n < 2; ++n) _Pragma("unroll") for (int k = 0; k < 2; ++k) dst[n][k] = *(const PG8_LAS bf16x8*)(lds + PG8_SB(b, h) + boff + n * 2048 + k * 1024); } while (0)
; #define PG8_MMA(ai, bj, At, Bt) do { __builtin_amdgcn_s_setprio(1); _Pragma("unroll") for (int m = 0; m < 4; ++m) _Pragma("unroll") for (int n = 0; n < 2; ++n) _Pragma("unroll") for (int k = 0; k < 2; ++k) \
;         acc[ai][bj][m][n] = __builtin_amdgcn_mfma_f32_16x16x32_bf16(Bt[n][k], At[m][k], acc[ai][bj][m][n], 0, 0, 0); __builtin_amdgcn_s_setprio(0); } while (0)
; #define PG8_WAIT_V(n) asm volatile("s_waitcnt vmcnt(" #n ")" ::: "memory")
; #define PG8_WAIT_L(n) asm volatile("s_waitcnt lgkmcnt(" #n ")" ::: "memory")
; #define PG8_BAR __builtin_amdgcn_s_barrier()
; #define PG8_SCHED __builtin_amdgcn_sched_barrier(0)
; template <class Epi, class Sched, bool ALIGN_EPI = false, bool SP2 = false>
; __device__ __forceinline__ void gemm_phase(PG8_LAS unsigned char* lds, const Gemm g, const Sched& S, const Epi& E, const bool skip_epi = false) {
;     ...
;             PG8_LDB(B0, 0, 0); PG8_LDB(B1, 0, 1); PG8_SCHED; PG8_LDA(At, 0, 0); PG8_STAGE_A(1, 1, a1, false);
;             PG8_WAIT_V(8); PG8_WAIT_L(0); PG8_BAR; PG8_MMA(0, 0, At, B0); PG8_MMA(0, 1, At, B1); PG8_BAR; PG8_SCHED;
;             PG8_LDA(At, 0, 1); PG8_STAGE(PG8_SB(0, 0), b2, voffB); PG8_STAGE(PG8_SB(0, 1), b2 + hstep, voffB); PG8_STAGE_A(0, 0, a2, true);
;             PG8_WAIT_V(8); PG8_WAIT_L(0); PG8_BAR; PG8_MMA(1, 0, At, B0); PG8_MMA(1, 1, At, B1); PG8_BAR; PG8_SCHED;
	s_setprio 3
	s_waitcnt lgkmcnt(0)
	v_mfma_f32_16x16x32_bf16 v[142:145], v[98:101], v[162:165], v[142:145]
	v_mfma_f32_16x16x32_bf16 v[138:141], v[122:125], v[162:165], v[138:141]
	v_mfma_f32_16x16x32_bf16 v[118:121], v[98:101], v[170:173], v[118:121]
	v_mfma_f32_16x16x32_bf16 v[114:117], v[122:125], v[170:173], v[114:117]
	v_mfma_f32_16x16x32_bf16 v[94:97], v[98:101], v[178:181], v[94:97]
	v_mfma_f32_16x16x32_bf16 v[90:93], v[122:125], v[178:181], v[90:93]
	v_mfma_f32_16x16x32_bf16 v[78:81], v[98:101], v[202:205], v[78:81]
	v_mfma_f32_16x16x32_bf16 v[74:77], v[122:125], v[202:205], v[74:77]
	v_mfma_f32_16x16x32_bf16 v[142:145], v[110:113], v[166:169], v[142:145]
	v_mfma_f32_16x16x32_bf16 v[138:141], v[130:133], v[166:169], v[138:141]
	v_mfma_f32_16x16x32_bf16 v[118:121], v[110:113], v[174:177], v[118:121]
	v_mfma_f32_16x16x32_bf16 v[114:117], v[130:133], v[174:177], v[114:117]
	v_mfma_f32_16x16x32_bf16 v[94:97], v[110:113], v[182:185], v[94:97]
	v_mfma_f32_16x16x32_bf16 v[90:93], v[130:133], v[182:185], v[90:93]
	v_mfma_f32_16x16x32_bf16 v[78:81], v[110:113], v[206:209], v[78:81]
	v_mfma_f32_16x16x32_bf16 v[74:77], v[130:133], v[206:209], v[74:77]
	s_setprio 0
	s_setprio 3
	v_mfma_f32_16x16x32_bf16 v[134:137], v[146:149], v[162:165], v[134:137]
	v_mfma_f32_16x16x32_bf16 v[126:129], v[154:157], v[162:165], v[126:129]
	v_mfma_f32_16x16x32_bf16 v[106:109], v[146:149], v[170:173], v[106:109]
	v_mfma_f32_16x16x32_bf16 v[102:105], v[154:157], v[170:173], v[102:105]
	v_mfma_f32_16x16x32_bf16 v[86:89], v[146:149], v[178:181], v[86:89]
	v_mfma_f32_16x16x32_bf16 v[82:85], v[154:157], v[178:181], v[82:85]
	v_mfma_f32_16x16x32_bf16 v[70:73], v[146:149], v[202:205], v[70:73]
	v_mfma_f32_16x16x32_bf16 v[66:69], v[154:157], v[202:205], v[66:69]
	v_mfma_f32_16x16x32_bf16 v[134:137], v[150:153], v[166:169], v[134:137]
	v_mfma_f32_16x16x32_bf16 v[126:129], v[158:161], v[166:169], v[126:129]
	v_mfma_f32_16x16x32_bf16 v[106:109], v[150:153], v[174:177], v[106:109]
	v_mfma_f32_16x16x32_bf16 v[102:105], v[158:161], v[174:177], v[102:105]
	v_mfma_f32_16x16x32_bf16 v[86:89], v[150:153], v[182:185], v[86:89]
	v_mfma_f32_16x16x32_bf16 v[82:85], v[158:161], v[182:185], v[82:85]
	v_mfma_f32_16x16x32_bf16 v[70:73], v[150:153], v[206:209], v[70:73]
	v_mfma_f32_16x16x32_bf16 v[66:69], v[158:161], v[206:209], v[66:69]
	s_setprio 0
	s_barrier
	s_add_i32 s64, s57, s40
	v_lshl_add_u64 v[210:211], s[36:37], 0, v[188:189]
	s_mov_b32 m0, s64
	ds_read_b128 v[162:165], v227 offset:16384
	ds_read_b128 v[166:169], v227 offset:17408
	ds_read_b128 v[170:173], v227 offset:18432
	ds_read_b128 v[174:177], v227 offset:19456
	ds_read_b128 v[178:181], v227 offset:20480
	ds_read_b128 v[182:185], v227 offset:21504
	ds_read_b128 v[202:205], v227 offset:22528
	ds_read_b128 v[206:209], v227 offset:23552
	global_load_lds_dwordx4 v[210:211], off
	s_add_i32 m0, s64, 0x2000
	s_add_u32 s64, s36, 0x40000
	v_lshl_add_u64 v[212:213], s[36:37], 0, v[192:193]
	s_addc_u32 s65, s37, 0
	s_add_i32 s66, s58, s40
	global_load_lds_dwordx4 v[212:213], off
	s_mov_b32 m0, s66
	v_lshl_add_u64 v[216:217], s[38:39], 0, v[190:191]
	global_load_lds_dwordx4 v188, s[64:65]
	s_add_i32 m0, s66, 0x2000
	s_nop 0
	global_load_lds_dwordx4 v192, s[64:65]
	v_lshl_add_u64 v[214:215], s[38:39], 0, v[186:187]
	s_mov_b32 m0, s41
	s_nop 0
	global_load_lds_dwordx4 v[214:215], off
	s_mov_b32 m0, s44
	s_nop 0
	global_load_lds_dwordx4 v[216:217], off
	s_waitcnt vmcnt(8)
	s_waitcnt lgkmcnt(0)
	s_barrier
	s_setprio 3
	s_waitcnt lgkmcnt(0)
	v_mfma_f32_16x16x32_bf16 v[62:65], v[98:101], v[162:165], v[62:65]
	v_mfma_f32_16x16x32_bf16 v[58:61], v[122:125], v[162:165], v[58:61]
	v_mfma_f32_16x16x32_bf16 v[46:49], v[98:101], v[170:173], v[46:49]
	v_mfma_f32_16x16x32_bf16 v[42:45], v[122:125], v[170:173], v[42:45]
	v_mfma_f32_16x16x32_bf16 v[30:33], v[98:101], v[178:181], v[30:33]
	v_mfma_f32_16x16x32_bf16 v[26:29], v[122:125], v[178:181], v[26:29]
	v_mfma_f32_16x16x32_bf16 v[14:17], v[98:101], v[202:205], v[14:17]
	v_mfma_f32_16x16x32_bf16 v[10:13], v[122:125], v[202:205], v[10:13]
	v_mfma_f32_16x16x32_bf16 v[62:65], v[110:113], v[166:169], v[62:65]
	v_mfma_f32_16x16x32_bf16 v[58:61], v[130:133], v[166:169], v[58:61]
	v_mfma_f32_16x16x32_bf16 v[46:49], v[110:113], v[174:177], v[46:49]
	v_mfma_f32_16x16x32_bf16 v[42:45], v[130:133], v[174:177], v[42:45]
	v_mfma_f32_16x16x32_bf16 v[30:33], v[110:113], v[182:185], v[30:33]
	v_mfma_f32_16x16x32_bf16 v[26:29], v[130:133], v[182:185], v[26:29]
	v_mfma_f32_16x16x32_bf16 v[14:17], v[110:113], v[206:209], v[14:17]
	v_mfma_f32_16x16x32_bf16 v[10:13], v[130:133], v[206:209], v[10:13]
	s_setprio 0
	s_setprio 3
	v_mfma_f32_16x16x32_bf16 v[54:57], v[146:149], v[162:165], v[54:57]
	v_mfma_f32_16x16x32_bf16 v[50:53], v[154:157], v[162:165], v[50:53]
	v_mfma_f32_16x16x32_bf16 v[38:41], v[146:149], v[170:173], v[38:41]
	v_mfma_f32_16x16x32_bf16 v[34:37], v[154:157], v[170:173], v[34:37]
	v_mfma_f32_16x16x32_bf16 v[22:25], v[146:149], v[178:181], v[22:25]
	v_mfma_f32_16x16x32_bf16 v[18:21], v[154:157], v[178:181], v[18:21]
	v_mfma_f32_16x16x32_bf16 v[6:9], v[146:149], v[202:205], v[6:9]
	v_mfma_f32_16x16x32_bf16 v[2:5], v[154:157], v[202:205], v[2:5]
	v_mfma_f32_16x16x32_bf16 v[54:57], v[150:153], v[166:169], v[54:57]
	v_mfma_f32_16x16x32_bf16 v[50:53], v[158:161], v[166:169], v[50:53]
	v_mfma_f32_16x16x32_bf16 v[38:41], v[150:153], v[174:177], v[38:41]
	v_mfma_f32_16x16x32_bf16 v[34:37], v[158:161], v[174:177], v[34:37]
	v_mfma_f32_16x16x32_bf16 v[22:25], v[150:153], v[182:185], v[22:25]
	v_mfma_f32_16x16x32_bf16 v[18:21], v[158:161], v[182:185], v[18:21]
	v_mfma_f32_16x16x32_bf16 v[6:9], v[150:153], v[206:209], v[6:9]
	v_mfma_f32_16x16x32_bf16 v[2:5], v[158:161], v[206:209], v[2:5]
	s_setprio 0
	s_barrier
; #define PG8_STAGE_A(b, h, ptr, NX) do { if constexpr (Sched::GATHER) { unsigned gs_[2]; gs_[0] = ((NX) && last_) ? gN[h][0] : gA[h][0]; gs_[1] = ((NX) && last_) ? gN[h][1] : gA[h][1]; PG8_STAGE(PG8_SA(b, h), ptr, gs_); } \
;         else PG8_STAGE(PG8_SA(b, h), (ptr) + ((h) ? hstep : (size_t)0), voffA); } while (0)
; #define PG8_STAGE(bufoff, gbase, voff) do { _Pragma("unroll") for (int _i = 0; _i < 2; ++_i) \
;         __builtin_amdgcn_global_load_lds((const unsigned*)((const char*)(gbase) + (voff)[_i]), (PG8_LAS unsigned*)(lds + (bufoff) + ldsw + _i * 8192), 16, 0, 0); } while (0)
; #define PG8_LDA(dst, b, h) do { _Pragma("unroll") for (int m = 0; m < 4; ++m) _Pragma("unroll") for (int k = 0; k < 2; ++k) dst[m][k] = *(const PG8_LAS bf16x8*)(lds + PG8_SA(b, h) + aoff + m * 2048 + k * 1024); } while (0)
; #define PG8_LDB(dst, b, h) do { _Pragma("unroll") for (int n = 0; n < 2; ++n) _Pragma("unroll") for (int k = 0; k < 2; ++k) dst[n][k] = *(const PG8_LAS bf16x8*)(lds + PG8_SB(b, h) + boff + n * 2048 + k * 1024); } while (0)
; #define PG8_MMA(ai, bj, At, Bt) do { __builtin_amdgcn_s_setprio(1); _Pragma("unroll") for (int m = 0; m < 4; ++m) _Pragma("unroll") for (int n = 0; n < 2; ++n) _Pragma("unroll") for (int k = 0; k < 2; ++k) \
;         acc[ai][bj][m][n] = __builtin_amdgcn_mfma_f32_16x16x32_bf16(Bt[n][k], At[m][k], acc[ai][bj][m][n], 0, 0, 0); __builtin_amdgcn_s_setprio(0); } while (0)
; #define PG8_WAIT_V(n) asm volatile("s_waitcnt vmcnt(" #n ")" ::: "memory")
; #define PG8_WAIT_L(n) asm volatile("s_waitcnt lgkmcnt(" #n ")" ::: "memory")
; #define PG8_BAR __builtin_amdgcn_s_barrier()
; #define PG8_SCHED __builtin_amdgcn_sched_barrier(0)
; template <class Epi, class Sched, bool ALIGN_EPI = false, bool SP2 = false>
; __device__ __forceinline__ void gemm_phase(PG8_LAS unsigned char* lds, const Gemm g, const Sched& S, const Epi& E, const bool skip_epi = false) {
;     ...
;             PG8_LDB(B0, 1, 0); PG8_LDB(B1, 1, 1); PG8_SCHED; PG8_LDA(At, 1, 0); PG8_STAGE_A(0, 1, a2, true);
;             PG8_WAIT_V(8); PG8_WAIT_L(0); PG8_BAR; PG8_MMA(0, 0, At, B0); PG8_MMA(0, 1, At, B1); PG8_BAR; PG8_SCHED;
;             PG8_LDA(At, 1, 1); PG8_STAGE(PG8_SB(1, 0), b3, voffB); PG8_STAGE(PG8_SB(1, 1), b3 + hstep, voffB); PG8_STAGE_A(1, 0, a3, true);
;             PG8_WAIT_V(8); PG8_WAIT_L(0); PG8_BAR; PG8_MMA(1, 0, At, B0); PG8_MMA(1, 1, At, B1); PG8_BAR; PG8_SCHED;
	s_add_i32 s64, 0, 0x18000
	s_add_i32 s65, 0, 0x1c000
	v_add_u32_e32 v130, s64, v220
	v_add_u32_e32 v158, s65, v220
	ds_read_b128 v[98:101], v130
	ds_read_b128 v[110:113], v130 offset:1024
	ds_read_b128 v[122:125], v130 offset:2048
	ds_read_b128 v[130:133], v130 offset:3072
	ds_read_b128 v[146:149], v158
	ds_read_b128 v[150:153], v158 offset:1024
	ds_read_b128 v[154:157], v158 offset:2048
	ds_read_b128 v[158:161], v158 offset:3072
	s_add_u32 s38, s38, 0x40000
	s_addc_u32 s39, s39, 0
	s_mov_b32 m0, s45
	ds_read_b128 v[162:165], v227 offset:32768
	ds_read_b128 v[166:169], v227 offset:33792
	ds_read_b128 v[170:173], v227 offset:34816
	ds_read_b128 v[174:177], v227 offset:35840
	ds_read_b128 v[178:181], v227 offset:36864
	ds_read_b128 v[182:185], v227 offset:37888
	ds_read_b128 v[202:205], v227 offset:38912
	ds_read_b128 v[206:209], v227 offset:39936
	global_load_lds_dwordx4 v186, s[38:39]
	s_mov_b32 m0, s48
	s_nop 0
	global_load_lds_dwordx4 v190, s[38:39]
	s_waitcnt vmcnt(8)
	s_waitcnt lgkmcnt(0)
	s_barrier
	s_setprio 3
	s_waitcnt lgkmcnt(0)
	v_mfma_f32_16x16x32_bf16 v[142:145], v[98:101], v[162:165], v[142:145]
	v_mfma_f32_16x16x32_bf16 v[138:141], v[122:125], v[162:165], v[138:141]
	v_mfma_f32_16x16x32_bf16 v[118:121], v[98:101], v[170:173], v[118:121]
	v_mfma_f32_16x16x32_bf16 v[114:117], v[122:125], v[170:173], v[114:117]
	v_mfma_f32_16x16x32_bf16 v[94:97], v[98:101], v[178:181], v[94:97]
	v_mfma_f32_16x16x32_bf16 v[90:93], v[122:125], v[178:181], v[90:93]
	v_mfma_f32_16x16x32_bf16 v[78:81], v[98:101], v[202:205], v[78:81]
	v_mfma_f32_16x16x32_bf16 v[74:77], v[122:125], v[202:205], v[74:77]
	v_mfma_f32_16x16x32_bf16 v[142:145], v[110:113], v[166:169], v[142:145]
	v_mfma_f32_16x16x32_bf16 v[138:141], v[130:133], v[166:169], v[138:141]
	v_mfma_f32_16x16x32_bf16 v[118:121], v[110:113], v[174:177], v[118:121]
	v_mfma_f32_16x16x32_bf16 v[114:117], v[130:133], v[174:177], v[114:117]
	v_mfma_f32_16x16x32_bf16 v[94:97], v[110:113], v[182:185], v[94:97]
	v_mfma_f32_16x16x32_bf16 v[90:93], v[130:133], v[182:185], v[90:93]
	v_mfma_f32_16x16x32_bf16 v[78:81], v[110:113], v[206:209], v[78:81]
	v_mfma_f32_16x16x32_bf16 v[74:77], v[130:133], v[206:209], v[74:77]
	s_setprio 0
	s_setprio 3
	v_mfma_f32_16x16x32_bf16 v[134:137], v[146:149], v[162:165], v[134:137]
	v_mfma_f32_16x16x32_bf16 v[126:129], v[154:157], v[162:165], v[126:129]
	v_mfma_f32_16x16x32_bf16 v[106:109], v[146:149], v[170:173], v[106:109]
	v_mfma_f32_16x16x32_bf16 v[102:105], v[154:157], v[170:173], v[102:105]
	v_mfma_f32_16x16x32_bf16 v[86:89], v[146:149], v[178:181], v[86:89]
	v_mfma_f32_16x16x32_bf16 v[82:85], v[154:157], v[178:181], v[82:85]
	v_mfma_f32_16x16x32_bf16 v[70:73], v[146:149], v[202:205], v[70:73]
	v_mfma_f32_16x16x32_bf16 v[66:69], v[154:157], v[202:205], v[66:69]
	v_mfma_f32_16x16x32_bf16 v[134:137], v[150:153], v[166:169], v[134:137]
	v_mfma_f32_16x16x32_bf16 v[126:129], v[158:161], v[166:169], v[126:129]
	v_mfma_f32_16x16x32_bf16 v[106:109], v[150:153], v[174:177], v[106:109]
	v_mfma_f32_16x16x32_bf16 v[102:105], v[158:161], v[174:177], v[102:105]
	v_mfma_f32_16x16x32_bf16 v[86:89], v[150:153], v[182:185], v[86:89]
	v_mfma_f32_16x16x32_bf16 v[82:85], v[158:161], v[182:185], v[82:85]
	v_mfma_f32_16x16x32_bf16 v[70:73], v[150:153], v[206:209], v[70:73]
	v_mfma_f32_16x16x32_bf16 v[66:69], v[158:161], v[206:209], v[66:69]
	s_setprio 0
	s_barrier
	s_add_i32 s38, s64, s40
	s_add_i32 m0, s38, 0xffffff80
	ds_read_b128 v[162:165], v227 offset:49152
	ds_read_b128 v[166:169], v227 offset:50176
	ds_read_b128 v[170:173], v227 offset:51200
	ds_read_b128 v[174:177], v227 offset:52224
	ds_read_b128 v[178:181], v227 offset:53248
	ds_read_b128 v[182:185], v227 offset:54272
	ds_read_b128 v[202:205], v227 offset:55296
	ds_read_b128 v[206:209], v227 offset:56320
	global_load_lds_dwordx4 v[210:211], off offset:128
	s_add_i32 m0, s38, 0x1f80
	s_add_u32 s36, s36, 0x40080
	s_addc_u32 s37, s37, 0
	s_add_i32 s38, s65, s40
	global_load_lds_dwordx4 v[212:213], off offset:128
	s_mov_b32 m0, s38
	s_nop 0
	global_load_lds_dwordx4 v188, s[36:37]
	s_add_i32 m0, s38, 0x2000
	s_nop 0
	global_load_lds_dwordx4 v192, s[36:37]
	s_add_i32 m0, s53, 0xffffff80
	s_nop 0
	global_load_lds_dwordx4 v[214:215], off offset:128
	s_add_i32 m0, s54, 0xffffff80
	s_nop 0
	global_load_lds_dwordx4 v[216:217], off offset:128
	s_waitcnt vmcnt(8)
	s_waitcnt lgkmcnt(0)
	s_barrier
	s_setprio 3
	s_waitcnt lgkmcnt(0)
	v_mfma_f32_16x16x32_bf16 v[62:65], v[98:101], v[162:165], v[62:65]
	v_mfma_f32_16x16x32_bf16 v[58:61], v[122:125], v[162:165], v[58:61]
	v_mfma_f32_16x16x32_bf16 v[46:49], v[98:101], v[170:173], v[46:49]
	v_mfma_f32_16x16x32_bf16 v[42:45], v[122:125], v[170:173], v[42:45]
	v_mfma_f32_16x16x32_bf16 v[30:33], v[98:101], v[178:181], v[30:33]
	v_mfma_f32_16x16x32_bf16 v[26:29], v[122:125], v[178:181], v[26:29]
	v_mfma_f32_16x16x32_bf16 v[14:17], v[98:101], v[202:205], v[14:17]
	v_mfma_f32_16x16x32_bf16 v[10:13], v[122:125], v[202:205], v[10:13]
	v_mfma_f32_16x16x32_bf16 v[62:65], v[110:113], v[166:169], v[62:65]
	v_mfma_f32_16x16x32_bf16 v[58:61], v[130:133], v[166:169], v[58:61]
	v_mfma_f32_16x16x32_bf16 v[46:49], v[110:113], v[174:177], v[46:49]
	v_mfma_f32_16x16x32_bf16 v[42:45], v[130:133], v[174:177], v[42:45]
	v_mfma_f32_16x16x32_bf16 v[30:33], v[110:113], v[182:185], v[30:33]
	v_mfma_f32_16x16x32_bf16 v[26:29], v[130:133], v[182:185], v[26:29]
	v_mfma_f32_16x16x32_bf16 v[14:17], v[110:113], v[206:209], v[14:17]
	v_mfma_f32_16x16x32_bf16 v[10:13], v[130:133], v[206:209], v[10:13]
	s_setprio 0
	s_setprio 3
	v_mfma_f32_16x16x32_bf16 v[54:57], v[146:149], v[162:165], v[54:57]
	v_mfma_f32_16x16x32_bf16 v[50:53], v[154:157], v[162:165], v[50:53]
	v_mfma_f32_16x16x32_bf16 v[38:41], v[146:149], v[170:173], v[38:41]
	v_mfma_f32_16x16x32_bf16 v[34:37], v[154:157], v[170:173], v[34:37]
	v_mfma_f32_16x16x32_bf16 v[22:25], v[146:149], v[178:181], v[22:25]
	v_mfma_f32_16x16x32_bf16 v[18:21], v[154:157], v[178:181], v[18:21]
	v_mfma_f32_16x16x32_bf16 v[6:9], v[146:149], v[202:205], v[6:9]
	v_mfma_f32_16x16x32_bf16 v[2:5], v[154:157], v[202:205], v[2:5]
	v_mfma_f32_16x16x32_bf16 v[54:57], v[150:153], v[166:169], v[54:57]
	v_mfma_f32_16x16x32_bf16 v[50:53], v[158:161], v[166:169], v[50:53]
	v_mfma_f32_16x16x32_bf16 v[38:41], v[150:153], v[174:177], v[38:41]
	v_mfma_f32_16x16x32_bf16 v[34:37], v[158:161], v[174:177], v[34:37]
	v_mfma_f32_16x16x32_bf16 v[22:25], v[150:153], v[182:185], v[22:25]
	v_mfma_f32_16x16x32_bf16 v[18:21], v[158:161], v[182:185], v[18:21]
	v_mfma_f32_16x16x32_bf16 v[6:9], v[150:153], v[206:209], v[6:9]
	v_mfma_f32_16x16x32_bf16 v[2:5], v[158:161], v[206:209], v[2:5]
	s_setprio 0
	s_barrier
	s_add_i32 s63, s63, 2
	s_add_u32 s34, s34, 0x100
	s_addc_u32 s35, s35, 0
	s_add_u32 s61, s61, 0x100
	s_addc_u32 s62, s62, 0
	s_cmp_gt_u32 s63, 13
	s_cbranch_scc0 .LBB0_1324
	s_and_b64 vcc, exec, s[14:15]
	s_cbranch_vccz .LBB0_1327
	s_barrier

; #define PG8_GIDX(G_, PM_) do { if constexpr (Sched::GATHER) { _Pragma("unroll") for (int h_ = 0; h_ < 2; ++h_) _Pragma("unroll") for (int i_ = 0; i_ < 2; ++i_) { int R_, C_; stage_rc(tid * 16 + i_ * 8192, R_, C_); \
;         const int src_ = S.rowsrc[(PM_) * BM + h_ * HALF + R_]; G_[h_][i_] = (unsigned)(src_ * K + C_) * 2u; } } } while (0)
; #define PG8_STAGE_A(b, h, ptr, NX) do { if constexpr (Sched::GATHER) { unsigned gs_[2]; gs_[0] = ((NX) && last_) ? gN[h][0] : gA[h][0]; gs_[1] = ((NX) && last_) ? gN[h][1] : gA[h][1]; PG8_STAGE(PG8_SA(b, h), ptr, gs_); } \
;         else PG8_STAGE(PG8_SA(b, h), (ptr) + ((h) ? hstep : (size_t)0), voffA); } while (0)
; #define PG8_STAGE(bufoff, gbase, voff) do { _Pragma("unroll") for (int _i = 0; _i < 2; ++_i) \
;         __builtin_amdgcn_global_load_lds((const unsigned*)((const char*)(gbase) + (voff)[_i]), (PG8_LAS unsigned*)(lds + (bufoff) + ldsw + _i * 8192), 16, 0, 0); } while (0)
; #define PG8_WAIT_V(n) asm volatile("s_waitcnt vmcnt(" #n ")" ::: "memory")
; #define PG8_BAR __builtin_amdgcn_s_barrier()
; template <class Epi, class Sched, bool ALIGN_EPI = false, bool SP2 = false>
; __device__ __forceinline__ void gemm_phase(PG8_LAS unsigned char* lds, const Gemm g, const Sched& S, const Epi& E, const bool skip_epi = false) {
;     ...
;         PG8_STAGE(PG8_SB(1, 0), cB + kstep, voffB); PG8_STAGE_A(1, 0, cA + kstep, false); PG8_STAGE(PG8_SB(1, 1), cB + hstep + kstep, voffB);
;         PG8_WAIT_V(6); PG8_BAR;
;     } else {
;         PG8_STAGE(PG8_SB(0, 0), cB, voffB); PG8_STAGE_A(0, 0, cA, false); PG8_STAGE(PG8_SB(0, 1), cB + hstep, voffB); PG8_STAGE_A(0, 1, cA, false);
;         if (wr == 1) PG8_BAR;
;         PG8_WAIT_V(4); PG8_BAR;
;         PG8_STAGE(PG8_SB(1, 0), cB + kstep, voffB); PG8_STAGE_A(1, 0, cA + kstep, false); PG8_STAGE(PG8_SB(1, 1), cB + hstep + kstep, voffB);
;         PG8_WAIT_V(6); PG8_BAR;
;     }
;     for (;;) {
;         const bool has_next = S.next(ui + 1, nxt);
;         if (has_next) PG8_GIDX(gN, nxt.pm);
;         const char* nA = has_next ? (const char*)g.A + (size_t)nxt.pm * pmstepA + nxt.ko : cA; const char* nB = has_next ? (const char*)g.Bt + (size_t)nxt.pn * tstep + nxt.ko : cB;
.LBB0_1716:
	s_lshl_b32 s6, s6, 5
	s_mov_b64 s[22:23], 0x80
	s_and_b32 s28, s6, 0x60
	s_add_i32 m0, s37, 0x18000
	v_lshl_add_u64 v[4:5], v[4:5], 0, s[22:23]
	s_lshl_b32 s54, s7, 6
	s_lshl_b32 s27, s7, 13
	s_lshl_b32 s29, s28, 7
	s_waitcnt vmcnt(2)
	s_barrier
	global_load_lds_dwordx4 v[4:5], off
	s_add_i32 m0, s37, 0x1a000
	s_add_u32 s24, s78, 0x1aa00080
	v_lshl_add_u64 v[2:3], v[2:3], 0, s[22:23]
	s_addc_u32 s25, s79, 0
	s_add_i32 s55, s37, 0x8000
	s_add_i32 s56, s37, 0xa000
	global_load_lds_dwordx4 v[2:3], off
	s_mov_b32 m0, s55
	s_add_u32 s6, s40, 0x40080
	global_load_lds_dwordx4 v132, s[24:25]
	s_mov_b32 m0, s56
	s_addc_u32 s7, s41, 0
	global_load_lds_dwordx4 v144, s[24:25]
	s_add_i32 m0, s37, 0x1c000
	s_nop 0
	global_load_lds_dwordx4 v134, s[6:7]
	s_add_i32 m0, s37, 0x1e000
	v_and_b32_e32 v145, 15, v6
	global_load_lds_dwordx4 v136, s[6:7]
	v_and_b32_e32 v2, 48, v6
	v_lshlrev_b32_e32 v3, 2, v6
	v_lshl_or_b32 v2, v145, 6, v2
	v_and_b32_e32 v3, 32, v3
	s_waitcnt vmcnt(6)
	s_cmpk_lt_u32 s26, 0x100
	v_bitop3_b32 v4, v2, s27, v3 bitop3:0xde
	v_bitop3_b32 v154, s29, v2, v3 bitop3:0xf6
	s_cselect_b64 s[26:27], -1, 0
	v_and_b32_e32 v2, 3, v6
	v_and_b32_e32 v3, 60, v6
	s_add_i32 s58, 0, 0x10000
	s_add_i32 s59, 0, 0x14000
	v_bfe_u32 v155, v6, 2, 4
	v_lshl_or_b32 v156, v2, 6, v3
	s_ashr_i32 s57, s97, 31
	v_lshl_or_b32 v157, v2, 3, s28
	v_mov_b64_e32 v[138:139], s[4:5]
	v_add_u32_e32 v158, s58, v154
	v_add_u32_e32 v159, s59, v154
	v_add_u32_e32 v160, 0, v4
	s_movk_i32 s60, 0x1c00
	v_mov_b32_e32 v161, v133
	v_mov_b32_e32 v162, v133
	v_mov_b32_e32 v163, v133
	v_mov_b32_e32 v164, v133
	v_mov_b32_e32 v130, v132
	s_barrier
	s_branch .LBB0_1719

; #define PG8_GIDX(G_, PM_) do { if constexpr (Sched::GATHER) { _Pragma("unroll") for (int h_ = 0; h_ < 2; ++h_) _Pragma("unroll") for (int i_ = 0; i_ < 2; ++i_) { int R_, C_; stage_rc(tid * 16 + i_ * 8192, R_, C_); \
;         const int src_ = S.rowsrc[(PM_) * BM + h_ * HALF + R_]; G_[h_][i_] = (unsigned)(src_ * K + C_) * 2u; } } } while (0)
; #define PG8_STAGE_A(b, h, ptr, NX) do { if constexpr (Sched::GATHER) { unsigned gs_[2]; gs_[0] = ((NX) && last_) ? gN[h][0] : gA[h][0]; gs_[1] = ((NX) && last_) ? gN[h][1] : gA[h][1]; PG8_STAGE(PG8_SA(b, h), ptr, gs_); } \
;         else PG8_STAGE(PG8_SA(b, h), (ptr) + ((h) ? hstep : (size_t)0), voffA); } while (0)
; #define PG8_LDA(dst, b, h) do { _Pragma("unroll") for (int m = 0; m < 4; ++m) _Pragma("unroll") for (int k = 0; k < 2; ++k) dst[m][k] = *(const PG8_LAS bf16x8*)(lds + PG8_SA(b, h) + aoff + m * 2048 + k * 1024); } while (0)
; template <class Epi, class Sched, bool ALIGN_EPI = false, bool SP2 = false>
; __device__ __forceinline__ void gemm_phase(PG8_LAS unsigned char* lds, const Gemm g, const Sched& S, const Epi& E, const bool skip_epi = false) {
;     ...
;         const bool has_next = S.next(ui + 1, nxt);
;         if (has_next) PG8_GIDX(gN, nxt.pm);
;         const char* nA = has_next ? (const char*)g.A + (size_t)nxt.pm * pmstepA + nxt.ko : cA; const char* nB = has_next ? (const char*)g.Bt + (size_t)nxt.pn * tstep + nxt.ko : cB;
;         for (int t = 0; t < nt; t += 2) {
;             const bool last = (t == nt - 2); last_ = last && has_next;
;             const char* a1 = cA + (size_t)(t + 1) * kstep;
;             const char* a2 = last ? nA : cA + (size_t)(t + 2) * kstep; const char* b2 = last ? nB : cB + (size_t)(t + 2) * kstep;
;             const char* a3 = a2 + kstep; const char* b3 = b2 + kstep;
;             if (last && has_next) S.a_ready(nxt);
;             if constexpr (SP2) {
;             PG8_LDB(B0, 0, 0); PG8_LDB(B1, 0, 1); PG8_SCHED; PG8_LDA(At, 0, 0); PG8_STAGE_A(1, 1, a1, false);
;             PG8_WAIT_V(8); PG8_WAIT_L(0); PG8_BAR; PG8_MMA(0, 0, At, B0); PG8_MMA(0, 1, At, B1); PG8_BAR; PG8_SCHED;
;             PG8_LDA(At, 0, 1); PG8_STAGE(PG8_SB(0, 0), b2, voffB); PG8_STAGE(PG8_SB(0, 1), b2 + hstep, voffB); PG8_STAGE_A(0, 0, a2, true);
;             PG8_WAIT_V(8); PG8_WAIT_L(0); PG8_BAR; PG8_MMA(1, 0, At, B0); PG8_MMA(1, 1, At, B1); PG8_BAR; PG8_SCHED;
.Lg5_zero:
.LBB0_1727:
	s_mov_b32 s29, s41
	s_mov_b32 s31, s40
	v_mov_b32_e32 v143, v133
	v_mov_b32_e32 v141, v133
	s_add_u32 s61, s40, 0x100
	v_lshl_add_u64 v[146:147], s[24:25], 0, v[140:141]
	v_lshl_add_u64 v[148:149], s[24:25], 0, v[142:143]
	s_addc_u32 s62, s41, 0
	s_mov_b32 s63, -2
	s_mov_b64 s[40:41], 0
	ds_read_b128 v[166:169], v158
	ds_read_b128 v[170:173], v158 offset:1024
	ds_read_b128 v[174:177], v158 offset:2048
	ds_read_b128 v[178:181], v158 offset:3072
	ds_read_b128 v[182:185], v159
	ds_read_b128 v[186:189], v159 offset:1024
	ds_read_b128 v[190:193], v159 offset:2048
	ds_read_b128 v[194:197], v159 offset:3072
	s_add_u32 s42, s78, s40
	s_addc_u32 s43, s79, s41
	s_add_u32 s44, s42, 0x1aa00100
	s_addc_u32 s45, s43, 0
	s_add_u32 s66, s61, s40
	s_addc_u32 s67, s62, s41
	s_cmpk_eq_i32 s40, 0x700
	s_cselect_b64 s[64:65], -1, 0
	s_and_b64 s[42:43], s[64:65], exec
	s_cselect_b32 s45, s87, s45
	s_cselect_b32 s44, s86, s44
	s_cselect_b32 s42, s31, s66
	s_cselect_b32 s43, s29, s67
	s_and_b64 vcc, s[6:7], s[64:65]
	v_lshl_add_u64 v[226:227], v[148:149], 0, s[40:41]
	s_add_i32 m0, s37, 0xc000
	ds_read_b128 v[198:201], v160
	ds_read_b128 v[202:205], v160 offset:1024
	ds_read_b128 v[206:209], v160 offset:2048
	ds_read_b128 v[210:213], v160 offset:3072
	ds_read_b128 v[214:217], v160 offset:4096
	ds_read_b128 v[218:221], v160 offset:5120
	ds_read_b128 v[222:225], v160 offset:6144
	ds_read_b128 v[230:233], v160 offset:7168
	global_load_lds_dwordx4 v[226:227], off
	v_lshl_add_u64 v[226:227], v[146:147], 0, s[40:41]
	s_add_i32 m0, s37, 0xe000
	s_nop 0
	global_load_lds_dwordx4 v[226:227], off
	s_waitcnt vmcnt(8)
	s_waitcnt lgkmcnt(0)
	s_barrier
	s_setprio 3
	s_waitcnt lgkmcnt(0)
	v_mfma_f32_16x16x32_bf16 v[126:129], v[166:169], v[198:201], 0
	v_mfma_f32_16x16x32_bf16 v[122:125], v[174:177], v[198:201], 0
	v_mfma_f32_16x16x32_bf16 v[110:113], v[166:169], v[206:209], 0
	v_mfma_f32_16x16x32_bf16 v[106:109], v[174:177], v[206:209], 0
	v_mfma_f32_16x16x32_bf16 v[94:97], v[166:169], v[214:217], 0
	v_mfma_f32_16x16x32_bf16 v[90:93], v[174:177], v[214:217], 0
	v_mfma_f32_16x16x32_bf16 v[78:81], v[166:169], v[222:225], 0
	v_mfma_f32_16x16x32_bf16 v[74:77], v[174:177], v[222:225], 0
	v_mfma_f32_16x16x32_bf16 v[126:129], v[170:173], v[202:205], v[126:129]
	v_mfma_f32_16x16x32_bf16 v[122:125], v[178:181], v[202:205], v[122:125]
	v_mfma_f32_16x16x32_bf16 v[110:113], v[170:173], v[210:213], v[110:113]
	v_mfma_f32_16x16x32_bf16 v[106:109], v[178:181], v[210:213], v[106:109]
	v_mfma_f32_16x16x32_bf16 v[94:97], v[170:173], v[218:221], v[94:97]
	v_mfma_f32_16x16x32_bf16 v[90:93], v[178:181], v[218:221], v[90:93]
	v_mfma_f32_16x16x32_bf16 v[78:81], v[170:173], v[230:233], v[78:81]
	v_mfma_f32_16x16x32_bf16 v[74:77], v[178:181], v[230:233], v[74:77]
	s_setprio 0
	s_setprio 3
	v_mfma_f32_16x16x32_bf16 v[118:121], v[182:185], v[198:201], 0
	v_mfma_f32_16x16x32_bf16 v[114:117], v[190:193], v[198:201], 0
	v_mfma_f32_16x16x32_bf16 v[102:105], v[182:185], v[206:209], 0
	v_mfma_f32_16x16x32_bf16 v[98:101], v[190:193], v[206:209], 0
	v_mfma_f32_16x16x32_bf16 v[86:89], v[182:185], v[214:217], 0
	v_mfma_f32_16x16x32_bf16 v[82:85], v[190:193], v[214:217], 0
	v_mfma_f32_16x16x32_bf16 v[70:73], v[182:185], v[222:225], 0
	v_mfma_f32_16x16x32_bf16 v[66:69], v[190:193], v[222:225], 0
	v_mfma_f32_16x16x32_bf16 v[118:121], v[186:189], v[202:205], v[118:121]
	v_mfma_f32_16x16x32_bf16 v[114:117], v[194:197], v[202:205], v[114:117]
	v_mfma_f32_16x16x32_bf16 v[102:105], v[186:189], v[210:213], v[102:105]
	v_mfma_f32_16x16x32_bf16 v[98:101], v[194:197], v[210:213], v[98:101]
	v_mfma_f32_16x16x32_bf16 v[86:89], v[186:189], v[218:221], v[86:89]
	v_mfma_f32_16x16x32_bf16 v[82:85], v[194:197], v[218:221], v[82:85]
	v_mfma_f32_16x16x32_bf16 v[70:73], v[186:189], v[230:233], v[70:73]
	v_mfma_f32_16x16x32_bf16 v[66:69], v[194:197], v[230:233], v[66:69]
	s_setprio 0
	s_barrier
	s_add_i32 s64, s58, s50
	v_lshl_add_u64 v[226:227], s[42:43], 0, v[134:135]
	s_mov_b32 m0, s64
	ds_read_b128 v[198:201], v160 offset:16384
	ds_read_b128 v[202:205], v160 offset:17408
	ds_read_b128 v[206:209], v160 offset:18432
	ds_read_b128 v[210:213], v160 offset:19456
	ds_read_b128 v[214:217], v160 offset:20480
	ds_read_b128 v[218:221], v160 offset:21504
	ds_read_b128 v[222:225], v160 offset:22528
	ds_read_b128 v[230:233], v160 offset:23552
	global_load_lds_dwordx4 v[226:227], off
	s_add_i32 m0, s64, 0x2000
	s_add_u32 s64, s42, 0x40000
	v_lshl_add_u64 v[234:235], s[42:43], 0, v[136:137]
	s_addc_u32 s65, s43, 0
	s_add_i32 s66, s59, s50
	global_load_lds_dwordx4 v[234:235], off
	s_mov_b32 m0, s66
	v_cndmask_b32_e32 v132, v130, v164, vcc
	global_load_lds_dwordx4 v134, s[64:65]
	s_add_i32 m0, s66, 0x2000
	v_lshl_add_u64 v[238:239], s[44:45], 0, v[132:133]
	global_load_lds_dwordx4 v136, s[64:65]
	s_mov_b32 m0, s37
	v_cndmask_b32_e32 v236, v144, v163, vcc
	global_load_lds_dwordx4 v132, s[44:45]
	s_mov_b32 m0, s39
	v_mov_b32_e32 v237, v133
	global_load_lds_dwordx4 v236, s[44:45]
	s_waitcnt vmcnt(8)
	s_waitcnt lgkmcnt(0)
	v_lshl_add_u64 v[236:237], s[44:45], 0, v[236:237]
	s_barrier
; #define PG8_STAGE_A(b, h, ptr, NX) do { if constexpr (Sched::GATHER) { unsigned gs_[2]; gs_[0] = ((NX) && last_) ? gN[h][0] : gA[h][0]; gs_[1] = ((NX) && last_) ? gN[h][1] : gA[h][1]; PG8_STAGE(PG8_SA(b, h), ptr, gs_); } \
;         else PG8_STAGE(PG8_SA(b, h), (ptr) + ((h) ? hstep : (size_t)0), voffA); } while (0)
; #define PG8_LDA(dst, b, h) do { _Pragma("unroll") for (int m = 0; m < 4; ++m) _Pragma("unroll") for (int k = 0; k < 2; ++k) dst[m][k] = *(const PG8_LAS bf16x8*)(lds + PG8_SA(b, h) + aoff + m * 2048 + k * 1024); } while (0)
; #define PG8_LDB(dst, b, h) do { _Pragma("unroll") for (int n = 0; n < 2; ++n) _Pragma("unroll") for (int k = 0; k < 2; ++k) dst[n][k] = *(const PG8_LAS bf16x8*)(lds + PG8_SB(b, h) + boff + n * 2048 + k * 1024); } while (0)
; #define PG8_MMA(ai, bj, At, Bt) do { __builtin_amdgcn_s_setprio(1); _Pragma("unroll") for (int m = 0; m < 4; ++m) _Pragma("unroll") for (int n = 0; n < 2; ++n) _Pragma("unroll") for (int k = 0; k < 2; ++k) \
;         acc[ai][bj][m][n] = __builtin_amdgcn_mfma_f32_16x16x32_bf16(Bt[n][k], At[m][k], acc[ai][bj][m][n], 0, 0, 0); __builtin_amdgcn_s_setprio(0); } while (0)
; #define PG8_WAIT_V(n) asm volatile("s_waitcnt vmcnt(" #n ")" ::: "memory")
; #define PG8_WAIT_L(n) asm volatile("s_waitcnt lgkmcnt(" #n ")" ::: "memory")
; #define PG8_BAR __builtin_amdgcn_s_barrier()
; #define PG8_SCHED __builtin_amdgcn_sched_barrier(0)
; template <class Epi, class Sched, bool ALIGN_EPI = false, bool SP2 = false>
; __device__ __forceinline__ void gemm_phase(PG8_LAS unsigned char* lds, const Gemm g, const Sched& S, const Epi& E, const bool skip_epi = false) {
;     ...
;             PG8_WAIT_V(8); PG8_WAIT_L(0); PG8_BAR; PG8_MMA(1, 0, At, B0); PG8_MMA(1, 1, At, B1); PG8_BAR; PG8_SCHED;
;             PG8_LDB(B0, 1, 0); PG8_LDB(B1, 1, 1); PG8_SCHED; PG8_LDA(At, 1, 0); PG8_STAGE_A(0, 1, a2, true);
;             PG8_WAIT_V(8); PG8_WAIT_L(0); PG8_BAR; PG8_MMA(0, 0, At, B0); PG8_MMA(0, 1, At, B1); PG8_BAR; PG8_SCHED;
	s_setprio 3
	s_waitcnt lgkmcnt(0)
	v_mfma_f32_16x16x32_bf16 v[62:65], v[166:169], v[198:201], 0
	v_mfma_f32_16x16x32_bf16 v[58:61], v[174:177], v[198:201], 0
	v_mfma_f32_16x16x32_bf16 v[38:41], v[166:169], v[206:209], 0
	v_mfma_f32_16x16x32_bf16 v[34:37], v[174:177], v[206:209], 0
	v_mfma_f32_16x16x32_bf16 v[22:25], v[166:169], v[214:217], 0
	v_mfma_f32_16x16x32_bf16 v[18:21], v[174:177], v[214:217], 0
	v_mfma_f32_16x16x32_bf16 v[6:9], v[166:169], v[222:225], 0
	v_mfma_f32_16x16x32_bf16 v[2:5], v[174:177], v[222:225], 0
	v_mfma_f32_16x16x32_bf16 v[62:65], v[170:173], v[202:205], v[62:65]
	v_mfma_f32_16x16x32_bf16 v[58:61], v[178:181], v[202:205], v[58:61]
	v_mfma_f32_16x16x32_bf16 v[38:41], v[170:173], v[210:213], v[38:41]
	v_mfma_f32_16x16x32_bf16 v[34:37], v[178:181], v[210:213], v[34:37]
	v_mfma_f32_16x16x32_bf16 v[22:25], v[170:173], v[218:221], v[22:25]
	v_mfma_f32_16x16x32_bf16 v[18:21], v[178:181], v[218:221], v[18:21]
	v_mfma_f32_16x16x32_bf16 v[6:9], v[170:173], v[230:233], v[6:9]
	v_mfma_f32_16x16x32_bf16 v[2:5], v[178:181], v[230:233], v[2:5]
	s_setprio 0
	s_setprio 3
	v_mfma_f32_16x16x32_bf16 v[50:53], v[182:185], v[198:201], 0
	v_mfma_f32_16x16x32_bf16 v[42:45], v[190:193], v[198:201], 0
	v_mfma_f32_16x16x32_bf16 v[54:57], v[182:185], v[206:209], 0
	v_mfma_f32_16x16x32_bf16 v[46:49], v[190:193], v[206:209], 0
	v_mfma_f32_16x16x32_bf16 v[30:33], v[182:185], v[214:217], 0
	v_mfma_f32_16x16x32_bf16 v[26:29], v[190:193], v[214:217], 0
	v_mfma_f32_16x16x32_bf16 v[14:17], v[182:185], v[222:225], 0
	v_mfma_f32_16x16x32_bf16 v[10:13], v[190:193], v[222:225], 0
	v_mfma_f32_16x16x32_bf16 v[50:53], v[186:189], v[202:205], v[50:53]
	v_mfma_f32_16x16x32_bf16 v[42:45], v[194:197], v[202:205], v[42:45]
	v_mfma_f32_16x16x32_bf16 v[54:57], v[186:189], v[210:213], v[54:57]
	v_mfma_f32_16x16x32_bf16 v[46:49], v[194:197], v[210:213], v[46:49]
	v_mfma_f32_16x16x32_bf16 v[30:33], v[186:189], v[218:221], v[30:33]
	v_mfma_f32_16x16x32_bf16 v[26:29], v[194:197], v[218:221], v[26:29]
	v_mfma_f32_16x16x32_bf16 v[14:17], v[186:189], v[230:233], v[14:17]
	v_mfma_f32_16x16x32_bf16 v[10:13], v[194:197], v[230:233], v[10:13]
	s_setprio 0
	s_barrier
	s_add_i32 s64, 0, 0x18000
	v_add_u32_e32 v132, s64, v154
	s_add_i32 s65, 0, 0x1c000
	ds_read_b128 v[166:169], v132
	ds_read_b128 v[170:173], v132 offset:1024
	ds_read_b128 v[174:177], v132 offset:2048
	ds_read_b128 v[178:181], v132 offset:3072
	v_add_u32_e32 v132, s65, v154
	ds_read_b128 v[182:185], v132
	ds_read_b128 v[186:189], v132 offset:1024
	ds_read_b128 v[190:193], v132 offset:2048
	ds_read_b128 v[194:197], v132 offset:3072
	s_mov_b32 m0, s51
	v_cndmask_b32_e32 v132, v142, v162, vcc
	ds_read_b128 v[198:201], v160 offset:32768
	ds_read_b128 v[202:205], v160 offset:33792
	ds_read_b128 v[206:209], v160 offset:34816
	ds_read_b128 v[210:213], v160 offset:35840
	ds_read_b128 v[214:217], v160 offset:36864
	ds_read_b128 v[218:221], v160 offset:37888
	ds_read_b128 v[222:225], v160 offset:38912
	ds_read_b128 v[230:233], v160 offset:39936
	v_cndmask_b32_e32 v141, v140, v161, vcc
	global_load_lds_dwordx4 v132, s[44:45]
	s_mov_b32 m0, s52
	s_nop 0
	global_load_lds_dwordx4 v141, s[44:45]
	s_waitcnt vmcnt(8)
	s_waitcnt lgkmcnt(0)
	s_barrier
	s_setprio 3
	s_waitcnt lgkmcnt(0)
	v_mfma_f32_16x16x32_bf16 v[126:129], v[166:169], v[198:201], v[126:129]
	v_mfma_f32_16x16x32_bf16 v[122:125], v[174:177], v[198:201], v[122:125]
	v_mfma_f32_16x16x32_bf16 v[110:113], v[166:169], v[206:209], v[110:113]
	v_mfma_f32_16x16x32_bf16 v[106:109], v[174:177], v[206:209], v[106:109]
	v_mfma_f32_16x16x32_bf16 v[94:97], v[166:169], v[214:217], v[94:97]
	v_mfma_f32_16x16x32_bf16 v[90:93], v[174:177], v[214:217], v[90:93]
	v_mfma_f32_16x16x32_bf16 v[78:81], v[166:169], v[222:225], v[78:81]
	v_mfma_f32_16x16x32_bf16 v[74:77], v[174:177], v[222:225], v[74:77]
	v_mfma_f32_16x16x32_bf16 v[126:129], v[170:173], v[202:205], v[126:129]
	v_mfma_f32_16x16x32_bf16 v[122:125], v[178:181], v[202:205], v[122:125]
	v_mfma_f32_16x16x32_bf16 v[110:113], v[170:173], v[210:213], v[110:113]
	v_mfma_f32_16x16x32_bf16 v[106:109], v[178:181], v[210:213], v[106:109]
	v_mfma_f32_16x16x32_bf16 v[94:97], v[170:173], v[218:221], v[94:97]
	v_mfma_f32_16x16x32_bf16 v[90:93], v[178:181], v[218:221], v[90:93]
	v_mfma_f32_16x16x32_bf16 v[78:81], v[170:173], v[230:233], v[78:81]
	v_mfma_f32_16x16x32_bf16 v[74:77], v[178:181], v[230:233], v[74:77]
	s_setprio 0
	s_setprio 3
	v_mfma_f32_16x16x32_bf16 v[118:121], v[182:185], v[198:201], v[118:121]
	v_mfma_f32_16x16x32_bf16 v[114:117], v[190:193], v[198:201], v[114:117]
	v_mfma_f32_16x16x32_bf16 v[102:105], v[182:185], v[206:209], v[102:105]
	v_mfma_f32_16x16x32_bf16 v[98:101], v[190:193], v[206:209], v[98:101]
	v_mfma_f32_16x16x32_bf16 v[86:89], v[182:185], v[214:217], v[86:89]
	v_mfma_f32_16x16x32_bf16 v[82:85], v[190:193], v[214:217], v[82:85]
	v_mfma_f32_16x16x32_bf16 v[70:73], v[182:185], v[222:225], v[70:73]
	v_mfma_f32_16x16x32_bf16 v[66:69], v[190:193], v[222:225], v[66:69]
	v_mfma_f32_16x16x32_bf16 v[118:121], v[186:189], v[202:205], v[118:121]
	v_mfma_f32_16x16x32_bf16 v[114:117], v[194:197], v[202:205], v[114:117]
	v_mfma_f32_16x16x32_bf16 v[102:105], v[186:189], v[210:213], v[102:105]
	v_mfma_f32_16x16x32_bf16 v[98:101], v[194:197], v[210:213], v[98:101]
	v_mfma_f32_16x16x32_bf16 v[86:89], v[186:189], v[218:221], v[86:89]
	v_mfma_f32_16x16x32_bf16 v[82:85], v[194:197], v[218:221], v[82:85]
	v_mfma_f32_16x16x32_bf16 v[70:73], v[186:189], v[230:233], v[70:73]
	v_mfma_f32_16x16x32_bf16 v[66:69], v[194:197], v[230:233], v[66:69]
	s_setprio 0
	s_barrier
; #define PG8_GIDX(G_, PM_) do { if constexpr (Sched::GATHER) { _Pragma("unroll") for (int h_ = 0; h_ < 2; ++h_) _Pragma("unroll") for (int i_ = 0; i_ < 2; ++i_) { int R_, C_; stage_rc(tid * 16 + i_ * 8192, R_, C_); \
;         const int src_ = S.rowsrc[(PM_) * BM + h_ * HALF + R_]; G_[h_][i_] = (unsigned)(src_ * K + C_) * 2u; } } } while (0)
; #define PG8_STAGE_A(b, h, ptr, NX) do { if constexpr (Sched::GATHER) { unsigned gs_[2]; gs_[0] = ((NX) && last_) ? gN[h][0] : gA[h][0]; gs_[1] = ((NX) && last_) ? gN[h][1] : gA[h][1]; PG8_STAGE(PG8_SA(b, h), ptr, gs_); } \
;         else PG8_STAGE(PG8_SA(b, h), (ptr) + ((h) ? hstep : (size_t)0), voffA); } while (0)
; #define PG8_STAGE(bufoff, gbase, voff) do { _Pragma("unroll") for (int _i = 0; _i < 2; ++_i) \
;         __builtin_amdgcn_global_load_lds((const unsigned*)((const char*)(gbase) + (voff)[_i]), (PG8_LAS unsigned*)(lds + (bufoff) + ldsw + _i * 8192), 16, 0, 0); } while (0)
; #define PG8_LDA(dst, b, h) do { _Pragma("unroll") for (int m = 0; m < 4; ++m) _Pragma("unroll") for (int k = 0; k < 2; ++k) dst[m][k] = *(const PG8_LAS bf16x8*)(lds + PG8_SA(b, h) + aoff + m * 2048 + k * 1024); } while (0)
; #define PG8_MMA(ai, bj, At, Bt) do { __builtin_amdgcn_s_setprio(1); _Pragma("unroll") for (int m = 0; m < 4; ++m) _Pragma("unroll") for (int n = 0; n < 2; ++n) _Pragma("unroll") for (int k = 0; k < 2; ++k) \
;         acc[ai][bj][m][n] = __builtin_amdgcn_mfma_f32_16x16x32_bf16(Bt[n][k], At[m][k], acc[ai][bj][m][n], 0, 0, 0); __builtin_amdgcn_s_setprio(0); } while (0)
; #define PG8_WAIT_V(n) asm volatile("s_waitcnt vmcnt(" #n ")" ::: "memory")
; template <class Epi, class Sched, bool ALIGN_EPI = false, bool SP2 = false>
; __device__ __forceinline__ void gemm_phase(PG8_LAS unsigned char* lds, const Gemm g, const Sched& S, const Epi& E, const bool skip_epi = false) {
;     ...
;         const bool has_next = S.next(ui + 1, nxt);
;         if (has_next) PG8_GIDX(gN, nxt.pm);
;         const char* nA = has_next ? (const char*)g.A + (size_t)nxt.pm * pmstepA + nxt.ko : cA; const char* nB = has_next ? (const char*)g.Bt + (size_t)nxt.pn * tstep + nxt.ko : cB;
;     ...
;             PG8_LDA(At, 1, 1); PG8_STAGE(PG8_SB(1, 0), b3, voffB); PG8_STAGE(PG8_SB(1, 1), b3 + hstep, voffB); PG8_STAGE_A(1, 0, a3, true);
;             PG8_WAIT_V(8); PG8_WAIT_L(0); PG8_BAR; PG8_MMA(1, 0, At, B0); PG8_MMA(1, 1, At, B1); PG8_BAR; PG8_SCHED;
	s_add_i32 s44, s64, s50
	s_add_i32 m0, s44, 0xffffff80
	ds_read_b128 v[198:201], v160 offset:49152
	ds_read_b128 v[202:205], v160 offset:50176
	ds_read_b128 v[206:209], v160 offset:51200
	ds_read_b128 v[210:213], v160 offset:52224
	ds_read_b128 v[214:217], v160 offset:53248
	ds_read_b128 v[218:221], v160 offset:54272
	ds_read_b128 v[222:225], v160 offset:55296
	ds_read_b128 v[230:233], v160 offset:56320
	global_load_lds_dwordx4 v[226:227], off offset:128
	s_add_i32 m0, s44, 0x1f80
	s_add_u32 s42, s42, 0x40080
	s_addc_u32 s43, s43, 0
	s_add_i32 s44, s65, s50
	global_load_lds_dwordx4 v[234:235], off offset:128
	s_mov_b32 m0, s44
	s_nop 0
	global_load_lds_dwordx4 v134, s[42:43]
	s_add_i32 m0, s44, 0x2000
	s_nop 0
	global_load_lds_dwordx4 v136, s[42:43]
	s_add_i32 m0, s55, 0xffffff80
	s_nop 0
	global_load_lds_dwordx4 v[238:239], off offset:128
	s_add_i32 m0, s56, 0xffffff80
	s_nop 0
	global_load_lds_dwordx4 v[236:237], off offset:128
	s_waitcnt vmcnt(8)
	s_waitcnt lgkmcnt(0)
	s_barrier
	s_setprio 3
	s_waitcnt lgkmcnt(0)
	v_mfma_f32_16x16x32_bf16 v[62:65], v[166:169], v[198:201], v[62:65]
	v_mfma_f32_16x16x32_bf16 v[58:61], v[174:177], v[198:201], v[58:61]
	v_mfma_f32_16x16x32_bf16 v[38:41], v[166:169], v[206:209], v[38:41]
	v_mfma_f32_16x16x32_bf16 v[34:37], v[174:177], v[206:209], v[34:37]
	v_mfma_f32_16x16x32_bf16 v[22:25], v[166:169], v[214:217], v[22:25]
	v_mfma_f32_16x16x32_bf16 v[18:21], v[174:177], v[214:217], v[18:21]
	v_mfma_f32_16x16x32_bf16 v[6:9], v[166:169], v[222:225], v[6:9]
	v_mfma_f32_16x16x32_bf16 v[2:5], v[174:177], v[222:225], v[2:5]
	v_mfma_f32_16x16x32_bf16 v[62:65], v[170:173], v[202:205], v[62:65]
	v_mfma_f32_16x16x32_bf16 v[58:61], v[178:181], v[202:205], v[58:61]
	v_mfma_f32_16x16x32_bf16 v[38:41], v[170:173], v[210:213], v[38:41]
	v_mfma_f32_16x16x32_bf16 v[34:37], v[178:181], v[210:213], v[34:37]
	v_mfma_f32_16x16x32_bf16 v[22:25], v[170:173], v[218:221], v[22:25]
	v_mfma_f32_16x16x32_bf16 v[18:21], v[178:181], v[218:221], v[18:21]
	v_mfma_f32_16x16x32_bf16 v[6:9], v[170:173], v[230:233], v[6:9]
	v_mfma_f32_16x16x32_bf16 v[2:5], v[178:181], v[230:233], v[2:5]
	s_setprio 0
	s_setprio 3
	v_mfma_f32_16x16x32_bf16 v[50:53], v[182:185], v[198:201], v[50:53]
	v_mfma_f32_16x16x32_bf16 v[42:45], v[190:193], v[198:201], v[42:45]
	v_mfma_f32_16x16x32_bf16 v[54:57], v[182:185], v[206:209], v[54:57]
	v_mfma_f32_16x16x32_bf16 v[46:49], v[190:193], v[206:209], v[46:49]
	v_mfma_f32_16x16x32_bf16 v[30:33], v[182:185], v[214:217], v[30:33]
	v_mfma_f32_16x16x32_bf16 v[26:29], v[190:193], v[214:217], v[26:29]
	v_mfma_f32_16x16x32_bf16 v[14:17], v[182:185], v[222:225], v[14:17]
	v_mfma_f32_16x16x32_bf16 v[10:13], v[190:193], v[222:225], v[10:13]
	v_mfma_f32_16x16x32_bf16 v[50:53], v[186:189], v[202:205], v[50:53]
	v_mfma_f32_16x16x32_bf16 v[42:45], v[194:197], v[202:205], v[42:45]
	v_mfma_f32_16x16x32_bf16 v[54:57], v[186:189], v[210:213], v[54:57]
	v_mfma_f32_16x16x32_bf16 v[46:49], v[194:197], v[210:213], v[46:49]
	v_mfma_f32_16x16x32_bf16 v[30:33], v[186:189], v[218:221], v[30:33]
	v_mfma_f32_16x16x32_bf16 v[26:29], v[194:197], v[218:221], v[26:29]
	v_mfma_f32_16x16x32_bf16 v[14:17], v[186:189], v[230:233], v[14:17]
	v_mfma_f32_16x16x32_bf16 v[10:13], v[194:197], v[230:233], v[10:13]
	s_setprio 0
	s_barrier
	s_add_i32 s63, s63, 2
	s_add_u32 s40, s40, 0x100
	s_addc_u32 s41, s41, 0
	s_cmp_gt_u32 s63, 13
	s_andn2_b64 vcc, exec, s[6:7]
	s_cbranch_vccnz .Lg5_nonext
	s_waitcnt vmcnt(8)
	v_readfirstlane_b32 s34, v250
	v_lshl_add_u32 v164, v229, 11, v152
	v_lshl_add_u32 v163, v251, 11, v153
	v_lshl_add_u32 v162, v252, 11, v152
	v_lshl_add_u32 v161, v253, 11, v153
	s_mul_i32 s34, s34, 28
	s_add_i32 s30, s34, s30
	s_ashr_i32 s31, s30, 31
	s_lshl_b64 s[34:35], s[30:31], 19
	v_readlane_b32 s42, v254, 29
	v_readlane_b32 s43, v254, 30
	s_add_u32 s34, s42, s34
	s_addc_u32 s35, s43, s35
	s_mov_b32 s29, s35
	s_mov_b32 s31, s34
.Lg5_nonext:
.LBB0_1728:
	ds_read_b128 v[166:169], v158
	ds_read_b128 v[170:173], v158 offset:1024
	ds_read_b128 v[174:177], v158 offset:2048
	ds_read_b128 v[178:181], v158 offset:3072
	ds_read_b128 v[182:185], v159
	ds_read_b128 v[186:189], v159 offset:1024
	ds_read_b128 v[190:193], v159 offset:2048
	ds_read_b128 v[194:197], v159 offset:3072
	s_add_u32 s42, s78, s40
	s_addc_u32 s43, s79, s41
	s_add_u32 s44, s42, 0x1aa00100
	s_addc_u32 s45, s43, 0
	s_add_u32 s66, s61, s40
	s_addc_u32 s67, s62, s41
	s_cmpk_eq_i32 s40, 0x700
	s_cselect_b64 s[64:65], -1, 0
	s_and_b64 s[42:43], s[64:65], exec
	s_cselect_b32 s45, s87, s45
	s_cselect_b32 s44, s86, s44
	s_cselect_b32 s42, s31, s66
	s_cselect_b32 s43, s29, s67
	s_and_b64 vcc, s[6:7], s[64:65]
	v_lshl_add_u64 v[226:227], v[148:149], 0, s[40:41]
	s_add_i32 m0, s37, 0xc000
	ds_read_b128 v[198:201], v160
	ds_read_b128 v[202:205], v160 offset:1024
	ds_read_b128 v[206:209], v160 offset:2048
	ds_read_b128 v[210:213], v160 offset:3072
	ds_read_b128 v[214:217], v160 offset:4096
	ds_read_b128 v[218:221], v160 offset:5120
	ds_read_b128 v[222:225], v160 offset:6144
	ds_read_b128 v[230:233], v160 offset:7168
	global_load_lds_dwordx4 v[226:227], off
	v_lshl_add_u64 v[226:227], v[146:147], 0, s[40:41]
	s_add_i32 m0, s37, 0xe000
	s_nop 0
	global_load_lds_dwordx4 v[226:227], off
	s_waitcnt vmcnt(8)
	s_waitcnt lgkmcnt(0)
	s_barrier
; #define PG8_STAGE_A(b, h, ptr, NX) do { if constexpr (Sched::GATHER) { unsigned gs_[2]; gs_[0] = ((NX) && last_) ? gN[h][0] : gA[h][0]; gs_[1] = ((NX) && last_) ? gN[h][1] : gA[h][1]; PG8_STAGE(PG8_SA(b, h), ptr, gs_); } \
;         else PG8_STAGE(PG8_SA(b, h), (ptr) + ((h) ? hstep : (size_t)0), voffA); } while (0)
; #define PG8_STAGE(bufoff, gbase, voff) do { _Pragma("unroll") for (int _i = 0; _i < 2; ++_i) \
;         __builtin_amdgcn_global_load_lds((const unsigned*)((const char*)(gbase) + (voff)[_i]), (PG8_LAS unsigned*)(lds + (bufoff) + ldsw + _i * 8192), 16, 0, 0); } while (0)
; #define PG8_LDA(dst, b, h) do { _Pragma("unroll") for (int m = 0; m < 4; ++m) _Pragma("unroll") for (int k = 0; k < 2; ++k) dst[m][k] = *(const PG8_LAS bf16x8*)(lds + PG8_SA(b, h) + aoff + m * 2048 + k * 1024); } while (0)
; #define PG8_LDB(dst, b, h) do { _Pragma("unroll") for (int n = 0; n < 2; ++n) _Pragma("unroll") for (int k = 0; k < 2; ++k) dst[n][k] = *(const PG8_LAS bf16x8*)(lds + PG8_SB(b, h) + boff + n * 2048 + k * 1024); } while (0)
; #define PG8_MMA(ai, bj, At, Bt) do { __builtin_amdgcn_s_setprio(1); _Pragma("unroll") for (int m = 0; m < 4; ++m) _Pragma("unroll") for (int n = 0; n < 2; ++n) _Pragma("unroll") for (int k = 0; k < 2; ++k) \
;         acc[ai][bj][m][n] = __builtin_amdgcn_mfma_f32_16x16x32_bf16(Bt[n][k], At[m][k], acc[ai][bj][m][n], 0, 0, 0); __builtin_amdgcn_s_setprio(0); } while (0)
; #define PG8_WAIT_V(n) asm volatile("s_waitcnt vmcnt(" #n ")" ::: "memory")
; #define PG8_WAIT_L(n) asm volatile("s_waitcnt lgkmcnt(" #n ")" ::: "memory")
; #define PG8_BAR __builtin_amdgcn_s_barrier()
; #define PG8_SCHED __builtin_amdgcn_sched_barrier(0)
; template <class Epi, class Sched, bool ALIGN_EPI = false, bool SP2 = false>
; __device__ __forceinline__ void gemm_phase(PG8_LAS unsigned char* lds, const Gemm g, const Sched& S, const Epi& E, const bool skip_epi = false) {
;     ...
;             PG8_LDB(B0, 0, 0); PG8_LDB(B1, 0, 1); PG8_SCHED; PG8_LDA(At, 0, 0); PG8_STAGE_A(1, 1, a1, false);
;             PG8_WAIT_V(8); PG8_WAIT_L(0); PG8_BAR; PG8_MMA(0, 0, At, B0); PG8_MMA(0, 1, At, B1); PG8_BAR; PG8_SCHED;
;             PG8_LDA(At, 0, 1); PG8_STAGE(PG8_SB(0, 0), b2, voffB); PG8_STAGE(PG8_SB(0, 1), b2 + hstep, voffB); PG8_STAGE_A(0, 0, a2, true);
;             PG8_WAIT_V(8); PG8_WAIT_L(0); PG8_BAR; PG8_MMA(1, 0, At, B0); PG8_MMA(1, 1, At, B1); PG8_BAR; PG8_SCHED;
	s_setprio 3
	s_waitcnt lgkmcnt(0)
	v_mfma_f32_16x16x32_bf16 v[126:129], v[166:169], v[198:201], v[126:129]
	v_mfma_f32_16x16x32_bf16 v[122:125], v[174:177], v[198:201], v[122:125]
	v_mfma_f32_16x16x32_bf16 v[110:113], v[166:169], v[206:209], v[110:113]
	v_mfma_f32_16x16x32_bf16 v[106:109], v[174:177], v[206:209], v[106:109]
	v_mfma_f32_16x16x32_bf16 v[94:97], v[166:169], v[214:217], v[94:97]
	v_mfma_f32_16x16x32_bf16 v[90:93], v[174:177], v[214:217], v[90:93]
	v_mfma_f32_16x16x32_bf16 v[78:81], v[166:169], v[222:225], v[78:81]
	v_mfma_f32_16x16x32_bf16 v[74:77], v[174:177], v[222:225], v[74:77]
	v_mfma_f32_16x16x32_bf16 v[126:129], v[170:173], v[202:205], v[126:129]
	v_mfma_f32_16x16x32_bf16 v[122:125], v[178:181], v[202:205], v[122:125]
	v_mfma_f32_16x16x32_bf16 v[110:113], v[170:173], v[210:213], v[110:113]
	v_mfma_f32_16x16x32_bf16 v[106:109], v[178:181], v[210:213], v[106:109]
	v_mfma_f32_16x16x32_bf16 v[94:97], v[170:173], v[218:221], v[94:97]
	v_mfma_f32_16x16x32_bf16 v[90:93], v[178:181], v[218:221], v[90:93]
	v_mfma_f32_16x16x32_bf16 v[78:81], v[170:173], v[230:233], v[78:81]
	v_mfma_f32_16x16x32_bf16 v[74:77], v[178:181], v[230:233], v[74:77]
	s_setprio 0
	s_setprio 3
	v_mfma_f32_16x16x32_bf16 v[118:121], v[182:185], v[198:201], v[118:121]
	v_mfma_f32_16x16x32_bf16 v[114:117], v[190:193], v[198:201], v[114:117]
	v_mfma_f32_16x16x32_bf16 v[102:105], v[182:185], v[206:209], v[102:105]
	v_mfma_f32_16x16x32_bf16 v[98:101], v[190:193], v[206:209], v[98:101]
	v_mfma_f32_16x16x32_bf16 v[86:89], v[182:185], v[214:217], v[86:89]
	v_mfma_f32_16x16x32_bf16 v[82:85], v[190:193], v[214:217], v[82:85]
	v_mfma_f32_16x16x32_bf16 v[70:73], v[182:185], v[222:225], v[70:73]
	v_mfma_f32_16x16x32_bf16 v[66:69], v[190:193], v[222:225], v[66:69]
	v_mfma_f32_16x16x32_bf16 v[118:121], v[186:189], v[202:205], v[118:121]
	v_mfma_f32_16x16x32_bf16 v[114:117], v[194:197], v[202:205], v[114:117]
	v_mfma_f32_16x16x32_bf16 v[102:105], v[186:189], v[210:213], v[102:105]
	v_mfma_f32_16x16x32_bf16 v[98:101], v[194:197], v[210:213], v[98:101]
	v_mfma_f32_16x16x32_bf16 v[86:89], v[186:189], v[218:221], v[86:89]
	v_mfma_f32_16x16x32_bf16 v[82:85], v[194:197], v[218:221], v[82:85]
	v_mfma_f32_16x16x32_bf16 v[70:73], v[186:189], v[230:233], v[70:73]
	v_mfma_f32_16x16x32_bf16 v[66:69], v[194:197], v[230:233], v[66:69]
	s_setprio 0
	s_barrier
	s_add_i32 s64, s58, s50
	v_lshl_add_u64 v[226:227], s[42:43], 0, v[134:135]
	s_mov_b32 m0, s64
	ds_read_b128 v[198:201], v160 offset:16384
	ds_read_b128 v[202:205], v160 offset:17408
	ds_read_b128 v[206:209], v160 offset:18432
	ds_read_b128 v[210:213], v160 offset:19456
	ds_read_b128 v[214:217], v160 offset:20480
	ds_read_b128 v[218:221], v160 offset:21504
	ds_read_b128 v[222:225], v160 offset:22528
	ds_read_b128 v[230:233], v160 offset:23552
	global_load_lds_dwordx4 v[226:227], off
	s_add_i32 m0, s64, 0x2000
	s_add_u32 s64, s42, 0x40000
	v_lshl_add_u64 v[234:235], s[42:43], 0, v[136:137]
	s_addc_u32 s65, s43, 0
	s_add_i32 s66, s59, s50
	global_load_lds_dwordx4 v[234:235], off
	s_mov_b32 m0, s66
	v_cndmask_b32_e32 v132, v130, v164, vcc
	global_load_lds_dwordx4 v134, s[64:65]
	s_add_i32 m0, s66, 0x2000
	v_lshl_add_u64 v[238:239], s[44:45], 0, v[132:133]
	global_load_lds_dwordx4 v136, s[64:65]
	s_mov_b32 m0, s37
	v_cndmask_b32_e32 v236, v144, v163, vcc
	global_load_lds_dwordx4 v132, s[44:45]
	s_mov_b32 m0, s39
	v_mov_b32_e32 v237, v133
	global_load_lds_dwordx4 v236, s[44:45]
	s_waitcnt vmcnt(8)
	s_waitcnt lgkmcnt(0)
	v_lshl_add_u64 v[236:237], s[44:45], 0, v[236:237]
	s_barrier
	s_setprio 3
	s_waitcnt lgkmcnt(0)
	v_mfma_f32_16x16x32_bf16 v[62:65], v[166:169], v[198:201], v[62:65]
	v_mfma_f32_16x16x32_bf16 v[58:61], v[174:177], v[198:201], v[58:61]
	v_mfma_f32_16x16x32_bf16 v[38:41], v[166:169], v[206:209], v[38:41]
	v_mfma_f32_16x16x32_bf16 v[34:37], v[174:177], v[206:209], v[34:37]
	v_mfma_f32_16x16x32_bf16 v[22:25], v[166:169], v[214:217], v[22:25]
	v_mfma_f32_16x16x32_bf16 v[18:21], v[174:177], v[214:217], v[18:21]
	v_mfma_f32_16x16x32_bf16 v[6:9], v[166:169], v[222:225], v[6:9]
	v_mfma_f32_16x16x32_bf16 v[2:5], v[174:177], v[222:225], v[2:5]
	v_mfma_f32_16x16x32_bf16 v[62:65], v[170:173], v[202:205], v[62:65]
	v_mfma_f32_16x16x32_bf16 v[58:61], v[178:181], v[202:205], v[58:61]
	v_mfma_f32_16x16x32_bf16 v[38:41], v[170:173], v[210:213], v[38:41]
	v_mfma_f32_16x16x32_bf16 v[34:37], v[178:181], v[210:213], v[34:37]
	v_mfma_f32_16x16x32_bf16 v[22:25], v[170:173], v[218:221], v[22:25]
	v_mfma_f32_16x16x32_bf16 v[18:21], v[178:181], v[218:221], v[18:21]
	v_mfma_f32_16x16x32_bf16 v[6:9], v[170:173], v[230:233], v[6:9]
	v_mfma_f32_16x16x32_bf16 v[2:5], v[178:181], v[230:233], v[2:5]
	s_setprio 0
	s_setprio 3
	v_mfma_f32_16x16x32_bf16 v[50:53], v[182:185], v[198:201], v[50:53]
	v_mfma_f32_16x16x32_bf16 v[42:45], v[190:193], v[198:201], v[42:45]
	v_mfma_f32_16x16x32_bf16 v[54:57], v[182:185], v[206:209], v[54:57]
	v_mfma_f32_16x16x32_bf16 v[46:49], v[190:193], v[206:209], v[46:49]
	v_mfma_f32_16x16x32_bf16 v[30:33], v[182:185], v[214:217], v[30:33]
	v_mfma_f32_16x16x32_bf16 v[26:29], v[190:193], v[214:217], v[26:29]
	v_mfma_f32_16x16x32_bf16 v[14:17], v[182:185], v[222:225], v[14:17]
	v_mfma_f32_16x16x32_bf16 v[10:13], v[190:193], v[222:225], v[10:13]
	v_mfma_f32_16x16x32_bf16 v[50:53], v[186:189], v[202:205], v[50:53]
	v_mfma_f32_16x16x32_bf16 v[42:45], v[194:197], v[202:205], v[42:45]
	v_mfma_f32_16x16x32_bf16 v[54:57], v[186:189], v[210:213], v[54:57]
	v_mfma_f32_16x16x32_bf16 v[46:49], v[194:197], v[210:213], v[46:49]
	v_mfma_f32_16x16x32_bf16 v[30:33], v[186:189], v[218:221], v[30:33]
	v_mfma_f32_16x16x32_bf16 v[26:29], v[194:197], v[218:221], v[26:29]
	v_mfma_f32_16x16x32_bf16 v[14:17], v[186:189], v[230:233], v[14:17]
	v_mfma_f32_16x16x32_bf16 v[10:13], v[194:197], v[230:233], v[10:13]
	s_setprio 0
	s_barrier
; #define PG8_STAGE_A(b, h, ptr, NX) do { if constexpr (Sched::GATHER) { unsigned gs_[2]; gs_[0] = ((NX) && last_) ? gN[h][0] : gA[h][0]; gs_[1] = ((NX) && last_) ? gN[h][1] : gA[h][1]; PG8_STAGE(PG8_SA(b, h), ptr, gs_); } \
;         else PG8_STAGE(PG8_SA(b, h), (ptr) + ((h) ? hstep : (size_t)0), voffA); } while (0)
; #define PG8_STAGE(bufoff, gbase, voff) do { _Pragma("unroll") for (int _i = 0; _i < 2; ++_i) \
;         __builtin_amdgcn_global_load_lds((const unsigned*)((const char*)(gbase) + (voff)[_i]), (PG8_LAS unsigned*)(lds + (bufoff) + ldsw + _i * 8192), 16, 0, 0); } while (0)
; #define PG8_WAIT_V(n) asm volatile("s_waitcnt vmcnt(" #n ")" ::: "memory")
; #define PG8_BAR __builtin_amdgcn_s_barrier()
; template <class Epi, class Sched, bool ALIGN_EPI = false, bool SP2 = false>
; __device__ __forceinline__ void gemm_phase(PG8_LAS unsigned char* lds, const Gemm g, const Sched& S, const Epi& E, const bool skip_epi = false) {
;     ...
;         for (int t = 0; t < nt; t += 2) {
;             const bool last = (t == nt - 2); last_ = last && has_next;
;             const char* a1 = cA + (size_t)(t + 1) * kstep;
;             const char* a2 = last ? nA : cA + (size_t)(t + 2) * kstep; const char* b2 = last ? nB : cB + (size_t)(t + 2) * kstep;
;             const char* a3 = a2 + kstep; const char* b3 = b2 + kstep;
;             if (last && has_next) S.a_ready(nxt);
;             if constexpr (SP2) {
;             PG8_LDB(B0, 0, 0); PG8_LDB(B1, 0, 1); PG8_SCHED; PG8_LDA(At, 0, 0); PG8_STAGE_A(1, 1, a1, false);
;             PG8_WAIT_V(8); PG8_WAIT_L(0); PG8_BAR; PG8_MMA(0, 0, At, B0); PG8_MMA(0, 1, At, B1); PG8_BAR; PG8_SCHED;
;             PG8_LDA(At, 0, 1); PG8_STAGE(PG8_SB(0, 0), b2, voffB); PG8_STAGE(PG8_SB(0, 1), b2 + hstep, voffB); PG8_STAGE_A(0, 0, a2, true);
;             PG8_WAIT_V(8); PG8_WAIT_L(0); PG8_BAR; PG8_MMA(1, 0, At, B0); PG8_MMA(1, 1, At, B1); PG8_BAR; PG8_SCHED;
;             PG8_LDB(B0, 1, 0); PG8_LDB(B1, 1, 1); PG8_SCHED; PG8_LDA(At, 1, 0); PG8_STAGE_A(0, 1, a2, true);
;             PG8_WAIT_V(8); PG8_WAIT_L(0); PG8_BAR; PG8_MMA(0, 0, At, B0); PG8_MMA(0, 1, At, B1); PG8_BAR; PG8_SCHED;
;             PG8_LDA(At, 1, 1); PG8_STAGE(PG8_SB(1, 0), b3, voffB); PG8_STAGE(PG8_SB(1, 1), b3 + hstep, voffB); PG8_STAGE_A(1, 0, a3, true);
;             PG8_WAIT_V(8); PG8_WAIT_L(0); PG8_BAR; PG8_MMA(1, 0, At, B0); PG8_MMA(1, 1, At, B1); PG8_BAR; PG8_SCHED;
	s_add_i32 s64, 0, 0x18000
	v_add_u32_e32 v132, s64, v154
	s_add_i32 s65, 0, 0x1c000
	ds_read_b128 v[166:169], v132
	ds_read_b128 v[170:173], v132 offset:1024
	ds_read_b128 v[174:177], v132 offset:2048
	ds_read_b128 v[178:181], v132 offset:3072
	v_add_u32_e32 v132, s65, v154
	ds_read_b128 v[182:185], v132
	ds_read_b128 v[186:189], v132 offset:1024
	ds_read_b128 v[190:193], v132 offset:2048
	ds_read_b128 v[194:197], v132 offset:3072
	s_mov_b32 m0, s51
	v_cndmask_b32_e32 v132, v142, v162, vcc
	ds_read_b128 v[198:201], v160 offset:32768
	ds_read_b128 v[202:205], v160 offset:33792
	ds_read_b128 v[206:209], v160 offset:34816
	ds_read_b128 v[210:213], v160 offset:35840
	ds_read_b128 v[214:217], v160 offset:36864
	ds_read_b128 v[218:221], v160 offset:37888
	ds_read_b128 v[222:225], v160 offset:38912
	ds_read_b128 v[230:233], v160 offset:39936
	v_cndmask_b32_e32 v141, v140, v161, vcc
	global_load_lds_dwordx4 v132, s[44:45]
	s_mov_b32 m0, s52
	s_nop 0
	global_load_lds_dwordx4 v141, s[44:45]
	s_waitcnt vmcnt(8)
	s_waitcnt lgkmcnt(0)
	s_barrier
	s_setprio 3
	s_waitcnt lgkmcnt(0)
	v_mfma_f32_16x16x32_bf16 v[126:129], v[166:169], v[198:201], v[126:129]
	v_mfma_f32_16x16x32_bf16 v[122:125], v[174:177], v[198:201], v[122:125]
	v_mfma_f32_16x16x32_bf16 v[110:113], v[166:169], v[206:209], v[110:113]
	v_mfma_f32_16x16x32_bf16 v[106:109], v[174:177], v[206:209], v[106:109]
	v_mfma_f32_16x16x32_bf16 v[94:97], v[166:169], v[214:217], v[94:97]
	v_mfma_f32_16x16x32_bf16 v[90:93], v[174:177], v[214:217], v[90:93]
	v_mfma_f32_16x16x32_bf16 v[78:81], v[166:169], v[222:225], v[78:81]
	v_mfma_f32_16x16x32_bf16 v[74:77], v[174:177], v[222:225], v[74:77]
	v_mfma_f32_16x16x32_bf16 v[126:129], v[170:173], v[202:205], v[126:129]
	v_mfma_f32_16x16x32_bf16 v[122:125], v[178:181], v[202:205], v[122:125]
	v_mfma_f32_16x16x32_bf16 v[110:113], v[170:173], v[210:213], v[110:113]
	v_mfma_f32_16x16x32_bf16 v[106:109], v[178:181], v[210:213], v[106:109]
	v_mfma_f32_16x16x32_bf16 v[94:97], v[170:173], v[218:221], v[94:97]
	v_mfma_f32_16x16x32_bf16 v[90:93], v[178:181], v[218:221], v[90:93]
	v_mfma_f32_16x16x32_bf16 v[78:81], v[170:173], v[230:233], v[78:81]
	v_mfma_f32_16x16x32_bf16 v[74:77], v[178:181], v[230:233], v[74:77]
	s_setprio 0
	s_setprio 3
	v_mfma_f32_16x16x32_bf16 v[118:121], v[182:185], v[198:201], v[118:121]
	v_mfma_f32_16x16x32_bf16 v[114:117], v[190:193], v[198:201], v[114:117]
	v_mfma_f32_16x16x32_bf16 v[102:105], v[182:185], v[206:209], v[102:105]
	v_mfma_f32_16x16x32_bf16 v[98:101], v[190:193], v[206:209], v[98:101]
	v_mfma_f32_16x16x32_bf16 v[86:89], v[182:185], v[214:217], v[86:89]
	v_mfma_f32_16x16x32_bf16 v[82:85], v[190:193], v[214:217], v[82:85]
	v_mfma_f32_16x16x32_bf16 v[70:73], v[182:185], v[222:225], v[70:73]
	v_mfma_f32_16x16x32_bf16 v[66:69], v[190:193], v[222:225], v[66:69]
	v_mfma_f32_16x16x32_bf16 v[118:121], v[186:189], v[202:205], v[118:121]
	v_mfma_f32_16x16x32_bf16 v[114:117], v[194:197], v[202:205], v[114:117]
	v_mfma_f32_16x16x32_bf16 v[102:105], v[186:189], v[210:213], v[102:105]
	v_mfma_f32_16x16x32_bf16 v[98:101], v[194:197], v[210:213], v[98:101]
	v_mfma_f32_16x16x32_bf16 v[86:89], v[186:189], v[218:221], v[86:89]
	v_mfma_f32_16x16x32_bf16 v[82:85], v[194:197], v[218:221], v[82:85]
	v_mfma_f32_16x16x32_bf16 v[70:73], v[186:189], v[230:233], v[70:73]
	v_mfma_f32_16x16x32_bf16 v[66:69], v[194:197], v[230:233], v[66:69]
	s_setprio 0
	s_barrier
	s_add_i32 s44, s64, s50
	s_add_i32 m0, s44, 0xffffff80
	ds_read_b128 v[198:201], v160 offset:49152
	ds_read_b128 v[202:205], v160 offset:50176
	ds_read_b128 v[206:209], v160 offset:51200
	ds_read_b128 v[210:213], v160 offset:52224
	ds_read_b128 v[214:217], v160 offset:53248
	ds_read_b128 v[218:221], v160 offset:54272
	ds_read_b128 v[222:225], v160 offset:55296
	ds_read_b128 v[230:233], v160 offset:56320
	global_load_lds_dwordx4 v[226:227], off offset:128
	s_add_i32 m0, s44, 0x1f80
	s_add_u32 s42, s42, 0x40080
	s_addc_u32 s43, s43, 0
	s_add_i32 s44, s65, s50
	global_load_lds_dwordx4 v[234:235], off offset:128
	s_mov_b32 m0, s44
	s_nop 0
	global_load_lds_dwordx4 v134, s[42:43]
	s_add_i32 m0, s44, 0x2000
	s_nop 0
	global_load_lds_dwordx4 v136, s[42:43]
	s_add_i32 m0, s55, 0xffffff80
	s_nop 0
	global_load_lds_dwordx4 v[238:239], off offset:128
	s_add_i32 m0, s56, 0xffffff80
	s_nop 0
	global_load_lds_dwordx4 v[236:237], off offset:128
	s_waitcnt vmcnt(8)
	s_waitcnt lgkmcnt(0)
	s_barrier
	s_setprio 3
	s_waitcnt lgkmcnt(0)
	v_mfma_f32_16x16x32_bf16 v[62:65], v[166:169], v[198:201], v[62:65]
	v_mfma_f32_16x16x32_bf16 v[58:61], v[174:177], v[198:201], v[58:61]
	v_mfma_f32_16x16x32_bf16 v[38:41], v[166:169], v[206:209], v[38:41]
	v_mfma_f32_16x16x32_bf16 v[34:37], v[174:177], v[206:209], v[34:37]
	v_mfma_f32_16x16x32_bf16 v[22:25], v[166:169], v[214:217], v[22:25]
	v_mfma_f32_16x16x32_bf16 v[18:21], v[174:177], v[214:217], v[18:21]
	v_mfma_f32_16x16x32_bf16 v[6:9], v[166:169], v[222:225], v[6:9]
	v_mfma_f32_16x16x32_bf16 v[2:5], v[174:177], v[222:225], v[2:5]
	v_mfma_f32_16x16x32_bf16 v[62:65], v[170:173], v[202:205], v[62:65]
	v_mfma_f32_16x16x32_bf16 v[58:61], v[178:181], v[202:205], v[58:61]
	v_mfma_f32_16x16x32_bf16 v[38:41], v[170:173], v[210:213], v[38:41]
	v_mfma_f32_16x16x32_bf16 v[34:37], v[178:181], v[210:213], v[34:37]
	v_mfma_f32_16x16x32_bf16 v[22:25], v[170:173], v[218:221], v[22:25]
	v_mfma_f32_16x16x32_bf16 v[18:21], v[178:181], v[218:221], v[18:21]
	v_mfma_f32_16x16x32_bf16 v[6:9], v[170:173], v[230:233], v[6:9]
	v_mfma_f32_16x16x32_bf16 v[2:5], v[178:181], v[230:233], v[2:5]
	s_setprio 0
	s_setprio 3
	v_mfma_f32_16x16x32_bf16 v[50:53], v[182:185], v[198:201], v[50:53]
	v_mfma_f32_16x16x32_bf16 v[42:45], v[190:193], v[198:201], v[42:45]
	v_mfma_f32_16x16x32_bf16 v[54:57], v[182:185], v[206:209], v[54:57]
	v_mfma_f32_16x16x32_bf16 v[46:49], v[190:193], v[206:209], v[46:49]
	v_mfma_f32_16x16x32_bf16 v[30:33], v[182:185], v[214:217], v[30:33]
	v_mfma_f32_16x16x32_bf16 v[26:29], v[190:193], v[214:217], v[26:29]
	v_mfma_f32_16x16x32_bf16 v[14:17], v[182:185], v[222:225], v[14:17]
	v_mfma_f32_16x16x32_bf16 v[10:13], v[190:193], v[222:225], v[10:13]
	v_mfma_f32_16x16x32_bf16 v[50:53], v[186:189], v[202:205], v[50:53]
	v_mfma_f32_16x16x32_bf16 v[42:45], v[194:197], v[202:205], v[42:45]
	v_mfma_f32_16x16x32_bf16 v[54:57], v[186:189], v[210:213], v[54:57]
	v_mfma_f32_16x16x32_bf16 v[46:49], v[194:197], v[210:213], v[46:49]
	v_mfma_f32_16x16x32_bf16 v[30:33], v[186:189], v[218:221], v[30:33]
	v_mfma_f32_16x16x32_bf16 v[26:29], v[194:197], v[218:221], v[26:29]
	v_mfma_f32_16x16x32_bf16 v[14:17], v[186:189], v[230:233], v[14:17]
	v_mfma_f32_16x16x32_bf16 v[10:13], v[194:197], v[230:233], v[10:13]
	s_setprio 0
	s_barrier
	s_add_i32 s63, s63, 2
	s_add_u32 s40, s40, 0x100
	s_addc_u32 s41, s41, 0
	s_cmp_gt_u32 s63, 13
	s_cbranch_scc0 .LBB0_1728
	s_and_b64 vcc, exec, s[26:27]
	s_cbranch_vccz .LBB0_1731
	s_barrier

; #define PG8_STAGE_A(b, h, ptr, NX) do { if constexpr (Sched::GATHER) { unsigned gs_[2]; gs_[0] = ((NX) && last_) ? gN[h][0] : gA[h][0]; gs_[1] = ((NX) && last_) ? gN[h][1] : gA[h][1]; PG8_STAGE(PG8_SA(b, h), ptr, gs_); } \
;         else PG8_STAGE(PG8_SA(b, h), (ptr) + ((h) ? hstep : (size_t)0), voffA); } while (0)
; #define PG8_STAGE(bufoff, gbase, voff) do { _Pragma("unroll") for (int _i = 0; _i < 2; ++_i) \
;         __builtin_amdgcn_global_load_lds((const unsigned*)((const char*)(gbase) + (voff)[_i]), (PG8_LAS unsigned*)(lds + (bufoff) + ldsw + _i * 8192), 16, 0, 0); } while (0)
; #define PG8_WAIT_V(n) asm volatile("s_waitcnt vmcnt(" #n ")" ::: "memory")
; #define PG8_BAR __builtin_amdgcn_s_barrier()
; template <class Epi, class Sched, bool ALIGN_EPI = false, bool SP2 = false>
; __device__ __forceinline__ void gemm_phase(PG8_LAS unsigned char* lds, const Gemm g, const Sched& S, const Epi& E, const bool skip_epi = false) {
;     ...
;     for (int i = 0; i < 2; ++i) { int R, C; stage_rc(tid * 16 + i * 8192, R, C); const int Rb = Epi::PERM ? ((R & ~31) + perm32(R & 31)) : R;
;         voffA[i] = (unsigned)(R * K + C) * 2u; voffB[i] = (unsigned)(Rb * K + C) * 2u; }
;     const size_t kstep = (size_t)(BK * 2);
;     const size_t hstep = (size_t)HALF * K * 2;
;     const size_t tstep = 2 * hstep;
;     const size_t pmstepA = Sched::GATHER ? (size_t)0 : tstep;
;     unsigned gA[2][2] = {{0u, 0u}, {0u, 0u}}, gN[2][2] = {{0u, 0u}, {0u, 0u}}; bool last_ = false; (void)gA; (void)gN; (void)last_;
;     ...
;     const unsigned ldsw = (unsigned)wid * 1024u;
;     const int aoff = lds_byte(wr * 64 + fr, fq * 8), boff = lds_byte(wc * 32 + fr, fq * 8);
;     ...
;         PG8_STAGE(PG8_SB(1, 0), cB + kstep, voffB); PG8_STAGE_A(1, 0, cA + kstep, false); PG8_STAGE(PG8_SB(1, 1), cB + hstep + kstep, voffB);
;         PG8_WAIT_V(6); PG8_BAR;
.LBB0_1809:
	s_lshl_b32 s56, s18, 6
	s_lshl_b32 s21, s18, 13
	s_lshl_b32 s7, s7, 5
	s_mov_b64 s[18:19], 0x80
	s_and_b32 s7, s7, 0x60
	s_add_i32 m0, s37, 0x18000
	v_lshl_add_u64 v[8:9], v[8:9], 0, s[18:19]
	s_lshl_b32 s24, s7, 7
	s_waitcnt vmcnt(2)
	s_barrier
	global_load_lds_dwordx4 v[8:9], off
	v_lshl_add_u64 v[6:7], v[6:7], 0, s[18:19]
	s_add_i32 m0, s37, 0x1a000
	s_add_i32 s57, s37, 0x8000
	s_add_i32 s58, s37, 0xa000
	global_load_lds_dwordx4 v[6:7], off
	v_lshl_add_u64 v[2:3], v[2:3], 0, s[18:19]
	s_mov_b32 m0, s57
	s_add_u32 s22, s40, 0xe0080
	global_load_lds_dwordx4 v[2:3], off
	v_lshl_add_u64 v[2:3], v[4:5], 0, s[18:19]
	s_mov_b32 m0, s58
	s_addc_u32 s23, s41, 0
	global_load_lds_dwordx4 v[2:3], off
	s_add_i32 m0, s37, 0x1c000
	s_nop 0
	global_load_lds_dwordx4 v134, s[22:23]
	s_add_i32 m0, s37, 0x1e000
	v_and_b32_e32 v1, 15, v10
	global_load_lds_dwordx4 v138, s[22:23]
	v_and_b32_e32 v2, 48, v10
	v_lshlrev_b32_e32 v3, 2, v10
	v_lshl_or_b32 v2, v1, 6, v2
	v_and_b32_e32 v3, 32, v3
	v_bitop3_b32 v4, v2, s21, v3 bitop3:0xde
	v_bitop3_b32 v147, s24, v2, v3 bitop3:0xf6
	v_and_b32_e32 v2, 3, v10
	v_and_b32_e32 v3, 60, v10
	v_lshl_or_b32 v149, v2, 6, v3
	v_lshl_or_b32 v155, v2, 3, s7
	v_lshrrev_b32_e32 v3, 1, v11
	v_mul_lo_u32 v2, v15, s6
	s_mov_b32 s7, 0xe000
	v_mad_u64_u32 v[2:3], s[24:25], v3, s7, v[2:3]
	v_or_b32_e32 v2, v2, v13
	v_add_lshl_u32 v130, v2, v16, 1
	v_lshrrev_b32_e32 v3, 1, v12
	v_mul_lo_u32 v2, v17, s6
	v_mad_u64_u32 v[2:3], s[6:7], v3, s7, v[2:3]
	s_mov_b64 s[22:23], 0xe0080
	s_waitcnt vmcnt(6)
	s_cmpk_lt_u32 s20, 0x100
	v_or_b32_e32 v2, v2, v14
	s_cselect_b64 s[20:21], -1, 0
	v_lshl_add_u64 v[140:141], v[130:131], 0, s[22:23]
	v_add_lshl_u32 v130, v2, v18, 1
	s_add_i32 s60, 0, 0x10000
	s_add_i32 s61, 0, 0x14000
	v_bfe_u32 v151, v10, 2, 4
	s_ashr_i32 s59, s97, 31
	v_lshl_add_u64 v[142:143], v[130:131], 0, s[22:23]
	v_mov_b64_e32 v[144:145], s[4:5]
	v_add_u32_e32 v157, s60, v147
	v_add_u32_e32 v158, s61, v147
	v_add_u32_e32 v159, 0, v4
	s_mov_b64 s[22:23], 0x40000
	s_mov_b32 s62, 0x40000
	s_mov_b64 s[24:25], 0x48000
	s_mov_b32 s63, 0x48000
	s_mov_b64 s[26:27], 0x50000
	s_mov_b32 s64, 0x50000
	s_mov_b64 s[28:29], 0x58000
	s_mov_b32 s65, 0x58000
	s_barrier
	s_branch .LBB0_1812

; #define PG8_STAGE_A(b, h, ptr, NX) do { if constexpr (Sched::GATHER) { unsigned gs_[2]; gs_[0] = ((NX) && last_) ? gN[h][0] : gA[h][0]; gs_[1] = ((NX) && last_) ? gN[h][1] : gA[h][1]; PG8_STAGE(PG8_SA(b, h), ptr, gs_); } \
;         else PG8_STAGE(PG8_SA(b, h), (ptr) + ((h) ? hstep : (size_t)0), voffA); } while (0)
; #define PG8_STAGE(bufoff, gbase, voff) do { _Pragma("unroll") for (int _i = 0; _i < 2; ++_i) \
;         __builtin_amdgcn_global_load_lds((const unsigned*)((const char*)(gbase) + (voff)[_i]), (PG8_LAS unsigned*)(lds + (bufoff) + ldsw + _i * 8192), 16, 0, 0); } while (0)
; #define PG8_LDA(dst, b, h) do { _Pragma("unroll") for (int m = 0; m < 4; ++m) _Pragma("unroll") for (int k = 0; k < 2; ++k) dst[m][k] = *(const PG8_LAS bf16x8*)(lds + PG8_SA(b, h) + aoff + m * 2048 + k * 1024); } while (0)
; #define PG8_LDB(dst, b, h) do { _Pragma("unroll") for (int n = 0; n < 2; ++n) _Pragma("unroll") for (int k = 0; k < 2; ++k) dst[n][k] = *(const PG8_LAS bf16x8*)(lds + PG8_SB(b, h) + boff + n * 2048 + k * 1024); } while (0)
; #define PG8_WAIT_V(n) asm volatile("s_waitcnt vmcnt(" #n ")" ::: "memory")
; #define PG8_WAIT_L(n) asm volatile("s_waitcnt lgkmcnt(" #n ")" ::: "memory")
; template <class Epi, class Sched, bool ALIGN_EPI = false, bool SP2 = false>
; __device__ __forceinline__ void gemm_phase(PG8_LAS unsigned char* lds, const Gemm g, const Sched& S, const Epi& E, const bool skip_epi = false) {
;     ...
;         for (int t = 0; t < nt; t += 2) {
;             const bool last = (t == nt - 2); last_ = last && has_next;
;             const char* a1 = cA + (size_t)(t + 1) * kstep;
;             const char* a2 = last ? nA : cA + (size_t)(t + 2) * kstep; const char* b2 = last ? nB : cB + (size_t)(t + 2) * kstep;
;             const char* a3 = a2 + kstep; const char* b3 = b2 + kstep;
;             if (last && has_next) S.a_ready(nxt);
;             if constexpr (SP2) {
;             PG8_LDB(B0, 0, 0); PG8_LDB(B1, 0, 1); PG8_SCHED; PG8_LDA(At, 0, 0); PG8_STAGE_A(1, 1, a1, false);
;             PG8_WAIT_V(8); PG8_WAIT_L(0); PG8_BAR; PG8_MMA(0, 0, At, B0); PG8_MMA(0, 1, At, B1); PG8_BAR; PG8_SCHED;
;             PG8_LDA(At, 0, 1); PG8_STAGE(PG8_SB(0, 0), b2, voffB); PG8_STAGE(PG8_SB(0, 1), b2 + hstep, voffB); PG8_STAGE_A(0, 0, a2, true);
;             PG8_WAIT_V(8); PG8_WAIT_L(0); PG8_BAR; PG8_MMA(1, 0, At, B0); PG8_MMA(1, 1, At, B1); PG8_BAR; PG8_SCHED;
.LBB0_1822:
	s_add_u32 s67, s40, 0x100
	s_addc_u32 s68, s41, 0
	s_mov_b32 s69, -2
	ds_read_b128 v[160:163], v157
	ds_read_b128 v[164:167], v157 offset:1024
	ds_read_b128 v[168:171], v157 offset:2048
	ds_read_b128 v[172:175], v157 offset:3072
	ds_read_b128 v[176:179], v158
	ds_read_b128 v[180:183], v158 offset:1024
	ds_read_b128 v[184:187], v158 offset:2048
	ds_read_b128 v[188:191], v158 offset:3072
	s_add_u32 s40, s38, 0x100
	s_addc_u32 s41, s39, 0
	s_cmp_eq_u32 s69, 52
	s_cselect_b32 s45, s7, s41
	s_cselect_b32 s44, s6, s40
	s_cselect_b32 s43, s35, s68
	s_cselect_b32 s42, s34, s67
	v_lshl_add_u64 v[152:153], s[38:39], 0, v[140:141]
	s_add_i32 m0, s37, 0xc000
	ds_read_b128 v[192:195], v159
	ds_read_b128 v[196:199], v159 offset:1024
	ds_read_b128 v[200:203], v159 offset:2048
	ds_read_b128 v[204:207], v159 offset:3072
	ds_read_b128 v[208:211], v159 offset:4096
	ds_read_b128 v[212:215], v159 offset:5120
	ds_read_b128 v[216:219], v159 offset:6144
	ds_read_b128 v[220:223], v159 offset:7168
	global_load_lds_dwordx4 v[152:153], off
	v_lshl_add_u64 v[152:153], s[38:39], 0, v[142:143]
	s_add_i32 m0, s37, 0xe000
	s_nop 0
	global_load_lds_dwordx4 v[152:153], off
	s_waitcnt vmcnt(8)
	s_waitcnt lgkmcnt(0)
	s_barrier
	s_setprio 3
	s_waitcnt lgkmcnt(0)
	v_mfma_f32_16x16x32_bf16 v[126:129], v[160:163], v[192:195], 0
	v_mfma_f32_16x16x32_bf16 v[122:125], v[168:171], v[192:195], 0
	v_mfma_f32_16x16x32_bf16 v[118:121], v[160:163], v[200:203], 0
	v_mfma_f32_16x16x32_bf16 v[114:117], v[168:171], v[200:203], 0
	v_mfma_f32_16x16x32_bf16 v[106:109], v[160:163], v[208:211], 0
	v_mfma_f32_16x16x32_bf16 v[98:101], v[168:171], v[208:211], 0
	v_mfma_f32_16x16x32_bf16 v[78:81], v[160:163], v[216:219], 0
	v_mfma_f32_16x16x32_bf16 v[74:77], v[168:171], v[216:219], 0
	v_mfma_f32_16x16x32_bf16 v[126:129], v[164:167], v[196:199], v[126:129]
	v_mfma_f32_16x16x32_bf16 v[122:125], v[172:175], v[196:199], v[122:125]
	v_mfma_f32_16x16x32_bf16 v[118:121], v[164:167], v[204:207], v[118:121]
	v_mfma_f32_16x16x32_bf16 v[114:117], v[172:175], v[204:207], v[114:117]
	v_mfma_f32_16x16x32_bf16 v[106:109], v[164:167], v[212:215], v[106:109]
	v_mfma_f32_16x16x32_bf16 v[98:101], v[172:175], v[212:215], v[98:101]
	v_mfma_f32_16x16x32_bf16 v[78:81], v[164:167], v[220:223], v[78:81]
	v_mfma_f32_16x16x32_bf16 v[74:77], v[172:175], v[220:223], v[74:77]
	s_setprio 0
	s_setprio 3
	v_mfma_f32_16x16x32_bf16 v[110:113], v[176:179], v[192:195], 0
	v_mfma_f32_16x16x32_bf16 v[102:105], v[184:187], v[192:195], 0
	v_mfma_f32_16x16x32_bf16 v[94:97], v[176:179], v[200:203], 0
	v_mfma_f32_16x16x32_bf16 v[90:93], v[184:187], v[200:203], 0
	v_mfma_f32_16x16x32_bf16 v[86:89], v[176:179], v[208:211], 0
	v_mfma_f32_16x16x32_bf16 v[82:85], v[184:187], v[208:211], 0
	v_mfma_f32_16x16x32_bf16 v[70:73], v[176:179], v[216:219], 0
	v_mfma_f32_16x16x32_bf16 v[66:69], v[184:187], v[216:219], 0
	v_mfma_f32_16x16x32_bf16 v[110:113], v[180:183], v[196:199], v[110:113]
	v_mfma_f32_16x16x32_bf16 v[102:105], v[188:191], v[196:199], v[102:105]
	v_mfma_f32_16x16x32_bf16 v[94:97], v[180:183], v[204:207], v[94:97]
	v_mfma_f32_16x16x32_bf16 v[90:93], v[188:191], v[204:207], v[90:93]
	v_mfma_f32_16x16x32_bf16 v[86:89], v[180:183], v[212:215], v[86:89]
	v_mfma_f32_16x16x32_bf16 v[82:85], v[188:191], v[212:215], v[82:85]
	v_mfma_f32_16x16x32_bf16 v[70:73], v[180:183], v[220:223], v[70:73]
	v_mfma_f32_16x16x32_bf16 v[66:69], v[188:191], v[220:223], v[66:69]
	s_setprio 0
	s_barrier
	s_add_i32 s38, s60, s51
	v_lshl_add_u64 v[152:153], s[42:43], 0, v[134:135]
	s_mov_b32 m0, s38
	ds_read_b128 v[192:195], v159 offset:16384
	ds_read_b128 v[196:199], v159 offset:17408
	ds_read_b128 v[200:203], v159 offset:18432
	ds_read_b128 v[204:207], v159 offset:19456
	ds_read_b128 v[208:211], v159 offset:20480
	ds_read_b128 v[212:215], v159 offset:21504
	ds_read_b128 v[216:219], v159 offset:22528
	ds_read_b128 v[220:223], v159 offset:23552
	global_load_lds_dwordx4 v[152:153], off
	s_add_i32 m0, s38, 0x2000
	s_add_u32 s38, s42, 0xe0000
	v_lshl_add_u64 v[224:225], s[42:43], 0, v[138:139]
	s_addc_u32 s39, s43, 0
	s_add_i32 s70, s61, s51
	global_load_lds_dwordx4 v[224:225], off
	s_mov_b32 m0, s70
	v_lshl_add_u64 v[230:231], s[44:45], 0, v[136:137]
	global_load_lds_dwordx4 v134, s[38:39]
	s_add_i32 m0, s70, 0x2000
	s_nop 0
	global_load_lds_dwordx4 v138, s[38:39]
	v_lshl_add_u64 v[226:227], s[44:45], 0, v[132:133]
	s_mov_b32 m0, s37
	s_nop 0
	global_load_lds_dwordx4 v[226:227], off
	s_mov_b32 m0, s52
	s_nop 0
	global_load_lds_dwordx4 v[230:231], off
	s_waitcnt vmcnt(8)
	s_waitcnt lgkmcnt(0)
	s_barrier
; #define PG8_STAGE_A(b, h, ptr, NX) do { if constexpr (Sched::GATHER) { unsigned gs_[2]; gs_[0] = ((NX) && last_) ? gN[h][0] : gA[h][0]; gs_[1] = ((NX) && last_) ? gN[h][1] : gA[h][1]; PG8_STAGE(PG8_SA(b, h), ptr, gs_); } \
;         else PG8_STAGE(PG8_SA(b, h), (ptr) + ((h) ? hstep : (size_t)0), voffA); } while (0)
; #define PG8_STAGE(bufoff, gbase, voff) do { _Pragma("unroll") for (int _i = 0; _i < 2; ++_i) \
;         __builtin_amdgcn_global_load_lds((const unsigned*)((const char*)(gbase) + (voff)[_i]), (PG8_LAS unsigned*)(lds + (bufoff) + ldsw + _i * 8192), 16, 0, 0); } while (0)
; #define PG8_LDA(dst, b, h) do { _Pragma("unroll") for (int m = 0; m < 4; ++m) _Pragma("unroll") for (int k = 0; k < 2; ++k) dst[m][k] = *(const PG8_LAS bf16x8*)(lds + PG8_SA(b, h) + aoff + m * 2048 + k * 1024); } while (0)
; #define PG8_LDB(dst, b, h) do { _Pragma("unroll") for (int n = 0; n < 2; ++n) _Pragma("unroll") for (int k = 0; k < 2; ++k) dst[n][k] = *(const PG8_LAS bf16x8*)(lds + PG8_SB(b, h) + boff + n * 2048 + k * 1024); } while (0)
; #define PG8_MMA(ai, bj, At, Bt) do { __builtin_amdgcn_s_setprio(1); _Pragma("unroll") for (int m = 0; m < 4; ++m) _Pragma("unroll") for (int n = 0; n < 2; ++n) _Pragma("unroll") for (int k = 0; k < 2; ++k) \
;         acc[ai][bj][m][n] = __builtin_amdgcn_mfma_f32_16x16x32_bf16(Bt[n][k], At[m][k], acc[ai][bj][m][n], 0, 0, 0); __builtin_amdgcn_s_setprio(0); } while (0)
; #define PG8_WAIT_V(n) asm volatile("s_waitcnt vmcnt(" #n ")" ::: "memory")
; #define PG8_BAR __builtin_amdgcn_s_barrier()
; template <class Epi, class Sched, bool ALIGN_EPI = false, bool SP2 = false>
; __device__ __forceinline__ void gemm_phase(PG8_LAS unsigned char* lds, const Gemm g, const Sched& S, const Epi& E, const bool skip_epi = false) {
;     ...
;             PG8_WAIT_V(8); PG8_WAIT_L(0); PG8_BAR; PG8_MMA(0, 0, At, B0); PG8_MMA(0, 1, At, B1); PG8_BAR; PG8_SCHED;
;             PG8_LDA(At, 0, 1); PG8_STAGE(PG8_SB(0, 0), b2, voffB); PG8_STAGE(PG8_SB(0, 1), b2 + hstep, voffB); PG8_STAGE_A(0, 0, a2, true);
;             PG8_WAIT_V(8); PG8_WAIT_L(0); PG8_BAR; PG8_MMA(1, 0, At, B0); PG8_MMA(1, 1, At, B1); PG8_BAR; PG8_SCHED;
;             PG8_LDB(B0, 1, 0); PG8_LDB(B1, 1, 1); PG8_SCHED; PG8_LDA(At, 1, 0); PG8_STAGE_A(0, 1, a2, true);
;             PG8_WAIT_V(8); PG8_WAIT_L(0); PG8_BAR; PG8_MMA(0, 0, At, B0); PG8_MMA(0, 1, At, B1); PG8_BAR; PG8_SCHED;
	s_setprio 3
	s_waitcnt lgkmcnt(0)
	v_mfma_f32_16x16x32_bf16 v[62:65], v[160:163], v[192:195], 0
	v_mfma_f32_16x16x32_bf16 v[58:61], v[168:171], v[192:195], 0
	v_mfma_f32_16x16x32_bf16 v[50:53], v[160:163], v[200:203], 0
	v_mfma_f32_16x16x32_bf16 v[42:45], v[168:171], v[200:203], 0
	v_mfma_f32_16x16x32_bf16 v[34:37], v[160:163], v[208:211], 0
	v_mfma_f32_16x16x32_bf16 v[26:29], v[168:171], v[208:211], 0
	v_mfma_f32_16x16x32_bf16 v[18:21], v[160:163], v[216:219], 0
	v_mfma_f32_16x16x32_bf16 v[10:13], v[168:171], v[216:219], 0
	v_mfma_f32_16x16x32_bf16 v[62:65], v[164:167], v[196:199], v[62:65]
	v_mfma_f32_16x16x32_bf16 v[58:61], v[172:175], v[196:199], v[58:61]
	v_mfma_f32_16x16x32_bf16 v[50:53], v[164:167], v[204:207], v[50:53]
	v_mfma_f32_16x16x32_bf16 v[42:45], v[172:175], v[204:207], v[42:45]
	v_mfma_f32_16x16x32_bf16 v[34:37], v[164:167], v[212:215], v[34:37]
	v_mfma_f32_16x16x32_bf16 v[26:29], v[172:175], v[212:215], v[26:29]
	v_mfma_f32_16x16x32_bf16 v[18:21], v[164:167], v[220:223], v[18:21]
	v_mfma_f32_16x16x32_bf16 v[10:13], v[172:175], v[220:223], v[10:13]
	s_setprio 0
	s_setprio 3
	v_mfma_f32_16x16x32_bf16 v[54:57], v[176:179], v[192:195], 0
	v_mfma_f32_16x16x32_bf16 v[46:49], v[184:187], v[192:195], 0
	v_mfma_f32_16x16x32_bf16 v[38:41], v[176:179], v[200:203], 0
	v_mfma_f32_16x16x32_bf16 v[30:33], v[184:187], v[200:203], 0
	v_mfma_f32_16x16x32_bf16 v[22:25], v[176:179], v[208:211], 0
	v_mfma_f32_16x16x32_bf16 v[14:17], v[184:187], v[208:211], 0
	v_mfma_f32_16x16x32_bf16 v[6:9], v[176:179], v[216:219], 0
	v_mfma_f32_16x16x32_bf16 v[2:5], v[184:187], v[216:219], 0
	v_mfma_f32_16x16x32_bf16 v[54:57], v[180:183], v[196:199], v[54:57]
	v_mfma_f32_16x16x32_bf16 v[46:49], v[188:191], v[196:199], v[46:49]
	v_mfma_f32_16x16x32_bf16 v[38:41], v[180:183], v[204:207], v[38:41]
	v_mfma_f32_16x16x32_bf16 v[30:33], v[188:191], v[204:207], v[30:33]
	v_mfma_f32_16x16x32_bf16 v[22:25], v[180:183], v[212:215], v[22:25]
	v_mfma_f32_16x16x32_bf16 v[14:17], v[188:191], v[212:215], v[14:17]
	v_mfma_f32_16x16x32_bf16 v[6:9], v[180:183], v[220:223], v[6:9]
	v_mfma_f32_16x16x32_bf16 v[2:5], v[188:191], v[220:223], v[2:5]
	s_setprio 0
	s_barrier
	s_add_i32 s70, 0, 0x18000
	v_add_u32_e32 v130, s70, v147
	s_add_i32 s71, 0, 0x1c000
	ds_read_b128 v[160:163], v130
	ds_read_b128 v[164:167], v130 offset:1024
	ds_read_b128 v[168:171], v130 offset:2048
	ds_read_b128 v[172:175], v130 offset:3072
	v_add_u32_e32 v130, s71, v147
	ds_read_b128 v[176:179], v130
	ds_read_b128 v[180:183], v130 offset:1024
	ds_read_b128 v[184:187], v130 offset:2048
	ds_read_b128 v[188:191], v130 offset:3072
	s_add_u32 s38, s44, 0xe0000
	s_addc_u32 s39, s45, 0
	s_mov_b32 m0, s53
	ds_read_b128 v[192:195], v159 offset:32768
	ds_read_b128 v[196:199], v159 offset:33792
	ds_read_b128 v[200:203], v159 offset:34816
	ds_read_b128 v[204:207], v159 offset:35840
	ds_read_b128 v[208:211], v159 offset:36864
	ds_read_b128 v[212:215], v159 offset:37888
	ds_read_b128 v[216:219], v159 offset:38912
	ds_read_b128 v[220:223], v159 offset:39936
	global_load_lds_dwordx4 v132, s[38:39]
	s_mov_b32 m0, s54
	s_nop 0
	global_load_lds_dwordx4 v136, s[38:39]
	s_waitcnt vmcnt(8)
	s_waitcnt lgkmcnt(0)
	s_barrier
	s_setprio 3
	s_waitcnt lgkmcnt(0)
	v_mfma_f32_16x16x32_bf16 v[126:129], v[160:163], v[192:195], v[126:129]
	v_mfma_f32_16x16x32_bf16 v[122:125], v[168:171], v[192:195], v[122:125]
	v_mfma_f32_16x16x32_bf16 v[118:121], v[160:163], v[200:203], v[118:121]
	v_mfma_f32_16x16x32_bf16 v[114:117], v[168:171], v[200:203], v[114:117]
	v_mfma_f32_16x16x32_bf16 v[106:109], v[160:163], v[208:211], v[106:109]
	v_mfma_f32_16x16x32_bf16 v[98:101], v[168:171], v[208:211], v[98:101]
	v_mfma_f32_16x16x32_bf16 v[78:81], v[160:163], v[216:219], v[78:81]
	v_mfma_f32_16x16x32_bf16 v[74:77], v[168:171], v[216:219], v[74:77]
	v_mfma_f32_16x16x32_bf16 v[126:129], v[164:167], v[196:199], v[126:129]
	v_mfma_f32_16x16x32_bf16 v[122:125], v[172:175], v[196:199], v[122:125]
	v_mfma_f32_16x16x32_bf16 v[118:121], v[164:167], v[204:207], v[118:121]
	v_mfma_f32_16x16x32_bf16 v[114:117], v[172:175], v[204:207], v[114:117]
	v_mfma_f32_16x16x32_bf16 v[106:109], v[164:167], v[212:215], v[106:109]
	v_mfma_f32_16x16x32_bf16 v[98:101], v[172:175], v[212:215], v[98:101]
	v_mfma_f32_16x16x32_bf16 v[78:81], v[164:167], v[220:223], v[78:81]
	v_mfma_f32_16x16x32_bf16 v[74:77], v[172:175], v[220:223], v[74:77]
	s_setprio 0
	s_setprio 3
	v_mfma_f32_16x16x32_bf16 v[110:113], v[176:179], v[192:195], v[110:113]
	v_mfma_f32_16x16x32_bf16 v[102:105], v[184:187], v[192:195], v[102:105]
	v_mfma_f32_16x16x32_bf16 v[94:97], v[176:179], v[200:203], v[94:97]
	v_mfma_f32_16x16x32_bf16 v[90:93], v[184:187], v[200:203], v[90:93]
	v_mfma_f32_16x16x32_bf16 v[86:89], v[176:179], v[208:211], v[86:89]
	v_mfma_f32_16x16x32_bf16 v[82:85], v[184:187], v[208:211], v[82:85]
	v_mfma_f32_16x16x32_bf16 v[70:73], v[176:179], v[216:219], v[70:73]
	v_mfma_f32_16x16x32_bf16 v[66:69], v[184:187], v[216:219], v[66:69]
	v_mfma_f32_16x16x32_bf16 v[110:113], v[180:183], v[196:199], v[110:113]
	v_mfma_f32_16x16x32_bf16 v[102:105], v[188:191], v[196:199], v[102:105]
	v_mfma_f32_16x16x32_bf16 v[94:97], v[180:183], v[204:207], v[94:97]
	v_mfma_f32_16x16x32_bf16 v[90:93], v[188:191], v[204:207], v[90:93]
	v_mfma_f32_16x16x32_bf16 v[86:89], v[180:183], v[212:215], v[86:89]
	v_mfma_f32_16x16x32_bf16 v[82:85], v[188:191], v[212:215], v[82:85]
	v_mfma_f32_16x16x32_bf16 v[70:73], v[180:183], v[220:223], v[70:73]
	v_mfma_f32_16x16x32_bf16 v[66:69], v[188:191], v[220:223], v[66:69]
	s_setprio 0
	s_barrier
; #define PG8_STAGE_A(b, h, ptr, NX) do { if constexpr (Sched::GATHER) { unsigned gs_[2]; gs_[0] = ((NX) && last_) ? gN[h][0] : gA[h][0]; gs_[1] = ((NX) && last_) ? gN[h][1] : gA[h][1]; PG8_STAGE(PG8_SA(b, h), ptr, gs_); } \
;         else PG8_STAGE(PG8_SA(b, h), (ptr) + ((h) ? hstep : (size_t)0), voffA); } while (0)
; #define PG8_STAGE(bufoff, gbase, voff) do { _Pragma("unroll") for (int _i = 0; _i < 2; ++_i) \
;         __builtin_amdgcn_global_load_lds((const unsigned*)((const char*)(gbase) + (voff)[_i]), (PG8_LAS unsigned*)(lds + (bufoff) + ldsw + _i * 8192), 16, 0, 0); } while (0)
; #define PG8_WAIT_V(n) asm volatile("s_waitcnt vmcnt(" #n ")" ::: "memory")
; #define PG8_BAR __builtin_amdgcn_s_barrier()
; template <class Epi, class Sched, bool ALIGN_EPI = false, bool SP2 = false>
; __device__ __forceinline__ void gemm_phase(PG8_LAS unsigned char* lds, const Gemm g, const Sched& S, const Epi& E, const bool skip_epi = false) {
;     ...
;         for (int t = 0; t < nt; t += 2) {
;             const bool last = (t == nt - 2); last_ = last && has_next;
;             const char* a1 = cA + (size_t)(t + 1) * kstep;
;             const char* a2 = last ? nA : cA + (size_t)(t + 2) * kstep; const char* b2 = last ? nB : cB + (size_t)(t + 2) * kstep;
;             const char* a3 = a2 + kstep; const char* b3 = b2 + kstep;
;             if (last && has_next) S.a_ready(nxt);
;             if constexpr (SP2) {
;             PG8_LDB(B0, 0, 0); PG8_LDB(B1, 0, 1); PG8_SCHED; PG8_LDA(At, 0, 0); PG8_STAGE_A(1, 1, a1, false);
;             PG8_WAIT_V(8); PG8_WAIT_L(0); PG8_BAR; PG8_MMA(0, 0, At, B0); PG8_MMA(0, 1, At, B1); PG8_BAR; PG8_SCHED;
;             PG8_LDA(At, 0, 1); PG8_STAGE(PG8_SB(0, 0), b2, voffB); PG8_STAGE(PG8_SB(0, 1), b2 + hstep, voffB); PG8_STAGE_A(0, 0, a2, true);
;             PG8_WAIT_V(8); PG8_WAIT_L(0); PG8_BAR; PG8_MMA(1, 0, At, B0); PG8_MMA(1, 1, At, B1); PG8_BAR; PG8_SCHED;
;             PG8_LDB(B0, 1, 0); PG8_LDB(B1, 1, 1); PG8_SCHED; PG8_LDA(At, 1, 0); PG8_STAGE_A(0, 1, a2, true);
;             PG8_WAIT_V(8); PG8_WAIT_L(0); PG8_BAR; PG8_MMA(0, 0, At, B0); PG8_MMA(0, 1, At, B1); PG8_BAR; PG8_SCHED;
;             PG8_LDA(At, 1, 1); PG8_STAGE(PG8_SB(1, 0), b3, voffB); PG8_STAGE(PG8_SB(1, 1), b3 + hstep, voffB); PG8_STAGE_A(1, 0, a3, true);
;             PG8_WAIT_V(8); PG8_WAIT_L(0); PG8_BAR; PG8_MMA(1, 0, At, B0); PG8_MMA(1, 1, At, B1); PG8_BAR; PG8_SCHED;
	s_add_i32 s38, s70, s51
	s_add_i32 m0, s38, 0xffffff80
	ds_read_b128 v[192:195], v159 offset:49152
	ds_read_b128 v[196:199], v159 offset:50176
	ds_read_b128 v[200:203], v159 offset:51200
	ds_read_b128 v[204:207], v159 offset:52224
	ds_read_b128 v[208:211], v159 offset:53248
	ds_read_b128 v[212:215], v159 offset:54272
	ds_read_b128 v[216:219], v159 offset:55296
	ds_read_b128 v[220:223], v159 offset:56320
	global_load_lds_dwordx4 v[152:153], off offset:128
	s_add_i32 m0, s38, 0x1f80
	s_add_u32 s38, s42, 0xe0080
	s_addc_u32 s39, s43, 0
	s_add_i32 s42, s71, s51
	global_load_lds_dwordx4 v[224:225], off offset:128
	s_mov_b32 m0, s42
	s_nop 0
	global_load_lds_dwordx4 v134, s[38:39]
	s_add_i32 m0, s42, 0x2000
	s_nop 0
	global_load_lds_dwordx4 v138, s[38:39]
	s_add_i32 m0, s57, 0xffffff80
	s_nop 0
	global_load_lds_dwordx4 v[226:227], off offset:128
	s_add_i32 m0, s58, 0xffffff80
	s_nop 0
	global_load_lds_dwordx4 v[230:231], off offset:128
	s_waitcnt vmcnt(8)
	s_waitcnt lgkmcnt(0)
	s_barrier
	s_setprio 3
	s_waitcnt lgkmcnt(0)
	v_mfma_f32_16x16x32_bf16 v[62:65], v[160:163], v[192:195], v[62:65]
	v_mfma_f32_16x16x32_bf16 v[58:61], v[168:171], v[192:195], v[58:61]
	v_mfma_f32_16x16x32_bf16 v[50:53], v[160:163], v[200:203], v[50:53]
	v_mfma_f32_16x16x32_bf16 v[42:45], v[168:171], v[200:203], v[42:45]
	v_mfma_f32_16x16x32_bf16 v[34:37], v[160:163], v[208:211], v[34:37]
	v_mfma_f32_16x16x32_bf16 v[26:29], v[168:171], v[208:211], v[26:29]
	v_mfma_f32_16x16x32_bf16 v[18:21], v[160:163], v[216:219], v[18:21]
	v_mfma_f32_16x16x32_bf16 v[10:13], v[168:171], v[216:219], v[10:13]
	v_mfma_f32_16x16x32_bf16 v[62:65], v[164:167], v[196:199], v[62:65]
	v_mfma_f32_16x16x32_bf16 v[58:61], v[172:175], v[196:199], v[58:61]
	v_mfma_f32_16x16x32_bf16 v[50:53], v[164:167], v[204:207], v[50:53]
	v_mfma_f32_16x16x32_bf16 v[42:45], v[172:175], v[204:207], v[42:45]
	v_mfma_f32_16x16x32_bf16 v[34:37], v[164:167], v[212:215], v[34:37]
	v_mfma_f32_16x16x32_bf16 v[26:29], v[172:175], v[212:215], v[26:29]
	v_mfma_f32_16x16x32_bf16 v[18:21], v[164:167], v[220:223], v[18:21]
	v_mfma_f32_16x16x32_bf16 v[10:13], v[172:175], v[220:223], v[10:13]
	s_setprio 0
	s_setprio 3
	v_mfma_f32_16x16x32_bf16 v[54:57], v[176:179], v[192:195], v[54:57]
	v_mfma_f32_16x16x32_bf16 v[46:49], v[184:187], v[192:195], v[46:49]
	v_mfma_f32_16x16x32_bf16 v[38:41], v[176:179], v[200:203], v[38:41]
	v_mfma_f32_16x16x32_bf16 v[30:33], v[184:187], v[200:203], v[30:33]
	v_mfma_f32_16x16x32_bf16 v[22:25], v[176:179], v[208:211], v[22:25]
	v_mfma_f32_16x16x32_bf16 v[14:17], v[184:187], v[208:211], v[14:17]
	v_mfma_f32_16x16x32_bf16 v[6:9], v[176:179], v[216:219], v[6:9]
	v_mfma_f32_16x16x32_bf16 v[2:5], v[184:187], v[216:219], v[2:5]
	v_mfma_f32_16x16x32_bf16 v[54:57], v[180:183], v[196:199], v[54:57]
	v_mfma_f32_16x16x32_bf16 v[46:49], v[188:191], v[196:199], v[46:49]
	v_mfma_f32_16x16x32_bf16 v[38:41], v[180:183], v[204:207], v[38:41]
	v_mfma_f32_16x16x32_bf16 v[30:33], v[188:191], v[204:207], v[30:33]
	v_mfma_f32_16x16x32_bf16 v[22:25], v[180:183], v[212:215], v[22:25]
	v_mfma_f32_16x16x32_bf16 v[14:17], v[188:191], v[212:215], v[14:17]
	v_mfma_f32_16x16x32_bf16 v[6:9], v[180:183], v[220:223], v[6:9]
	v_mfma_f32_16x16x32_bf16 v[2:5], v[188:191], v[220:223], v[2:5]
	s_setprio 0
	s_barrier
	s_add_i32 s69, s69, 2
	s_add_u32 s67, s67, 0x100
	s_addc_u32 s68, s68, 0
	s_cmp_gt_u32 s69, 53
	s_mov_b64 s[38:39], s[40:41]
.LBB0_1823:
	ds_read_b128 v[160:163], v157
	ds_read_b128 v[164:167], v157 offset:1024
	ds_read_b128 v[168:171], v157 offset:2048
	ds_read_b128 v[172:175], v157 offset:3072
	ds_read_b128 v[176:179], v158
	ds_read_b128 v[180:183], v158 offset:1024
	ds_read_b128 v[184:187], v158 offset:2048
	ds_read_b128 v[188:191], v158 offset:3072
	s_add_u32 s40, s38, 0x100
	s_addc_u32 s41, s39, 0
	s_cmp_eq_u32 s69, 52
	s_cselect_b32 s45, s7, s41
	s_cselect_b32 s44, s6, s40
	s_cselect_b32 s43, s35, s68
	s_cselect_b32 s42, s34, s67
	v_lshl_add_u64 v[152:153], s[38:39], 0, v[140:141]
	s_add_i32 m0, s37, 0xc000
	ds_read_b128 v[192:195], v159
	ds_read_b128 v[196:199], v159 offset:1024
	ds_read_b128 v[200:203], v159 offset:2048
	ds_read_b128 v[204:207], v159 offset:3072
	ds_read_b128 v[208:211], v159 offset:4096
	ds_read_b128 v[212:215], v159 offset:5120
	ds_read_b128 v[216:219], v159 offset:6144
	ds_read_b128 v[220:223], v159 offset:7168
	global_load_lds_dwordx4 v[152:153], off
	v_lshl_add_u64 v[152:153], s[38:39], 0, v[142:143]
	s_add_i32 m0, s37, 0xe000
	s_nop 0
	global_load_lds_dwordx4 v[152:153], off
	s_waitcnt vmcnt(8)
	s_waitcnt lgkmcnt(0)
	s_barrier
; #define PG8_STAGE_A(b, h, ptr, NX) do { if constexpr (Sched::GATHER) { unsigned gs_[2]; gs_[0] = ((NX) && last_) ? gN[h][0] : gA[h][0]; gs_[1] = ((NX) && last_) ? gN[h][1] : gA[h][1]; PG8_STAGE(PG8_SA(b, h), ptr, gs_); } \
;         else PG8_STAGE(PG8_SA(b, h), (ptr) + ((h) ? hstep : (size_t)0), voffA); } while (0)
; #define PG8_STAGE(bufoff, gbase, voff) do { _Pragma("unroll") for (int _i = 0; _i < 2; ++_i) \
;         __builtin_amdgcn_global_load_lds((const unsigned*)((const char*)(gbase) + (voff)[_i]), (PG8_LAS unsigned*)(lds + (bufoff) + ldsw + _i * 8192), 16, 0, 0); } while (0)
; #define PG8_LDA(dst, b, h) do { _Pragma("unroll") for (int m = 0; m < 4; ++m) _Pragma("unroll") for (int k = 0; k < 2; ++k) dst[m][k] = *(const PG8_LAS bf16x8*)(lds + PG8_SA(b, h) + aoff + m * 2048 + k * 1024); } while (0)
; #define PG8_LDB(dst, b, h) do { _Pragma("unroll") for (int n = 0; n < 2; ++n) _Pragma("unroll") for (int k = 0; k < 2; ++k) dst[n][k] = *(const PG8_LAS bf16x8*)(lds + PG8_SB(b, h) + boff + n * 2048 + k * 1024); } while (0)
; #define PG8_MMA(ai, bj, At, Bt) do { __builtin_amdgcn_s_setprio(1); _Pragma("unroll") for (int m = 0; m < 4; ++m) _Pragma("unroll") for (int n = 0; n < 2; ++n) _Pragma("unroll") for (int k = 0; k < 2; ++k) \
;         acc[ai][bj][m][n] = __builtin_amdgcn_mfma_f32_16x16x32_bf16(Bt[n][k], At[m][k], acc[ai][bj][m][n], 0, 0, 0); __builtin_amdgcn_s_setprio(0); } while (0)
; #define PG8_WAIT_V(n) asm volatile("s_waitcnt vmcnt(" #n ")" ::: "memory")
; #define PG8_WAIT_L(n) asm volatile("s_waitcnt lgkmcnt(" #n ")" ::: "memory")
; #define PG8_BAR __builtin_amdgcn_s_barrier()
; #define PG8_SCHED __builtin_amdgcn_sched_barrier(0)
; template <class Epi, class Sched, bool ALIGN_EPI = false, bool SP2 = false>
; __device__ __forceinline__ void gemm_phase(PG8_LAS unsigned char* lds, const Gemm g, const Sched& S, const Epi& E, const bool skip_epi = false) {
;     ...
;             PG8_LDB(B0, 0, 0); PG8_LDB(B1, 0, 1); PG8_SCHED; PG8_LDA(At, 0, 0); PG8_STAGE_A(1, 1, a1, false);
;             PG8_WAIT_V(8); PG8_WAIT_L(0); PG8_BAR; PG8_MMA(0, 0, At, B0); PG8_MMA(0, 1, At, B1); PG8_BAR; PG8_SCHED;
;             PG8_LDA(At, 0, 1); PG8_STAGE(PG8_SB(0, 0), b2, voffB); PG8_STAGE(PG8_SB(0, 1), b2 + hstep, voffB); PG8_STAGE_A(0, 0, a2, true);
;             PG8_WAIT_V(8); PG8_WAIT_L(0); PG8_BAR; PG8_MMA(1, 0, At, B0); PG8_MMA(1, 1, At, B1); PG8_BAR; PG8_SCHED;
	s_setprio 3
	s_waitcnt lgkmcnt(0)
	v_mfma_f32_16x16x32_bf16 v[126:129], v[160:163], v[192:195], v[126:129]
	v_mfma_f32_16x16x32_bf16 v[122:125], v[168:171], v[192:195], v[122:125]
	v_mfma_f32_16x16x32_bf16 v[118:121], v[160:163], v[200:203], v[118:121]
	v_mfma_f32_16x16x32_bf16 v[114:117], v[168:171], v[200:203], v[114:117]
	v_mfma_f32_16x16x32_bf16 v[106:109], v[160:163], v[208:211], v[106:109]
	v_mfma_f32_16x16x32_bf16 v[98:101], v[168:171], v[208:211], v[98:101]
	v_mfma_f32_16x16x32_bf16 v[78:81], v[160:163], v[216:219], v[78:81]
	v_mfma_f32_16x16x32_bf16 v[74:77], v[168:171], v[216:219], v[74:77]
	v_mfma_f32_16x16x32_bf16 v[126:129], v[164:167], v[196:199], v[126:129]
	v_mfma_f32_16x16x32_bf16 v[122:125], v[172:175], v[196:199], v[122:125]
	v_mfma_f32_16x16x32_bf16 v[118:121], v[164:167], v[204:207], v[118:121]
	v_mfma_f32_16x16x32_bf16 v[114:117], v[172:175], v[204:207], v[114:117]
	v_mfma_f32_16x16x32_bf16 v[106:109], v[164:167], v[212:215], v[106:109]
	v_mfma_f32_16x16x32_bf16 v[98:101], v[172:175], v[212:215], v[98:101]
	v_mfma_f32_16x16x32_bf16 v[78:81], v[164:167], v[220:223], v[78:81]
	v_mfma_f32_16x16x32_bf16 v[74:77], v[172:175], v[220:223], v[74:77]
	s_setprio 0
	s_setprio 3
	v_mfma_f32_16x16x32_bf16 v[110:113], v[176:179], v[192:195], v[110:113]
	v_mfma_f32_16x16x32_bf16 v[102:105], v[184:187], v[192:195], v[102:105]
	v_mfma_f32_16x16x32_bf16 v[94:97], v[176:179], v[200:203], v[94:97]
	v_mfma_f32_16x16x32_bf16 v[90:93], v[184:187], v[200:203], v[90:93]
	v_mfma_f32_16x16x32_bf16 v[86:89], v[176:179], v[208:211], v[86:89]
	v_mfma_f32_16x16x32_bf16 v[82:85], v[184:187], v[208:211], v[82:85]
	v_mfma_f32_16x16x32_bf16 v[70:73], v[176:179], v[216:219], v[70:73]
	v_mfma_f32_16x16x32_bf16 v[66:69], v[184:187], v[216:219], v[66:69]
	v_mfma_f32_16x16x32_bf16 v[110:113], v[180:183], v[196:199], v[110:113]
	v_mfma_f32_16x16x32_bf16 v[102:105], v[188:191], v[196:199], v[102:105]
	v_mfma_f32_16x16x32_bf16 v[94:97], v[180:183], v[204:207], v[94:97]
	v_mfma_f32_16x16x32_bf16 v[90:93], v[188:191], v[204:207], v[90:93]
	v_mfma_f32_16x16x32_bf16 v[86:89], v[180:183], v[212:215], v[86:89]
	v_mfma_f32_16x16x32_bf16 v[82:85], v[188:191], v[212:215], v[82:85]
	v_mfma_f32_16x16x32_bf16 v[70:73], v[180:183], v[220:223], v[70:73]
	v_mfma_f32_16x16x32_bf16 v[66:69], v[188:191], v[220:223], v[66:69]
	s_setprio 0
	s_barrier
	s_add_i32 s38, s60, s51
	v_lshl_add_u64 v[152:153], s[42:43], 0, v[134:135]
	s_mov_b32 m0, s38
	ds_read_b128 v[192:195], v159 offset:16384
	ds_read_b128 v[196:199], v159 offset:17408
	ds_read_b128 v[200:203], v159 offset:18432
	ds_read_b128 v[204:207], v159 offset:19456
	ds_read_b128 v[208:211], v159 offset:20480
	ds_read_b128 v[212:215], v159 offset:21504
	ds_read_b128 v[216:219], v159 offset:22528
	ds_read_b128 v[220:223], v159 offset:23552
	global_load_lds_dwordx4 v[152:153], off
	s_add_i32 m0, s38, 0x2000
	s_add_u32 s38, s42, 0xe0000
	v_lshl_add_u64 v[224:225], s[42:43], 0, v[138:139]
	s_addc_u32 s39, s43, 0
	s_add_i32 s70, s61, s51
	global_load_lds_dwordx4 v[224:225], off
	s_mov_b32 m0, s70
	v_lshl_add_u64 v[230:231], s[44:45], 0, v[136:137]
	global_load_lds_dwordx4 v134, s[38:39]
	s_add_i32 m0, s70, 0x2000
	s_nop 0
	global_load_lds_dwordx4 v138, s[38:39]
	v_lshl_add_u64 v[226:227], s[44:45], 0, v[132:133]
	s_mov_b32 m0, s37
	s_nop 0
	global_load_lds_dwordx4 v[226:227], off
	s_mov_b32 m0, s52
	s_nop 0
	global_load_lds_dwordx4 v[230:231], off
	s_waitcnt vmcnt(8)
	s_waitcnt lgkmcnt(0)
	s_barrier
	s_setprio 3
	s_waitcnt lgkmcnt(0)
	v_mfma_f32_16x16x32_bf16 v[62:65], v[160:163], v[192:195], v[62:65]
	v_mfma_f32_16x16x32_bf16 v[58:61], v[168:171], v[192:195], v[58:61]
	v_mfma_f32_16x16x32_bf16 v[50:53], v[160:163], v[200:203], v[50:53]
	v_mfma_f32_16x16x32_bf16 v[42:45], v[168:171], v[200:203], v[42:45]
	v_mfma_f32_16x16x32_bf16 v[34:37], v[160:163], v[208:211], v[34:37]
	v_mfma_f32_16x16x32_bf16 v[26:29], v[168:171], v[208:211], v[26:29]
	v_mfma_f32_16x16x32_bf16 v[18:21], v[160:163], v[216:219], v[18:21]
	v_mfma_f32_16x16x32_bf16 v[10:13], v[168:171], v[216:219], v[10:13]
	v_mfma_f32_16x16x32_bf16 v[62:65], v[164:167], v[196:199], v[62:65]
	v_mfma_f32_16x16x32_bf16 v[58:61], v[172:175], v[196:199], v[58:61]
	v_mfma_f32_16x16x32_bf16 v[50:53], v[164:167], v[204:207], v[50:53]
	v_mfma_f32_16x16x32_bf16 v[42:45], v[172:175], v[204:207], v[42:45]
	v_mfma_f32_16x16x32_bf16 v[34:37], v[164:167], v[212:215], v[34:37]
	v_mfma_f32_16x16x32_bf16 v[26:29], v[172:175], v[212:215], v[26:29]
	v_mfma_f32_16x16x32_bf16 v[18:21], v[164:167], v[220:223], v[18:21]
	v_mfma_f32_16x16x32_bf16 v[10:13], v[172:175], v[220:223], v[10:13]
	s_setprio 0
	s_setprio 3
	v_mfma_f32_16x16x32_bf16 v[54:57], v[176:179], v[192:195], v[54:57]
	v_mfma_f32_16x16x32_bf16 v[46:49], v[184:187], v[192:195], v[46:49]
	v_mfma_f32_16x16x32_bf16 v[38:41], v[176:179], v[200:203], v[38:41]
	v_mfma_f32_16x16x32_bf16 v[30:33], v[184:187], v[200:203], v[30:33]
	v_mfma_f32_16x16x32_bf16 v[22:25], v[176:179], v[208:211], v[22:25]
	v_mfma_f32_16x16x32_bf16 v[14:17], v[184:187], v[208:211], v[14:17]
	v_mfma_f32_16x16x32_bf16 v[6:9], v[176:179], v[216:219], v[6:9]
	v_mfma_f32_16x16x32_bf16 v[2:5], v[184:187], v[216:219], v[2:5]
	v_mfma_f32_16x16x32_bf16 v[54:57], v[180:183], v[196:199], v[54:57]
	v_mfma_f32_16x16x32_bf16 v[46:49], v[188:191], v[196:199], v[46:49]
	v_mfma_f32_16x16x32_bf16 v[38:41], v[180:183], v[204:207], v[38:41]
	v_mfma_f32_16x16x32_bf16 v[30:33], v[188:191], v[204:207], v[30:33]
	v_mfma_f32_16x16x32_bf16 v[22:25], v[180:183], v[212:215], v[22:25]
	v_mfma_f32_16x16x32_bf16 v[14:17], v[188:191], v[212:215], v[14:17]
	v_mfma_f32_16x16x32_bf16 v[6:9], v[180:183], v[220:223], v[6:9]
	v_mfma_f32_16x16x32_bf16 v[2:5], v[188:191], v[220:223], v[2:5]
	s_setprio 0
	s_barrier
; #define PG8_STAGE_A(b, h, ptr, NX) do { if constexpr (Sched::GATHER) { unsigned gs_[2]; gs_[0] = ((NX) && last_) ? gN[h][0] : gA[h][0]; gs_[1] = ((NX) && last_) ? gN[h][1] : gA[h][1]; PG8_STAGE(PG8_SA(b, h), ptr, gs_); } \
;         else PG8_STAGE(PG8_SA(b, h), (ptr) + ((h) ? hstep : (size_t)0), voffA); } while (0)
; #define PG8_STAGE(bufoff, gbase, voff) do { _Pragma("unroll") for (int _i = 0; _i < 2; ++_i) \
;         __builtin_amdgcn_global_load_lds((const unsigned*)((const char*)(gbase) + (voff)[_i]), (PG8_LAS unsigned*)(lds + (bufoff) + ldsw + _i * 8192), 16, 0, 0); } while (0)
; #define PG8_LDA(dst, b, h) do { _Pragma("unroll") for (int m = 0; m < 4; ++m) _Pragma("unroll") for (int k = 0; k < 2; ++k) dst[m][k] = *(const PG8_LAS bf16x8*)(lds + PG8_SA(b, h) + aoff + m * 2048 + k * 1024); } while (0)
; #define PG8_LDB(dst, b, h) do { _Pragma("unroll") for (int n = 0; n < 2; ++n) _Pragma("unroll") for (int k = 0; k < 2; ++k) dst[n][k] = *(const PG8_LAS bf16x8*)(lds + PG8_SB(b, h) + boff + n * 2048 + k * 1024); } while (0)
; #define PG8_MMA(ai, bj, At, Bt) do { __builtin_amdgcn_s_setprio(1); _Pragma("unroll") for (int m = 0; m < 4; ++m) _Pragma("unroll") for (int n = 0; n < 2; ++n) _Pragma("unroll") for (int k = 0; k < 2; ++k) \
;         acc[ai][bj][m][n] = __builtin_amdgcn_mfma_f32_16x16x32_bf16(Bt[n][k], At[m][k], acc[ai][bj][m][n], 0, 0, 0); __builtin_amdgcn_s_setprio(0); } while (0)
; #define PG8_WAIT_V(n) asm volatile("s_waitcnt vmcnt(" #n ")" ::: "memory")
; #define PG8_WAIT_L(n) asm volatile("s_waitcnt lgkmcnt(" #n ")" ::: "memory")
; #define PG8_BAR __builtin_amdgcn_s_barrier()
; #define PG8_SCHED __builtin_amdgcn_sched_barrier(0)
; template <class Epi, class Sched, bool ALIGN_EPI = false, bool SP2 = false>
; __device__ __forceinline__ void gemm_phase(PG8_LAS unsigned char* lds, const Gemm g, const Sched& S, const Epi& E, const bool skip_epi = false) {
;     ...
;             PG8_LDB(B0, 1, 0); PG8_LDB(B1, 1, 1); PG8_SCHED; PG8_LDA(At, 1, 0); PG8_STAGE_A(0, 1, a2, true);
;             PG8_WAIT_V(8); PG8_WAIT_L(0); PG8_BAR; PG8_MMA(0, 0, At, B0); PG8_MMA(0, 1, At, B1); PG8_BAR; PG8_SCHED;
;             PG8_LDA(At, 1, 1); PG8_STAGE(PG8_SB(1, 0), b3, voffB); PG8_STAGE(PG8_SB(1, 1), b3 + hstep, voffB); PG8_STAGE_A(1, 0, a3, true);
;             PG8_WAIT_V(8); PG8_WAIT_L(0); PG8_BAR; PG8_MMA(1, 0, At, B0); PG8_MMA(1, 1, At, B1); PG8_BAR; PG8_SCHED;
	s_add_i32 s70, 0, 0x18000
	v_add_u32_e32 v130, s70, v147
	s_add_i32 s71, 0, 0x1c000
	ds_read_b128 v[160:163], v130
	ds_read_b128 v[164:167], v130 offset:1024
	ds_read_b128 v[168:171], v130 offset:2048
	ds_read_b128 v[172:175], v130 offset:3072
	v_add_u32_e32 v130, s71, v147
	ds_read_b128 v[176:179], v130
	ds_read_b128 v[180:183], v130 offset:1024
	ds_read_b128 v[184:187], v130 offset:2048
	ds_read_b128 v[188:191], v130 offset:3072
	s_add_u32 s38, s44, 0xe0000
	s_addc_u32 s39, s45, 0
	s_mov_b32 m0, s53
	ds_read_b128 v[192:195], v159 offset:32768
	ds_read_b128 v[196:199], v159 offset:33792
	ds_read_b128 v[200:203], v159 offset:34816
	ds_read_b128 v[204:207], v159 offset:35840
	ds_read_b128 v[208:211], v159 offset:36864
	ds_read_b128 v[212:215], v159 offset:37888
	ds_read_b128 v[216:219], v159 offset:38912
	ds_read_b128 v[220:223], v159 offset:39936
	global_load_lds_dwordx4 v132, s[38:39]
	s_mov_b32 m0, s54
	s_nop 0
	global_load_lds_dwordx4 v136, s[38:39]
	s_waitcnt vmcnt(8)
	s_waitcnt lgkmcnt(0)
	s_barrier
	s_setprio 3
	s_waitcnt lgkmcnt(0)
	v_mfma_f32_16x16x32_bf16 v[126:129], v[160:163], v[192:195], v[126:129]
	v_mfma_f32_16x16x32_bf16 v[122:125], v[168:171], v[192:195], v[122:125]
	v_mfma_f32_16x16x32_bf16 v[118:121], v[160:163], v[200:203], v[118:121]
	v_mfma_f32_16x16x32_bf16 v[114:117], v[168:171], v[200:203], v[114:117]
	v_mfma_f32_16x16x32_bf16 v[106:109], v[160:163], v[208:211], v[106:109]
	v_mfma_f32_16x16x32_bf16 v[98:101], v[168:171], v[208:211], v[98:101]
	v_mfma_f32_16x16x32_bf16 v[78:81], v[160:163], v[216:219], v[78:81]
	v_mfma_f32_16x16x32_bf16 v[74:77], v[168:171], v[216:219], v[74:77]
	v_mfma_f32_16x16x32_bf16 v[126:129], v[164:167], v[196:199], v[126:129]
	v_mfma_f32_16x16x32_bf16 v[122:125], v[172:175], v[196:199], v[122:125]
	v_mfma_f32_16x16x32_bf16 v[118:121], v[164:167], v[204:207], v[118:121]
	v_mfma_f32_16x16x32_bf16 v[114:117], v[172:175], v[204:207], v[114:117]
	v_mfma_f32_16x16x32_bf16 v[106:109], v[164:167], v[212:215], v[106:109]
	v_mfma_f32_16x16x32_bf16 v[98:101], v[172:175], v[212:215], v[98:101]
	v_mfma_f32_16x16x32_bf16 v[78:81], v[164:167], v[220:223], v[78:81]
	v_mfma_f32_16x16x32_bf16 v[74:77], v[172:175], v[220:223], v[74:77]
	s_setprio 0
	s_setprio 3
	v_mfma_f32_16x16x32_bf16 v[110:113], v[176:179], v[192:195], v[110:113]
	v_mfma_f32_16x16x32_bf16 v[102:105], v[184:187], v[192:195], v[102:105]
	v_mfma_f32_16x16x32_bf16 v[94:97], v[176:179], v[200:203], v[94:97]
	v_mfma_f32_16x16x32_bf16 v[90:93], v[184:187], v[200:203], v[90:93]
	v_mfma_f32_16x16x32_bf16 v[86:89], v[176:179], v[208:211], v[86:89]
	v_mfma_f32_16x16x32_bf16 v[82:85], v[184:187], v[208:211], v[82:85]
	v_mfma_f32_16x16x32_bf16 v[70:73], v[176:179], v[216:219], v[70:73]
	v_mfma_f32_16x16x32_bf16 v[66:69], v[184:187], v[216:219], v[66:69]
	v_mfma_f32_16x16x32_bf16 v[110:113], v[180:183], v[196:199], v[110:113]
	v_mfma_f32_16x16x32_bf16 v[102:105], v[188:191], v[196:199], v[102:105]
	v_mfma_f32_16x16x32_bf16 v[94:97], v[180:183], v[204:207], v[94:97]
	v_mfma_f32_16x16x32_bf16 v[90:93], v[188:191], v[204:207], v[90:93]
	v_mfma_f32_16x16x32_bf16 v[86:89], v[180:183], v[212:215], v[86:89]
	v_mfma_f32_16x16x32_bf16 v[82:85], v[188:191], v[212:215], v[82:85]
	v_mfma_f32_16x16x32_bf16 v[70:73], v[180:183], v[220:223], v[70:73]
	v_mfma_f32_16x16x32_bf16 v[66:69], v[188:191], v[220:223], v[66:69]
	s_setprio 0
	s_barrier
	s_add_i32 s38, s70, s51
	s_add_i32 m0, s38, 0xffffff80
	ds_read_b128 v[192:195], v159 offset:49152
	ds_read_b128 v[196:199], v159 offset:50176
	ds_read_b128 v[200:203], v159 offset:51200
	ds_read_b128 v[204:207], v159 offset:52224
	ds_read_b128 v[208:211], v159 offset:53248
	ds_read_b128 v[212:215], v159 offset:54272
	ds_read_b128 v[216:219], v159 offset:55296
	ds_read_b128 v[220:223], v159 offset:56320
	global_load_lds_dwordx4 v[152:153], off offset:128
	s_add_i32 m0, s38, 0x1f80
	s_add_u32 s38, s42, 0xe0080
	s_addc_u32 s39, s43, 0
	s_add_i32 s42, s71, s51
	global_load_lds_dwordx4 v[224:225], off offset:128
	s_mov_b32 m0, s42
	s_nop 0
	global_load_lds_dwordx4 v134, s[38:39]
	s_add_i32 m0, s42, 0x2000
	s_nop 0
	global_load_lds_dwordx4 v138, s[38:39]
	s_add_i32 m0, s57, 0xffffff80
	s_nop 0
	global_load_lds_dwordx4 v[226:227], off offset:128
	s_add_i32 m0, s58, 0xffffff80
	s_nop 0
	global_load_lds_dwordx4 v[230:231], off offset:128
	s_waitcnt vmcnt(8)
	s_waitcnt lgkmcnt(0)
	s_barrier
	s_setprio 3
	s_waitcnt lgkmcnt(0)
	v_mfma_f32_16x16x32_bf16 v[62:65], v[160:163], v[192:195], v[62:65]
	v_mfma_f32_16x16x32_bf16 v[58:61], v[168:171], v[192:195], v[58:61]
	v_mfma_f32_16x16x32_bf16 v[50:53], v[160:163], v[200:203], v[50:53]
	v_mfma_f32_16x16x32_bf16 v[42:45], v[168:171], v[200:203], v[42:45]
	v_mfma_f32_16x16x32_bf16 v[34:37], v[160:163], v[208:211], v[34:37]
	v_mfma_f32_16x16x32_bf16 v[26:29], v[168:171], v[208:211], v[26:29]
	v_mfma_f32_16x16x32_bf16 v[18:21], v[160:163], v[216:219], v[18:21]
	v_mfma_f32_16x16x32_bf16 v[10:13], v[168:171], v[216:219], v[10:13]
	v_mfma_f32_16x16x32_bf16 v[62:65], v[164:167], v[196:199], v[62:65]
	v_mfma_f32_16x16x32_bf16 v[58:61], v[172:175], v[196:199], v[58:61]
	v_mfma_f32_16x16x32_bf16 v[50:53], v[164:167], v[204:207], v[50:53]
	v_mfma_f32_16x16x32_bf16 v[42:45], v[172:175], v[204:207], v[42:45]
	v_mfma_f32_16x16x32_bf16 v[34:37], v[164:167], v[212:215], v[34:37]
	v_mfma_f32_16x16x32_bf16 v[26:29], v[172:175], v[212:215], v[26:29]
	v_mfma_f32_16x16x32_bf16 v[18:21], v[164:167], v[220:223], v[18:21]
	v_mfma_f32_16x16x32_bf16 v[10:13], v[172:175], v[220:223], v[10:13]
	s_setprio 0
	s_setprio 3
	v_mfma_f32_16x16x32_bf16 v[54:57], v[176:179], v[192:195], v[54:57]
	v_mfma_f32_16x16x32_bf16 v[46:49], v[184:187], v[192:195], v[46:49]
	v_mfma_f32_16x16x32_bf16 v[38:41], v[176:179], v[200:203], v[38:41]
	v_mfma_f32_16x16x32_bf16 v[30:33], v[184:187], v[200:203], v[30:33]
	v_mfma_f32_16x16x32_bf16 v[22:25], v[176:179], v[208:211], v[22:25]
	v_mfma_f32_16x16x32_bf16 v[14:17], v[184:187], v[208:211], v[14:17]
	v_mfma_f32_16x16x32_bf16 v[6:9], v[176:179], v[216:219], v[6:9]
	v_mfma_f32_16x16x32_bf16 v[2:5], v[184:187], v[216:219], v[2:5]
	v_mfma_f32_16x16x32_bf16 v[54:57], v[180:183], v[196:199], v[54:57]
	v_mfma_f32_16x16x32_bf16 v[46:49], v[188:191], v[196:199], v[46:49]
	v_mfma_f32_16x16x32_bf16 v[38:41], v[180:183], v[204:207], v[38:41]
	v_mfma_f32_16x16x32_bf16 v[30:33], v[188:191], v[204:207], v[30:33]
	v_mfma_f32_16x16x32_bf16 v[22:25], v[180:183], v[212:215], v[22:25]
	v_mfma_f32_16x16x32_bf16 v[14:17], v[188:191], v[212:215], v[14:17]
	v_mfma_f32_16x16x32_bf16 v[6:9], v[180:183], v[220:223], v[6:9]
	v_mfma_f32_16x16x32_bf16 v[2:5], v[188:191], v[220:223], v[2:5]
	s_setprio 0
	s_barrier
	s_add_i32 s69, s69, 2
	s_add_u32 s67, s67, 0x100
	s_addc_u32 s68, s68, 0
	s_cmp_gt_u32 s69, 53
	s_mov_b64 s[38:39], s[40:41]
	s_cbranch_scc0 .LBB0_1823
	s_and_b64 vcc, exec, s[20:21]
	s_cbranch_vccz .LBB0_1826
	s_barrier

; #define PG8_STAGE_A(b, h, ptr, NX) do { if constexpr (Sched::GATHER) { unsigned gs_[2]; gs_[0] = ((NX) && last_) ? gN[h][0] : gA[h][0]; gs_[1] = ((NX) && last_) ? gN[h][1] : gA[h][1]; PG8_STAGE(PG8_SA(b, h), ptr, gs_); } \
;         else PG8_STAGE(PG8_SA(b, h), (ptr) + ((h) ? hstep : (size_t)0), voffA); } while (0)
; #define PG8_STAGE(bufoff, gbase, voff) do { _Pragma("unroll") for (int _i = 0; _i < 2; ++_i) \
;         __builtin_amdgcn_global_load_lds((const unsigned*)((const char*)(gbase) + (voff)[_i]), (PG8_LAS unsigned*)(lds + (bufoff) + ldsw + _i * 8192), 16, 0, 0); } while (0)
; #define PG8_WAIT_V(n) asm volatile("s_waitcnt vmcnt(" #n ")" ::: "memory")
; #define PG8_BAR __builtin_amdgcn_s_barrier()
; template <class Epi, class Sched, bool ALIGN_EPI = false, bool SP2 = false>
; __device__ __forceinline__ void gemm_phase(PG8_LAS unsigned char* lds, const Gemm g, const Sched& S, const Epi& E, const bool skip_epi = false) {
;     ...
;     for (int i = 0; i < 2; ++i) { int R, C; stage_rc(tid * 16 + i * 8192, R, C); const int Rb = Epi::PERM ? ((R & ~31) + perm32(R & 31)) : R;
;         voffA[i] = (unsigned)(R * K + C) * 2u; voffB[i] = (unsigned)(Rb * K + C) * 2u; }
;     const size_t kstep = (size_t)(BK * 2);
;     const size_t hstep = (size_t)HALF * K * 2;
;     const size_t tstep = 2 * hstep;
;     const size_t pmstepA = Sched::GATHER ? (size_t)0 : tstep;
;     unsigned gA[2][2] = {{0u, 0u}, {0u, 0u}}, gN[2][2] = {{0u, 0u}, {0u, 0u}}; bool last_ = false; (void)gA; (void)gN; (void)last_;
;     ...
;     const unsigned ldsw = (unsigned)wid * 1024u;
;     const int aoff = lds_byte(wr * 64 + fr, fq * 8), boff = lds_byte(wc * 32 + fr, fq * 8);
;     ...
;         PG8_STAGE(PG8_SB(1, 0), cB + kstep, voffB); PG8_STAGE_A(1, 0, cA + kstep, false); PG8_STAGE(PG8_SB(1, 1), cB + hstep + kstep, voffB);
;         PG8_WAIT_V(6); PG8_BAR;
.LBB0_1834:
	s_add_u32 s42, s78, 0x4c00000
	s_addc_u32 s43, s79, 0
	s_lshl_b32 s45, s18, 6
	s_lshl_b32 s23, s18, 13
	s_lshl_b32 s7, s7, 5
	s_mov_b64 s[18:19], 0x80
	s_and_b32 s7, s7, 0x60
	s_add_i32 m0, s38, 0x18000
	v_lshl_add_u64 v[8:9], v[8:9], 0, s[18:19]
	s_lshl_b32 s44, s2, 8
	s_lshl_b32 s24, s7, 7
	s_waitcnt vmcnt(2)
	s_barrier
	global_load_lds_dwordx4 v[8:9], off
	v_lshl_add_u64 v[6:7], v[6:7], 0, s[18:19]
	s_add_i32 m0, s38, 0x1a000
	s_add_i32 s46, s38, 0x8000
	s_add_i32 s47, s38, 0xa000
	global_load_lds_dwordx4 v[6:7], off
	v_lshl_add_u64 v[2:3], v[2:3], 0, s[18:19]
	s_mov_b32 m0, s46
	s_add_u32 s20, s30, 0xe0080
	global_load_lds_dwordx4 v[2:3], off
	v_lshl_add_u64 v[2:3], v[4:5], 0, s[18:19]
	s_mov_b32 m0, s47
	s_addc_u32 s21, s31, 0
	global_load_lds_dwordx4 v[2:3], off
	s_add_i32 m0, s38, 0x1c000
	s_nop 0
	global_load_lds_dwordx4 v132, s[20:21]
	s_add_i32 m0, s38, 0x1e000
	v_and_b32_e32 v1, 15, v10
	global_load_lds_dwordx4 v134, s[20:21]
	v_and_b32_e32 v2, 48, v10
	v_lshlrev_b32_e32 v3, 2, v10
	v_lshl_or_b32 v2, v1, 6, v2
	v_and_b32_e32 v3, 32, v3
	v_bitop3_b32 v4, v2, s23, v3 bitop3:0xde
	v_bitop3_b32 v146, s24, v2, v3 bitop3:0xf6
	v_and_b32_e32 v2, 3, v10
	v_and_b32_e32 v3, 60, v10
	v_lshl_or_b32 v148, v2, 6, v3
	v_lshl_or_b32 v149, v2, 2, s7
	v_lshrrev_b32_e32 v3, 1, v12
	v_mul_lo_u32 v2, v15, s22
	s_mov_b32 s23, 0xe000
	s_cmpk_lt_u32 s6, 0x100
	v_mad_u64_u32 v[2:3], s[6:7], v3, s23, v[2:3]
	v_or_b32_e32 v2, v2, v14
	v_add_lshl_u32 v130, v2, v18, 1
	v_lshrrev_b32_e32 v3, 1, v11
	v_mul_lo_u32 v2, v16, s22
	v_mad_u64_u32 v[2:3], s[6:7], v3, s23, v[2:3]
	s_mov_b64 s[24:25], 0xe0080
	s_waitcnt vmcnt(6)
	v_or_b32_e32 v2, v2, v13
	s_cselect_b64 s[20:21], -1, 0
	v_lshl_add_u64 v[136:137], v[130:131], 0, s[24:25]
	v_add_lshl_u32 v130, v2, v17, 1
	s_add_i32 s50, 0, 0x10000
	s_add_i32 s51, 0, 0x14000
	s_mov_b32 s48, 0
	v_bfe_u32 v147, v10, 2, 4
	s_ashr_i32 s49, s97, 31
	v_lshl_add_u64 v[138:139], v[130:131], 0, s[24:25]
	v_mov_b64_e32 v[140:141], s[4:5]
	v_add_u32_e32 v150, s50, v146
	v_add_u32_e32 v151, s51, v146
	v_add_u32_e32 v152, 0, v4
	s_barrier
	s_branch .LBB0_1837

; #define PG8_STAGE_A(b, h, ptr, NX) do { if constexpr (Sched::GATHER) { unsigned gs_[2]; gs_[0] = ((NX) && last_) ? gN[h][0] : gA[h][0]; gs_[1] = ((NX) && last_) ? gN[h][1] : gA[h][1]; PG8_STAGE(PG8_SA(b, h), ptr, gs_); } \
;         else PG8_STAGE(PG8_SA(b, h), (ptr) + ((h) ? hstep : (size_t)0), voffA); } while (0)
; #define PG8_STAGE(bufoff, gbase, voff) do { _Pragma("unroll") for (int _i = 0; _i < 2; ++_i) \
;         __builtin_amdgcn_global_load_lds((const unsigned*)((const char*)(gbase) + (voff)[_i]), (PG8_LAS unsigned*)(lds + (bufoff) + ldsw + _i * 8192), 16, 0, 0); } while (0)
; #define PG8_LDA(dst, b, h) do { _Pragma("unroll") for (int m = 0; m < 4; ++m) _Pragma("unroll") for (int k = 0; k < 2; ++k) dst[m][k] = *(const PG8_LAS bf16x8*)(lds + PG8_SA(b, h) + aoff + m * 2048 + k * 1024); } while (0)
; #define PG8_LDB(dst, b, h) do { _Pragma("unroll") for (int n = 0; n < 2; ++n) _Pragma("unroll") for (int k = 0; k < 2; ++k) dst[n][k] = *(const PG8_LAS bf16x8*)(lds + PG8_SB(b, h) + boff + n * 2048 + k * 1024); } while (0)
; #define PG8_WAIT_V(n) asm volatile("s_waitcnt vmcnt(" #n ")" ::: "memory")
; #define PG8_WAIT_L(n) asm volatile("s_waitcnt lgkmcnt(" #n ")" ::: "memory")
; template <class Epi, class Sched, bool ALIGN_EPI = false, bool SP2 = false>
; __device__ __forceinline__ void gemm_phase(PG8_LAS unsigned char* lds, const Gemm g, const Sched& S, const Epi& E, const bool skip_epi = false) {
;     ...
;         for (int t = 0; t < nt; t += 2) {
;             const bool last = (t == nt - 2); last_ = last && has_next;
;             const char* a1 = cA + (size_t)(t + 1) * kstep;
;             const char* a2 = last ? nA : cA + (size_t)(t + 2) * kstep; const char* b2 = last ? nB : cB + (size_t)(t + 2) * kstep;
;             const char* a3 = a2 + kstep; const char* b3 = b2 + kstep;
;             if (last && has_next) S.a_ready(nxt);
;             if constexpr (SP2) {
;             PG8_LDB(B0, 0, 0); PG8_LDB(B1, 0, 1); PG8_SCHED; PG8_LDA(At, 0, 0); PG8_STAGE_A(1, 1, a1, false);
;             PG8_WAIT_V(8); PG8_WAIT_L(0); PG8_BAR; PG8_MMA(0, 0, At, B0); PG8_MMA(0, 1, At, B1); PG8_BAR; PG8_SCHED;
;             PG8_LDA(At, 0, 1); PG8_STAGE(PG8_SB(0, 0), b2, voffB); PG8_STAGE(PG8_SB(0, 1), b2 + hstep, voffB); PG8_STAGE_A(0, 0, a2, true);
;             PG8_WAIT_V(8); PG8_WAIT_L(0); PG8_BAR; PG8_MMA(1, 0, At, B0); PG8_MMA(1, 1, At, B1); PG8_BAR; PG8_SCHED;
.LBB0_1843:
	s_add_u32 s54, s30, 0x100
	s_addc_u32 s55, s31, 0
	s_mov_b32 s56, -2
	ds_read_b128 v[142:145], v150
	ds_read_b128 v[154:157], v150 offset:1024
	ds_read_b128 v[158:161], v150 offset:2048
	ds_read_b128 v[162:165], v150 offset:3072
	ds_read_b128 v[166:169], v151
	ds_read_b128 v[170:173], v151 offset:1024
	ds_read_b128 v[174:177], v151 offset:2048
	ds_read_b128 v[178:181], v151 offset:3072
	s_add_u32 s30, s28, 0x100
	s_addc_u32 s31, s29, 0
	s_cmp_eq_u32 s56, 10
	s_cselect_b32 s37, s7, s31
	s_cselect_b32 s36, s6, s30
	s_cselect_b32 s35, s25, s55
	s_cselect_b32 s34, s24, s54
	v_lshl_add_u64 v[214:215], s[28:29], 0, v[136:137]
	s_add_i32 m0, s38, 0xc000
	ds_read_b128 v[182:185], v152
	ds_read_b128 v[186:189], v152 offset:1024
	ds_read_b128 v[190:193], v152 offset:2048
	ds_read_b128 v[194:197], v152 offset:3072
	ds_read_b128 v[198:201], v152 offset:4096
	ds_read_b128 v[202:205], v152 offset:5120
	ds_read_b128 v[206:209], v152 offset:6144
	ds_read_b128 v[210:213], v152 offset:7168
	global_load_lds_dwordx4 v[214:215], off
	v_lshl_add_u64 v[214:215], s[28:29], 0, v[138:139]
	s_add_i32 m0, s38, 0xe000
	s_nop 0
	global_load_lds_dwordx4 v[214:215], off
	s_waitcnt vmcnt(8)
	s_waitcnt lgkmcnt(0)
	s_barrier
	s_setprio 3
	s_waitcnt lgkmcnt(0)
	v_mfma_f32_16x16x32_bf16 v[126:129], v[142:145], v[182:185], 0
	v_mfma_f32_16x16x32_bf16 v[122:125], v[158:161], v[182:185], 0
	v_mfma_f32_16x16x32_bf16 v[110:113], v[142:145], v[190:193], 0
	v_mfma_f32_16x16x32_bf16 v[106:109], v[158:161], v[190:193], 0
	v_mfma_f32_16x16x32_bf16 v[94:97], v[142:145], v[198:201], 0
	v_mfma_f32_16x16x32_bf16 v[90:93], v[158:161], v[198:201], 0
	v_mfma_f32_16x16x32_bf16 v[78:81], v[142:145], v[206:209], 0
	v_mfma_f32_16x16x32_bf16 v[74:77], v[158:161], v[206:209], 0
	v_mfma_f32_16x16x32_bf16 v[126:129], v[154:157], v[186:189], v[126:129]
	v_mfma_f32_16x16x32_bf16 v[122:125], v[162:165], v[186:189], v[122:125]
	v_mfma_f32_16x16x32_bf16 v[110:113], v[154:157], v[194:197], v[110:113]
	v_mfma_f32_16x16x32_bf16 v[106:109], v[162:165], v[194:197], v[106:109]
	v_mfma_f32_16x16x32_bf16 v[94:97], v[154:157], v[202:205], v[94:97]
	v_mfma_f32_16x16x32_bf16 v[90:93], v[162:165], v[202:205], v[90:93]
	v_mfma_f32_16x16x32_bf16 v[78:81], v[154:157], v[210:213], v[78:81]
	v_mfma_f32_16x16x32_bf16 v[74:77], v[162:165], v[210:213], v[74:77]
	s_setprio 0
	s_setprio 3
	v_mfma_f32_16x16x32_bf16 v[118:121], v[166:169], v[182:185], 0
	v_mfma_f32_16x16x32_bf16 v[114:117], v[174:177], v[182:185], 0
	v_mfma_f32_16x16x32_bf16 v[102:105], v[166:169], v[190:193], 0
	v_mfma_f32_16x16x32_bf16 v[98:101], v[174:177], v[190:193], 0
	v_mfma_f32_16x16x32_bf16 v[86:89], v[166:169], v[198:201], 0
	v_mfma_f32_16x16x32_bf16 v[82:85], v[174:177], v[198:201], 0
	v_mfma_f32_16x16x32_bf16 v[70:73], v[166:169], v[206:209], 0
	v_mfma_f32_16x16x32_bf16 v[66:69], v[174:177], v[206:209], 0
	v_mfma_f32_16x16x32_bf16 v[118:121], v[170:173], v[186:189], v[118:121]
	v_mfma_f32_16x16x32_bf16 v[114:117], v[178:181], v[186:189], v[114:117]
	v_mfma_f32_16x16x32_bf16 v[102:105], v[170:173], v[194:197], v[102:105]
	v_mfma_f32_16x16x32_bf16 v[98:101], v[178:181], v[194:197], v[98:101]
	v_mfma_f32_16x16x32_bf16 v[86:89], v[170:173], v[202:205], v[86:89]
	v_mfma_f32_16x16x32_bf16 v[82:85], v[178:181], v[202:205], v[82:85]
	v_mfma_f32_16x16x32_bf16 v[70:73], v[170:173], v[210:213], v[70:73]
	v_mfma_f32_16x16x32_bf16 v[66:69], v[178:181], v[210:213], v[66:69]
	s_setprio 0
	s_barrier
	s_add_i32 s28, s50, s3
	v_lshl_add_u64 v[214:215], s[34:35], 0, v[132:133]
	s_mov_b32 m0, s28
	ds_read_b128 v[182:185], v152 offset:16384
	ds_read_b128 v[186:189], v152 offset:17408
	ds_read_b128 v[190:193], v152 offset:18432
	ds_read_b128 v[194:197], v152 offset:19456
	ds_read_b128 v[198:201], v152 offset:20480
	ds_read_b128 v[202:205], v152 offset:21504
	ds_read_b128 v[206:209], v152 offset:22528
	ds_read_b128 v[210:213], v152 offset:23552
	global_load_lds_dwordx4 v[214:215], off
	s_add_i32 m0, s28, 0x2000
	s_add_u32 s28, s34, 0xe0000
	v_lshl_add_u64 v[216:217], s[34:35], 0, v[134:135]
	s_addc_u32 s29, s35, 0
	s_add_i32 s57, s51, s3
	global_load_lds_dwordx4 v[216:217], off
	s_mov_b32 m0, s57
	v_lshl_add_u64 v[220:221], s[36:37], 0, v[134:135]
	global_load_lds_dwordx4 v132, s[28:29]
	s_add_i32 m0, s57, 0x2000
	s_nop 0
	global_load_lds_dwordx4 v134, s[28:29]
	v_lshl_add_u64 v[218:219], s[36:37], 0, v[132:133]
	s_mov_b32 m0, s38
	s_nop 0
	global_load_lds_dwordx4 v[218:219], off
	s_mov_b32 m0, s39
	s_nop 0
	global_load_lds_dwordx4 v[220:221], off
	s_waitcnt vmcnt(8)
	s_waitcnt lgkmcnt(0)
	s_barrier
; #define PG8_STAGE_A(b, h, ptr, NX) do { if constexpr (Sched::GATHER) { unsigned gs_[2]; gs_[0] = ((NX) && last_) ? gN[h][0] : gA[h][0]; gs_[1] = ((NX) && last_) ? gN[h][1] : gA[h][1]; PG8_STAGE(PG8_SA(b, h), ptr, gs_); } \
;         else PG8_STAGE(PG8_SA(b, h), (ptr) + ((h) ? hstep : (size_t)0), voffA); } while (0)
; #define PG8_STAGE(bufoff, gbase, voff) do { _Pragma("unroll") for (int _i = 0; _i < 2; ++_i) \
;         __builtin_amdgcn_global_load_lds((const unsigned*)((const char*)(gbase) + (voff)[_i]), (PG8_LAS unsigned*)(lds + (bufoff) + ldsw + _i * 8192), 16, 0, 0); } while (0)
; #define PG8_LDA(dst, b, h) do { _Pragma("unroll") for (int m = 0; m < 4; ++m) _Pragma("unroll") for (int k = 0; k < 2; ++k) dst[m][k] = *(const PG8_LAS bf16x8*)(lds + PG8_SA(b, h) + aoff + m * 2048 + k * 1024); } while (0)
; #define PG8_LDB(dst, b, h) do { _Pragma("unroll") for (int n = 0; n < 2; ++n) _Pragma("unroll") for (int k = 0; k < 2; ++k) dst[n][k] = *(const PG8_LAS bf16x8*)(lds + PG8_SB(b, h) + boff + n * 2048 + k * 1024); } while (0)
; #define PG8_MMA(ai, bj, At, Bt) do { __builtin_amdgcn_s_setprio(1); _Pragma("unroll") for (int m = 0; m < 4; ++m) _Pragma("unroll") for (int n = 0; n < 2; ++n) _Pragma("unroll") for (int k = 0; k < 2; ++k) \
;         acc[ai][bj][m][n] = __builtin_amdgcn_mfma_f32_16x16x32_bf16(Bt[n][k], At[m][k], acc[ai][bj][m][n], 0, 0, 0); __builtin_amdgcn_s_setprio(0); } while (0)
; #define PG8_WAIT_V(n) asm volatile("s_waitcnt vmcnt(" #n ")" ::: "memory")
; #define PG8_BAR __builtin_amdgcn_s_barrier()
; template <class Epi, class Sched, bool ALIGN_EPI = false, bool SP2 = false>
; __device__ __forceinline__ void gemm_phase(PG8_LAS unsigned char* lds, const Gemm g, const Sched& S, const Epi& E, const bool skip_epi = false) {
;     ...
;             PG8_WAIT_V(8); PG8_WAIT_L(0); PG8_BAR; PG8_MMA(0, 0, At, B0); PG8_MMA(0, 1, At, B1); PG8_BAR; PG8_SCHED;
;             PG8_LDA(At, 0, 1); PG8_STAGE(PG8_SB(0, 0), b2, voffB); PG8_STAGE(PG8_SB(0, 1), b2 + hstep, voffB); PG8_STAGE_A(0, 0, a2, true);
;             PG8_WAIT_V(8); PG8_WAIT_L(0); PG8_BAR; PG8_MMA(1, 0, At, B0); PG8_MMA(1, 1, At, B1); PG8_BAR; PG8_SCHED;
;             PG8_LDB(B0, 1, 0); PG8_LDB(B1, 1, 1); PG8_SCHED; PG8_LDA(At, 1, 0); PG8_STAGE_A(0, 1, a2, true);
;             PG8_WAIT_V(8); PG8_WAIT_L(0); PG8_BAR; PG8_MMA(0, 0, At, B0); PG8_MMA(0, 1, At, B1); PG8_BAR; PG8_SCHED;
	s_setprio 3
	s_waitcnt lgkmcnt(0)
	v_mfma_f32_16x16x32_bf16 v[62:65], v[142:145], v[182:185], 0
	v_mfma_f32_16x16x32_bf16 v[58:61], v[158:161], v[182:185], 0
	v_mfma_f32_16x16x32_bf16 v[46:49], v[142:145], v[190:193], 0
	v_mfma_f32_16x16x32_bf16 v[42:45], v[158:161], v[190:193], 0
	v_mfma_f32_16x16x32_bf16 v[30:33], v[142:145], v[198:201], 0
	v_mfma_f32_16x16x32_bf16 v[26:29], v[158:161], v[198:201], 0
	v_mfma_f32_16x16x32_bf16 v[14:17], v[142:145], v[206:209], 0
	v_mfma_f32_16x16x32_bf16 v[10:13], v[158:161], v[206:209], 0
	v_mfma_f32_16x16x32_bf16 v[62:65], v[154:157], v[186:189], v[62:65]
	v_mfma_f32_16x16x32_bf16 v[58:61], v[162:165], v[186:189], v[58:61]
	v_mfma_f32_16x16x32_bf16 v[46:49], v[154:157], v[194:197], v[46:49]
	v_mfma_f32_16x16x32_bf16 v[42:45], v[162:165], v[194:197], v[42:45]
	v_mfma_f32_16x16x32_bf16 v[30:33], v[154:157], v[202:205], v[30:33]
	v_mfma_f32_16x16x32_bf16 v[26:29], v[162:165], v[202:205], v[26:29]
	v_mfma_f32_16x16x32_bf16 v[14:17], v[154:157], v[210:213], v[14:17]
	v_mfma_f32_16x16x32_bf16 v[10:13], v[162:165], v[210:213], v[10:13]
	s_setprio 0
	s_setprio 3
	v_mfma_f32_16x16x32_bf16 v[54:57], v[166:169], v[182:185], 0
	v_mfma_f32_16x16x32_bf16 v[50:53], v[174:177], v[182:185], 0
	v_mfma_f32_16x16x32_bf16 v[38:41], v[166:169], v[190:193], 0
	v_mfma_f32_16x16x32_bf16 v[34:37], v[174:177], v[190:193], 0
	v_mfma_f32_16x16x32_bf16 v[22:25], v[166:169], v[198:201], 0
	v_mfma_f32_16x16x32_bf16 v[18:21], v[174:177], v[198:201], 0
	v_mfma_f32_16x16x32_bf16 v[6:9], v[166:169], v[206:209], 0
	v_mfma_f32_16x16x32_bf16 v[2:5], v[174:177], v[206:209], 0
	v_mfma_f32_16x16x32_bf16 v[54:57], v[170:173], v[186:189], v[54:57]
	v_mfma_f32_16x16x32_bf16 v[50:53], v[178:181], v[186:189], v[50:53]
	v_mfma_f32_16x16x32_bf16 v[38:41], v[170:173], v[194:197], v[38:41]
	v_mfma_f32_16x16x32_bf16 v[34:37], v[178:181], v[194:197], v[34:37]
	v_mfma_f32_16x16x32_bf16 v[22:25], v[170:173], v[202:205], v[22:25]
	v_mfma_f32_16x16x32_bf16 v[18:21], v[178:181], v[202:205], v[18:21]
	v_mfma_f32_16x16x32_bf16 v[6:9], v[170:173], v[210:213], v[6:9]
	v_mfma_f32_16x16x32_bf16 v[2:5], v[178:181], v[210:213], v[2:5]
	s_setprio 0
	s_barrier
	s_add_i32 s57, 0, 0x18000
	v_add_u32_e32 v130, s57, v146
	s_add_i32 s58, 0, 0x1c000
	ds_read_b128 v[142:145], v130
	ds_read_b128 v[154:157], v130 offset:1024
	ds_read_b128 v[158:161], v130 offset:2048
	ds_read_b128 v[162:165], v130 offset:3072
	v_add_u32_e32 v130, s58, v146
	ds_read_b128 v[166:169], v130
	ds_read_b128 v[170:173], v130 offset:1024
	ds_read_b128 v[174:177], v130 offset:2048
	ds_read_b128 v[178:181], v130 offset:3072
	s_add_u32 s28, s36, 0xe0000
	s_addc_u32 s29, s37, 0
	s_mov_b32 m0, s40
	ds_read_b128 v[182:185], v152 offset:32768
	ds_read_b128 v[186:189], v152 offset:33792
	ds_read_b128 v[190:193], v152 offset:34816
	ds_read_b128 v[194:197], v152 offset:35840
	ds_read_b128 v[198:201], v152 offset:36864
	ds_read_b128 v[202:205], v152 offset:37888
	ds_read_b128 v[206:209], v152 offset:38912
	ds_read_b128 v[210:213], v152 offset:39936
	global_load_lds_dwordx4 v132, s[28:29]
	s_mov_b32 m0, s41
	s_nop 0
	global_load_lds_dwordx4 v134, s[28:29]
	s_waitcnt vmcnt(8)
	s_waitcnt lgkmcnt(0)
	s_barrier
	s_setprio 3
	s_waitcnt lgkmcnt(0)
	v_mfma_f32_16x16x32_bf16 v[126:129], v[142:145], v[182:185], v[126:129]
	v_mfma_f32_16x16x32_bf16 v[122:125], v[158:161], v[182:185], v[122:125]
	v_mfma_f32_16x16x32_bf16 v[110:113], v[142:145], v[190:193], v[110:113]
	v_mfma_f32_16x16x32_bf16 v[106:109], v[158:161], v[190:193], v[106:109]
	v_mfma_f32_16x16x32_bf16 v[94:97], v[142:145], v[198:201], v[94:97]
	v_mfma_f32_16x16x32_bf16 v[90:93], v[158:161], v[198:201], v[90:93]
	v_mfma_f32_16x16x32_bf16 v[78:81], v[142:145], v[206:209], v[78:81]
	v_mfma_f32_16x16x32_bf16 v[74:77], v[158:161], v[206:209], v[74:77]
	v_mfma_f32_16x16x32_bf16 v[126:129], v[154:157], v[186:189], v[126:129]
	v_mfma_f32_16x16x32_bf16 v[122:125], v[162:165], v[186:189], v[122:125]
	v_mfma_f32_16x16x32_bf16 v[110:113], v[154:157], v[194:197], v[110:113]
	v_mfma_f32_16x16x32_bf16 v[106:109], v[162:165], v[194:197], v[106:109]
	v_mfma_f32_16x16x32_bf16 v[94:97], v[154:157], v[202:205], v[94:97]
	v_mfma_f32_16x16x32_bf16 v[90:93], v[162:165], v[202:205], v[90:93]
	v_mfma_f32_16x16x32_bf16 v[78:81], v[154:157], v[210:213], v[78:81]
	v_mfma_f32_16x16x32_bf16 v[74:77], v[162:165], v[210:213], v[74:77]
	s_setprio 0
	s_setprio 3
	v_mfma_f32_16x16x32_bf16 v[118:121], v[166:169], v[182:185], v[118:121]
	v_mfma_f32_16x16x32_bf16 v[114:117], v[174:177], v[182:185], v[114:117]
	v_mfma_f32_16x16x32_bf16 v[102:105], v[166:169], v[190:193], v[102:105]
	v_mfma_f32_16x16x32_bf16 v[98:101], v[174:177], v[190:193], v[98:101]
	v_mfma_f32_16x16x32_bf16 v[86:89], v[166:169], v[198:201], v[86:89]
	v_mfma_f32_16x16x32_bf16 v[82:85], v[174:177], v[198:201], v[82:85]
	v_mfma_f32_16x16x32_bf16 v[70:73], v[166:169], v[206:209], v[70:73]
	v_mfma_f32_16x16x32_bf16 v[66:69], v[174:177], v[206:209], v[66:69]
	v_mfma_f32_16x16x32_bf16 v[118:121], v[170:173], v[186:189], v[118:121]
	v_mfma_f32_16x16x32_bf16 v[114:117], v[178:181], v[186:189], v[114:117]
	v_mfma_f32_16x16x32_bf16 v[102:105], v[170:173], v[194:197], v[102:105]
	v_mfma_f32_16x16x32_bf16 v[98:101], v[178:181], v[194:197], v[98:101]
	v_mfma_f32_16x16x32_bf16 v[86:89], v[170:173], v[202:205], v[86:89]
	v_mfma_f32_16x16x32_bf16 v[82:85], v[178:181], v[202:205], v[82:85]
	v_mfma_f32_16x16x32_bf16 v[70:73], v[170:173], v[210:213], v[70:73]
	v_mfma_f32_16x16x32_bf16 v[66:69], v[178:181], v[210:213], v[66:69]
	s_setprio 0
	s_barrier
; #define PG8_STAGE_A(b, h, ptr, NX) do { if constexpr (Sched::GATHER) { unsigned gs_[2]; gs_[0] = ((NX) && last_) ? gN[h][0] : gA[h][0]; gs_[1] = ((NX) && last_) ? gN[h][1] : gA[h][1]; PG8_STAGE(PG8_SA(b, h), ptr, gs_); } \
;         else PG8_STAGE(PG8_SA(b, h), (ptr) + ((h) ? hstep : (size_t)0), voffA); } while (0)
; #define PG8_STAGE(bufoff, gbase, voff) do { _Pragma("unroll") for (int _i = 0; _i < 2; ++_i) \
;         __builtin_amdgcn_global_load_lds((const unsigned*)((const char*)(gbase) + (voff)[_i]), (PG8_LAS unsigned*)(lds + (bufoff) + ldsw + _i * 8192), 16, 0, 0); } while (0)
; #define PG8_WAIT_V(n) asm volatile("s_waitcnt vmcnt(" #n ")" ::: "memory")
; #define PG8_BAR __builtin_amdgcn_s_barrier()
; template <class Epi, class Sched, bool ALIGN_EPI = false, bool SP2 = false>
; __device__ __forceinline__ void gemm_phase(PG8_LAS unsigned char* lds, const Gemm g, const Sched& S, const Epi& E, const bool skip_epi = false) {
;     ...
;         for (int t = 0; t < nt; t += 2) {
;             const bool last = (t == nt - 2); last_ = last && has_next;
;             const char* a1 = cA + (size_t)(t + 1) * kstep;
;             const char* a2 = last ? nA : cA + (size_t)(t + 2) * kstep; const char* b2 = last ? nB : cB + (size_t)(t + 2) * kstep;
;             const char* a3 = a2 + kstep; const char* b3 = b2 + kstep;
;             if (last && has_next) S.a_ready(nxt);
;             if constexpr (SP2) {
;             PG8_LDB(B0, 0, 0); PG8_LDB(B1, 0, 1); PG8_SCHED; PG8_LDA(At, 0, 0); PG8_STAGE_A(1, 1, a1, false);
;             PG8_WAIT_V(8); PG8_WAIT_L(0); PG8_BAR; PG8_MMA(0, 0, At, B0); PG8_MMA(0, 1, At, B1); PG8_BAR; PG8_SCHED;
;             PG8_LDA(At, 0, 1); PG8_STAGE(PG8_SB(0, 0), b2, voffB); PG8_STAGE(PG8_SB(0, 1), b2 + hstep, voffB); PG8_STAGE_A(0, 0, a2, true);
;             PG8_WAIT_V(8); PG8_WAIT_L(0); PG8_BAR; PG8_MMA(1, 0, At, B0); PG8_MMA(1, 1, At, B1); PG8_BAR; PG8_SCHED;
;             PG8_LDB(B0, 1, 0); PG8_LDB(B1, 1, 1); PG8_SCHED; PG8_LDA(At, 1, 0); PG8_STAGE_A(0, 1, a2, true);
;             PG8_WAIT_V(8); PG8_WAIT_L(0); PG8_BAR; PG8_MMA(0, 0, At, B0); PG8_MMA(0, 1, At, B1); PG8_BAR; PG8_SCHED;
;             PG8_LDA(At, 1, 1); PG8_STAGE(PG8_SB(1, 0), b3, voffB); PG8_STAGE(PG8_SB(1, 1), b3 + hstep, voffB); PG8_STAGE_A(1, 0, a3, true);
;             PG8_WAIT_V(8); PG8_WAIT_L(0); PG8_BAR; PG8_MMA(1, 0, At, B0); PG8_MMA(1, 1, At, B1); PG8_BAR; PG8_SCHED;
	s_add_i32 s28, s57, s3
	s_add_i32 m0, s28, 0xffffff80
	ds_read_b128 v[182:185], v152 offset:49152
	ds_read_b128 v[186:189], v152 offset:50176
	ds_read_b128 v[190:193], v152 offset:51200
	ds_read_b128 v[194:197], v152 offset:52224
	ds_read_b128 v[198:201], v152 offset:53248
	ds_read_b128 v[202:205], v152 offset:54272
	ds_read_b128 v[206:209], v152 offset:55296
	ds_read_b128 v[210:213], v152 offset:56320
	global_load_lds_dwordx4 v[214:215], off offset:128
	s_add_i32 m0, s28, 0x1f80
	s_add_u32 s28, s34, 0xe0080
	s_addc_u32 s29, s35, 0
	s_add_i32 s34, s58, s3
	global_load_lds_dwordx4 v[216:217], off offset:128
	s_mov_b32 m0, s34
	s_nop 0
	global_load_lds_dwordx4 v132, s[28:29]
	s_add_i32 m0, s34, 0x2000
	s_nop 0
	global_load_lds_dwordx4 v134, s[28:29]
	s_add_i32 m0, s46, 0xffffff80
	s_nop 0
	global_load_lds_dwordx4 v[218:219], off offset:128
	s_add_i32 m0, s47, 0xffffff80
	s_nop 0
	global_load_lds_dwordx4 v[220:221], off offset:128
	s_waitcnt vmcnt(8)
	s_waitcnt lgkmcnt(0)
	s_barrier
	s_setprio 3
	s_waitcnt lgkmcnt(0)
	v_mfma_f32_16x16x32_bf16 v[62:65], v[142:145], v[182:185], v[62:65]
	v_mfma_f32_16x16x32_bf16 v[58:61], v[158:161], v[182:185], v[58:61]
	v_mfma_f32_16x16x32_bf16 v[46:49], v[142:145], v[190:193], v[46:49]
	v_mfma_f32_16x16x32_bf16 v[42:45], v[158:161], v[190:193], v[42:45]
	v_mfma_f32_16x16x32_bf16 v[30:33], v[142:145], v[198:201], v[30:33]
	v_mfma_f32_16x16x32_bf16 v[26:29], v[158:161], v[198:201], v[26:29]
	v_mfma_f32_16x16x32_bf16 v[14:17], v[142:145], v[206:209], v[14:17]
	v_mfma_f32_16x16x32_bf16 v[10:13], v[158:161], v[206:209], v[10:13]
	v_mfma_f32_16x16x32_bf16 v[62:65], v[154:157], v[186:189], v[62:65]
	v_mfma_f32_16x16x32_bf16 v[58:61], v[162:165], v[186:189], v[58:61]
	v_mfma_f32_16x16x32_bf16 v[46:49], v[154:157], v[194:197], v[46:49]
	v_mfma_f32_16x16x32_bf16 v[42:45], v[162:165], v[194:197], v[42:45]
	v_mfma_f32_16x16x32_bf16 v[30:33], v[154:157], v[202:205], v[30:33]
	v_mfma_f32_16x16x32_bf16 v[26:29], v[162:165], v[202:205], v[26:29]
	v_mfma_f32_16x16x32_bf16 v[14:17], v[154:157], v[210:213], v[14:17]
	v_mfma_f32_16x16x32_bf16 v[10:13], v[162:165], v[210:213], v[10:13]
	s_setprio 0
	s_setprio 3
	v_mfma_f32_16x16x32_bf16 v[54:57], v[166:169], v[182:185], v[54:57]
	v_mfma_f32_16x16x32_bf16 v[50:53], v[174:177], v[182:185], v[50:53]
	v_mfma_f32_16x16x32_bf16 v[38:41], v[166:169], v[190:193], v[38:41]
	v_mfma_f32_16x16x32_bf16 v[34:37], v[174:177], v[190:193], v[34:37]
	v_mfma_f32_16x16x32_bf16 v[22:25], v[166:169], v[198:201], v[22:25]
	v_mfma_f32_16x16x32_bf16 v[18:21], v[174:177], v[198:201], v[18:21]
	v_mfma_f32_16x16x32_bf16 v[6:9], v[166:169], v[206:209], v[6:9]
	v_mfma_f32_16x16x32_bf16 v[2:5], v[174:177], v[206:209], v[2:5]
	v_mfma_f32_16x16x32_bf16 v[54:57], v[170:173], v[186:189], v[54:57]
	v_mfma_f32_16x16x32_bf16 v[50:53], v[178:181], v[186:189], v[50:53]
	v_mfma_f32_16x16x32_bf16 v[38:41], v[170:173], v[194:197], v[38:41]
	v_mfma_f32_16x16x32_bf16 v[34:37], v[178:181], v[194:197], v[34:37]
	v_mfma_f32_16x16x32_bf16 v[22:25], v[170:173], v[202:205], v[22:25]
	v_mfma_f32_16x16x32_bf16 v[18:21], v[178:181], v[202:205], v[18:21]
	v_mfma_f32_16x16x32_bf16 v[6:9], v[170:173], v[210:213], v[6:9]
	v_mfma_f32_16x16x32_bf16 v[2:5], v[178:181], v[210:213], v[2:5]
	s_setprio 0
	s_barrier
	s_add_i32 s56, s56, 2
	s_add_u32 s54, s54, 0x100
	s_addc_u32 s55, s55, 0
	s_cmp_gt_u32 s56, 11
	s_mov_b64 s[28:29], s[30:31]
.LBB0_1844:
	ds_read_b128 v[142:145], v150
	ds_read_b128 v[154:157], v150 offset:1024
	ds_read_b128 v[158:161], v150 offset:2048
	ds_read_b128 v[162:165], v150 offset:3072
	ds_read_b128 v[166:169], v151
	ds_read_b128 v[170:173], v151 offset:1024
	ds_read_b128 v[174:177], v151 offset:2048
	ds_read_b128 v[178:181], v151 offset:3072
	s_add_u32 s30, s28, 0x100
	s_addc_u32 s31, s29, 0
	s_cmp_eq_u32 s56, 10
	s_cselect_b32 s37, s7, s31
	s_cselect_b32 s36, s6, s30
	s_cselect_b32 s35, s25, s55
	s_cselect_b32 s34, s24, s54
	v_lshl_add_u64 v[214:215], s[28:29], 0, v[136:137]
	s_add_i32 m0, s38, 0xc000
	ds_read_b128 v[182:185], v152
	ds_read_b128 v[186:189], v152 offset:1024
	ds_read_b128 v[190:193], v152 offset:2048
	ds_read_b128 v[194:197], v152 offset:3072
	ds_read_b128 v[198:201], v152 offset:4096
	ds_read_b128 v[202:205], v152 offset:5120
	ds_read_b128 v[206:209], v152 offset:6144
	ds_read_b128 v[210:213], v152 offset:7168
	global_load_lds_dwordx4 v[214:215], off
	v_lshl_add_u64 v[214:215], s[28:29], 0, v[138:139]
	s_add_i32 m0, s38, 0xe000
	s_nop 0
	global_load_lds_dwordx4 v[214:215], off
	s_waitcnt vmcnt(8)
	s_waitcnt lgkmcnt(0)
	s_barrier
; #define PG8_STAGE_A(b, h, ptr, NX) do { if constexpr (Sched::GATHER) { unsigned gs_[2]; gs_[0] = ((NX) && last_) ? gN[h][0] : gA[h][0]; gs_[1] = ((NX) && last_) ? gN[h][1] : gA[h][1]; PG8_STAGE(PG8_SA(b, h), ptr, gs_); } \
;         else PG8_STAGE(PG8_SA(b, h), (ptr) + ((h) ? hstep : (size_t)0), voffA); } while (0)
; #define PG8_STAGE(bufoff, gbase, voff) do { _Pragma("unroll") for (int _i = 0; _i < 2; ++_i) \
;         __builtin_amdgcn_global_load_lds((const unsigned*)((const char*)(gbase) + (voff)[_i]), (PG8_LAS unsigned*)(lds + (bufoff) + ldsw + _i * 8192), 16, 0, 0); } while (0)
; #define PG8_LDA(dst, b, h) do { _Pragma("unroll") for (int m = 0; m < 4; ++m) _Pragma("unroll") for (int k = 0; k < 2; ++k) dst[m][k] = *(const PG8_LAS bf16x8*)(lds + PG8_SA(b, h) + aoff + m * 2048 + k * 1024); } while (0)
; #define PG8_LDB(dst, b, h) do { _Pragma("unroll") for (int n = 0; n < 2; ++n) _Pragma("unroll") for (int k = 0; k < 2; ++k) dst[n][k] = *(const PG8_LAS bf16x8*)(lds + PG8_SB(b, h) + boff + n * 2048 + k * 1024); } while (0)
; #define PG8_MMA(ai, bj, At, Bt) do { __builtin_amdgcn_s_setprio(1); _Pragma("unroll") for (int m = 0; m < 4; ++m) _Pragma("unroll") for (int n = 0; n < 2; ++n) _Pragma("unroll") for (int k = 0; k < 2; ++k) \
;         acc[ai][bj][m][n] = __builtin_amdgcn_mfma_f32_16x16x32_bf16(Bt[n][k], At[m][k], acc[ai][bj][m][n], 0, 0, 0); __builtin_amdgcn_s_setprio(0); } while (0)
; #define PG8_WAIT_V(n) asm volatile("s_waitcnt vmcnt(" #n ")" ::: "memory")
; #define PG8_WAIT_L(n) asm volatile("s_waitcnt lgkmcnt(" #n ")" ::: "memory")
; #define PG8_BAR __builtin_amdgcn_s_barrier()
; #define PG8_SCHED __builtin_amdgcn_sched_barrier(0)
; template <class Epi, class Sched, bool ALIGN_EPI = false, bool SP2 = false>
; __device__ __forceinline__ void gemm_phase(PG8_LAS unsigned char* lds, const Gemm g, const Sched& S, const Epi& E, const bool skip_epi = false) {
;     ...
;             PG8_LDB(B0, 0, 0); PG8_LDB(B1, 0, 1); PG8_SCHED; PG8_LDA(At, 0, 0); PG8_STAGE_A(1, 1, a1, false);
;             PG8_WAIT_V(8); PG8_WAIT_L(0); PG8_BAR; PG8_MMA(0, 0, At, B0); PG8_MMA(0, 1, At, B1); PG8_BAR; PG8_SCHED;
;             PG8_LDA(At, 0, 1); PG8_STAGE(PG8_SB(0, 0), b2, voffB); PG8_STAGE(PG8_SB(0, 1), b2 + hstep, voffB); PG8_STAGE_A(0, 0, a2, true);
;             PG8_WAIT_V(8); PG8_WAIT_L(0); PG8_BAR; PG8_MMA(1, 0, At, B0); PG8_MMA(1, 1, At, B1); PG8_BAR; PG8_SCHED;
	s_setprio 3
	s_waitcnt lgkmcnt(0)
	v_mfma_f32_16x16x32_bf16 v[126:129], v[142:145], v[182:185], v[126:129]
	v_mfma_f32_16x16x32_bf16 v[122:125], v[158:161], v[182:185], v[122:125]
	v_mfma_f32_16x16x32_bf16 v[110:113], v[142:145], v[190:193], v[110:113]
	v_mfma_f32_16x16x32_bf16 v[106:109], v[158:161], v[190:193], v[106:109]
	v_mfma_f32_16x16x32_bf16 v[94:97], v[142:145], v[198:201], v[94:97]
	v_mfma_f32_16x16x32_bf16 v[90:93], v[158:161], v[198:201], v[90:93]
	v_mfma_f32_16x16x32_bf16 v[78:81], v[142:145], v[206:209], v[78:81]
	v_mfma_f32_16x16x32_bf16 v[74:77], v[158:161], v[206:209], v[74:77]
	v_mfma_f32_16x16x32_bf16 v[126:129], v[154:157], v[186:189], v[126:129]
	v_mfma_f32_16x16x32_bf16 v[122:125], v[162:165], v[186:189], v[122:125]
	v_mfma_f32_16x16x32_bf16 v[110:113], v[154:157], v[194:197], v[110:113]
	v_mfma_f32_16x16x32_bf16 v[106:109], v[162:165], v[194:197], v[106:109]
	v_mfma_f32_16x16x32_bf16 v[94:97], v[154:157], v[202:205], v[94:97]
	v_mfma_f32_16x16x32_bf16 v[90:93], v[162:165], v[202:205], v[90:93]
	v_mfma_f32_16x16x32_bf16 v[78:81], v[154:157], v[210:213], v[78:81]
	v_mfma_f32_16x16x32_bf16 v[74:77], v[162:165], v[210:213], v[74:77]
	s_setprio 0
	s_setprio 3
	v_mfma_f32_16x16x32_bf16 v[118:121], v[166:169], v[182:185], v[118:121]
	v_mfma_f32_16x16x32_bf16 v[114:117], v[174:177], v[182:185], v[114:117]
	v_mfma_f32_16x16x32_bf16 v[102:105], v[166:169], v[190:193], v[102:105]
	v_mfma_f32_16x16x32_bf16 v[98:101], v[174:177], v[190:193], v[98:101]
	v_mfma_f32_16x16x32_bf16 v[86:89], v[166:169], v[198:201], v[86:89]
	v_mfma_f32_16x16x32_bf16 v[82:85], v[174:177], v[198:201], v[82:85]
	v_mfma_f32_16x16x32_bf16 v[70:73], v[166:169], v[206:209], v[70:73]
	v_mfma_f32_16x16x32_bf16 v[66:69], v[174:177], v[206:209], v[66:69]
	v_mfma_f32_16x16x32_bf16 v[118:121], v[170:173], v[186:189], v[118:121]
	v_mfma_f32_16x16x32_bf16 v[114:117], v[178:181], v[186:189], v[114:117]
	v_mfma_f32_16x16x32_bf16 v[102:105], v[170:173], v[194:197], v[102:105]
	v_mfma_f32_16x16x32_bf16 v[98:101], v[178:181], v[194:197], v[98:101]
	v_mfma_f32_16x16x32_bf16 v[86:89], v[170:173], v[202:205], v[86:89]
	v_mfma_f32_16x16x32_bf16 v[82:85], v[178:181], v[202:205], v[82:85]
	v_mfma_f32_16x16x32_bf16 v[70:73], v[170:173], v[210:213], v[70:73]
	v_mfma_f32_16x16x32_bf16 v[66:69], v[178:181], v[210:213], v[66:69]
	s_setprio 0
	s_barrier
	s_add_i32 s28, s50, s3
	v_lshl_add_u64 v[214:215], s[34:35], 0, v[132:133]
	s_mov_b32 m0, s28
	ds_read_b128 v[182:185], v152 offset:16384
	ds_read_b128 v[186:189], v152 offset:17408
	ds_read_b128 v[190:193], v152 offset:18432
	ds_read_b128 v[194:197], v152 offset:19456
	ds_read_b128 v[198:201], v152 offset:20480
	ds_read_b128 v[202:205], v152 offset:21504
	ds_read_b128 v[206:209], v152 offset:22528
	ds_read_b128 v[210:213], v152 offset:23552
	global_load_lds_dwordx4 v[214:215], off
	s_add_i32 m0, s28, 0x2000
	s_add_u32 s28, s34, 0xe0000
	v_lshl_add_u64 v[216:217], s[34:35], 0, v[134:135]
	s_addc_u32 s29, s35, 0
	s_add_i32 s57, s51, s3
	global_load_lds_dwordx4 v[216:217], off
	s_mov_b32 m0, s57
	v_lshl_add_u64 v[220:221], s[36:37], 0, v[134:135]
	global_load_lds_dwordx4 v132, s[28:29]
	s_add_i32 m0, s57, 0x2000
	s_nop 0
	global_load_lds_dwordx4 v134, s[28:29]
	v_lshl_add_u64 v[218:219], s[36:37], 0, v[132:133]
	s_mov_b32 m0, s38
	s_nop 0
	global_load_lds_dwordx4 v[218:219], off
	s_mov_b32 m0, s39
	s_nop 0
	global_load_lds_dwordx4 v[220:221], off
	s_waitcnt vmcnt(8)
	s_waitcnt lgkmcnt(0)
	s_barrier
	s_setprio 3
	s_waitcnt lgkmcnt(0)
	v_mfma_f32_16x16x32_bf16 v[62:65], v[142:145], v[182:185], v[62:65]
	v_mfma_f32_16x16x32_bf16 v[58:61], v[158:161], v[182:185], v[58:61]
	v_mfma_f32_16x16x32_bf16 v[46:49], v[142:145], v[190:193], v[46:49]
	v_mfma_f32_16x16x32_bf16 v[42:45], v[158:161], v[190:193], v[42:45]
	v_mfma_f32_16x16x32_bf16 v[30:33], v[142:145], v[198:201], v[30:33]
	v_mfma_f32_16x16x32_bf16 v[26:29], v[158:161], v[198:201], v[26:29]
	v_mfma_f32_16x16x32_bf16 v[14:17], v[142:145], v[206:209], v[14:17]
	v_mfma_f32_16x16x32_bf16 v[10:13], v[158:161], v[206:209], v[10:13]
	v_mfma_f32_16x16x32_bf16 v[62:65], v[154:157], v[186:189], v[62:65]
	v_mfma_f32_16x16x32_bf16 v[58:61], v[162:165], v[186:189], v[58:61]
	v_mfma_f32_16x16x32_bf16 v[46:49], v[154:157], v[194:197], v[46:49]
	v_mfma_f32_16x16x32_bf16 v[42:45], v[162:165], v[194:197], v[42:45]
	v_mfma_f32_16x16x32_bf16 v[30:33], v[154:157], v[202:205], v[30:33]
	v_mfma_f32_16x16x32_bf16 v[26:29], v[162:165], v[202:205], v[26:29]
	v_mfma_f32_16x16x32_bf16 v[14:17], v[154:157], v[210:213], v[14:17]
	v_mfma_f32_16x16x32_bf16 v[10:13], v[162:165], v[210:213], v[10:13]
	s_setprio 0
	s_setprio 3
	v_mfma_f32_16x16x32_bf16 v[54:57], v[166:169], v[182:185], v[54:57]
	v_mfma_f32_16x16x32_bf16 v[50:53], v[174:177], v[182:185], v[50:53]
	v_mfma_f32_16x16x32_bf16 v[38:41], v[166:169], v[190:193], v[38:41]
	v_mfma_f32_16x16x32_bf16 v[34:37], v[174:177], v[190:193], v[34:37]
	v_mfma_f32_16x16x32_bf16 v[22:25], v[166:169], v[198:201], v[22:25]
	v_mfma_f32_16x16x32_bf16 v[18:21], v[174:177], v[198:201], v[18:21]
	v_mfma_f32_16x16x32_bf16 v[6:9], v[166:169], v[206:209], v[6:9]
	v_mfma_f32_16x16x32_bf16 v[2:5], v[174:177], v[206:209], v[2:5]
	v_mfma_f32_16x16x32_bf16 v[54:57], v[170:173], v[186:189], v[54:57]
	v_mfma_f32_16x16x32_bf16 v[50:53], v[178:181], v[186:189], v[50:53]
	v_mfma_f32_16x16x32_bf16 v[38:41], v[170:173], v[194:197], v[38:41]
	v_mfma_f32_16x16x32_bf16 v[34:37], v[178:181], v[194:197], v[34:37]
	v_mfma_f32_16x16x32_bf16 v[22:25], v[170:173], v[202:205], v[22:25]
	v_mfma_f32_16x16x32_bf16 v[18:21], v[178:181], v[202:205], v[18:21]
	v_mfma_f32_16x16x32_bf16 v[6:9], v[170:173], v[210:213], v[6:9]
	v_mfma_f32_16x16x32_bf16 v[2:5], v[178:181], v[210:213], v[2:5]
	s_setprio 0
	s_barrier
; #define PG8_STAGE_A(b, h, ptr, NX) do { if constexpr (Sched::GATHER) { unsigned gs_[2]; gs_[0] = ((NX) && last_) ? gN[h][0] : gA[h][0]; gs_[1] = ((NX) && last_) ? gN[h][1] : gA[h][1]; PG8_STAGE(PG8_SA(b, h), ptr, gs_); } \
;         else PG8_STAGE(PG8_SA(b, h), (ptr) + ((h) ? hstep : (size_t)0), voffA); } while (0)
; #define PG8_STAGE(bufoff, gbase, voff) do { _Pragma("unroll") for (int _i = 0; _i < 2; ++_i) \
;         __builtin_amdgcn_global_load_lds((const unsigned*)((const char*)(gbase) + (voff)[_i]), (PG8_LAS unsigned*)(lds + (bufoff) + ldsw + _i * 8192), 16, 0, 0); } while (0)
; #define PG8_LDA(dst, b, h) do { _Pragma("unroll") for (int m = 0; m < 4; ++m) _Pragma("unroll") for (int k = 0; k < 2; ++k) dst[m][k] = *(const PG8_LAS bf16x8*)(lds + PG8_SA(b, h) + aoff + m * 2048 + k * 1024); } while (0)
; #define PG8_LDB(dst, b, h) do { _Pragma("unroll") for (int n = 0; n < 2; ++n) _Pragma("unroll") for (int k = 0; k < 2; ++k) dst[n][k] = *(const PG8_LAS bf16x8*)(lds + PG8_SB(b, h) + boff + n * 2048 + k * 1024); } while (0)
; #define PG8_MMA(ai, bj, At, Bt) do { __builtin_amdgcn_s_setprio(1); _Pragma("unroll") for (int m = 0; m < 4; ++m) _Pragma("unroll") for (int n = 0; n < 2; ++n) _Pragma("unroll") for (int k = 0; k < 2; ++k) \
;         acc[ai][bj][m][n] = __builtin_amdgcn_mfma_f32_16x16x32_bf16(Bt[n][k], At[m][k], acc[ai][bj][m][n], 0, 0, 0); __builtin_amdgcn_s_setprio(0); } while (0)
; #define PG8_WAIT_V(n) asm volatile("s_waitcnt vmcnt(" #n ")" ::: "memory")
; #define PG8_WAIT_L(n) asm volatile("s_waitcnt lgkmcnt(" #n ")" ::: "memory")
; #define PG8_BAR __builtin_amdgcn_s_barrier()
; #define PG8_SCHED __builtin_amdgcn_sched_barrier(0)
; template <class Epi, class Sched, bool ALIGN_EPI = false, bool SP2 = false>
; __device__ __forceinline__ void gemm_phase(PG8_LAS unsigned char* lds, const Gemm g, const Sched& S, const Epi& E, const bool skip_epi = false) {
;     ...
;             PG8_LDB(B0, 1, 0); PG8_LDB(B1, 1, 1); PG8_SCHED; PG8_LDA(At, 1, 0); PG8_STAGE_A(0, 1, a2, true);
;             PG8_WAIT_V(8); PG8_WAIT_L(0); PG8_BAR; PG8_MMA(0, 0, At, B0); PG8_MMA(0, 1, At, B1); PG8_BAR; PG8_SCHED;
;             PG8_LDA(At, 1, 1); PG8_STAGE(PG8_SB(1, 0), b3, voffB); PG8_STAGE(PG8_SB(1, 1), b3 + hstep, voffB); PG8_STAGE_A(1, 0, a3, true);
;             PG8_WAIT_V(8); PG8_WAIT_L(0); PG8_BAR; PG8_MMA(1, 0, At, B0); PG8_MMA(1, 1, At, B1); PG8_BAR; PG8_SCHED;
	s_add_i32 s57, 0, 0x18000
	v_add_u32_e32 v130, s57, v146
	s_add_i32 s58, 0, 0x1c000
	ds_read_b128 v[142:145], v130
	ds_read_b128 v[154:157], v130 offset:1024
	ds_read_b128 v[158:161], v130 offset:2048
	ds_read_b128 v[162:165], v130 offset:3072
	v_add_u32_e32 v130, s58, v146
	ds_read_b128 v[166:169], v130
	ds_read_b128 v[170:173], v130 offset:1024
	ds_read_b128 v[174:177], v130 offset:2048
	ds_read_b128 v[178:181], v130 offset:3072
	s_add_u32 s28, s36, 0xe0000
	s_addc_u32 s29, s37, 0
	s_mov_b32 m0, s40
	ds_read_b128 v[182:185], v152 offset:32768
	ds_read_b128 v[186:189], v152 offset:33792
	ds_read_b128 v[190:193], v152 offset:34816
	ds_read_b128 v[194:197], v152 offset:35840
	ds_read_b128 v[198:201], v152 offset:36864
	ds_read_b128 v[202:205], v152 offset:37888
	ds_read_b128 v[206:209], v152 offset:38912
	ds_read_b128 v[210:213], v152 offset:39936
	global_load_lds_dwordx4 v132, s[28:29]
	s_mov_b32 m0, s41
	s_nop 0
	global_load_lds_dwordx4 v134, s[28:29]
	s_waitcnt vmcnt(8)
	s_waitcnt lgkmcnt(0)
	s_barrier
	s_setprio 3
	s_waitcnt lgkmcnt(0)
	v_mfma_f32_16x16x32_bf16 v[126:129], v[142:145], v[182:185], v[126:129]
	v_mfma_f32_16x16x32_bf16 v[122:125], v[158:161], v[182:185], v[122:125]
	v_mfma_f32_16x16x32_bf16 v[110:113], v[142:145], v[190:193], v[110:113]
	v_mfma_f32_16x16x32_bf16 v[106:109], v[158:161], v[190:193], v[106:109]
	v_mfma_f32_16x16x32_bf16 v[94:97], v[142:145], v[198:201], v[94:97]
	v_mfma_f32_16x16x32_bf16 v[90:93], v[158:161], v[198:201], v[90:93]
	v_mfma_f32_16x16x32_bf16 v[78:81], v[142:145], v[206:209], v[78:81]
	v_mfma_f32_16x16x32_bf16 v[74:77], v[158:161], v[206:209], v[74:77]
	v_mfma_f32_16x16x32_bf16 v[126:129], v[154:157], v[186:189], v[126:129]
	v_mfma_f32_16x16x32_bf16 v[122:125], v[162:165], v[186:189], v[122:125]
	v_mfma_f32_16x16x32_bf16 v[110:113], v[154:157], v[194:197], v[110:113]
	v_mfma_f32_16x16x32_bf16 v[106:109], v[162:165], v[194:197], v[106:109]
	v_mfma_f32_16x16x32_bf16 v[94:97], v[154:157], v[202:205], v[94:97]
	v_mfma_f32_16x16x32_bf16 v[90:93], v[162:165], v[202:205], v[90:93]
	v_mfma_f32_16x16x32_bf16 v[78:81], v[154:157], v[210:213], v[78:81]
	v_mfma_f32_16x16x32_bf16 v[74:77], v[162:165], v[210:213], v[74:77]
	s_setprio 0
	s_setprio 3
	v_mfma_f32_16x16x32_bf16 v[118:121], v[166:169], v[182:185], v[118:121]
	v_mfma_f32_16x16x32_bf16 v[114:117], v[174:177], v[182:185], v[114:117]
	v_mfma_f32_16x16x32_bf16 v[102:105], v[166:169], v[190:193], v[102:105]
	v_mfma_f32_16x16x32_bf16 v[98:101], v[174:177], v[190:193], v[98:101]
	v_mfma_f32_16x16x32_bf16 v[86:89], v[166:169], v[198:201], v[86:89]
	v_mfma_f32_16x16x32_bf16 v[82:85], v[174:177], v[198:201], v[82:85]
	v_mfma_f32_16x16x32_bf16 v[70:73], v[166:169], v[206:209], v[70:73]
	v_mfma_f32_16x16x32_bf16 v[66:69], v[174:177], v[206:209], v[66:69]
	v_mfma_f32_16x16x32_bf16 v[118:121], v[170:173], v[186:189], v[118:121]
	v_mfma_f32_16x16x32_bf16 v[114:117], v[178:181], v[186:189], v[114:117]
	v_mfma_f32_16x16x32_bf16 v[102:105], v[170:173], v[194:197], v[102:105]
	v_mfma_f32_16x16x32_bf16 v[98:101], v[178:181], v[194:197], v[98:101]
	v_mfma_f32_16x16x32_bf16 v[86:89], v[170:173], v[202:205], v[86:89]
	v_mfma_f32_16x16x32_bf16 v[82:85], v[178:181], v[202:205], v[82:85]
	v_mfma_f32_16x16x32_bf16 v[70:73], v[170:173], v[210:213], v[70:73]
	v_mfma_f32_16x16x32_bf16 v[66:69], v[178:181], v[210:213], v[66:69]
	s_setprio 0
	s_barrier
	s_add_i32 s28, s57, s3
	s_add_i32 m0, s28, 0xffffff80
	ds_read_b128 v[182:185], v152 offset:49152
	ds_read_b128 v[186:189], v152 offset:50176
	ds_read_b128 v[190:193], v152 offset:51200
	ds_read_b128 v[194:197], v152 offset:52224
	ds_read_b128 v[198:201], v152 offset:53248
	ds_read_b128 v[202:205], v152 offset:54272
	ds_read_b128 v[206:209], v152 offset:55296
	ds_read_b128 v[210:213], v152 offset:56320
	global_load_lds_dwordx4 v[214:215], off offset:128
	s_add_i32 m0, s28, 0x1f80
	s_add_u32 s28, s34, 0xe0080
	s_addc_u32 s29, s35, 0
	s_add_i32 s34, s58, s3
	global_load_lds_dwordx4 v[216:217], off offset:128
	s_mov_b32 m0, s34
	s_nop 0
	global_load_lds_dwordx4 v132, s[28:29]
	s_add_i32 m0, s34, 0x2000
	s_nop 0
	global_load_lds_dwordx4 v134, s[28:29]
	s_add_i32 m0, s46, 0xffffff80
	s_nop 0
	global_load_lds_dwordx4 v[218:219], off offset:128
	s_add_i32 m0, s47, 0xffffff80
	s_nop 0
	global_load_lds_dwordx4 v[220:221], off offset:128
	s_waitcnt vmcnt(8)
	s_waitcnt lgkmcnt(0)
	s_barrier
	s_setprio 3
	s_waitcnt lgkmcnt(0)
	v_mfma_f32_16x16x32_bf16 v[62:65], v[142:145], v[182:185], v[62:65]
	v_mfma_f32_16x16x32_bf16 v[58:61], v[158:161], v[182:185], v[58:61]
	v_mfma_f32_16x16x32_bf16 v[46:49], v[142:145], v[190:193], v[46:49]
	v_mfma_f32_16x16x32_bf16 v[42:45], v[158:161], v[190:193], v[42:45]
	v_mfma_f32_16x16x32_bf16 v[30:33], v[142:145], v[198:201], v[30:33]
	v_mfma_f32_16x16x32_bf16 v[26:29], v[158:161], v[198:201], v[26:29]
	v_mfma_f32_16x16x32_bf16 v[14:17], v[142:145], v[206:209], v[14:17]
	v_mfma_f32_16x16x32_bf16 v[10:13], v[158:161], v[206:209], v[10:13]
	v_mfma_f32_16x16x32_bf16 v[62:65], v[154:157], v[186:189], v[62:65]
	v_mfma_f32_16x16x32_bf16 v[58:61], v[162:165], v[186:189], v[58:61]
	v_mfma_f32_16x16x32_bf16 v[46:49], v[154:157], v[194:197], v[46:49]
	v_mfma_f32_16x16x32_bf16 v[42:45], v[162:165], v[194:197], v[42:45]
	v_mfma_f32_16x16x32_bf16 v[30:33], v[154:157], v[202:205], v[30:33]
	v_mfma_f32_16x16x32_bf16 v[26:29], v[162:165], v[202:205], v[26:29]
	v_mfma_f32_16x16x32_bf16 v[14:17], v[154:157], v[210:213], v[14:17]
	v_mfma_f32_16x16x32_bf16 v[10:13], v[162:165], v[210:213], v[10:13]
	s_setprio 0
	s_setprio 3
	v_mfma_f32_16x16x32_bf16 v[54:57], v[166:169], v[182:185], v[54:57]
	v_mfma_f32_16x16x32_bf16 v[50:53], v[174:177], v[182:185], v[50:53]
	v_mfma_f32_16x16x32_bf16 v[38:41], v[166:169], v[190:193], v[38:41]
	v_mfma_f32_16x16x32_bf16 v[34:37], v[174:177], v[190:193], v[34:37]
	v_mfma_f32_16x16x32_bf16 v[22:25], v[166:169], v[198:201], v[22:25]
	v_mfma_f32_16x16x32_bf16 v[18:21], v[174:177], v[198:201], v[18:21]
	v_mfma_f32_16x16x32_bf16 v[6:9], v[166:169], v[206:209], v[6:9]
	v_mfma_f32_16x16x32_bf16 v[2:5], v[174:177], v[206:209], v[2:5]
	v_mfma_f32_16x16x32_bf16 v[54:57], v[170:173], v[186:189], v[54:57]
	v_mfma_f32_16x16x32_bf16 v[50:53], v[178:181], v[186:189], v[50:53]
	v_mfma_f32_16x16x32_bf16 v[38:41], v[170:173], v[194:197], v[38:41]
	v_mfma_f32_16x16x32_bf16 v[34:37], v[178:181], v[194:197], v[34:37]
	v_mfma_f32_16x16x32_bf16 v[22:25], v[170:173], v[202:205], v[22:25]
	v_mfma_f32_16x16x32_bf16 v[18:21], v[178:181], v[202:205], v[18:21]
	v_mfma_f32_16x16x32_bf16 v[6:9], v[170:173], v[210:213], v[6:9]
	v_mfma_f32_16x16x32_bf16 v[2:5], v[178:181], v[210:213], v[2:5]
	s_setprio 0
	s_barrier
	s_add_i32 s56, s56, 2
	s_add_u32 s54, s54, 0x100
	s_addc_u32 s55, s55, 0
	s_cmp_gt_u32 s56, 11
	s_mov_b64 s[28:29], s[30:31]
	s_cbranch_scc0 .LBB0_1844
	s_and_b64 vcc, exec, s[20:21]
	s_cbranch_vccz .LBB0_1847
	s_barrier
